# nt on once-read f32 streams: expert-weight loads in P1/P6/P16 converters, P0 x rows and projection weights, P4 residual x (G_P1=128)
# speedup vs baseline: 1.0116x; 1.0004x over previous
; #define LAS __attribute__((address_space(3)))
; #define LDS_WAIT() asm volatile("s_waitcnt lgkmcnt(0)" ::: "memory")
; __device__ __forceinline__ void cvt_item8(const float* __restrict__ src, int K, int N, unsigned char* dst, int kb, int nb, int drow0, float wscale, LAS float* scr, int lane) {
;     const int k0 = kb * 64, n0 = nb * 64;
;     const float* s = src + (size_t)(k0 + (lane >> 4)) * N + n0 + 4 * (lane & 15);
;     f32x4 v[16];
; #pragma unroll
;     for (int i = 0; i < 16; ++i) v[i] = *(const f32x4*)(s + (size_t)(4 * i) * N);
; #pragma unroll
;     for (int i = 0; i < 16; ++i) { LAS float* p = scr + (4 * i + (lane >> 4)) * 65 + 4 * (lane & 15); p[0] = v[i].x * wscale; p[1] = v[i].y * wscale; p[2] = v[i].z * wscale; p[3] = v[i].w * wscale; }
;     LDS_WAIT();
; __device__ __forceinline__ void cvt_dense8(const float* w, int K, int N, unsigned char* dst, LAS float* scr, int gw, int NGW, int lane) {
;     const int nnb = N / 64, items = (K / 64) * nnb;
;     for (int it = gw; it < items; it += NGW) cvt_item8(w, K, N, dst, it / nnb, it % nnb, (it % nnb) * 64, 64.f, scr, lane);
; }
.LBB0_10:
	s_mul_hi_i32 s2, s23, 0x38e38e39
	s_lshr_b32 s3, s2, 31
	s_ashr_i32 s2, s2, 3
	s_add_i32 s2, s2, s3
	s_mul_i32 s3, s2, 0xfffff700
	s_lshl_b32 s2, s2, 6
	s_add_i32 s24, s0, s3
	v_or_b32_e32 v24, s2, v1
	s_movk_i32 s25, 0x2400
	v_mad_i64_i32 v[24:25], s[26:27], v24, s25, v[22:23]
	s_ashr_i32 s25, s24, 31
	s_ashr_i32 s3, s2, 31
	v_lshl_add_u64 v[24:25], s[24:25], 2, v[24:25]
	v_lshl_add_u64 v[30:31], v[20:21], 0, s[2:3]
	v_lshl_add_u64 v[136:137], v[24:25], 0, v[18:19]
	s_mov_b32 s2, 0x9000
	v_add_co_u32_e32 v78, vcc, s2, v136
	v_add_u32_e32 v26, s24, v32
	s_mov_b64 s[2:3], vcc
	s_mov_b32 s24, 0x12000
	v_add_co_u32_e32 v80, vcc, s24, v136
	v_addc_co_u32_e64 v79, s[2:3], 0, v137, s[2:3]
	s_mov_b64 s[2:3], vcc
	s_mov_b32 s24, 0x1b000
	v_add_co_u32_e32 v82, vcc, s24, v136
	v_addc_co_u32_e64 v81, s[2:3], 0, v137, s[2:3]
	s_mov_b64 s[2:3], vcc
	s_mov_b32 s24, 0x24000
	v_add_co_u32_e32 v86, vcc, s24, v136
	v_addc_co_u32_e64 v83, s[2:3], 0, v137, s[2:3]
	s_mov_b64 s[2:3], vcc
	s_mov_b32 s24, 0x2d000
	v_add_co_u32_e32 v90, vcc, s24, v136
	v_addc_co_u32_e64 v87, s[2:3], 0, v137, s[2:3]
	s_mov_b64 s[2:3], vcc
	v_add_co_u32_e32 v94, vcc, s5, v136
	v_addc_co_u32_e64 v91, s[2:3], 0, v137, s[2:3]
	s_mov_b64 s[2:3], vcc
	v_add_co_u32_e32 v98, vcc, s8, v136
	v_addc_co_u32_e64 v95, s[2:3], 0, v137, s[2:3]
	v_add_u32_e32 v28, 16, v26
	v_add_u32_e32 v74, 32, v26
	v_add_u32_e32 v76, 48, v26
	s_mov_b64 s[2:3], vcc
	v_ashrrev_i32_e32 v27, 31, v26
	v_ashrrev_i32_e32 v29, 31, v28
	v_ashrrev_i32_e32 v75, 31, v74
	v_ashrrev_i32_e32 v77, 31, v76
	v_add_co_u32_e32 v102, vcc, s9, v136
	v_addc_co_u32_e64 v99, s[2:3], 0, v137, s[2:3]
	v_lshlrev_b64 v[24:25], 10, v[26:27]
	global_load_dwordx4 v[70:73], v[136:137], off nt
	v_lshlrev_b64 v[26:27], 10, v[28:29]
	v_lshlrev_b64 v[28:29], 10, v[74:75]
	v_lshlrev_b64 v[74:75], 10, v[76:77]
	s_mov_b64 s[2:3], vcc
	v_lshl_add_u64 v[24:25], v[30:31], 0, v[24:25]
	v_lshl_add_u64 v[26:27], v[30:31], 0, v[26:27]
	v_lshl_add_u64 v[28:29], v[30:31], 0, v[28:29]
	v_lshl_add_u64 v[30:31], v[30:31], 0, v[74:75]
	global_load_dwordx4 v[74:77], v[78:79], off nt
	v_add_co_u32_e32 v106, vcc, s10, v136
	v_addc_co_u32_e64 v103, s[2:3], 0, v137, s[2:3]
	global_load_dwordx4 v[82:85], v[82:83], off nt
	s_mov_b64 s[2:3], vcc
	global_load_dwordx4 v[78:81], v[80:81], off nt
	v_add_co_u32_e32 v110, vcc, s11, v136
	v_addc_co_u32_e64 v107, s[2:3], 0, v137, s[2:3]
	global_load_dwordx4 v[86:89], v[86:87], off nt
	s_mov_b64 s[2:3], vcc
	global_load_dwordx4 v[90:93], v[90:91], off nt
	v_add_co_u32_e32 v114, vcc, s18, v136
	v_addc_co_u32_e64 v111, s[2:3], 0, v137, s[2:3]
	global_load_dwordx4 v[94:97], v[94:95], off nt
	s_mov_b64 s[2:3], vcc
	global_load_dwordx4 v[98:101], v[98:99], off nt
	v_add_co_u32_e32 v118, vcc, s19, v136
	v_addc_co_u32_e64 v115, s[2:3], 0, v137, s[2:3]
	global_load_dwordx4 v[102:105], v[102:103], off nt
	s_mov_b64 s[2:3], vcc
	global_load_dwordx4 v[106:109], v[106:107], off nt
	v_add_co_u32_e32 v122, vcc, s20, v136
	v_addc_co_u32_e64 v119, s[2:3], 0, v137, s[2:3]
	global_load_dwordx4 v[110:113], v[110:111], off nt
	s_mov_b64 s[2:3], vcc
	global_load_dwordx4 v[114:117], v[114:115], off nt
	v_add_co_u32_e32 v126, vcc, s21, v136
	v_addc_co_u32_e64 v123, s[2:3], 0, v137, s[2:3]
	global_load_dwordx4 v[118:121], v[118:119], off nt
	s_mov_b64 s[2:3], vcc
	global_load_dwordx4 v[122:125], v[122:123], off nt
	v_add_co_u32_e32 v136, vcc, s22, v136
	v_addc_co_u32_e64 v127, s[2:3], 0, v137, s[2:3]
	global_load_dwordx4 v[126:129], v[126:127], off nt
	v_addc_co_u32_e32 v137, vcc, 0, v137, vcc
	global_load_dwordx4 v[136:139], v[136:137], off nt
	v_mov_b32_e32 v2, 0
	v_mov_b32_e32 v3, 0
	v_mov_b32_e32 v4, 0
	v_mov_b32_e32 v5, 0
	v_mov_b32_e32 v6, 0
	v_mov_b32_e32 v7, 0
	v_mov_b32_e32 v8, 0
	v_mov_b32_e32 v9, 0
	v_mov_b32_e32 v10, 0
	v_mov_b32_e32 v11, 0
	v_mov_b32_e32 v12, 0
	v_mov_b32_e32 v13, 0
	v_mov_b32_e32 v14, 0
	v_mov_b32_e32 v15, 0
	v_mov_b32_e32 v16, 0
	v_mov_b32_e32 v17, 0
	s_add_i32 s23, s23, s28
	s_add_i32 s0, s0, s1
	s_cmpk_lt_i32 s23, 0x240
	s_waitcnt vmcnt(15)
	v_pk_mul_f32 v[70:71], v[70:71], s[4:5] op_sel_hi:[1,0]
	v_pk_mul_f32 v[72:73], v[72:73], s[4:5] op_sel_hi:[1,0]
	ds_write2_b32 v35, v70, v71 offset1:1
	ds_write2_b32 v35, v72, v73 offset0:2 offset1:3
	s_waitcnt vmcnt(14)
	v_pk_mul_f32 v[70:71], v[74:75], s[4:5] op_sel_hi:[1,0]
	v_pk_mul_f32 v[72:73], v[76:77], s[4:5] op_sel_hi:[1,0]
	ds_write2_b32 v36, v70, v71 offset1:1
	ds_write2_b32 v37, v72, v73 offset1:1
	s_waitcnt vmcnt(12)
	v_pk_mul_f32 v[70:71], v[78:79], s[4:5] op_sel_hi:[1,0]
	v_pk_mul_f32 v[72:73], v[80:81], s[4:5] op_sel_hi:[1,0]
	ds_write2_b32 v38, v70, v71 offset1:1
	ds_write2_b32 v39, v72, v73 offset1:1
	v_pk_mul_f32 v[70:71], v[82:83], s[4:5] op_sel_hi:[1,0]
	v_pk_mul_f32 v[72:73], v[84:85], s[4:5] op_sel_hi:[1,0]
	ds_write2_b32 v40, v70, v71 offset1:1
	ds_write2_b32 v41, v72, v73 offset1:1
	s_waitcnt vmcnt(11)
	v_pk_mul_f32 v[70:71], v[86:87], s[4:5] op_sel_hi:[1,0]
	v_pk_mul_f32 v[72:73], v[88:89], s[4:5] op_sel_hi:[1,0]
	ds_write2_b32 v42, v70, v71 offset1:1
	ds_write2_b32 v43, v72, v73 offset1:1
	s_waitcnt vmcnt(10)
	v_pk_mul_f32 v[70:71], v[90:91], s[4:5] op_sel_hi:[1,0]
	v_pk_mul_f32 v[72:73], v[92:93], s[4:5] op_sel_hi:[1,0]
	ds_write2_b32 v44, v70, v71 offset1:1
	ds_write2_b32 v45, v72, v73 offset1:1
	s_waitcnt vmcnt(9)
; __device__ __forceinline__ unsigned pk4_fp8(float a, float b, float c, float d) { unsigned w = 0u; w = __builtin_amdgcn_cvt_pk_fp8_f32(a, b, w, false); w = __builtin_amdgcn_cvt_pk_fp8_f32(c, d, w, true); return w; }
; #define LAS __attribute__((address_space(3)))
; #define LDS_WAIT() asm volatile("s_waitcnt lgkmcnt(0)" ::: "memory")
; __device__ __forceinline__ void cvt_item8(const float* __restrict__ src, int K, int N, unsigned char* dst, int kb, int nb, int drow0, float wscale, LAS float* scr, int lane) {
;     ...
; #pragma unroll
;     for (int i = 0; i < 16; ++i) { LAS float* p = scr + (4 * i + (lane >> 4)) * 65 + 4 * (lane & 15); p[0] = v[i].x * wscale; p[1] = v[i].y * wscale; p[2] = v[i].z * wscale; p[3] = v[i].w * wscale; }
;     LDS_WAIT();
;     const int c = lane & 3;
; #pragma unroll
;     for (int j = 0; j < 4; ++j) { const int n = (lane >> 2) + 16 * j; const LAS float* q = scr + (16 * c) * 65 + n;
;         v4u o; o.x = pg8::pk4_fp8(q[0], q[65], q[130], q[195]); o.y = pg8::pk4_fp8(q[260], q[325], q[390], q[455]);
;         o.z = pg8::pk4_fp8(q[520], q[585], q[650], q[715]); o.w = pg8::pk4_fp8(q[780], q[845], q[910], q[975]);
;         *(v4u*)(dst + (size_t)(drow0 + n) * K + k0 + 16 * c) = o; }
;     LDS_WAIT();
; }
	v_pk_mul_f32 v[70:71], v[94:95], s[4:5] op_sel_hi:[1,0]
	v_pk_mul_f32 v[72:73], v[96:97], s[4:5] op_sel_hi:[1,0]
	ds_write2_b32 v46, v70, v71 offset1:1
	ds_write2_b32 v47, v72, v73 offset1:1
	s_waitcnt vmcnt(8)
	v_pk_mul_f32 v[70:71], v[98:99], s[4:5] op_sel_hi:[1,0]
	v_pk_mul_f32 v[72:73], v[100:101], s[4:5] op_sel_hi:[1,0]
	ds_write2_b32 v48, v70, v71 offset1:1
	ds_write2_b32 v49, v72, v73 offset1:1
	s_waitcnt vmcnt(7)
	v_pk_mul_f32 v[70:71], v[102:103], s[4:5] op_sel_hi:[1,0]
	v_pk_mul_f32 v[72:73], v[104:105], s[4:5] op_sel_hi:[1,0]
	ds_write2_b32 v50, v70, v71 offset1:1
	ds_write2_b32 v51, v72, v73 offset1:1
	s_waitcnt vmcnt(6)
	v_pk_mul_f32 v[70:71], v[106:107], s[4:5] op_sel_hi:[1,0]
	v_pk_mul_f32 v[72:73], v[108:109], s[4:5] op_sel_hi:[1,0]
	ds_write2_b32 v52, v70, v71 offset1:1
	ds_write2_b32 v53, v72, v73 offset1:1
	s_waitcnt vmcnt(5)
	v_pk_mul_f32 v[70:71], v[110:111], s[4:5] op_sel_hi:[1,0]
	v_pk_mul_f32 v[72:73], v[112:113], s[4:5] op_sel_hi:[1,0]
	ds_write2_b32 v54, v70, v71 offset1:1
	ds_write2_b32 v55, v72, v73 offset1:1
	s_waitcnt vmcnt(4)
	v_pk_mul_f32 v[70:71], v[114:115], s[4:5] op_sel_hi:[1,0]
	v_pk_mul_f32 v[72:73], v[116:117], s[4:5] op_sel_hi:[1,0]
	ds_write2_b32 v56, v70, v71 offset1:1
	ds_write2_b32 v57, v72, v73 offset1:1
	s_waitcnt vmcnt(3)
	v_pk_mul_f32 v[70:71], v[118:119], s[4:5] op_sel_hi:[1,0]
	v_pk_mul_f32 v[72:73], v[120:121], s[4:5] op_sel_hi:[1,0]
	ds_write2_b32 v58, v70, v71 offset1:1
	ds_write2_b32 v59, v72, v73 offset1:1
	s_waitcnt vmcnt(2)
	v_pk_mul_f32 v[70:71], v[122:123], s[4:5] op_sel_hi:[1,0]
	v_pk_mul_f32 v[72:73], v[124:125], s[4:5] op_sel_hi:[1,0]
	ds_write2_b32 v60, v70, v71 offset1:1
	ds_write2_b32 v61, v72, v73 offset1:1
	s_waitcnt vmcnt(1)
	v_pk_mul_f32 v[70:71], v[126:127], s[4:5] op_sel_hi:[1,0]
	v_pk_mul_f32 v[72:73], v[128:129], s[4:5] op_sel_hi:[1,0]
	ds_write2_b32 v62, v70, v71 offset1:1
	ds_write2_b32 v63, v72, v73 offset1:1
	s_waitcnt vmcnt(0)
	v_pk_mul_f32 v[70:71], v[136:137], s[4:5] op_sel_hi:[1,0]
	v_pk_mul_f32 v[72:73], v[138:139], s[4:5] op_sel_hi:[1,0]
	ds_write2_b32 v64, v70, v71 offset1:1
	ds_write2_b32 v65, v72, v73 offset1:1
	s_waitcnt lgkmcnt(0)
	ds_read2_b32 v[70:71], v34 offset1:16
	ds_read2_b32 v[72:73], v34 offset0:65 offset1:81
	ds_read2_b32 v[74:75], v66 offset0:4 offset1:20
	ds_read2_b32 v[76:77], v66 offset0:69 offset1:85
	ds_read2_b32 v[78:79], v67 offset0:8 offset1:24
	ds_read2_b32 v[80:81], v67 offset0:73 offset1:89
	ds_read2_b32 v[82:83], v68 offset0:12 offset1:28
	ds_read2_b32 v[84:85], v68 offset0:77 offset1:93
	ds_read2_b32 v[86:87], v34 offset0:32 offset1:48
	ds_read2_b32 v[88:89], v34 offset0:97 offset1:113
	ds_read2_b32 v[90:91], v66 offset0:36 offset1:52
	ds_read2_b32 v[92:93], v66 offset0:101 offset1:117
	ds_read2_b32 v[94:95], v67 offset0:40 offset1:56
	ds_read2_b32 v[96:97], v67 offset0:105 offset1:121
	ds_read2_b32 v[98:99], v68 offset0:44 offset1:60
	ds_read2_b32 v[100:101], v68 offset0:109 offset1:125
	ds_read2_b32 v[102:103], v34 offset0:130 offset1:146
	ds_read2_b32 v[104:105], v34 offset0:195 offset1:211
	ds_read2_b32 v[106:107], v66 offset0:134 offset1:150
	ds_read2_b32 v[108:109], v66 offset0:199 offset1:215
	ds_read2_b32 v[110:111], v67 offset0:138 offset1:154
	ds_read2_b32 v[112:113], v67 offset0:203 offset1:219
	ds_read2_b32 v[114:115], v68 offset0:142 offset1:158
	ds_read2_b32 v[116:117], v68 offset0:207 offset1:223
	ds_read2_b32 v[118:119], v34 offset0:162 offset1:178
	ds_read2_b32 v[120:121], v34 offset0:227 offset1:243
	ds_read2_b32 v[122:123], v66 offset0:166 offset1:182
	ds_read2_b32 v[124:125], v66 offset0:231 offset1:247
	ds_read2_b32 v[126:127], v67 offset0:170 offset1:186
	ds_read2_b32 v[128:129], v67 offset0:235 offset1:251
	ds_read2_b32 v[136:137], v68 offset0:174 offset1:190
	ds_read2_b32 v[138:139], v68 offset0:239 offset1:255
	s_waitcnt lgkmcnt(14)
	v_cvt_pk_fp8_f32 v2, v70, v72
	v_cvt_pk_fp8_f32 v3, v74, v76
	v_cvt_pk_fp8_f32 v4, v78, v80
	v_cvt_pk_fp8_f32 v5, v82, v84
	v_cvt_pk_fp8_f32 v6, v71, v73
	v_cvt_pk_fp8_f32 v7, v75, v77
	v_cvt_pk_fp8_f32 v8, v79, v81
	v_cvt_pk_fp8_f32 v9, v83, v85
	v_cvt_pk_fp8_f32 v10, v86, v88
	v_cvt_pk_fp8_f32 v11, v90, v92
	v_cvt_pk_fp8_f32 v12, v94, v96
	v_cvt_pk_fp8_f32 v13, v98, v100
	v_cvt_pk_fp8_f32 v14, v87, v89
	v_cvt_pk_fp8_f32 v15, v91, v93
	v_cvt_pk_fp8_f32 v16, v95, v97
	v_cvt_pk_fp8_f32 v17, v99, v101
	v_cvt_pk_fp8_f32 v2, v102, v104 op_sel:[0,0,1]
	s_waitcnt lgkmcnt(12)
	v_cvt_pk_fp8_f32 v3, v106, v108 op_sel:[0,0,1]
	s_waitcnt lgkmcnt(10)
	v_cvt_pk_fp8_f32 v4, v110, v112 op_sel:[0,0,1]
	s_waitcnt lgkmcnt(8)
	v_cvt_pk_fp8_f32 v5, v114, v116 op_sel:[0,0,1]
	v_cvt_pk_fp8_f32 v6, v103, v105 op_sel:[0,0,1]
	v_cvt_pk_fp8_f32 v7, v107, v109 op_sel:[0,0,1]
	v_cvt_pk_fp8_f32 v8, v111, v113 op_sel:[0,0,1]
	v_cvt_pk_fp8_f32 v9, v115, v117 op_sel:[0,0,1]
	s_waitcnt lgkmcnt(6)
	v_cvt_pk_fp8_f32 v10, v118, v120 op_sel:[0,0,1]
	s_waitcnt lgkmcnt(4)
	v_cvt_pk_fp8_f32 v11, v122, v124 op_sel:[0,0,1]
	s_waitcnt lgkmcnt(2)
	v_cvt_pk_fp8_f32 v12, v126, v128 op_sel:[0,0,1]
	s_waitcnt lgkmcnt(0)
	v_cvt_pk_fp8_f32 v13, v136, v138 op_sel:[0,0,1]
	v_cvt_pk_fp8_f32 v14, v119, v121 op_sel:[0,0,1]
	v_cvt_pk_fp8_f32 v15, v123, v125 op_sel:[0,0,1]
	v_cvt_pk_fp8_f32 v16, v127, v129 op_sel:[0,0,1]
	v_cvt_pk_fp8_f32 v17, v137, v139 op_sel:[0,0,1]
	global_store_dwordx4 v[24:25], v[2:5], off
	global_store_dwordx4 v[26:27], v[6:9], off
	global_store_dwordx4 v[28:29], v[10:13], off
	global_store_dwordx4 v[30:31], v[14:17], off
	s_waitcnt lgkmcnt(0)
	s_cbranch_scc1 .LBB0_10

; #define LAS __attribute__((address_space(3)))
; __device__ __forceinline__ void cvt_item8(const float* __restrict__ src, int K, int N, unsigned char* dst, int kb, int nb, int drow0, float wscale, LAS float* scr, int lane) {
;     const int k0 = kb * 64, n0 = nb * 64;
;     const float* s = src + (size_t)(k0 + (lane >> 4)) * N + n0 + 4 * (lane & 15);
;     f32x4 v[16];
; #pragma unroll
;     for (int i = 0; i < 16; ++i) v[i] = *(const f32x4*)(s + (size_t)(4 * i) * N);
; #pragma unroll
;     for (int i = 0; i < 16; ++i) { LAS float* p = scr + (4 * i + (lane >> 4)) * 65 + 4 * (lane & 15); p[0] = v[i].x * wscale; p[1] = v[i].y * wscale; p[2] = v[i].z * wscale; p[3] = v[i].w * wscale; }
; __device__ __forceinline__ void cvt_dense8(const float* w, int K, int N, unsigned char* dst, LAS float* scr, int gw, int NGW, int lane) {
;     const int nnb = N / 64, items = (K / 64) * nnb;
;     for (int it = gw; it < items; it += NGW) cvt_item8(w, K, N, dst, it / nnb, it % nnb, (it % nnb) * 64, 64.f, scr, lane);
; }
.LBB0_13:
	s_ashr_i32 s23, s22, 31
	s_lshr_b32 s23, s23, 28
	s_add_i32 s23, s22, s23
	s_ashr_i32 s23, s23, 4
	s_lshl_b32 s24, s23, 6
	v_or_b32_e32 v22, s24, v1
	s_lshl_b32 s25, s23, 10
	v_ashrrev_i32_e32 v23, 31, v22
	s_sub_i32 s26, s0, s25
	v_lshlrev_b64 v[22:23], 12, v[22:23]
	s_ashr_i32 s27, s26, 31
	v_lshl_add_u64 v[22:23], s[76:77], 0, v[22:23]
	v_lshl_add_u64 v[72:73], s[26:27], 2, v[22:23]
	v_lshl_add_u64 v[72:73], v[72:73], 0, v[18:19]
	s_movk_i32 s23, 0x4000
	v_add_co_u32_e32 v74, vcc, s23, v72
	s_mov_b32 s23, 0x8000
	s_nop 0
	v_addc_co_u32_e32 v75, vcc, 0, v73, vcc
	v_add_co_u32_e32 v76, vcc, s23, v72
	s_mov_b32 s23, 0xc000
	s_nop 0
	v_addc_co_u32_e32 v77, vcc, 0, v73, vcc
	v_add_co_u32_e32 v80, vcc, s23, v72
	s_mov_b32 s23, 0x10000
	s_nop 0
	v_addc_co_u32_e32 v81, vcc, 0, v73, vcc
	v_add_co_u32_e32 v84, vcc, s23, v72
	s_mov_b32 s23, 0x14000
	s_nop 0
	v_addc_co_u32_e32 v85, vcc, 0, v73, vcc
	v_add_co_u32_e32 v88, vcc, s23, v72
	s_mov_b32 s23, 0x18000
	s_nop 0
	v_addc_co_u32_e32 v89, vcc, 0, v73, vcc
	v_add_co_u32_e32 v92, vcc, s23, v72
	v_add_u32_e32 v24, s26, v32
	s_nop 0
	v_addc_co_u32_e32 v93, vcc, 0, v73, vcc
	v_add_co_u32_e32 v96, vcc, s3, v72
	s_ashr_i32 s25, s24, 31
	s_nop 0
	v_addc_co_u32_e32 v97, vcc, 0, v73, vcc
	v_add_co_u32_e32 v100, vcc, s8, v72
	v_ashrrev_i32_e32 v25, 31, v24
	s_nop 0
	v_addc_co_u32_e32 v101, vcc, 0, v73, vcc
	v_add_co_u32_e32 v104, vcc, s9, v72
	v_add_u32_e32 v26, 16, v24
	s_nop 0
	v_addc_co_u32_e32 v105, vcc, 0, v73, vcc
	v_add_co_u32_e32 v108, vcc, s10, v72
	v_add_u32_e32 v68, 32, v24
	s_nop 0
	v_addc_co_u32_e32 v109, vcc, 0, v73, vcc
	v_add_co_u32_e32 v112, vcc, s11, v72
	v_add_u32_e32 v70, 48, v24
	s_nop 0
	v_addc_co_u32_e32 v113, vcc, 0, v73, vcc
	v_add_co_u32_e32 v116, vcc, s18, v72
	v_lshl_add_u64 v[28:29], v[20:21], 0, s[24:25]
	s_nop 0
	v_addc_co_u32_e32 v117, vcc, 0, v73, vcc
	v_add_co_u32_e32 v120, vcc, s19, v72
	v_lshlrev_b64 v[24:25], 10, v[24:25]
	v_ashrrev_i32_e32 v27, 31, v26
	v_ashrrev_i32_e32 v69, 31, v68
	v_ashrrev_i32_e32 v71, 31, v70
	v_addc_co_u32_e32 v121, vcc, 0, v73, vcc
	v_lshl_add_u64 v[22:23], v[28:29], 0, v[24:25]
	v_lshlrev_b64 v[24:25], 10, v[26:27]
	v_lshlrev_b64 v[26:27], 10, v[68:69]
	v_lshlrev_b64 v[68:69], 10, v[70:71]
	v_add_co_u32_e32 v124, vcc, s20, v72
	v_lshl_add_u64 v[24:25], v[28:29], 0, v[24:25]
	v_lshl_add_u64 v[26:27], v[28:29], 0, v[26:27]
	v_lshl_add_u64 v[28:29], v[28:29], 0, v[68:69]
	global_load_dwordx4 v[68:71], v[72:73], off nt
	v_addc_co_u32_e32 v125, vcc, 0, v73, vcc
	v_add_co_u32_e32 v128, vcc, s21, v72
	v_mov_b32_e32 v2, 0
	s_nop 0
	v_addc_co_u32_e32 v129, vcc, 0, v73, vcc
	global_load_dwordx4 v[72:75], v[74:75], off nt
	s_nop 0
	global_load_dwordx4 v[76:79], v[76:77], off nt
	s_nop 0
	global_load_dwordx4 v[80:83], v[80:81], off nt
	s_nop 0
	global_load_dwordx4 v[84:87], v[84:85], off nt
	s_nop 0
	global_load_dwordx4 v[88:91], v[88:89], off nt
	s_nop 0
	global_load_dwordx4 v[92:95], v[92:93], off nt
	s_nop 0
	global_load_dwordx4 v[96:99], v[96:97], off nt
	s_nop 0
	global_load_dwordx4 v[100:103], v[100:101], off nt
	s_nop 0
	global_load_dwordx4 v[104:107], v[104:105], off nt
	s_nop 0
	global_load_dwordx4 v[108:111], v[108:109], off nt
	s_nop 0
	global_load_dwordx4 v[112:115], v[112:113], off nt
	s_nop 0
	global_load_dwordx4 v[116:119], v[116:117], off nt
	s_nop 0
	global_load_dwordx4 v[120:123], v[120:121], off nt
	s_nop 0
	global_load_dwordx4 v[124:127], v[124:125], off nt
	s_nop 0
	global_load_dwordx4 v[136:139], v[128:129], off nt
	v_mov_b32_e32 v3, 0
	v_mov_b32_e32 v4, 0
	v_mov_b32_e32 v5, 0
	v_mov_b32_e32 v6, 0
	v_mov_b32_e32 v7, 0
	v_mov_b32_e32 v8, 0
	v_mov_b32_e32 v9, 0
	v_mov_b32_e32 v10, 0
	v_mov_b32_e32 v11, 0
	v_mov_b32_e32 v12, 0
	v_mov_b32_e32 v13, 0
	v_mov_b32_e32 v14, 0
	v_mov_b32_e32 v15, 0
	v_mov_b32_e32 v16, 0
	v_mov_b32_e32 v17, 0
	s_add_i32 s22, s22, s28
	s_add_i32 s0, s0, s1
	s_cmpk_lt_i32 s22, 0x100
	s_waitcnt vmcnt(15)
	v_pk_mul_f32 v[68:69], v[68:69], s[2:3] op_sel_hi:[1,0]
	v_pk_mul_f32 v[70:71], v[70:71], s[2:3] op_sel_hi:[1,0]
	ds_write2_b32 v31, v68, v69 offset1:1
	ds_write2_b32 v31, v70, v71 offset0:2 offset1:3
	s_waitcnt vmcnt(14)
	v_pk_mul_f32 v[68:69], v[72:73], s[2:3] op_sel_hi:[1,0]
	v_pk_mul_f32 v[70:71], v[74:75], s[2:3] op_sel_hi:[1,0]
	s_waitcnt vmcnt(13)
	v_pk_mul_f32 v[72:73], v[76:77], s[2:3] op_sel_hi:[1,0]
	v_pk_mul_f32 v[74:75], v[78:79], s[2:3] op_sel_hi:[1,0]
	s_waitcnt vmcnt(12)
	v_pk_mul_f32 v[76:77], v[80:81], s[2:3] op_sel_hi:[1,0]
	v_pk_mul_f32 v[78:79], v[82:83], s[2:3] op_sel_hi:[1,0]
	s_waitcnt vmcnt(11)
	v_pk_mul_f32 v[80:81], v[84:85], s[2:3] op_sel_hi:[1,0]
	v_pk_mul_f32 v[82:83], v[86:87], s[2:3] op_sel_hi:[1,0]
	s_waitcnt vmcnt(10)
	v_pk_mul_f32 v[84:85], v[88:89], s[2:3] op_sel_hi:[1,0]
	v_pk_mul_f32 v[86:87], v[90:91], s[2:3] op_sel_hi:[1,0]
	s_waitcnt vmcnt(9)
	v_pk_mul_f32 v[88:89], v[92:93], s[2:3] op_sel_hi:[1,0]
	v_pk_mul_f32 v[90:91], v[94:95], s[2:3] op_sel_hi:[1,0]
	s_waitcnt vmcnt(8)
	v_pk_mul_f32 v[92:93], v[96:97], s[2:3] op_sel_hi:[1,0]
	v_pk_mul_f32 v[94:95], v[98:99], s[2:3] op_sel_hi:[1,0]
	s_waitcnt vmcnt(7)
	v_pk_mul_f32 v[96:97], v[100:101], s[2:3] op_sel_hi:[1,0]
	v_pk_mul_f32 v[98:99], v[102:103], s[2:3] op_sel_hi:[1,0]
	s_waitcnt vmcnt(6)
	v_pk_mul_f32 v[100:101], v[104:105], s[2:3] op_sel_hi:[1,0]
	v_pk_mul_f32 v[102:103], v[106:107], s[2:3] op_sel_hi:[1,0]
	s_waitcnt vmcnt(5)
; __device__ __forceinline__ unsigned pk4_fp8(float a, float b, float c, float d) { unsigned w = 0u; w = __builtin_amdgcn_cvt_pk_fp8_f32(a, b, w, false); w = __builtin_amdgcn_cvt_pk_fp8_f32(c, d, w, true); return w; }
; #define LAS __attribute__((address_space(3)))
; #define LDS_WAIT() asm volatile("s_waitcnt lgkmcnt(0)" ::: "memory")
; __device__ __forceinline__ void cvt_item8(const float* __restrict__ src, int K, int N, unsigned char* dst, int kb, int nb, int drow0, float wscale, LAS float* scr, int lane) {
;     ...
;     for (int i = 0; i < 16; ++i) { LAS float* p = scr + (4 * i + (lane >> 4)) * 65 + 4 * (lane & 15); p[0] = v[i].x * wscale; p[1] = v[i].y * wscale; p[2] = v[i].z * wscale; p[3] = v[i].w * wscale; }
;     LDS_WAIT();
;     const int c = lane & 3;
; #pragma unroll
;     for (int j = 0; j < 4; ++j) { const int n = (lane >> 2) + 16 * j; const LAS float* q = scr + (16 * c) * 65 + n;
;         v4u o; o.x = pg8::pk4_fp8(q[0], q[65], q[130], q[195]); o.y = pg8::pk4_fp8(q[260], q[325], q[390], q[455]);
;         o.z = pg8::pk4_fp8(q[520], q[585], q[650], q[715]); o.w = pg8::pk4_fp8(q[780], q[845], q[910], q[975]);
;         *(v4u*)(dst + (size_t)(drow0 + n) * K + k0 + 16 * c) = o; }
;     LDS_WAIT();
	v_pk_mul_f32 v[104:105], v[108:109], s[2:3] op_sel_hi:[1,0]
	v_pk_mul_f32 v[106:107], v[110:111], s[2:3] op_sel_hi:[1,0]
	s_waitcnt vmcnt(4)
	v_pk_mul_f32 v[108:109], v[112:113], s[2:3] op_sel_hi:[1,0]
	v_pk_mul_f32 v[110:111], v[114:115], s[2:3] op_sel_hi:[1,0]
	s_waitcnt vmcnt(3)
	v_pk_mul_f32 v[112:113], v[116:117], s[2:3] op_sel_hi:[1,0]
	v_pk_mul_f32 v[114:115], v[118:119], s[2:3] op_sel_hi:[1,0]
	s_waitcnt vmcnt(2)
	v_pk_mul_f32 v[116:117], v[120:121], s[2:3] op_sel_hi:[1,0]
	v_pk_mul_f32 v[118:119], v[122:123], s[2:3] op_sel_hi:[1,0]
	s_waitcnt vmcnt(1)
	v_pk_mul_f32 v[120:121], v[124:125], s[2:3] op_sel_hi:[1,0]
	v_pk_mul_f32 v[122:123], v[126:127], s[2:3] op_sel_hi:[1,0]
	s_waitcnt vmcnt(0)
	v_pk_mul_f32 v[124:125], v[136:137], s[2:3] op_sel_hi:[1,0]
	v_pk_mul_f32 v[126:127], v[138:139], s[2:3] op_sel_hi:[1,0]
	ds_write2_b32 v34, v68, v69 offset1:1
	ds_write2_b32 v35, v70, v71 offset1:1
	ds_write2_b32 v36, v72, v73 offset1:1
	ds_write2_b32 v37, v74, v75 offset1:1
	ds_write2_b32 v38, v76, v77 offset1:1
	ds_write2_b32 v39, v78, v79 offset1:1
	ds_write2_b32 v40, v80, v81 offset1:1
	ds_write2_b32 v41, v82, v83 offset1:1
	ds_write2_b32 v42, v84, v85 offset1:1
	ds_write2_b32 v43, v86, v87 offset1:1
	ds_write2_b32 v44, v88, v89 offset1:1
	ds_write2_b32 v45, v90, v91 offset1:1
	ds_write2_b32 v46, v92, v93 offset1:1
	ds_write2_b32 v47, v94, v95 offset1:1
	ds_write2_b32 v48, v96, v97 offset1:1
	ds_write2_b32 v49, v98, v99 offset1:1
	ds_write2_b32 v50, v100, v101 offset1:1
	ds_write2_b32 v51, v102, v103 offset1:1
	ds_write2_b32 v52, v104, v105 offset1:1
	ds_write2_b32 v53, v106, v107 offset1:1
	ds_write2_b32 v54, v108, v109 offset1:1
	ds_write2_b32 v55, v110, v111 offset1:1
	ds_write2_b32 v56, v112, v113 offset1:1
	ds_write2_b32 v57, v114, v115 offset1:1
	ds_write2_b32 v58, v116, v117 offset1:1
	ds_write2_b32 v59, v118, v119 offset1:1
	ds_write2_b32 v60, v120, v121 offset1:1
	ds_write2_b32 v61, v122, v123 offset1:1
	ds_write2_b32 v62, v124, v125 offset1:1
	ds_write2_b32 v63, v126, v127 offset1:1
	s_waitcnt lgkmcnt(0)
	ds_read2_b32 v[68:69], v30 offset1:16
	ds_read2_b32 v[70:71], v30 offset0:65 offset1:81
	ds_read2_b32 v[72:73], v30 offset0:130 offset1:146
	ds_read2_b32 v[74:75], v30 offset0:195 offset1:211
	ds_read2_b32 v[76:77], v64 offset0:4 offset1:20
	ds_read2_b32 v[78:79], v64 offset0:69 offset1:85
	ds_read2_b32 v[80:81], v64 offset0:134 offset1:150
	ds_read2_b32 v[82:83], v64 offset0:199 offset1:215
	ds_read2_b32 v[84:85], v65 offset0:8 offset1:24
	ds_read2_b32 v[86:87], v65 offset0:73 offset1:89
	ds_read2_b32 v[88:89], v65 offset0:138 offset1:154
	ds_read2_b32 v[90:91], v65 offset0:203 offset1:219
	ds_read2_b32 v[92:93], v66 offset0:12 offset1:28
	ds_read2_b32 v[94:95], v66 offset0:77 offset1:93
	ds_read2_b32 v[96:97], v66 offset0:142 offset1:158
	ds_read2_b32 v[98:99], v66 offset0:207 offset1:223
	ds_read2_b32 v[100:101], v30 offset0:32 offset1:48
	ds_read2_b32 v[102:103], v30 offset0:97 offset1:113
	ds_read2_b32 v[104:105], v30 offset0:162 offset1:178
	ds_read2_b32 v[106:107], v64 offset0:36 offset1:52
	ds_read2_b32 v[108:109], v64 offset0:101 offset1:117
	ds_read2_b32 v[110:111], v65 offset0:40 offset1:56
	ds_read2_b32 v[112:113], v65 offset0:105 offset1:121
	ds_read2_b32 v[114:115], v66 offset0:44 offset1:60
	ds_read2_b32 v[116:117], v66 offset0:109 offset1:125
	ds_read2_b32 v[118:119], v30 offset0:227 offset1:243
	ds_read2_b32 v[120:121], v64 offset0:166 offset1:182
	ds_read2_b32 v[122:123], v64 offset0:231 offset1:247
	ds_read2_b32 v[124:125], v65 offset0:170 offset1:186
	ds_read2_b32 v[126:127], v65 offset0:235 offset1:251
	ds_read2_b32 v[128:129], v66 offset0:174 offset1:190
	ds_read2_b32 v[136:137], v66 offset0:239 offset1:255
	s_waitcnt lgkmcnt(14)
	v_cvt_pk_fp8_f32 v2, v68, v70
	v_cvt_pk_fp8_f32 v3, v76, v78
	v_cvt_pk_fp8_f32 v4, v84, v86
	v_cvt_pk_fp8_f32 v5, v92, v94
	v_cvt_pk_fp8_f32 v6, v69, v71
	v_cvt_pk_fp8_f32 v7, v77, v79
	v_cvt_pk_fp8_f32 v8, v85, v87
	v_cvt_pk_fp8_f32 v9, v93, v95
	v_cvt_pk_fp8_f32 v10, v100, v102
	s_waitcnt lgkmcnt(11)
	v_cvt_pk_fp8_f32 v11, v106, v108
	s_waitcnt lgkmcnt(9)
	v_cvt_pk_fp8_f32 v12, v110, v112
	s_waitcnt lgkmcnt(7)
	v_cvt_pk_fp8_f32 v13, v114, v116
	v_cvt_pk_fp8_f32 v14, v101, v103
	v_cvt_pk_fp8_f32 v15, v107, v109
	v_cvt_pk_fp8_f32 v16, v111, v113
	v_cvt_pk_fp8_f32 v17, v115, v117
	v_cvt_pk_fp8_f32 v2, v72, v74 op_sel:[0,0,1]
	v_cvt_pk_fp8_f32 v3, v80, v82 op_sel:[0,0,1]
	v_cvt_pk_fp8_f32 v4, v88, v90 op_sel:[0,0,1]
	v_cvt_pk_fp8_f32 v5, v96, v98 op_sel:[0,0,1]
	v_cvt_pk_fp8_f32 v6, v73, v75 op_sel:[0,0,1]
	v_cvt_pk_fp8_f32 v7, v81, v83 op_sel:[0,0,1]
	v_cvt_pk_fp8_f32 v8, v89, v91 op_sel:[0,0,1]
	v_cvt_pk_fp8_f32 v9, v97, v99 op_sel:[0,0,1]
	s_waitcnt lgkmcnt(6)
	v_cvt_pk_fp8_f32 v10, v104, v118 op_sel:[0,0,1]
	s_waitcnt lgkmcnt(4)
	v_cvt_pk_fp8_f32 v11, v120, v122 op_sel:[0,0,1]
	s_waitcnt lgkmcnt(2)
	v_cvt_pk_fp8_f32 v12, v124, v126 op_sel:[0,0,1]
	s_waitcnt lgkmcnt(0)
	v_cvt_pk_fp8_f32 v13, v128, v136 op_sel:[0,0,1]
	v_cvt_pk_fp8_f32 v14, v105, v119 op_sel:[0,0,1]
	v_cvt_pk_fp8_f32 v15, v121, v123 op_sel:[0,0,1]
	v_cvt_pk_fp8_f32 v16, v125, v127 op_sel:[0,0,1]
	v_cvt_pk_fp8_f32 v17, v129, v137 op_sel:[0,0,1]
	global_store_dwordx4 v[22:23], v[2:5], off
	global_store_dwordx4 v[24:25], v[6:9], off
	global_store_dwordx4 v[26:27], v[10:13], off
	global_store_dwordx4 v[28:29], v[14:17], off
	s_waitcnt lgkmcnt(0)
	s_cbranch_scc1 .LBB0_13
	v_readlane_b32 s22, v254, 51

; #define LAS __attribute__((address_space(3)))
; __device__ __forceinline__ void cvt_item8(const float* __restrict__ src, int K, int N, unsigned char* dst, int kb, int nb, int drow0, float wscale, LAS float* scr, int lane) {
;     const int k0 = kb * 64, n0 = nb * 64;
;     const float* s = src + (size_t)(k0 + (lane >> 4)) * N + n0 + 4 * (lane & 15);
;     f32x4 v[16];
; #pragma unroll
;     for (int i = 0; i < 16; ++i) v[i] = *(const f32x4*)(s + (size_t)(4 * i) * N);
; #pragma unroll
;     for (int i = 0; i < 16; ++i) { LAS float* p = scr + (4 * i + (lane >> 4)) * 65 + 4 * (lane & 15); p[0] = v[i].x * wscale; p[1] = v[i].y * wscale; p[2] = v[i].z * wscale; p[3] = v[i].w * wscale; }
; __device__ __forceinline__ void cvt_dense8(const float* w, int K, int N, unsigned char* dst, LAS float* scr, int gw, int NGW, int lane) {
;     const int nnb = N / 64, items = (K / 64) * nnb;
;     for (int it = gw; it < items; it += NGW) cvt_item8(w, K, N, dst, it / nnb, it % nnb, (it % nnb) * 64, 64.f, scr, lane);
; }
.LBB0_17:
	s_mul_hi_i32 s2, s27, 0x2aaaaaab
	s_lshr_b32 s3, s2, 31
	s_ashr_i32 s2, s2, 2
	s_add_i32 s2, s2, s3
	s_mul_i32 s3, s2, 0xfffffa00
	s_lshl_b32 s2, s2, 6
	s_add_i32 s28, s0, s3
	v_or_b32_e32 v24, s2, v1
	s_movk_i32 s29, 0x1800
	v_mad_i64_i32 v[24:25], s[30:31], v24, s29, v[22:23]
	s_ashr_i32 s29, s28, 31
	s_ashr_i32 s3, s2, 31
	v_lshl_add_u64 v[24:25], s[28:29], 2, v[24:25]
	v_lshl_add_u64 v[30:31], v[20:21], 0, s[2:3]
	v_lshl_add_u64 v[136:137], v[24:25], 0, v[18:19]
	s_movk_i32 s2, 0x6000
	v_add_co_u32_e32 v78, vcc, s2, v136
	v_add_u32_e32 v26, s28, v32
	s_mov_b64 s[2:3], vcc
	s_mov_b32 s28, 0xc000
	v_add_co_u32_e32 v80, vcc, s28, v136
	v_addc_co_u32_e64 v79, s[2:3], 0, v137, s[2:3]
	s_mov_b64 s[2:3], vcc
	s_mov_b32 s28, 0x12000
	v_add_co_u32_e32 v82, vcc, s28, v136
	v_addc_co_u32_e64 v81, s[2:3], 0, v137, s[2:3]
	s_mov_b64 s[2:3], vcc
	v_add_co_u32_e32 v86, vcc, s9, v136
	v_addc_co_u32_e64 v83, s[2:3], 0, v137, s[2:3]
	s_mov_b64 s[2:3], vcc
	v_add_co_u32_e32 v90, vcc, s10, v136
	v_addc_co_u32_e64 v87, s[2:3], 0, v137, s[2:3]
	s_mov_b64 s[2:3], vcc
	v_add_co_u32_e32 v94, vcc, s11, v136
	v_addc_co_u32_e64 v91, s[2:3], 0, v137, s[2:3]
	s_mov_b64 s[2:3], vcc
	v_add_co_u32_e32 v98, vcc, s18, v136
	v_addc_co_u32_e64 v95, s[2:3], 0, v137, s[2:3]
	v_add_u32_e32 v28, 16, v26
	v_add_u32_e32 v74, 32, v26
	v_add_u32_e32 v76, 48, v26
	s_mov_b64 s[2:3], vcc
	v_ashrrev_i32_e32 v27, 31, v26
	v_ashrrev_i32_e32 v29, 31, v28
	v_ashrrev_i32_e32 v75, 31, v74
	v_ashrrev_i32_e32 v77, 31, v76
	v_add_co_u32_e32 v102, vcc, s19, v136
	v_addc_co_u32_e64 v99, s[2:3], 0, v137, s[2:3]
	v_lshlrev_b64 v[24:25], 10, v[26:27]
	global_load_dwordx4 v[70:73], v[136:137], off nt
	v_lshlrev_b64 v[26:27], 10, v[28:29]
	v_lshlrev_b64 v[28:29], 10, v[74:75]
	v_lshlrev_b64 v[74:75], 10, v[76:77]
	s_mov_b64 s[2:3], vcc
	v_lshl_add_u64 v[24:25], v[30:31], 0, v[24:25]
	v_lshl_add_u64 v[26:27], v[30:31], 0, v[26:27]
	v_lshl_add_u64 v[28:29], v[30:31], 0, v[28:29]
	v_lshl_add_u64 v[30:31], v[30:31], 0, v[74:75]
	global_load_dwordx4 v[74:77], v[78:79], off nt
	v_add_co_u32_e32 v106, vcc, s20, v136
	v_addc_co_u32_e64 v103, s[2:3], 0, v137, s[2:3]
	global_load_dwordx4 v[82:85], v[82:83], off nt
	s_mov_b64 s[2:3], vcc
	global_load_dwordx4 v[78:81], v[80:81], off nt
	v_add_co_u32_e32 v110, vcc, s21, v136
	v_addc_co_u32_e64 v107, s[2:3], 0, v137, s[2:3]
	global_load_dwordx4 v[86:89], v[86:87], off nt
	s_mov_b64 s[2:3], vcc
	global_load_dwordx4 v[90:93], v[90:91], off nt
	v_add_co_u32_e32 v114, vcc, s22, v136
	v_addc_co_u32_e64 v111, s[2:3], 0, v137, s[2:3]
	global_load_dwordx4 v[94:97], v[94:95], off nt
	s_mov_b64 s[2:3], vcc
	global_load_dwordx4 v[98:101], v[98:99], off nt
	v_add_co_u32_e32 v118, vcc, s23, v136
	v_addc_co_u32_e64 v115, s[2:3], 0, v137, s[2:3]
	global_load_dwordx4 v[102:105], v[102:103], off nt
	s_mov_b64 s[2:3], vcc
	global_load_dwordx4 v[106:109], v[106:107], off nt
	v_add_co_u32_e32 v122, vcc, s24, v136
	v_addc_co_u32_e64 v119, s[2:3], 0, v137, s[2:3]
	global_load_dwordx4 v[110:113], v[110:111], off nt
	s_mov_b64 s[2:3], vcc
	global_load_dwordx4 v[114:117], v[114:115], off nt
	v_add_co_u32_e32 v126, vcc, s25, v136
	v_addc_co_u32_e64 v123, s[2:3], 0, v137, s[2:3]
	global_load_dwordx4 v[118:121], v[118:119], off nt
	s_mov_b64 s[2:3], vcc
	global_load_dwordx4 v[122:125], v[122:123], off nt
	v_add_co_u32_e32 v136, vcc, s26, v136
	v_addc_co_u32_e64 v127, s[2:3], 0, v137, s[2:3]
	global_load_dwordx4 v[126:129], v[126:127], off nt
	v_addc_co_u32_e32 v137, vcc, 0, v137, vcc
	global_load_dwordx4 v[136:139], v[136:137], off nt
	v_mov_b32_e32 v2, 0
	v_mov_b32_e32 v3, 0
	v_mov_b32_e32 v4, 0
	v_mov_b32_e32 v5, 0
	v_mov_b32_e32 v6, 0
	v_mov_b32_e32 v7, 0
	v_mov_b32_e32 v8, 0
	v_mov_b32_e32 v9, 0
	v_mov_b32_e32 v10, 0
	v_mov_b32_e32 v11, 0
	v_mov_b32_e32 v12, 0
	v_mov_b32_e32 v13, 0
	v_mov_b32_e32 v14, 0
	v_mov_b32_e32 v15, 0
	v_mov_b32_e32 v16, 0
	v_mov_b32_e32 v17, 0
	s_add_i32 s27, s27, s33
	s_add_i32 s0, s0, s1
	s_cmpk_lt_i32 s27, 0x180
	s_waitcnt vmcnt(15)
	v_pk_mul_f32 v[70:71], v[70:71], s[8:9] op_sel_hi:[1,0]
	v_pk_mul_f32 v[72:73], v[72:73], s[8:9] op_sel_hi:[1,0]
	ds_write2_b32 v35, v70, v71 offset1:1
	ds_write2_b32 v35, v72, v73 offset0:2 offset1:3
	s_waitcnt vmcnt(14)
	v_pk_mul_f32 v[70:71], v[74:75], s[8:9] op_sel_hi:[1,0]
	v_pk_mul_f32 v[72:73], v[76:77], s[8:9] op_sel_hi:[1,0]
	ds_write2_b32 v36, v70, v71 offset1:1
	ds_write2_b32 v37, v72, v73 offset1:1
	s_waitcnt vmcnt(12)
	v_pk_mul_f32 v[70:71], v[78:79], s[8:9] op_sel_hi:[1,0]
	v_pk_mul_f32 v[72:73], v[80:81], s[8:9] op_sel_hi:[1,0]
	ds_write2_b32 v38, v70, v71 offset1:1
	ds_write2_b32 v39, v72, v73 offset1:1
	v_pk_mul_f32 v[70:71], v[82:83], s[8:9] op_sel_hi:[1,0]
	v_pk_mul_f32 v[72:73], v[84:85], s[8:9] op_sel_hi:[1,0]
	ds_write2_b32 v40, v70, v71 offset1:1
	ds_write2_b32 v41, v72, v73 offset1:1
	s_waitcnt vmcnt(11)
	v_pk_mul_f32 v[70:71], v[86:87], s[8:9] op_sel_hi:[1,0]
	v_pk_mul_f32 v[72:73], v[88:89], s[8:9] op_sel_hi:[1,0]
	ds_write2_b32 v42, v70, v71 offset1:1
	ds_write2_b32 v43, v72, v73 offset1:1
	s_waitcnt vmcnt(10)
	v_pk_mul_f32 v[70:71], v[90:91], s[8:9] op_sel_hi:[1,0]
	v_pk_mul_f32 v[72:73], v[92:93], s[8:9] op_sel_hi:[1,0]
	ds_write2_b32 v44, v70, v71 offset1:1
	ds_write2_b32 v45, v72, v73 offset1:1
	s_waitcnt vmcnt(9)
; __device__ __forceinline__ unsigned pk4_fp8(float a, float b, float c, float d) { unsigned w = 0u; w = __builtin_amdgcn_cvt_pk_fp8_f32(a, b, w, false); w = __builtin_amdgcn_cvt_pk_fp8_f32(c, d, w, true); return w; }
; #define LAS __attribute__((address_space(3)))
; #define LDS_WAIT() asm volatile("s_waitcnt lgkmcnt(0)" ::: "memory")
; __device__ __forceinline__ void cvt_item8(const float* __restrict__ src, int K, int N, unsigned char* dst, int kb, int nb, int drow0, float wscale, LAS float* scr, int lane) {
;     ...
;     for (int i = 0; i < 16; ++i) { LAS float* p = scr + (4 * i + (lane >> 4)) * 65 + 4 * (lane & 15); p[0] = v[i].x * wscale; p[1] = v[i].y * wscale; p[2] = v[i].z * wscale; p[3] = v[i].w * wscale; }
;     LDS_WAIT();
;     const int c = lane & 3;
; #pragma unroll
;     for (int j = 0; j < 4; ++j) { const int n = (lane >> 2) + 16 * j; const LAS float* q = scr + (16 * c) * 65 + n;
;         v4u o; o.x = pg8::pk4_fp8(q[0], q[65], q[130], q[195]); o.y = pg8::pk4_fp8(q[260], q[325], q[390], q[455]);
;         o.z = pg8::pk4_fp8(q[520], q[585], q[650], q[715]); o.w = pg8::pk4_fp8(q[780], q[845], q[910], q[975]);
;         *(v4u*)(dst + (size_t)(drow0 + n) * K + k0 + 16 * c) = o; }
;     LDS_WAIT();
	v_pk_mul_f32 v[70:71], v[94:95], s[8:9] op_sel_hi:[1,0]
	v_pk_mul_f32 v[72:73], v[96:97], s[8:9] op_sel_hi:[1,0]
	ds_write2_b32 v46, v70, v71 offset1:1
	ds_write2_b32 v47, v72, v73 offset1:1
	s_waitcnt vmcnt(8)
	v_pk_mul_f32 v[70:71], v[98:99], s[8:9] op_sel_hi:[1,0]
	v_pk_mul_f32 v[72:73], v[100:101], s[8:9] op_sel_hi:[1,0]
	ds_write2_b32 v48, v70, v71 offset1:1
	ds_write2_b32 v49, v72, v73 offset1:1
	s_waitcnt vmcnt(7)
	v_pk_mul_f32 v[70:71], v[102:103], s[8:9] op_sel_hi:[1,0]
	v_pk_mul_f32 v[72:73], v[104:105], s[8:9] op_sel_hi:[1,0]
	ds_write2_b32 v50, v70, v71 offset1:1
	ds_write2_b32 v51, v72, v73 offset1:1
	s_waitcnt vmcnt(6)
	v_pk_mul_f32 v[70:71], v[106:107], s[8:9] op_sel_hi:[1,0]
	v_pk_mul_f32 v[72:73], v[108:109], s[8:9] op_sel_hi:[1,0]
	ds_write2_b32 v52, v70, v71 offset1:1
	ds_write2_b32 v53, v72, v73 offset1:1
	s_waitcnt vmcnt(5)
	v_pk_mul_f32 v[70:71], v[110:111], s[8:9] op_sel_hi:[1,0]
	v_pk_mul_f32 v[72:73], v[112:113], s[8:9] op_sel_hi:[1,0]
	ds_write2_b32 v54, v70, v71 offset1:1
	ds_write2_b32 v55, v72, v73 offset1:1
	s_waitcnt vmcnt(4)
	v_pk_mul_f32 v[70:71], v[114:115], s[8:9] op_sel_hi:[1,0]
	v_pk_mul_f32 v[72:73], v[116:117], s[8:9] op_sel_hi:[1,0]
	ds_write2_b32 v56, v70, v71 offset1:1
	ds_write2_b32 v57, v72, v73 offset1:1
	s_waitcnt vmcnt(3)
	v_pk_mul_f32 v[70:71], v[118:119], s[8:9] op_sel_hi:[1,0]
	v_pk_mul_f32 v[72:73], v[120:121], s[8:9] op_sel_hi:[1,0]
	ds_write2_b32 v58, v70, v71 offset1:1
	ds_write2_b32 v59, v72, v73 offset1:1
	s_waitcnt vmcnt(2)
	v_pk_mul_f32 v[70:71], v[122:123], s[8:9] op_sel_hi:[1,0]
	v_pk_mul_f32 v[72:73], v[124:125], s[8:9] op_sel_hi:[1,0]
	ds_write2_b32 v60, v70, v71 offset1:1
	ds_write2_b32 v61, v72, v73 offset1:1
	s_waitcnt vmcnt(1)
	v_pk_mul_f32 v[70:71], v[126:127], s[8:9] op_sel_hi:[1,0]
	v_pk_mul_f32 v[72:73], v[128:129], s[8:9] op_sel_hi:[1,0]
	ds_write2_b32 v62, v70, v71 offset1:1
	ds_write2_b32 v63, v72, v73 offset1:1
	s_waitcnt vmcnt(0)
	v_pk_mul_f32 v[70:71], v[136:137], s[8:9] op_sel_hi:[1,0]
	v_pk_mul_f32 v[72:73], v[138:139], s[8:9] op_sel_hi:[1,0]
	ds_write2_b32 v64, v70, v71 offset1:1
	ds_write2_b32 v65, v72, v73 offset1:1
	s_waitcnt lgkmcnt(0)
	ds_read2_b32 v[70:71], v34 offset1:16
	ds_read2_b32 v[72:73], v34 offset0:65 offset1:81
	ds_read2_b32 v[74:75], v34 offset0:130 offset1:146
	ds_read2_b32 v[76:77], v34 offset0:195 offset1:211
	ds_read2_b32 v[78:79], v66 offset0:4 offset1:20
	ds_read2_b32 v[80:81], v66 offset0:69 offset1:85
	ds_read2_b32 v[82:83], v66 offset0:134 offset1:150
	ds_read2_b32 v[84:85], v66 offset0:199 offset1:215
	ds_read2_b32 v[86:87], v67 offset0:8 offset1:24
	ds_read2_b32 v[88:89], v67 offset0:73 offset1:89
	ds_read2_b32 v[90:91], v67 offset0:138 offset1:154
	ds_read2_b32 v[92:93], v67 offset0:203 offset1:219
	ds_read2_b32 v[94:95], v68 offset0:12 offset1:28
	ds_read2_b32 v[96:97], v68 offset0:77 offset1:93
	ds_read2_b32 v[98:99], v68 offset0:142 offset1:158
	ds_read2_b32 v[100:101], v68 offset0:207 offset1:223
	ds_read2_b32 v[102:103], v34 offset0:32 offset1:48
	ds_read2_b32 v[104:105], v34 offset0:97 offset1:113
	ds_read2_b32 v[106:107], v34 offset0:162 offset1:178
	ds_read2_b32 v[108:109], v34 offset0:227 offset1:243
	ds_read2_b32 v[110:111], v66 offset0:36 offset1:52
	ds_read2_b32 v[112:113], v66 offset0:101 offset1:117
	ds_read2_b32 v[114:115], v66 offset0:166 offset1:182
	ds_read2_b32 v[116:117], v66 offset0:231 offset1:247
	ds_read2_b32 v[118:119], v67 offset0:40 offset1:56
	ds_read2_b32 v[120:121], v67 offset0:105 offset1:121
	ds_read2_b32 v[122:123], v67 offset0:170 offset1:186
	ds_read2_b32 v[124:125], v67 offset0:235 offset1:251
	ds_read2_b32 v[126:127], v68 offset0:44 offset1:60
	ds_read2_b32 v[128:129], v68 offset0:109 offset1:125
	ds_read2_b32 v[136:137], v68 offset0:174 offset1:190
	ds_read2_b32 v[138:139], v68 offset0:239 offset1:255
	s_waitcnt lgkmcnt(14)
	v_cvt_pk_fp8_f32 v2, v70, v72
	v_cvt_pk_fp8_f32 v3, v78, v80
	v_cvt_pk_fp8_f32 v4, v86, v88
	v_cvt_pk_fp8_f32 v5, v94, v96
	v_cvt_pk_fp8_f32 v6, v71, v73
	v_cvt_pk_fp8_f32 v7, v79, v81
	v_cvt_pk_fp8_f32 v8, v87, v89
	v_cvt_pk_fp8_f32 v9, v95, v97
	v_cvt_pk_fp8_f32 v10, v102, v104
	s_waitcnt lgkmcnt(10)
	v_cvt_pk_fp8_f32 v11, v110, v112
	s_waitcnt lgkmcnt(6)
	v_cvt_pk_fp8_f32 v12, v118, v120
	s_waitcnt lgkmcnt(2)
	v_cvt_pk_fp8_f32 v13, v126, v128
	v_cvt_pk_fp8_f32 v14, v103, v105
	v_cvt_pk_fp8_f32 v15, v111, v113
	v_cvt_pk_fp8_f32 v16, v119, v121
	v_cvt_pk_fp8_f32 v17, v127, v129
	v_cvt_pk_fp8_f32 v2, v74, v76 op_sel:[0,0,1]
	v_cvt_pk_fp8_f32 v3, v82, v84 op_sel:[0,0,1]
	v_cvt_pk_fp8_f32 v4, v90, v92 op_sel:[0,0,1]
	v_cvt_pk_fp8_f32 v5, v98, v100 op_sel:[0,0,1]
	v_cvt_pk_fp8_f32 v6, v75, v77 op_sel:[0,0,1]
	v_cvt_pk_fp8_f32 v7, v83, v85 op_sel:[0,0,1]
	v_cvt_pk_fp8_f32 v8, v91, v93 op_sel:[0,0,1]
	v_cvt_pk_fp8_f32 v9, v99, v101 op_sel:[0,0,1]
	v_cvt_pk_fp8_f32 v10, v106, v108 op_sel:[0,0,1]
	v_cvt_pk_fp8_f32 v11, v114, v116 op_sel:[0,0,1]
	v_cvt_pk_fp8_f32 v12, v122, v124 op_sel:[0,0,1]
	s_waitcnt lgkmcnt(0)
	v_cvt_pk_fp8_f32 v13, v136, v138 op_sel:[0,0,1]
	v_cvt_pk_fp8_f32 v14, v107, v109 op_sel:[0,0,1]
	v_cvt_pk_fp8_f32 v15, v115, v117 op_sel:[0,0,1]
	v_cvt_pk_fp8_f32 v16, v123, v125 op_sel:[0,0,1]
	v_cvt_pk_fp8_f32 v17, v137, v139 op_sel:[0,0,1]
	global_store_dwordx4 v[24:25], v[2:5], off
	global_store_dwordx4 v[26:27], v[6:9], off
	global_store_dwordx4 v[28:29], v[10:13], off
	global_store_dwordx4 v[30:31], v[14:17], off
	s_waitcnt lgkmcnt(0)
	s_cbranch_scc1 .LBB0_17

; #define LAS __attribute__((address_space(3)))
; __device__ __forceinline__ void cvt_item8(const float* __restrict__ src, int K, int N, unsigned char* dst, int kb, int nb, int drow0, float wscale, LAS float* scr, int lane) {
;     const int k0 = kb * 64, n0 = nb * 64;
;     const float* s = src + (size_t)(k0 + (lane >> 4)) * N + n0 + 4 * (lane & 15);
;     f32x4 v[16];
; #pragma unroll
;     for (int i = 0; i < 16; ++i) v[i] = *(const f32x4*)(s + (size_t)(4 * i) * N);
; #pragma unroll
;     for (int i = 0; i < 16; ++i) { LAS float* p = scr + (4 * i + (lane >> 4)) * 65 + 4 * (lane & 15); p[0] = v[i].x * wscale; p[1] = v[i].y * wscale; p[2] = v[i].z * wscale; p[3] = v[i].w * wscale; }
; __device__ __forceinline__ void cvt_dense8(const float* w, int K, int N, unsigned char* dst, LAS float* scr, int gw, int NGW, int lane) {
;     const int nnb = N / 64, items = (K / 64) * nnb;
;     for (int it = gw; it < items; it += NGW) cvt_item8(w, K, N, dst, it / nnb, it % nnb, (it % nnb) * 64, 64.f, scr, lane);
; }
.LBB0_20:
	s_ashr_i32 s27, s26, 31
	s_lshr_b32 s27, s27, 28
	s_add_i32 s27, s26, s27
	s_ashr_i32 s27, s27, 4
	s_lshl_b32 s28, s27, 6
	s_lshl_b32 s29, s27, 10
	v_or_b32_e32 v58, s28, v1
	s_sub_i32 s30, s0, s29
	v_ashrrev_i32_e32 v59, 31, v58
	v_add_u32_e32 v62, s30, v32
	v_lshlrev_b64 v[58:59], 12, v[58:59]
	s_ashr_i32 s29, s28, 31
	s_ashr_i32 s31, s30, 31
	v_ashrrev_i32_e32 v63, 31, v62
	v_add_u32_e32 v64, 16, v62
	v_add_u32_e32 v66, 32, v62
	v_add_u32_e32 v68, 48, v62
	v_lshl_add_u64 v[58:59], s[42:43], 0, v[58:59]
	v_lshl_add_u64 v[60:61], v[20:21], 0, s[28:29]
	v_lshlrev_b64 v[62:63], 10, v[62:63]
	v_ashrrev_i32_e32 v65, 31, v64
	v_ashrrev_i32_e32 v67, 31, v66
	v_ashrrev_i32_e32 v69, 31, v68
	v_lshl_add_u64 v[58:59], s[30:31], 2, v[58:59]
	v_lshl_add_u64 v[122:123], v[60:61], 0, v[62:63]
	v_lshlrev_b64 v[62:63], 10, v[64:65]
	v_lshlrev_b64 v[64:65], 10, v[66:67]
	v_lshlrev_b64 v[66:67], 10, v[68:69]
	v_lshl_add_u64 v[68:69], v[58:59], 0, v[18:19]
	v_lshl_add_u64 v[124:125], v[60:61], 0, v[62:63]
	v_add_co_u32_e32 v62, vcc, s3, v68
	v_lshl_add_u64 v[128:129], v[60:61], 0, v[66:67]
	s_nop 0
	v_addc_co_u32_e32 v63, vcc, 0, v69, vcc
	v_add_co_u32_e32 v66, vcc, s4, v68
	v_lshl_add_u64 v[126:127], v[60:61], 0, v[64:65]
	s_nop 0
	v_addc_co_u32_e32 v67, vcc, 0, v69, vcc
	v_add_co_u32_e32 v70, vcc, s5, v68
	global_load_dwordx4 v[58:61], v[68:69], off nt
	s_nop 0
	v_addc_co_u32_e32 v71, vcc, 0, v69, vcc
	v_add_co_u32_e32 v74, vcc, s8, v68
	v_mov_b32_e32 v2, 0
	s_nop 0
	v_addc_co_u32_e32 v75, vcc, 0, v69, vcc
	v_add_co_u32_e32 v78, vcc, s9, v68
	v_mov_b32_e32 v3, 0
	s_nop 0
	v_addc_co_u32_e32 v79, vcc, 0, v69, vcc
	v_add_co_u32_e32 v82, vcc, s10, v68
	v_mov_b32_e32 v4, 0
	s_nop 0
	v_addc_co_u32_e32 v83, vcc, 0, v69, vcc
	v_add_co_u32_e32 v86, vcc, s11, v68
	v_mov_b32_e32 v5, 0
	s_nop 0
	v_addc_co_u32_e32 v87, vcc, 0, v69, vcc
	v_add_co_u32_e32 v90, vcc, s18, v68
	v_mov_b32_e32 v6, 0
	s_nop 0
	v_addc_co_u32_e32 v91, vcc, 0, v69, vcc
	v_add_co_u32_e32 v94, vcc, s19, v68
	v_mov_b32_e32 v7, 0
	s_nop 0
	v_addc_co_u32_e32 v95, vcc, 0, v69, vcc
	v_add_co_u32_e32 v98, vcc, s20, v68
	v_mov_b32_e32 v8, 0
	s_nop 0
	v_addc_co_u32_e32 v99, vcc, 0, v69, vcc
	v_add_co_u32_e32 v102, vcc, s21, v68
	v_mov_b32_e32 v9, 0
	s_nop 0
	v_addc_co_u32_e32 v103, vcc, 0, v69, vcc
	v_add_co_u32_e32 v106, vcc, s22, v68
	v_mov_b32_e32 v10, 0
	s_nop 0
	v_addc_co_u32_e32 v107, vcc, 0, v69, vcc
	v_add_co_u32_e32 v110, vcc, s23, v68
	v_mov_b32_e32 v11, 0
	s_nop 0
	v_addc_co_u32_e32 v111, vcc, 0, v69, vcc
	v_add_co_u32_e32 v114, vcc, s24, v68
	v_mov_b32_e32 v12, 0
	s_nop 0
	v_addc_co_u32_e32 v115, vcc, 0, v69, vcc
	v_add_co_u32_e32 v118, vcc, s25, v68
	v_mov_b32_e32 v13, 0
	s_nop 0
	v_addc_co_u32_e32 v119, vcc, 0, v69, vcc
	global_load_dwordx4 v[62:65], v[62:63], off nt
	s_nop 0
	global_load_dwordx4 v[66:69], v[66:67], off nt
	s_nop 0
	global_load_dwordx4 v[70:73], v[70:71], off nt
	s_nop 0
	global_load_dwordx4 v[74:77], v[74:75], off nt
	s_nop 0
	global_load_dwordx4 v[78:81], v[78:79], off nt
	s_nop 0
	global_load_dwordx4 v[82:85], v[82:83], off nt
	s_nop 0
	global_load_dwordx4 v[86:89], v[86:87], off nt
	s_nop 0
	global_load_dwordx4 v[90:93], v[90:91], off nt
	s_nop 0
	global_load_dwordx4 v[94:97], v[94:95], off nt
	s_nop 0
	global_load_dwordx4 v[98:101], v[98:99], off nt
	s_nop 0
	global_load_dwordx4 v[102:105], v[102:103], off nt
	s_nop 0
	global_load_dwordx4 v[106:109], v[106:107], off nt
	s_nop 0
	global_load_dwordx4 v[110:113], v[110:111], off nt
	s_nop 0
	global_load_dwordx4 v[114:117], v[114:115], off nt
	s_nop 0
	global_load_dwordx4 v[118:121], v[118:119], off nt
	v_mov_b32_e32 v14, 0
	v_mov_b32_e32 v15, 0
	v_mov_b32_e32 v16, 0
	v_mov_b32_e32 v17, 0
	s_add_i32 s26, s26, s33
	s_add_i32 s0, s0, s1
	s_cmpk_lt_i32 s26, 0x100
	s_waitcnt vmcnt(15)
	v_pk_mul_f32 v[58:59], v[58:59], s[2:3] op_sel_hi:[1,0]
	v_pk_mul_f32 v[60:61], v[60:61], s[2:3] op_sel_hi:[1,0]
	ds_write2_b32 v23, v58, v59 offset1:1
	ds_write2_b32 v23, v60, v61 offset0:2 offset1:3
	s_waitcnt vmcnt(14)
	v_pk_mul_f32 v[58:59], v[62:63], s[2:3] op_sel_hi:[1,0]
	v_pk_mul_f32 v[60:61], v[64:65], s[2:3] op_sel_hi:[1,0]
	s_waitcnt vmcnt(13)
	v_pk_mul_f32 v[62:63], v[66:67], s[2:3] op_sel_hi:[1,0]
	v_pk_mul_f32 v[64:65], v[68:69], s[2:3] op_sel_hi:[1,0]
	s_waitcnt vmcnt(12)
	v_pk_mul_f32 v[66:67], v[70:71], s[2:3] op_sel_hi:[1,0]
	v_pk_mul_f32 v[68:69], v[72:73], s[2:3] op_sel_hi:[1,0]
	s_waitcnt vmcnt(11)
	v_pk_mul_f32 v[70:71], v[74:75], s[2:3] op_sel_hi:[1,0]
	v_pk_mul_f32 v[72:73], v[76:77], s[2:3] op_sel_hi:[1,0]
	s_waitcnt vmcnt(10)
	v_pk_mul_f32 v[74:75], v[78:79], s[2:3] op_sel_hi:[1,0]
	v_pk_mul_f32 v[76:77], v[80:81], s[2:3] op_sel_hi:[1,0]
	s_waitcnt vmcnt(9)
	v_pk_mul_f32 v[78:79], v[82:83], s[2:3] op_sel_hi:[1,0]
	v_pk_mul_f32 v[80:81], v[84:85], s[2:3] op_sel_hi:[1,0]
	s_waitcnt vmcnt(8)
	v_pk_mul_f32 v[82:83], v[86:87], s[2:3] op_sel_hi:[1,0]
	v_pk_mul_f32 v[84:85], v[88:89], s[2:3] op_sel_hi:[1,0]
	s_waitcnt vmcnt(7)
	v_pk_mul_f32 v[86:87], v[90:91], s[2:3] op_sel_hi:[1,0]
	v_pk_mul_f32 v[88:89], v[92:93], s[2:3] op_sel_hi:[1,0]
	s_waitcnt vmcnt(6)
	v_pk_mul_f32 v[90:91], v[94:95], s[2:3] op_sel_hi:[1,0]
	v_pk_mul_f32 v[92:93], v[96:97], s[2:3] op_sel_hi:[1,0]
	s_waitcnt vmcnt(5)
	v_pk_mul_f32 v[94:95], v[98:99], s[2:3] op_sel_hi:[1,0]
	v_pk_mul_f32 v[96:97], v[100:101], s[2:3] op_sel_hi:[1,0]
	s_waitcnt vmcnt(4)
	v_pk_mul_f32 v[98:99], v[102:103], s[2:3] op_sel_hi:[1,0]
	v_pk_mul_f32 v[100:101], v[104:105], s[2:3] op_sel_hi:[1,0]
	s_waitcnt vmcnt(3)
	v_pk_mul_f32 v[102:103], v[106:107], s[2:3] op_sel_hi:[1,0]
	v_pk_mul_f32 v[104:105], v[108:109], s[2:3] op_sel_hi:[1,0]
	s_waitcnt vmcnt(2)
; __device__ __forceinline__ unsigned pk4_fp8(float a, float b, float c, float d) { unsigned w = 0u; w = __builtin_amdgcn_cvt_pk_fp8_f32(a, b, w, false); w = __builtin_amdgcn_cvt_pk_fp8_f32(c, d, w, true); return w; }
; #define LAS __attribute__((address_space(3)))
; #define LDS_WAIT() asm volatile("s_waitcnt lgkmcnt(0)" ::: "memory")
; __device__ __forceinline__ void cvt_item8(const float* __restrict__ src, int K, int N, unsigned char* dst, int kb, int nb, int drow0, float wscale, LAS float* scr, int lane) {
;     ...
;     for (int i = 0; i < 16; ++i) { LAS float* p = scr + (4 * i + (lane >> 4)) * 65 + 4 * (lane & 15); p[0] = v[i].x * wscale; p[1] = v[i].y * wscale; p[2] = v[i].z * wscale; p[3] = v[i].w * wscale; }
;     LDS_WAIT();
;     const int c = lane & 3;
; #pragma unroll
;     for (int j = 0; j < 4; ++j) { const int n = (lane >> 2) + 16 * j; const LAS float* q = scr + (16 * c) * 65 + n;
;         v4u o; o.x = pg8::pk4_fp8(q[0], q[65], q[130], q[195]); o.y = pg8::pk4_fp8(q[260], q[325], q[390], q[455]);
;         o.z = pg8::pk4_fp8(q[520], q[585], q[650], q[715]); o.w = pg8::pk4_fp8(q[780], q[845], q[910], q[975]);
;         *(v4u*)(dst + (size_t)(drow0 + n) * K + k0 + 16 * c) = o; }
;     LDS_WAIT();
	v_pk_mul_f32 v[106:107], v[110:111], s[2:3] op_sel_hi:[1,0]
	v_pk_mul_f32 v[108:109], v[112:113], s[2:3] op_sel_hi:[1,0]
	s_waitcnt vmcnt(1)
	v_pk_mul_f32 v[110:111], v[114:115], s[2:3] op_sel_hi:[1,0]
	v_pk_mul_f32 v[112:113], v[116:117], s[2:3] op_sel_hi:[1,0]
	s_waitcnt vmcnt(0)
	v_pk_mul_f32 v[114:115], v[118:119], s[2:3] op_sel_hi:[1,0]
	v_pk_mul_f32 v[116:117], v[120:121], s[2:3] op_sel_hi:[1,0]
	ds_write2_b32 v24, v58, v59 offset1:1
	ds_write2_b32 v25, v60, v61 offset1:1
	ds_write2_b32 v26, v62, v63 offset1:1
	ds_write2_b32 v27, v64, v65 offset1:1
	ds_write2_b32 v28, v66, v67 offset1:1
	ds_write2_b32 v29, v68, v69 offset1:1
	ds_write2_b32 v30, v70, v71 offset1:1
	ds_write2_b32 v31, v72, v73 offset1:1
	ds_write2_b32 v33, v74, v75 offset1:1
	ds_write2_b32 v34, v76, v77 offset1:1
	ds_write2_b32 v35, v78, v79 offset1:1
	ds_write2_b32 v36, v80, v81 offset1:1
	ds_write2_b32 v37, v82, v83 offset1:1
	ds_write2_b32 v38, v84, v85 offset1:1
	ds_write2_b32 v39, v86, v87 offset1:1
	ds_write2_b32 v40, v88, v89 offset1:1
	ds_write2_b32 v41, v90, v91 offset1:1
	ds_write2_b32 v42, v92, v93 offset1:1
	ds_write2_b32 v43, v94, v95 offset1:1
	ds_write2_b32 v44, v96, v97 offset1:1
	ds_write2_b32 v45, v98, v99 offset1:1
	ds_write2_b32 v46, v100, v101 offset1:1
	ds_write2_b32 v47, v102, v103 offset1:1
	ds_write2_b32 v48, v104, v105 offset1:1
	ds_write2_b32 v49, v106, v107 offset1:1
	ds_write2_b32 v50, v108, v109 offset1:1
	ds_write2_b32 v51, v110, v111 offset1:1
	ds_write2_b32 v52, v112, v113 offset1:1
	ds_write2_b32 v53, v114, v115 offset1:1
	ds_write2_b32 v54, v116, v117 offset1:1
	s_waitcnt lgkmcnt(0)
	ds_read2_b32 v[58:59], v22 offset1:16
	ds_read2_b32 v[60:61], v22 offset0:65 offset1:81
	ds_read2_b32 v[62:63], v22 offset0:130 offset1:146
	ds_read2_b32 v[64:65], v22 offset0:195 offset1:211
	ds_read2_b32 v[66:67], v55 offset0:4 offset1:20
	ds_read2_b32 v[68:69], v55 offset0:69 offset1:85
	ds_read2_b32 v[70:71], v55 offset0:134 offset1:150
	ds_read2_b32 v[72:73], v55 offset0:199 offset1:215
	ds_read2_b32 v[74:75], v56 offset0:8 offset1:24
	ds_read2_b32 v[76:77], v56 offset0:73 offset1:89
	ds_read2_b32 v[78:79], v56 offset0:138 offset1:154
	ds_read2_b32 v[80:81], v56 offset0:203 offset1:219
	ds_read2_b32 v[82:83], v57 offset0:12 offset1:28
	ds_read2_b32 v[84:85], v57 offset0:77 offset1:93
	ds_read2_b32 v[86:87], v57 offset0:142 offset1:158
	ds_read2_b32 v[88:89], v57 offset0:207 offset1:223
	ds_read2_b32 v[90:91], v22 offset0:32 offset1:48
	ds_read2_b32 v[92:93], v22 offset0:97 offset1:113
	ds_read2_b32 v[94:95], v22 offset0:162 offset1:178
	ds_read2_b32 v[96:97], v22 offset0:227 offset1:243
	ds_read2_b32 v[98:99], v55 offset0:36 offset1:52
	ds_read2_b32 v[100:101], v55 offset0:101 offset1:117
	ds_read2_b32 v[102:103], v55 offset0:166 offset1:182
	ds_read2_b32 v[104:105], v55 offset0:231 offset1:247
	ds_read2_b32 v[106:107], v56 offset0:40 offset1:56
	ds_read2_b32 v[108:109], v56 offset0:105 offset1:121
	ds_read2_b32 v[110:111], v56 offset0:170 offset1:186
	ds_read2_b32 v[112:113], v56 offset0:235 offset1:251
	ds_read2_b32 v[114:115], v57 offset0:44 offset1:60
	ds_read2_b32 v[116:117], v57 offset0:109 offset1:125
	ds_read2_b32 v[118:119], v57 offset0:174 offset1:190
	ds_read2_b32 v[120:121], v57 offset0:239 offset1:255
	s_waitcnt lgkmcnt(14)
	v_cvt_pk_fp8_f32 v2, v58, v60
	v_cvt_pk_fp8_f32 v3, v66, v68
	v_cvt_pk_fp8_f32 v4, v74, v76
	v_cvt_pk_fp8_f32 v5, v82, v84
	v_cvt_pk_fp8_f32 v6, v59, v61
	v_cvt_pk_fp8_f32 v7, v67, v69
	v_cvt_pk_fp8_f32 v8, v75, v77
	v_cvt_pk_fp8_f32 v9, v83, v85
	v_cvt_pk_fp8_f32 v10, v90, v92
	s_waitcnt lgkmcnt(10)
	v_cvt_pk_fp8_f32 v11, v98, v100
	s_waitcnt lgkmcnt(6)
	v_cvt_pk_fp8_f32 v12, v106, v108
	s_waitcnt lgkmcnt(2)
	v_cvt_pk_fp8_f32 v13, v114, v116
	v_cvt_pk_fp8_f32 v14, v91, v93
	v_cvt_pk_fp8_f32 v15, v99, v101
	v_cvt_pk_fp8_f32 v16, v107, v109
	v_cvt_pk_fp8_f32 v17, v115, v117
	v_cvt_pk_fp8_f32 v2, v62, v64 op_sel:[0,0,1]
	v_cvt_pk_fp8_f32 v3, v70, v72 op_sel:[0,0,1]
	v_cvt_pk_fp8_f32 v4, v78, v80 op_sel:[0,0,1]
	v_cvt_pk_fp8_f32 v5, v86, v88 op_sel:[0,0,1]
	v_cvt_pk_fp8_f32 v6, v63, v65 op_sel:[0,0,1]
	v_cvt_pk_fp8_f32 v7, v71, v73 op_sel:[0,0,1]
	v_cvt_pk_fp8_f32 v8, v79, v81 op_sel:[0,0,1]
	v_cvt_pk_fp8_f32 v9, v87, v89 op_sel:[0,0,1]
	v_cvt_pk_fp8_f32 v10, v94, v96 op_sel:[0,0,1]
	v_cvt_pk_fp8_f32 v11, v102, v104 op_sel:[0,0,1]
	v_cvt_pk_fp8_f32 v12, v110, v112 op_sel:[0,0,1]
	s_waitcnt lgkmcnt(0)
	v_cvt_pk_fp8_f32 v13, v118, v120 op_sel:[0,0,1]
	v_cvt_pk_fp8_f32 v14, v95, v97 op_sel:[0,0,1]
	v_cvt_pk_fp8_f32 v15, v103, v105 op_sel:[0,0,1]
	v_cvt_pk_fp8_f32 v16, v111, v113 op_sel:[0,0,1]
	v_cvt_pk_fp8_f32 v17, v119, v121 op_sel:[0,0,1]
	global_store_dwordx4 v[122:123], v[2:5], off
	global_store_dwordx4 v[124:125], v[6:9], off
	global_store_dwordx4 v[126:127], v[10:13], off
	global_store_dwordx4 v[128:129], v[14:17], off
	s_waitcnt lgkmcnt(0)
	s_cbranch_scc1 .LBB0_20
; #define LAS __attribute__((address_space(3)))
; #define CVT_LOAD(v, c, s_) do { _Pragma("unroll") for (int i_ = 0; i_ < 16; ++i_) v[i_] = *(const f32x4*)((c).src + (size_t)(64 * (s_) + i_) * (c).N); } while (0)
; __device__ __forceinline__ CvtItem cvt_moe_item(int it, const float* wg, const float* wu, const float* wd, unsigned char* WGU, unsigned char* WDN, int lane) {
;     const int which = it >> 11, r = it & 2047, e = r >> 7, q = r & 127; CvtItem c; c.which = which;
;     if (which < 2) { const int nb = q & 31, k0 = (q >> 5) * 256; c.nb = nb;
;         c.N = DFF; c.K = DM; c.wscale = which ? 64.f / LOG2E : 64.f * LOG2E; c.src = (which ? wu : wg) + (size_t)e * DM * DFF + (size_t)(k0 + 16 * (lane >> 4)) * DFF + nb * 64 + 4 * (lane & 15);
;         c.dst = WGU + (size_t)e * 4096 * DM + k0; }
;     else { const int nb = q & 15, k0 = (q >> 4) * 256; c.nb = nb;
;         c.N = DM; c.K = DFF; c.wscale = 64.f; c.src = wd + (size_t)e * DFF * DM + (size_t)(k0 + 16 * (lane >> 4)) * DM + nb * 64 + 4 * (lane & 15);
;         c.dst = WDN + (size_t)e * DM * DFF + k0; }
;     return c;
; }
; __device__ __forceinline__ void cvt_moe_pipe2(const CvtSrc& A, const CvtSrc& B, LAS float* scr, int gw, int NGW, int lane) {
;     LAS unsigned char* blk = (LAS unsigned char*)scr;
;     f32x4 va[16], vb[16]; CvtItem c, cn;
;     const int it1 = A.n + B.n; int it = gw;
;     if (it < it1) { c = cvt_moe_item2(it, A, B, lane); CVT_LOAD(va, c, 0); }
.LBB0_21:
	v_readlane_b32 s0, v254, 9
	s_cmpk_lg_i32 s0, 0x100
	v_readlane_b32 s2, v254, 51
	s_cselect_b64 s[0:1], -1, 0
	s_cmpk_lt_i32 s2, 0x1800
	s_cselect_b64 s[2:3], -1, 0
	s_and_b64 s[0:1], s[0:1], s[2:3]
	s_andn2_b64 vcc, exec, s[0:1]
	s_cbranch_vccnz .LBB0_40
	v_readlane_b32 s26, v254, 51
	s_lshl_b32 s0, s26, 4
	s_and_b32 s8, s0, 0x700
	s_lshl_b32 s0, s26, 3
	s_ashr_i32 s39, s26, 11
	s_and_b32 s9, s0, 0x300
	s_cmpk_lt_u32 s26, 0x800
	s_cselect_b64 s[2:3], -1, 0
	s_and_b64 s[0:1], s[2:3], exec
	s_cselect_b32 s18, s82, s84
	s_cselect_b32 s19, s83, s85
	s_bfe_u32 s10, s26, 0x40007
	s_lshl_b32 s41, s10, 23
	s_cmp_lt_i32 s39, 2
	s_cselect_b64 s[4:5], -1, 0
	s_and_b64 s[0:1], s[4:5], exec
	s_cselect_b32 s52, s9, s8
	s_movk_i32 s9, 0x400
	s_cselect_b32 s8, 0x800, s9
	s_cselect_b32 s38, s9, 0x800
	s_movk_i32 s9, 0x7800
	s_cselect_b32 s51, s9, 0x3c00
	s_movk_i32 s9, 0x7000
	s_movk_i32 s22, 0x6000
	s_cselect_b32 s50, s9, 0x3800
	s_movk_i32 s9, 0x6800
	s_cselect_b32 s48, s22, 0x3000
	s_movk_i32 s22, 0x5800
	s_cselect_b32 s49, s9, 0x3400
	s_movk_i32 s9, 0x3000
	s_cselect_b32 s47, s22, 0x2c00
	s_movk_i32 s22, 0x5000
	s_mov_b32 s20, 0x5400000
	s_cselect_b32 s46, s22, 0x2800
	s_movk_i32 s22, 0x4800
	s_cselect_b32 s43, s9, 0x1800
	s_movk_i32 s9, 0x1400
	s_cselect_b32 s0, s20, 0x9400000
	s_cselect_b32 s20, s18, s86
	s_cselect_b32 s18, 31, 15
	s_cselect_b32 s45, s22, 0x2400
	s_movk_i32 s22, 0x1c00
	s_cselect_b32 s42, 0x2800, s9
	s_movk_i32 s9, 0xc00
	s_cselect_b32 s1, s19, s87
	s_cselect_b32 s21, 11, 10
	s_cselect_b32 s19, 22, 21
	s_cselect_b32 s44, 0x3800, s22
	s_cselect_b32 s9, 0x1800, s9
	s_and_b32 s40, s26, s18
	v_readlane_b32 s22, v254, 0
	s_mov_b32 s11, 0
	v_readlane_b32 s23, v254, 1
	s_add_u32 s0, s22, s0
	s_addc_u32 s22, s23, 0
	s_lshl_b64 s[18:19], s[10:11], s19
	s_add_u32 s0, s0, s18
	v_mov_b32_e32 v139, 0x42317218
	v_mov_b32_e32 v141, 0x42b8aa3b
	s_addc_u32 s10, s22, s19
	v_cndmask_b32_e64 v2, v139, v141, s[2:3]
	v_mov_b32_e32 v3, 0x42800000
	s_add_u32 s24, s0, s52
	v_and_b32_e32 v131, 48, v134
	v_cndmask_b32_e64 v149, v3, v2, s[4:5]
	s_addc_u32 s25, s10, 0
	v_or_b32_e32 v2, s52, v131
	s_add_u32 s0, s20, s41
	v_lshlrev_b32_e32 v138, s21, v2
	s_addc_u32 s1, s1, 0
	v_mov_b32_e32 v143, 0
	v_lshlrev_b32_e32 v142, 2, v138
	v_lshl_add_u64 v[2:3], s[0:1], 0, v[142:143]
	s_lshl_b32 s10, s40, 8
	v_and_b32_e32 v140, 60, v132
	v_lshl_add_u64 v[2:3], v[2:3], 0, s[10:11]
	v_lshlrev_b32_e32 v142, 2, v140
	v_lshl_add_u64 v[144:145], v[2:3], 0, v[142:143]
	s_lshl_b32 s10, s51, 2
	v_lshl_add_u64 v[2:3], v[144:145], 0, s[10:11]
	s_lshl_b32 s10, s50, 2
	v_lshl_add_u64 v[4:5], v[144:145], 0, s[10:11]
	s_lshl_b32 s10, s49, 2
	global_load_dwordx4 v[10:13], v[2:3], off nt
	global_load_dwordx4 v[6:9], v[4:5], off nt
	v_lshl_add_u64 v[2:3], v[144:145], 0, s[10:11]
	s_lshl_b32 s10, s48, 2
	v_lshl_add_u64 v[4:5], v[144:145], 0, s[10:11]
	s_lshl_b32 s10, s47, 2
	v_lshl_add_u64 v[14:15], v[144:145], 0, s[10:11]
	s_lshl_b32 s10, s46, 2
	v_lshl_add_u64 v[16:17], v[144:145], 0, s[10:11]
	s_lshl_b32 s10, s45, 2
	v_lshl_add_u64 v[18:19], v[144:145], 0, s[10:11]
	s_lshl_b32 s10, s8, 5
	v_lshl_add_u64 v[20:21], v[144:145], 0, s[10:11]
	s_lshl_b32 s10, s44, 2
	v_lshl_add_u64 v[34:35], v[144:145], 0, s[10:11]
	s_lshl_b32 s10, s43, 2
	v_lshl_add_u64 v[36:37], v[144:145], 0, s[10:11]
	s_lshl_b32 s10, s42, 2
	v_and_b32_e32 v54, 15, v134
	v_bitop3_b32 v55, v1, v134, 15 bitop3:0x78
	v_lshl_add_u64 v[38:39], v[144:145], 0, s[10:11]
	s_lshl_b32 s10, s8, 4
	v_lshlrev_b32_e32 v67, 4, v55
	v_bitop3_b32 v55, v1, v54, 4 bitop3:0x36
	v_lshl_add_u64 v[40:41], v[144:145], 0, s[10:11]
	s_lshl_b32 s10, s9, 2
	v_lshlrev_b32_e32 v68, 4, v55
	v_bitop3_b32 v55, v1, v54, 8 bitop3:0x36
	s_lshl_b32 s20, s8, 3
	s_mov_b32 s21, s11
	s_lshl_b32 s22, s8, 2
; __device__ __forceinline__ unsigned pk4_fp8(float a, float b, float c, float d) { unsigned w = 0u; w = __builtin_amdgcn_cvt_pk_fp8_f32(a, b, w, false); w = __builtin_amdgcn_cvt_pk_fp8_f32(c, d, w, true); return w; }
; #define LAS __attribute__((address_space(3)))
; #define CVT_LOAD(v, c, s_) do { _Pragma("unroll") for (int i_ = 0; i_ < 16; ++i_) v[i_] = *(const f32x4*)((c).src + (size_t)(64 * (s_) + i_) * (c).N); } while (0)
; __device__ __forceinline__ void cvt_pack8(const f32x4 (&v)[16], const CvtItem& c, LAS unsigned char* blk, int s4, int lane) {
;     const float w = c.wscale; const int cb = lane & 15, j = 4 * s4 + (lane >> 4);
; #pragma unroll
;     for (int jn = 0; jn < 4; ++jn) {
;         v4u o; o.x = pg8::pk4_fp8(v[0][jn] * w, v[1][jn] * w, v[2][jn] * w, v[3][jn] * w); o.y = pg8::pk4_fp8(v[4][jn] * w, v[5][jn] * w, v[6][jn] * w, v[7][jn] * w);
;         o.z = pg8::pk4_fp8(v[8][jn] * w, v[9][jn] * w, v[10][jn] * w, v[11][jn] * w); o.w = pg8::pk4_fp8(v[12][jn] * w, v[13][jn] * w, v[14][jn] * w, v[15][jn] * w);
;         *(LAS v4u*)(blk + (4 * cb + jn) * 256 + ((j ^ cb) * 16)) = o; }
; }
; __device__ __forceinline__ void cvt_moe_pipe2(const CvtSrc& A, const CvtSrc& B, LAS float* scr, int gw, int NGW, int lane) {
;     LAS unsigned char* blk = (LAS unsigned char*)scr;
;     f32x4 va[16], vb[16]; CvtItem c, cn;
;     const int it1 = A.n + B.n; int it = gw;
;     if (it < it1) { c = cvt_moe_item2(it, A, B, lane); CVT_LOAD(va, c, 0); }
	s_mov_b32 s23, s11
	v_lshl_add_u64 v[50:51], v[144:145], 0, s[10:11]
	v_readlane_b32 s0, v254, 60
	v_lshlrev_b32_e32 v69, 4, v55
	v_bitop3_b32 v55, v1, v54, 12 bitop3:0x36
	global_load_dwordx4 v[22:25], v[2:3], off nt
	s_nop 0
	global_load_dwordx4 v[2:5], v[4:5], off nt
	s_nop 0
	global_load_dwordx4 v[26:29], v[14:15], off nt
	s_nop 0
	global_load_dwordx4 v[14:17], v[16:17], off nt
	s_nop 0
	global_load_dwordx4 v[30:33], v[18:19], off nt
	s_nop 0
	global_load_dwordx4 v[18:21], v[20:21], off nt
	s_nop 0
	global_load_dwordx4 v[42:45], v[34:35], off nt
	s_nop 0
	global_load_dwordx4 v[34:37], v[36:37], off nt
	s_nop 0
	global_load_dwordx4 v[46:49], v[38:39], off nt
	s_nop 0
	global_load_dwordx4 v[38:41], v[40:41], off nt
	v_lshl_add_u64 v[52:53], v[144:145], 0, s[20:21]
	v_lshl_add_u32 v66, v54, 10, s0
	v_lshlrev_b32_e32 v70, 4, v55
	v_lshlrev_b32_e32 v136, 4, v54
	global_load_dwordx4 v[58:61], v[50:51], off nt
	global_load_dwordx4 v[54:57], v[52:53], off nt
	v_lshl_add_u64 v[50:51], v[144:145], 0, s[22:23]
	global_load_dwordx4 v[50:53], v[50:51], off nt
	s_nop 0
	global_load_dwordx4 v[62:65], v[144:145], off nt
	v_or_b32_e32 v133, 4, v1
	v_or_b32_e32 v135, 8, v1
	v_or_b32_e32 v148, 12, v1
	v_or_b32_e32 v150, 16, v1
	v_or_b32_e32 v151, 20, v1
	v_or_b32_e32 v152, 24, v1
	v_or_b32_e32 v153, 28, v1
	v_or_b32_e32 v154, 32, v1
	v_or_b32_e32 v155, 36, v1
	v_or_b32_e32 v156, 40, v1
	v_or_b32_e32 v157, 44, v1
	v_or_b32_e32 v158, 48, v1
	v_or_b32_e32 v159, 52, v1
	v_or_b32_e32 v160, 56, v1
	v_or_b32_e32 v161, 60, v1
	v_lshl_add_u32 v71, v1, 8, s0
	v_lshl_add_u32 v72, v133, 8, s0
	v_xor_b32_e32 v73, 16, v136
	v_lshl_add_u32 v74, v135, 8, s0
	v_xor_b32_e32 v75, 32, v136
	v_lshl_add_u32 v76, v148, 8, s0
	v_xor_b32_e32 v77, 48, v136
	v_lshl_add_u32 v78, v150, 8, s0
	v_xor_b32_e32 v79, 64, v136
	v_lshl_add_u32 v80, v151, 8, s0
	v_xor_b32_e32 v81, 0x50, v136
	v_lshl_add_u32 v82, v152, 8, s0
	v_xor_b32_e32 v83, 0x60, v136
	v_lshl_add_u32 v84, v153, 8, s0
	v_xor_b32_e32 v85, 0x70, v136
	v_lshl_add_u32 v86, v154, 8, s0
	v_xor_b32_e32 v87, 0x80, v136
	v_lshl_add_u32 v88, v155, 8, s0
	v_xor_b32_e32 v89, 0x90, v136
	v_lshl_add_u32 v90, v156, 8, s0
	v_xor_b32_e32 v91, 0xa0, v136
	v_lshl_add_u32 v92, v157, 8, s0
	v_xor_b32_e32 v93, 0xb0, v136
	v_lshl_add_u32 v94, v158, 8, s0
	v_xor_b32_e32 v95, 0xc0, v136
	v_lshl_add_u32 v96, v159, 8, s0
	v_xor_b32_e32 v97, 0xd0, v136
	v_lshl_add_u32 v98, v160, 8, s0
	v_xor_b32_e32 v99, 0xe0, v136
	v_lshl_add_u32 v100, v161, 8, s0
	v_xor_b32_e32 v101, 0xf0, v136
	s_lshl_b32 s53, s40, 6
	s_lshl_b32 s54, s8, 1
	v_mov_b32_e32 v137, v143
	v_add_u32_e32 v162, v71, v136
	v_add_u32_e32 v163, v66, v67
	v_mov_b32_e32 v182, 0xc4
	v_add_u32_e32 v164, v66, v68
	v_add_u32_e32 v165, v66, v69
	v_add_u32_e32 v166, v66, v70
	v_mov_b32_e32 v183, 0x43
	v_mov_b32_e32 v184, 0x47
	v_add_u32_e32 v167, v72, v73
	v_mov_b32_e32 v185, 0x4b
	v_add_u32_e32 v168, v74, v75
	v_mov_b32_e32 v186, 0x4f
	v_add_u32_e32 v169, v76, v77
	v_mov_b32_e32 v187, 0x53
	v_add_u32_e32 v170, v78, v79
	v_mov_b32_e32 v188, 0x57
	v_add_u32_e32 v171, v80, v81
	v_mov_b32_e32 v189, 0x5b
	v_add_u32_e32 v172, v82, v83
	v_mov_b32_e32 v190, 0x5f
	v_add_u32_e32 v173, v84, v85
	v_mov_b32_e32 v191, 0x63
	v_add_u32_e32 v174, v86, v87
	v_mov_b32_e32 v192, 0x67
	v_add_u32_e32 v175, v88, v89
	v_mov_b32_e32 v193, 0x6b
	v_add_u32_e32 v176, v90, v91
	v_mov_b32_e32 v194, 0x6f
	v_add_u32_e32 v177, v92, v93
	v_mov_b32_e32 v195, 0x73
	v_add_u32_e32 v178, v94, v95
	v_mov_b32_e32 v196, 0x77
	v_add_u32_e32 v179, v96, v97
	v_mov_b32_e32 v197, 0x7b
	v_add_u32_e32 v180, v98, v99
	v_mov_b32_e32 v198, 0x7f
	v_add_u32_e32 v181, v100, v101
	s_mov_b32 s1, s26
	s_mov_b32 s26, s8
	s_mov_b32 s23, s38
	s_mov_b32 s33, s39
	s_mov_b32 s56, s40
	v_mov_b32_e32 v200, v149
	s_branch .LBB0_26

; #define CVT_LOAD(v, c, s_) do { _Pragma("unroll") for (int i_ = 0; i_ < 16; ++i_) v[i_] = *(const f32x4*)((c).src + (size_t)(64 * (s_) + i_) * (c).N); } while (0)
; __device__ __forceinline__ CvtItem cvt_moe_item(int it, const float* wg, const float* wu, const float* wd, unsigned char* WGU, unsigned char* WDN, int lane) {
;     const int which = it >> 11, r = it & 2047, e = r >> 7, q = r & 127; CvtItem c; c.which = which;
;     if (which < 2) { const int nb = q & 31, k0 = (q >> 5) * 256; c.nb = nb;
;         c.N = DFF; c.K = DM; c.wscale = which ? 64.f / LOG2E : 64.f * LOG2E; c.src = (which ? wu : wg) + (size_t)e * DM * DFF + (size_t)(k0 + 16 * (lane >> 4)) * DFF + nb * 64 + 4 * (lane & 15);
;         c.dst = WGU + (size_t)e * 4096 * DM + k0; }
;     else { const int nb = q & 15, k0 = (q >> 4) * 256; c.nb = nb;
;         c.N = DM; c.K = DFF; c.wscale = 64.f; c.src = wd + (size_t)e * DFF * DM + (size_t)(k0 + 16 * (lane >> 4)) * DM + nb * 64 + 4 * (lane & 15);
;         c.dst = WDN + (size_t)e * DM * DFF + k0; }
;     return c;
; }
; __device__ __forceinline__ void cvt_moe_pipe2(const CvtSrc& A, const CvtSrc& B, LAS float* scr, int gw, int NGW, int lane) {
;     ...
;         if (more) { cn = cvt_moe_item2(i1, A, B, lane); CVT_LOAD(va, cn, 0); }
.LBB0_24:
	v_readlane_b32 s58, v254, 0
	v_readlane_b32 s59, v254, 1
	s_add_u32 s35, s58, s36
	s_addc_u32 s36, s59, s37
	s_bfe_u32 s10, s1, 0x40007
	s_lshl_b32 s37, s10, 23
	s_add_u32 s28, s28, s37
	v_or_b32_e32 v2, s57, v131
	s_addc_u32 s29, s29, 0
	v_lshlrev_b32_e32 v142, s27, v2
	v_lshl_add_u64 v[2:3], v[142:143], 2, s[28:29]
	s_lshl_b32 s28, s21, 6
	s_mov_b32 s29, s11
	v_lshl_add_u64 v[2:3], s[28:29], 2, v[2:3]
	v_lshlrev_b32_e32 v142, 2, v140
	v_lshl_add_u64 v[144:145], v[2:3], 0, v[142:143]
	s_lshl_b64 s[28:29], s[10:11], s34
	s_lshl_b32 s10, s26, 2
	v_lshl_add_u64 v[2:3], v[144:145], 0, s[10:11]
	s_lshl_b32 s10, s26, 3
	v_lshl_add_u64 v[4:5], v[144:145], 0, s[10:11]
	s_mul_i32 s10, s26, 12
	global_load_dwordx4 v[50:53], v[2:3], off nt
	global_load_dwordx4 v[54:57], v[4:5], off nt
	v_lshl_add_u64 v[2:3], v[144:145], 0, s[10:11]
	s_lshl_b32 s10, s26, 4
	v_lshl_add_u64 v[4:5], v[144:145], 0, s[10:11]
	s_mul_i32 s10, s26, 20
	global_load_dwordx4 v[58:61], v[2:3], off nt
	global_load_dwordx4 v[38:41], v[4:5], off nt
	v_lshl_add_u64 v[2:3], v[144:145], 0, s[10:11]
	s_mul_i32 s10, s26, 24
	v_lshl_add_u64 v[4:5], v[144:145], 0, s[10:11]
	s_mul_i32 s10, s26, 28
	global_load_dwordx4 v[46:49], v[2:3], off nt
	global_load_dwordx4 v[34:37], v[4:5], off nt
	v_lshl_add_u64 v[2:3], v[144:145], 0, s[10:11]
	s_lshl_b32 s10, s26, 5
	v_lshl_add_u64 v[4:5], v[144:145], 0, s[10:11]
	s_mul_i32 s10, s26, 36
	global_load_dwordx4 v[42:45], v[2:3], off nt
	global_load_dwordx4 v[18:21], v[4:5], off nt
	v_lshl_add_u64 v[2:3], v[144:145], 0, s[10:11]
	s_mul_i32 s10, s26, 40
	v_lshl_add_u64 v[4:5], v[144:145], 0, s[10:11]
	s_mul_i32 s10, s26, 44
	global_load_dwordx4 v[30:33], v[2:3], off nt
	global_load_dwordx4 v[14:17], v[4:5], off nt
	v_lshl_add_u64 v[2:3], v[144:145], 0, s[10:11]
	s_mul_i32 s10, s26, 48
	v_lshl_add_u64 v[4:5], v[144:145], 0, s[10:11]
	s_mul_i32 s10, s26, 52
	v_lshl_add_u64 v[6:7], v[144:145], 0, s[10:11]
	s_mul_i32 s10, s26, 56
	v_lshl_add_u64 v[8:9], v[144:145], 0, s[10:11]
	s_mul_i32 s10, s26, 60
	v_lshl_add_u64 v[10:11], v[144:145], 0, s[10:11]
	global_load_dwordx4 v[26:29], v[2:3], off nt
	s_nop 0
	global_load_dwordx4 v[2:5], v[4:5], off nt
	s_nop 0
	global_load_dwordx4 v[22:25], v[6:7], off nt
	s_nop 0
	global_load_dwordx4 v[6:9], v[8:9], off nt
	s_nop 0
	global_load_dwordx4 v[62:65], v[144:145], off nt
	s_nop 0
	global_load_dwordx4 v[10:13], v[10:11], off nt
	s_add_u32 s10, s35, s28
	s_addc_u32 s27, s36, s29
	s_add_u32 s28, s10, s57
	s_addc_u32 s29, s27, 0

; __device__ __forceinline__ unsigned pk4_fp8(float a, float b, float c, float d) { unsigned w = 0u; w = __builtin_amdgcn_cvt_pk_fp8_f32(a, b, w, false); w = __builtin_amdgcn_cvt_pk_fp8_f32(c, d, w, true); return w; }
; #define LAS __attribute__((address_space(3)))
; #define CVT_LOAD(v, c, s_) do { _Pragma("unroll") for (int i_ = 0; i_ < 16; ++i_) v[i_] = *(const f32x4*)((c).src + (size_t)(64 * (s_) + i_) * (c).N); } while (0)
; __device__ __forceinline__ void cvt_pack8(const f32x4 (&v)[16], const CvtItem& c, LAS unsigned char* blk, int s4, int lane) {
;     const float w = c.wscale; const int cb = lane & 15, j = 4 * s4 + (lane >> 4);
; #pragma unroll
;     for (int jn = 0; jn < 4; ++jn) {
;         v4u o; o.x = pg8::pk4_fp8(v[0][jn] * w, v[1][jn] * w, v[2][jn] * w, v[3][jn] * w); o.y = pg8::pk4_fp8(v[4][jn] * w, v[5][jn] * w, v[6][jn] * w, v[7][jn] * w);
;         o.z = pg8::pk4_fp8(v[8][jn] * w, v[9][jn] * w, v[10][jn] * w, v[11][jn] * w); o.w = pg8::pk4_fp8(v[12][jn] * w, v[13][jn] * w, v[14][jn] * w, v[15][jn] * w);
;         *(LAS v4u*)(blk + (4 * cb + jn) * 256 + ((j ^ cb) * 16)) = o; }
; }
; __device__ __forceinline__ void cvt_moe_pipe2(const CvtSrc& A, const CvtSrc& B, LAS float* scr, int gw, int NGW, int lane) {
;     ...
;     while (it < it1) {
;         const int i1 = it + NGW; const bool more = i1 < it1;
;         CVT_LOAD(vb, c, 1); cvt_pack8(va, c, blk, 0, lane);
;         CVT_LOAD(va, c, 2); cvt_pack8(vb, c, blk, 1, lane);
;         CVT_LOAD(vb, c, 3); cvt_pack8(va, c, blk, 2, lane);
.LBB0_26:
	s_ashr_i32 s27, s26, 31
	s_lshl_b64 s[30:31], s[26:27], 8
	v_lshl_add_u64 v[66:67], v[144:145], 0, s[30:31]
	s_lshl_b64 s[30:31], s[26:27], 2
	global_load_dwordx4 v[70:73], v[66:67], off nt
	v_lshl_add_u64 v[66:67], v[66:67], 0, s[30:31]
	global_load_dwordx4 v[98:101], v[66:67], off nt
	v_lshl_add_u64 v[66:67], v[66:67], 0, s[30:31]
	global_load_dwordx4 v[110:113], v[66:67], off nt
	v_lshl_add_u64 v[66:67], v[66:67], 0, s[30:31]
	global_load_dwordx4 v[118:121], v[66:67], off nt
	v_lshl_add_u64 v[66:67], v[66:67], 0, s[30:31]
	global_load_dwordx4 v[102:105], v[66:67], off nt
	v_lshl_add_u64 v[66:67], v[66:67], 0, s[30:31]
	global_load_dwordx4 v[114:117], v[66:67], off nt
	v_lshl_add_u64 v[66:67], v[66:67], 0, s[30:31]
	global_load_dwordx4 v[122:125], v[66:67], off nt
	v_lshl_add_u64 v[66:67], v[66:67], 0, s[30:31]
	v_lshl_add_u64 v[74:75], v[66:67], 0, s[30:31]
	global_load_dwordx4 v[126:129], v[66:67], off nt
	s_waitcnt vmcnt(16)
	v_mul_f32_e32 v18, v18, v200
	global_load_dwordx4 v[66:69], v[74:75], off nt
	v_lshl_add_u64 v[74:75], v[74:75], 0, s[30:31]
	global_load_dwordx4 v[90:93], v[74:75], off nt
	v_lshl_add_u64 v[74:75], v[74:75], 0, s[30:31]
	global_load_dwordx4 v[94:97], v[74:75], off nt
	v_lshl_add_u64 v[74:75], v[74:75], 0, s[30:31]
	v_lshl_add_u64 v[78:79], v[74:75], 0, s[30:31]
	v_lshl_add_u64 v[82:83], v[78:79], 0, s[30:31]
	global_load_dwordx4 v[106:109], v[74:75], off nt
	v_lshl_add_u64 v[86:87], v[82:83], 0, s[30:31]
	global_load_dwordx4 v[74:77], v[78:79], off nt
	v_lshl_add_u64 v[146:147], v[86:87], 0, s[30:31]
	global_load_dwordx4 v[78:81], v[82:83], off nt
	v_mul_f32_e32 v30, v30, v200
	global_load_dwordx4 v[82:85], v[86:87], off nt
	v_mov_b32_e32 v204, 0
	global_load_dwordx4 v[86:89], v[146:147], off nt
	v_cvt_pk_fp8_f32 v204, v18, v30
	v_mul_f32_e32 v14, v14, v200
	v_mul_f32_e32 v26, v26, v200
	s_waitcnt vmcnt(16)
	v_mul_f32_e32 v62, v62, v200
	v_mul_f32_e32 v50, v50, v200
	v_mov_b32_e32 v202, 0
	v_mul_f32_e32 v38, v38, v200
	v_mul_f32_e32 v46, v46, v200
	v_mov_b32_e32 v203, 0
	v_cvt_pk_fp8_f32 v204, v14, v26 op_sel:[0,0,1]
	v_mul_f32_e32 v2, v2, v200
	v_mul_f32_e32 v14, v22, v200
	v_mov_b32_e32 v205, 0
	v_cvt_pk_fp8_f32 v202, v62, v50
	v_cvt_pk_fp8_f32 v203, v38, v46
	v_cvt_pk_fp8_f32 v205, v2, v14
	v_mul_f32_e32 v54, v54, v200
	v_mul_f32_e32 v58, v58, v200
	v_mul_f32_e32 v34, v34, v200
	v_mul_f32_e32 v42, v42, v200
	v_mul_f32_e32 v6, v6, v200
	v_mul_f32_e32 v10, v10, v200
	v_cvt_pk_fp8_f32 v202, v54, v58 op_sel:[0,0,1]
	v_cvt_pk_fp8_f32 v203, v34, v42 op_sel:[0,0,1]
	v_cvt_pk_fp8_f32 v205, v6, v10 op_sel:[0,0,1]
	v_mul_f32_e32 v2, v63, v200
	v_mul_f32_e32 v6, v51, v200
	v_mul_f32_e32 v10, v55, v200
	ds_write_b128 v163, v[202:205]
	v_mov_b32_e32 v202, 0
	v_cvt_pk_fp8_f32 v202, v2, v6
	v_mul_f32_e32 v2, v39, v200
	v_mul_f32_e32 v6, v47, v200
	v_mov_b32_e32 v203, 0
	v_cvt_pk_fp8_f32 v203, v2, v6
	v_mul_f32_e32 v2, v19, v200
	v_mul_f32_e32 v6, v31, v200
	v_mov_b32_e32 v204, 0
	v_cvt_pk_fp8_f32 v204, v2, v6
	v_mul_f32_e32 v2, v3, v200
	v_mul_f32_e32 v3, v23, v200
	v_mov_b32_e32 v205, 0
	v_cvt_pk_fp8_f32 v205, v2, v3
	v_mul_f32_e32 v14, v59, v200
	v_cvt_pk_fp8_f32 v202, v10, v14 op_sel:[0,0,1]
	v_mul_f32_e32 v10, v35, v200
	v_mul_f32_e32 v14, v43, v200
	v_cvt_pk_fp8_f32 v203, v10, v14 op_sel:[0,0,1]
	v_mul_f32_e32 v10, v15, v200
	v_mul_f32_e32 v14, v27, v200
	v_mul_f32_e32 v6, v7, v200
	v_mul_f32_e32 v7, v11, v200
	v_cvt_pk_fp8_f32 v204, v10, v14 op_sel:[0,0,1]
	v_cvt_pk_fp8_f32 v205, v6, v7 op_sel:[0,0,1]
	v_mul_f32_e32 v2, v64, v200
	v_mul_f32_e32 v3, v52, v200
	v_mul_f32_e32 v6, v56, v200
	ds_write_b128 v163, v[202:205] offset:256
	v_mov_b32_e32 v202, 0
	v_cvt_pk_fp8_f32 v202, v2, v3
	v_mul_f32_e32 v2, v40, v200
	v_mul_f32_e32 v3, v48, v200
	v_mov_b32_e32 v203, 0
	v_cvt_pk_fp8_f32 v203, v2, v3
	v_mul_f32_e32 v2, v20, v200
	v_mul_f32_e32 v3, v32, v200
	v_mov_b32_e32 v204, 0
	v_cvt_pk_fp8_f32 v204, v2, v3
	v_mul_f32_e32 v2, v4, v200
	v_mul_f32_e32 v3, v24, v200
	v_mov_b32_e32 v205, 0
	v_mul_f32_e32 v7, v60, v200
	v_cvt_pk_fp8_f32 v205, v2, v3
	v_cvt_pk_fp8_f32 v202, v6, v7 op_sel:[0,0,1]
	v_mul_f32_e32 v6, v36, v200
	v_mul_f32_e32 v7, v44, v200
	v_cvt_pk_fp8_f32 v203, v6, v7 op_sel:[0,0,1]
	v_mul_f32_e32 v6, v16, v200
	v_mul_f32_e32 v7, v28, v200
	v_cvt_pk_fp8_f32 v204, v6, v7 op_sel:[0,0,1]
	v_mul_f32_e32 v4, v8, v200
	v_mul_f32_e32 v6, v12, v200
	v_cvt_pk_fp8_f32 v205, v4, v6 op_sel:[0,0,1]
	v_mul_f32_e32 v3, v65, v200
	v_mul_f32_e32 v4, v53, v200
	v_mov_b32_e32 v2, 0
	v_cvt_pk_fp8_f32 v2, v3, v4
	v_mul_f32_e32 v6, v57, v200
	v_mul_f32_e32 v7, v61, v200
	v_mul_f32_e32 v4, v41, v200
	v_cvt_pk_fp8_f32 v2, v6, v7 op_sel:[0,0,1]
	v_mul_f32_e32 v6, v49, v200
	v_mov_b32_e32 v3, 0
	v_cvt_pk_fp8_f32 v3, v4, v6
	v_mul_f32_e32 v7, v37, v200
	v_mul_f32_e32 v8, v45, v200
	v_mul_f32_e32 v6, v21, v200
	v_cvt_pk_fp8_f32 v3, v7, v8 op_sel:[0,0,1]
	v_mul_f32_e32 v7, v33, v200
	v_mov_b32_e32 v4, 0
	ds_write_b128 v163, v[202:205] offset:512
	v_cvt_pk_fp8_f32 v4, v6, v7
	v_mul_f32_e32 v6, v5, v200
	v_mul_f32_e32 v7, v25, v200
	v_mov_b32_e32 v5, 0
	s_waitcnt vmcnt(15)
	v_mul_f32_e32 v70, v200, v70
	s_waitcnt vmcnt(14)
	v_mul_f32_e32 v98, v200, v98
	v_mov_b32_e32 v202, 0
	v_cvt_pk_fp8_f32 v5, v6, v7
	v_cvt_pk_fp8_f32 v202, v70, v98
	s_waitcnt vmcnt(11)
	v_mul_f32_e32 v70, v200, v102
	s_waitcnt vmcnt(10)
	v_mul_f32_e32 v98, v200, v114
	v_mov_b32_e32 v203, 0
	v_cvt_pk_fp8_f32 v203, v70, v98
	s_waitcnt vmcnt(7)
	v_mul_f32_e32 v66, v200, v66
	s_waitcnt vmcnt(6)
	v_mul_f32_e32 v70, v200, v90
	v_mov_b32_e32 v204, 0
	v_mul_f32_e32 v8, v17, v200
	v_mul_f32_e32 v10, v29, v200
	v_cvt_pk_fp8_f32 v204, v66, v70
	s_waitcnt vmcnt(3)
; __device__ __forceinline__ unsigned pk4_fp8(float a, float b, float c, float d) { unsigned w = 0u; w = __builtin_amdgcn_cvt_pk_fp8_f32(a, b, w, false); w = __builtin_amdgcn_cvt_pk_fp8_f32(c, d, w, true); return w; }
; #define LAS __attribute__((address_space(3)))
; #define CVT_LOAD(v, c, s_) do { _Pragma("unroll") for (int i_ = 0; i_ < 16; ++i_) v[i_] = *(const f32x4*)((c).src + (size_t)(64 * (s_) + i_) * (c).N); } while (0)
; __device__ __forceinline__ void cvt_pack8(const f32x4 (&v)[16], const CvtItem& c, LAS unsigned char* blk, int s4, int lane) {
;     const float w = c.wscale; const int cb = lane & 15, j = 4 * s4 + (lane >> 4);
; #pragma unroll
;     for (int jn = 0; jn < 4; ++jn) {
;         v4u o; o.x = pg8::pk4_fp8(v[0][jn] * w, v[1][jn] * w, v[2][jn] * w, v[3][jn] * w); o.y = pg8::pk4_fp8(v[4][jn] * w, v[5][jn] * w, v[6][jn] * w, v[7][jn] * w);
;         o.z = pg8::pk4_fp8(v[8][jn] * w, v[9][jn] * w, v[10][jn] * w, v[11][jn] * w); o.w = pg8::pk4_fp8(v[12][jn] * w, v[13][jn] * w, v[14][jn] * w, v[15][jn] * w);
;         *(LAS v4u*)(blk + (4 * cb + jn) * 256 + ((j ^ cb) * 16)) = o; }
; }
; __device__ __forceinline__ void cvt_moe_pipe2(const CvtSrc& A, const CvtSrc& B, LAS float* scr, int gw, int NGW, int lane) {
;     ...
;     while (it < it1) {
;         const int i1 = it + NGW; const bool more = i1 < it1;
;         CVT_LOAD(vb, c, 1); cvt_pack8(va, c, blk, 0, lane);
;         CVT_LOAD(va, c, 2); cvt_pack8(vb, c, blk, 1, lane);
;         CVT_LOAD(vb, c, 3); cvt_pack8(va, c, blk, 2, lane);
;         if (more) { cn = cvt_moe_item2(i1, A, B, lane); CVT_LOAD(va, cn, 0); }
;         cvt_pack8(vb, c, blk, 3, lane);
	v_mul_f32_e32 v66, v200, v74
	s_waitcnt vmcnt(2)
	v_mul_f32_e32 v70, v200, v78
	v_mov_b32_e32 v205, 0
	v_cvt_pk_fp8_f32 v4, v8, v10 op_sel:[0,0,1]
	v_mul_f32_e32 v8, v9, v200
	v_mul_f32_e32 v9, v13, v200
	v_cvt_pk_fp8_f32 v205, v66, v70
	v_cvt_pk_fp8_f32 v5, v8, v9 op_sel:[0,0,1]
	v_mul_f32_e32 v110, v200, v110
	v_mul_f32_e32 v118, v200, v118
	v_cvt_pk_fp8_f32 v202, v110, v118 op_sel:[0,0,1]
	v_mul_f32_e32 v102, v200, v122
	v_mul_f32_e32 v110, v200, v126
	v_mul_f32_e32 v90, v200, v94
	v_mul_f32_e32 v94, v200, v106
	s_waitcnt vmcnt(1)
	v_mul_f32_e32 v74, v200, v82
	s_waitcnt vmcnt(0)
	v_mul_f32_e32 v78, v200, v86
	v_cvt_pk_fp8_f32 v203, v102, v110 op_sel:[0,0,1]
	v_cvt_pk_fp8_f32 v204, v90, v94 op_sel:[0,0,1]
	v_cvt_pk_fp8_f32 v205, v74, v78 op_sel:[0,0,1]
	ds_write_b128 v163, v[2:5] offset:768
	v_mad_i64_i32 v[2:3], s[34:35], s26, v182, v[146:147]
	global_load_dwordx4 v[62:65], v[2:3], off nt
	v_lshl_add_u64 v[2:3], v[2:3], 0, s[30:31]
	global_load_dwordx4 v[50:53], v[2:3], off nt
	v_lshl_add_u64 v[2:3], v[2:3], 0, s[30:31]
	global_load_dwordx4 v[54:57], v[2:3], off nt
	v_lshl_add_u64 v[2:3], v[2:3], 0, s[30:31]
	ds_write_b128 v164, v[202:205]
	v_mul_f32_e32 v66, v200, v71
	v_mul_f32_e32 v70, v200, v99
	v_mov_b32_e32 v202, 0
	global_load_dwordx4 v[58:61], v[2:3], off nt
	v_lshl_add_u64 v[2:3], v[2:3], 0, s[30:31]
	v_cvt_pk_fp8_f32 v202, v66, v70
	v_mul_f32_e32 v66, v200, v103
	v_mul_f32_e32 v70, v200, v115
	v_mov_b32_e32 v203, 0
	global_load_dwordx4 v[38:41], v[2:3], off nt
	v_lshl_add_u64 v[2:3], v[2:3], 0, s[30:31]
	v_cvt_pk_fp8_f32 v203, v66, v70
	v_mul_f32_e32 v66, v200, v67
	v_mul_f32_e32 v67, v200, v91
	v_mov_b32_e32 v204, 0
	global_load_dwordx4 v[46:49], v[2:3], off nt
	v_lshl_add_u64 v[2:3], v[2:3], 0, s[30:31]
	v_cvt_pk_fp8_f32 v204, v66, v67
	v_mul_f32_e32 v66, v200, v75
	v_mul_f32_e32 v67, v200, v79
	v_mov_b32_e32 v205, 0
	global_load_dwordx4 v[34:37], v[2:3], off nt
	v_lshl_add_u64 v[2:3], v[2:3], 0, s[30:31]
	v_mul_f32_e32 v71, v200, v111
	v_mul_f32_e32 v74, v200, v119
	v_cvt_pk_fp8_f32 v205, v66, v67
	global_load_dwordx4 v[42:45], v[2:3], off nt
	v_lshl_add_u64 v[2:3], v[2:3], 0, s[30:31]
	v_cvt_pk_fp8_f32 v202, v71, v74 op_sel:[0,0,1]
	v_mul_f32_e32 v71, v200, v123
	v_mul_f32_e32 v74, v200, v127
	global_load_dwordx4 v[18:21], v[2:3], off nt
	v_lshl_add_u64 v[2:3], v[2:3], 0, s[30:31]
	v_cvt_pk_fp8_f32 v203, v71, v74 op_sel:[0,0,1]
	v_mul_f32_e32 v70, v200, v95
	v_mul_f32_e32 v71, v200, v107
	global_load_dwordx4 v[30:33], v[2:3], off nt
	v_lshl_add_u64 v[2:3], v[2:3], 0, s[30:31]
	v_cvt_pk_fp8_f32 v204, v70, v71 op_sel:[0,0,1]
	v_mul_f32_e32 v70, v200, v83
	v_mul_f32_e32 v71, v200, v87
	global_load_dwordx4 v[14:17], v[2:3], off nt
	v_lshl_add_u64 v[2:3], v[2:3], 0, s[30:31]
	v_cvt_pk_fp8_f32 v205, v70, v71 op_sel:[0,0,1]
	v_lshl_add_u64 v[6:7], v[2:3], 0, s[30:31]
	global_load_dwordx4 v[26:29], v[2:3], off nt
	v_mul_f32_e32 v66, v200, v72
	global_load_dwordx4 v[2:5], v[6:7], off nt
	v_lshl_add_u64 v[6:7], v[6:7], 0, s[30:31]
	global_load_dwordx4 v[22:25], v[6:7], off nt
	ds_write_b128 v164, v[202:205] offset:256
	v_mul_f32_e32 v67, v200, v100
	v_mov_b32_e32 v202, 0
	v_lshl_add_u64 v[10:11], v[6:7], 0, s[30:31]
	v_cvt_pk_fp8_f32 v202, v66, v67
	v_mul_f32_e32 v66, v200, v104
	v_mul_f32_e32 v67, v200, v116
	v_mov_b32_e32 v203, 0
	v_lshl_add_u64 v[146:147], v[10:11], 0, s[30:31]
	v_cvt_pk_fp8_f32 v203, v66, v67
	v_mul_f32_e32 v66, v200, v68
	v_mul_f32_e32 v67, v200, v92
	v_mov_b32_e32 v204, 0
	global_load_dwordx4 v[6:9], v[10:11], off nt
	v_cvt_pk_fp8_f32 v204, v66, v67
	global_load_dwordx4 v[10:13], v[146:147], off nt
	v_mul_f32_e32 v66, v200, v76
	v_mul_f32_e32 v67, v200, v80
	v_mov_b32_e32 v205, 0
	v_mul_f32_e32 v70, v200, v112
	v_mul_f32_e32 v71, v200, v120
	v_cvt_pk_fp8_f32 v205, v66, v67
	v_cvt_pk_fp8_f32 v202, v70, v71 op_sel:[0,0,1]
	v_mul_f32_e32 v70, v200, v124
	v_mul_f32_e32 v71, v200, v128
	v_cvt_pk_fp8_f32 v203, v70, v71 op_sel:[0,0,1]
	v_mul_f32_e32 v68, v200, v96
	v_mul_f32_e32 v70, v200, v108
	v_cvt_pk_fp8_f32 v204, v68, v70 op_sel:[0,0,1]
	v_mul_f32_e32 v68, v200, v84
	v_mul_f32_e32 v70, v200, v88
	v_cvt_pk_fp8_f32 v205, v68, v70 op_sel:[0,0,1]
	v_mul_f32_e32 v67, v200, v73
	v_mul_f32_e32 v68, v200, v101
	v_mov_b32_e32 v66, 0
	v_cvt_pk_fp8_f32 v66, v67, v68
	v_mul_f32_e32 v70, v200, v113
	v_mul_f32_e32 v71, v200, v121
	v_mul_f32_e32 v68, v200, v105
	v_cvt_pk_fp8_f32 v66, v70, v71 op_sel:[0,0,1]
	v_mul_f32_e32 v70, v200, v117
	v_mov_b32_e32 v67, 0
	v_cvt_pk_fp8_f32 v67, v68, v70
	v_mul_f32_e32 v69, v200, v69
	v_mul_f32_e32 v70, v200, v93
	v_mov_b32_e32 v68, 0
	v_cvt_pk_fp8_f32 v68, v69, v70
	v_mul_f32_e32 v71, v200, v125
	v_mul_f32_e32 v72, v200, v129
	v_cvt_pk_fp8_f32 v67, v71, v72 op_sel:[0,0,1]
	v_mul_f32_e32 v71, v200, v97
	v_mul_f32_e32 v72, v200, v109
	v_cvt_pk_fp8_f32 v68, v71, v72 op_sel:[0,0,1]
	v_mul_f32_e32 v70, v200, v77
	v_mul_f32_e32 v71, v200, v81
	v_mov_b32_e32 v69, 0
	v_cvt_pk_fp8_f32 v69, v70, v71
	v_mul_f32_e32 v72, v200, v85
	v_mul_f32_e32 v73, v200, v89
	ds_write_b128 v164, v[202:205] offset:512
	v_cvt_pk_fp8_f32 v69, v72, v73 op_sel:[0,0,1]
	s_waitcnt vmcnt(15)
; __device__ __forceinline__ unsigned pk4_fp8(float a, float b, float c, float d) { unsigned w = 0u; w = __builtin_amdgcn_cvt_pk_fp8_f32(a, b, w, false); w = __builtin_amdgcn_cvt_pk_fp8_f32(c, d, w, true); return w; }
; #define LAS __attribute__((address_space(3)))
; #define CVT_LOAD(v, c, s_) do { _Pragma("unroll") for (int i_ = 0; i_ < 16; ++i_) v[i_] = *(const f32x4*)((c).src + (size_t)(64 * (s_) + i_) * (c).N); } while (0)
; __device__ __forceinline__ void cvt_pack8(const f32x4 (&v)[16], const CvtItem& c, LAS unsigned char* blk, int s4, int lane) {
;     const float w = c.wscale; const int cb = lane & 15, j = 4 * s4 + (lane >> 4);
; #pragma unroll
;     for (int jn = 0; jn < 4; ++jn) {
;         v4u o; o.x = pg8::pk4_fp8(v[0][jn] * w, v[1][jn] * w, v[2][jn] * w, v[3][jn] * w); o.y = pg8::pk4_fp8(v[4][jn] * w, v[5][jn] * w, v[6][jn] * w, v[7][jn] * w);
;         o.z = pg8::pk4_fp8(v[8][jn] * w, v[9][jn] * w, v[10][jn] * w, v[11][jn] * w); o.w = pg8::pk4_fp8(v[12][jn] * w, v[13][jn] * w, v[14][jn] * w, v[15][jn] * w);
;         *(LAS v4u*)(blk + (4 * cb + jn) * 256 + ((j ^ cb) * 16)) = o; }
; }
; __device__ __forceinline__ void cvt_moe_pipe2(const CvtSrc& A, const CvtSrc& B, LAS float* scr, int gw, int NGW, int lane) {
;     ...
;     while (it < it1) {
;         const int i1 = it + NGW; const bool more = i1 < it1;
;         CVT_LOAD(vb, c, 1); cvt_pack8(va, c, blk, 0, lane);
;         CVT_LOAD(va, c, 2); cvt_pack8(vb, c, blk, 1, lane);
;         CVT_LOAD(vb, c, 3); cvt_pack8(va, c, blk, 2, lane);
;         if (more) { cn = cvt_moe_item2(i1, A, B, lane); CVT_LOAD(va, cn, 0); }
;         cvt_pack8(vb, c, blk, 3, lane);
	v_mul_f32_e32 v142, v200, v62
	v_mov_b32_e32 v202, 0
	v_mov_b32_e32 v203, 0
	ds_write_b128 v164, v[66:69] offset:768
	v_mad_i64_i32 v[66:67], s[34:35], s26, v182, v[146:147]
	global_load_dwordx4 v[110:113], v[66:67], off nt
	v_lshl_add_u64 v[66:67], v[66:67], 0, s[30:31]
	global_load_dwordx4 v[118:121], v[66:67], off nt
	v_lshl_add_u64 v[66:67], v[66:67], 0, s[30:31]
	global_load_dwordx4 v[122:125], v[66:67], off nt
	v_lshl_add_u64 v[66:67], v[66:67], 0, s[30:31]
	global_load_dwordx4 v[126:129], v[66:67], off nt
	v_lshl_add_u64 v[66:67], v[66:67], 0, s[30:31]
	global_load_dwordx4 v[98:101], v[66:67], off nt
	v_lshl_add_u64 v[66:67], v[66:67], 0, s[30:31]
	global_load_dwordx4 v[102:105], v[66:67], off nt
	v_lshl_add_u64 v[66:67], v[66:67], 0, s[30:31]
	global_load_dwordx4 v[106:109], v[66:67], off nt
	v_lshl_add_u64 v[66:67], v[66:67], 0, s[30:31]
	global_load_dwordx4 v[114:117], v[66:67], off nt
	v_lshl_add_u64 v[66:67], v[66:67], 0, s[30:31]
	global_load_dwordx4 v[78:81], v[66:67], off nt
	v_lshl_add_u64 v[66:67], v[66:67], 0, s[30:31]
	global_load_dwordx4 v[86:89], v[66:67], off nt
	v_lshl_add_u64 v[66:67], v[66:67], 0, s[30:31]
	global_load_dwordx4 v[90:93], v[66:67], off nt
	v_lshl_add_u64 v[66:67], v[66:67], 0, s[30:31]
	v_lshl_add_u64 v[70:71], v[66:67], 0, s[30:31]
	v_lshl_add_u64 v[74:75], v[70:71], 0, s[30:31]
	v_lshl_add_u64 v[82:83], v[74:75], 0, s[30:31]
	global_load_dwordx4 v[94:97], v[66:67], off nt
	s_waitcnt vmcnt(26)
	v_mul_f32_e32 v146, v200, v50
	global_load_dwordx4 v[66:69], v[70:71], off nt
	v_cvt_pk_fp8_f32 v202, v142, v146
	global_load_dwordx4 v[70:73], v[74:75], off nt
	s_waitcnt vmcnt(25)
	v_mul_f32_e32 v142, v200, v38
	global_load_dwordx4 v[74:77], v[82:83], off nt
	v_lshl_add_u64 v[82:83], v[82:83], 0, s[30:31]
	global_load_dwordx4 v[82:85], v[82:83], off nt
	s_waitcnt vmcnt(26)
	v_mul_f32_e32 v146, v200, v46
	v_cvt_pk_fp8_f32 v203, v142, v146
	s_waitcnt vmcnt(23)
	v_mul_f32_e32 v142, v200, v18
	s_waitcnt vmcnt(22)
	v_mul_f32_e32 v146, v200, v30
	v_mov_b32_e32 v204, 0
	v_cvt_pk_fp8_f32 v204, v142, v146
	s_waitcnt vmcnt(19)
	v_mul_f32_e32 v142, v200, v2
	s_waitcnt vmcnt(18)
	v_mul_f32_e32 v146, v200, v22
	v_mov_b32_e32 v205, 0
	v_mul_f32_e32 v147, v200, v54
	v_mul_f32_e32 v201, v200, v58
	v_cvt_pk_fp8_f32 v205, v142, v146
	v_cvt_pk_fp8_f32 v202, v147, v201 op_sel:[0,0,1]
	v_mul_f32_e32 v147, v200, v34
	v_mul_f32_e32 v201, v200, v42
	v_cvt_pk_fp8_f32 v203, v147, v201 op_sel:[0,0,1]
	v_mul_f32_e32 v147, v200, v14
	v_mul_f32_e32 v201, v200, v26
	v_cvt_pk_fp8_f32 v204, v147, v201 op_sel:[0,0,1]
	s_waitcnt vmcnt(17)
	v_mul_f32_e32 v147, v200, v6
	s_waitcnt vmcnt(16)
	v_mul_f32_e32 v201, v200, v10
	v_cvt_pk_fp8_f32 v205, v147, v201 op_sel:[0,0,1]
	v_mul_f32_e32 v142, v200, v63
	v_mul_f32_e32 v146, v200, v51
	v_mul_f32_e32 v147, v200, v55
	ds_write_b128 v165, v[202:205]
	v_mov_b32_e32 v202, 0
	v_cvt_pk_fp8_f32 v202, v142, v146
	v_mul_f32_e32 v142, v200, v39
	v_mul_f32_e32 v146, v200, v47
	v_mov_b32_e32 v203, 0
	v_cvt_pk_fp8_f32 v203, v142, v146
	v_mul_f32_e32 v142, v200, v19
	v_mul_f32_e32 v146, v200, v31
	v_mov_b32_e32 v204, 0
	v_cvt_pk_fp8_f32 v204, v142, v146
	v_mul_f32_e32 v142, v200, v3
	v_mul_f32_e32 v146, v200, v23
	v_mov_b32_e32 v205, 0
	v_mul_f32_e32 v201, v200, v59
	v_cvt_pk_fp8_f32 v205, v142, v146
	v_cvt_pk_fp8_f32 v202, v147, v201 op_sel:[0,0,1]
	v_mul_f32_e32 v147, v200, v35
	v_mul_f32_e32 v201, v200, v43
	v_cvt_pk_fp8_f32 v203, v147, v201 op_sel:[0,0,1]
	v_mul_f32_e32 v147, v200, v15
	v_mul_f32_e32 v201, v200, v27
	v_cvt_pk_fp8_f32 v204, v147, v201 op_sel:[0,0,1]
	v_mul_f32_e32 v147, v200, v7
	v_mul_f32_e32 v201, v200, v11
	v_cvt_pk_fp8_f32 v205, v147, v201 op_sel:[0,0,1]
	v_mul_f32_e32 v142, v200, v64
	v_mul_f32_e32 v146, v200, v52
	v_mul_f32_e32 v147, v200, v56
	ds_write_b128 v165, v[202:205] offset:256
	v_mov_b32_e32 v202, 0
	v_cvt_pk_fp8_f32 v202, v142, v146
	v_mul_f32_e32 v142, v200, v40
	v_mul_f32_e32 v146, v200, v48
	v_mov_b32_e32 v203, 0
	v_cvt_pk_fp8_f32 v203, v142, v146
	v_mul_f32_e32 v142, v200, v20
	v_mul_f32_e32 v146, v200, v32
	v_mov_b32_e32 v204, 0
	v_cvt_pk_fp8_f32 v204, v142, v146
	v_mul_f32_e32 v142, v200, v4
	v_mul_f32_e32 v146, v200, v24
	v_mov_b32_e32 v205, 0
	v_mul_f32_e32 v201, v200, v60
	v_cvt_pk_fp8_f32 v205, v142, v146
	v_cvt_pk_fp8_f32 v202, v147, v201 op_sel:[0,0,1]
	v_mul_f32_e32 v147, v200, v36
	v_mul_f32_e32 v201, v200, v44
	v_cvt_pk_fp8_f32 v203, v147, v201 op_sel:[0,0,1]
	v_mul_f32_e32 v147, v200, v16
	v_mul_f32_e32 v201, v200, v28
	v_cvt_pk_fp8_f32 v204, v147, v201 op_sel:[0,0,1]
	v_mul_f32_e32 v147, v200, v8
	v_mul_f32_e32 v201, v200, v12
	v_cvt_pk_fp8_f32 v205, v147, v201 op_sel:[0,0,1]
	v_mul_f32_e32 v142, v200, v65
	v_mul_f32_e32 v146, v200, v53
	v_mul_f32_e32 v147, v200, v57
	ds_write_b128 v165, v[202:205] offset:512
	v_mov_b32_e32 v202, 0
	v_cvt_pk_fp8_f32 v202, v142, v146
	v_mul_f32_e32 v142, v200, v41
	v_mul_f32_e32 v146, v200, v49
	v_mov_b32_e32 v203, 0
	v_cvt_pk_fp8_f32 v203, v142, v146
	v_mul_f32_e32 v142, v200, v21
	v_mul_f32_e32 v146, v200, v33
	v_mov_b32_e32 v204, 0
	v_cvt_pk_fp8_f32 v204, v142, v146
	v_mul_f32_e32 v142, v200, v5
	v_mul_f32_e32 v146, v200, v25
	v_mov_b32_e32 v205, 0
	v_mul_f32_e32 v201, v200, v61
	v_cvt_pk_fp8_f32 v205, v142, v146
	v_cvt_pk_fp8_f32 v202, v147, v201 op_sel:[0,0,1]
	v_mul_f32_e32 v147, v200, v37
	v_mul_f32_e32 v201, v200, v45
	v_cvt_pk_fp8_f32 v203, v147, v201 op_sel:[0,0,1]
	v_mul_f32_e32 v147, v200, v17
	v_mul_f32_e32 v201, v200, v29
	v_readlane_b32 s10, v254, 52
	v_cvt_pk_fp8_f32 v204, v147, v201 op_sel:[0,0,1]
	v_mul_f32_e32 v147, v200, v9
	v_mul_f32_e32 v201, v200, v13
	s_add_i32 s1, s1, s10
	v_cvt_pk_fp8_f32 v205, v147, v201 op_sel:[0,0,1]
	s_cmpk_gt_i32 s1, 0x17ff
	s_cselect_b64 s[30:31], -1, 0
	s_and_b64 vcc, exec, s[30:31]
	ds_write_b128 v165, v[202:205] offset:768
	s_cbranch_vccnz .LBB0_25
	s_ashr_i32 s0, s1, 11
	s_and_b32 s10, s1, 0x7f
	s_cmp_gt_i32 s0, 1
	s_mov_b64 s[26:27], -1
	s_cbranch_scc0 .LBB0_29
	s_lshl_b32 s26, s10, 4
	s_and_b32 s21, s1, 15
	s_and_b32 s57, s26, 0x700
	s_mov_b64 s[26:27], 0
	s_mov_b64 s[28:29], s[86:87]

; #define LAS __attribute__((address_space(3)))
; #define CVT_LOAD(v, c, s_) do { _Pragma("unroll") for (int i_ = 0; i_ < 16; ++i_) v[i_] = *(const f32x4*)((c).src + (size_t)(64 * (s_) + i_) * (c).N); } while (0)
; __device__ __forceinline__ CvtItem cvt_moe_item(int it, const float* wg, const float* wu, const float* wd, unsigned char* WGU, unsigned char* WDN, int lane) {
;     const int which = it >> 11, r = it & 2047, e = r >> 7, q = r & 127; CvtItem c; c.which = which;
;     if (which < 2) { const int nb = q & 31, k0 = (q >> 5) * 256; c.nb = nb;
;         c.N = DFF; c.K = DM; c.wscale = which ? 64.f / LOG2E : 64.f * LOG2E; c.src = (which ? wu : wg) + (size_t)e * DM * DFF + (size_t)(k0 + 16 * (lane >> 4)) * DFF + nb * 64 + 4 * (lane & 15);
;         c.dst = WGU + (size_t)e * 4096 * DM + k0; }
;     else { const int nb = q & 15, k0 = (q >> 4) * 256; c.nb = nb;
;         c.N = DM; c.K = DFF; c.wscale = 64.f; c.src = wd + (size_t)e * DFF * DM + (size_t)(k0 + 16 * (lane >> 4)) * DM + nb * 64 + 4 * (lane & 15);
;         c.dst = WDN + (size_t)e * DM * DFF + k0; }
;     return c;
; }
; __device__ __forceinline__ void cvt_moe_pipe2(const CvtSrc& A, const CvtSrc& B, LAS float* scr, int gw, int NGW, int lane) {
;     LAS unsigned char* blk = (LAS unsigned char*)scr;
;     f32x4 va[16], vb[16]; CvtItem c, cn;
;     const int it1 = A.n + B.n; int it = gw;
;     if (it < it1) { c = cvt_moe_item2(it, A, B, lane); CVT_LOAD(va, c, 0); }
.LBB0_31:
	v_readlane_b32 s56, v254, 30
	s_and_b64 s[0:1], s[2:3], exec
	v_readlane_b32 s68, v254, 42
	v_readlane_b32 s69, v254, 43
	v_readlane_b32 s70, v254, 44
	v_readlane_b32 s71, v254, 45
	s_cselect_b32 s2, s68, s70
	s_cselect_b32 s10, s69, s71
	s_mov_b32 s3, 0xb400000
	s_and_b64 s[0:1], s[4:5], exec
	v_readlane_b32 s24, v254, 2
	s_cselect_b32 s0, s3, 0xf400000
	v_readlane_b32 s25, v254, 3
	v_readlane_b32 s4, v254, 0
	s_cselect_b32 s1, s10, s25
	s_cselect_b32 s2, s2, s24
	v_readlane_b32 s5, v254, 1
	s_add_u32 s0, s4, s0
	s_addc_u32 s4, s5, 0
	s_add_u32 s0, s0, s18
	s_addc_u32 s5, s4, s19
	s_add_u32 s4, s0, s52
	s_addc_u32 s5, s5, 0
	s_add_u32 s0, s2, s41
	s_addc_u32 s1, s1, 0
	v_lshlrev_b32_e32 v138, 2, v138
	v_mov_b32_e32 v139, 0
	s_mov_b32 s3, 0
	v_lshl_add_u64 v[2:3], s[0:1], 0, v[138:139]
	s_lshl_b32 s2, s53, 2
	v_lshl_add_u64 v[2:3], v[2:3], 0, s[2:3]
	v_lshlrev_b32_e32 v140, 2, v140
	v_mov_b32_e32 v141, v139
	v_lshl_add_u64 v[142:143], v[2:3], 0, v[140:141]
	s_lshl_b32 s2, s51, 2
	v_lshl_add_u64 v[2:3], v[142:143], 0, s[2:3]
	s_lshl_b32 s2, s50, 2
	v_lshl_add_u64 v[4:5], v[142:143], 0, s[2:3]
	s_lshl_b32 s2, s49, 2
	v_lshl_add_u64 v[6:7], v[142:143], 0, s[2:3]
	s_lshl_b32 s2, s48, 2
	v_lshl_add_u64 v[8:9], v[142:143], 0, s[2:3]
	s_lshl_b32 s2, s47, 2
	global_load_dwordx4 v[26:29], v[2:3], off nt
	s_nop 0
	global_load_dwordx4 v[2:5], v[4:5], off nt
	s_nop 0
	global_load_dwordx4 v[46:49], v[6:7], off nt
	global_load_dwordx4 v[14:17], v[8:9], off nt
	v_lshl_add_u64 v[6:7], v[142:143], 0, s[2:3]
	s_lshl_b32 s2, s46, 2
	v_lshl_add_u64 v[8:9], v[142:143], 0, s[2:3]
	s_lshl_b32 s2, s45, 2
	global_load_dwordx4 v[50:53], v[6:7], off nt
	global_load_dwordx4 v[18:21], v[8:9], off nt
	v_lshl_add_u64 v[6:7], v[142:143], 0, s[2:3]
	s_lshl_b32 s2, s20, 2
	v_lshl_add_u64 v[8:9], v[142:143], 0, s[2:3]
	s_lshl_b32 s2, s44, 2
	global_load_dwordx4 v[42:45], v[6:7], off nt
	global_load_dwordx4 v[10:13], v[8:9], off nt
	v_lshl_add_u64 v[6:7], v[142:143], 0, s[2:3]
	s_lshl_b32 s2, s43, 2
	v_lshl_add_u64 v[8:9], v[142:143], 0, s[2:3]
	s_lshl_b32 s2, s42, 2
	v_lshl_add_u64 v[22:23], v[142:143], 0, s[2:3]
	s_lshl_b32 s2, s22, 2
	v_lshl_add_u64 v[24:25], v[142:143], 0, s[2:3]
	s_lshl_b32 s2, s9, 2
	v_lshl_add_u64 v[30:31], v[142:143], 0, s[2:3]
	s_lshl_b32 s2, s54, 2
	v_lshl_add_u64 v[32:33], v[142:143], 0, s[2:3]
	s_lshl_b32 s2, s8, 2
	v_lshl_add_u64 v[34:35], v[142:143], 0, s[2:3]
	global_load_dwordx4 v[38:41], v[6:7], off nt
	s_nop 0
	global_load_dwordx4 v[6:9], v[8:9], off nt
	s_nop 0
	global_load_dwordx4 v[54:57], v[22:23], off nt
	s_nop 0
	global_load_dwordx4 v[22:25], v[24:25], off nt
	s_nop 0
	global_load_dwordx4 v[58:61], v[30:31], off nt
	s_nop 0
	global_load_dwordx4 v[30:33], v[32:33], off nt
	s_nop 0
	global_load_dwordx4 v[34:37], v[34:35], off nt
	s_nop 0
	global_load_dwordx4 v[62:65], v[142:143], off nt
	v_mov_b32_e32 v144, 0xc4
	v_mov_b32_e32 v145, 0x42317218
	v_mov_b32_e32 v146, 0x42b8aa3b
	v_mov_b32_e32 v147, 0x43
	v_mov_b32_e32 v182, 0x47
	v_mov_b32_e32 v183, 0x4b
	v_mov_b32_e32 v184, 0x4f
	v_mov_b32_e32 v185, 0x53
	v_mov_b32_e32 v186, 0x57
	v_mov_b32_e32 v187, 0x5b
	v_mov_b32_e32 v188, 0x5f
	v_mov_b32_e32 v189, 0x63
	v_mov_b32_e32 v190, 0x67
	v_mov_b32_e32 v191, 0x6b
	v_mov_b32_e32 v192, 0x6f
	v_mov_b32_e32 v193, 0x73
	v_mov_b32_e32 v194, 0x77
	v_mov_b32_e32 v195, 0x7b
	v_mov_b32_e32 v196, 0x7f
	v_readlane_b32 s1, v254, 51
	v_readlane_b32 s57, v254, 31
	v_readlane_b32 s58, v254, 32
	v_readlane_b32 s59, v254, 33
	v_readlane_b32 s60, v254, 34
	v_readlane_b32 s61, v254, 35
	v_readlane_b32 s62, v254, 36
	v_readlane_b32 s63, v254, 37
	v_readlane_b32 s64, v254, 38
	v_readlane_b32 s65, v254, 39
	v_readlane_b32 s66, v254, 40
	v_readlane_b32 s67, v254, 41
	v_readlane_b32 s26, v254, 4
	v_readlane_b32 s27, v254, 5
	s_branch .LBB0_35

; #define CVT_LOAD(v, c, s_) do { _Pragma("unroll") for (int i_ = 0; i_ < 16; ++i_) v[i_] = *(const f32x4*)((c).src + (size_t)(64 * (s_) + i_) * (c).N); } while (0)
; __device__ __forceinline__ CvtItem cvt_moe_item(int it, const float* wg, const float* wu, const float* wd, unsigned char* WGU, unsigned char* WDN, int lane) {
;     const int which = it >> 11, r = it & 2047, e = r >> 7, q = r & 127; CvtItem c; c.which = which;
;     if (which < 2) { const int nb = q & 31, k0 = (q >> 5) * 256; c.nb = nb;
;         c.N = DFF; c.K = DM; c.wscale = which ? 64.f / LOG2E : 64.f * LOG2E; c.src = (which ? wu : wg) + (size_t)e * DM * DFF + (size_t)(k0 + 16 * (lane >> 4)) * DFF + nb * 64 + 4 * (lane & 15);
;         c.dst = WGU + (size_t)e * 4096 * DM + k0; }
;     else { const int nb = q & 15, k0 = (q >> 4) * 256; c.nb = nb;
;         c.N = DM; c.K = DFF; c.wscale = 64.f; c.src = wd + (size_t)e * DFF * DM + (size_t)(k0 + 16 * (lane >> 4)) * DM + nb * 64 + 4 * (lane & 15);
;         c.dst = WDN + (size_t)e * DM * DFF + k0; }
;     return c;
; }
; __device__ __forceinline__ void cvt_moe_pipe2(const CvtSrc& A, const CvtSrc& B, LAS float* scr, int gw, int NGW, int lane) {
;     ...
;         if (more) { cn = cvt_moe_item2(i1, A, B, lane); CVT_LOAD(va, cn, 0); }
.LBB0_33:
	v_readlane_b32 s28, v254, 0
	v_readlane_b32 s29, v254, 1
	s_add_u32 s21, s28, s22
	s_addc_u32 s22, s29, s23
	s_bfe_u32 s2, s1, 0x40007
	s_lshl_b32 s23, s2, 23
	s_add_u32 s10, s10, s23
	v_or_b32_e32 v2, s26, v131
	s_addc_u32 s11, s11, 0
	v_lshlrev_b32_e32 v138, s9, v2
	v_lshl_add_u64 v[2:3], v[138:139], 2, s[10:11]
	s_lshl_b32 s10, s24, 6
	s_mov_b32 s11, s3
	v_lshl_add_u64 v[2:3], s[10:11], 2, v[2:3]
	v_mov_b32_e32 v141, v139
	v_lshl_add_u64 v[142:143], v[2:3], 0, v[140:141]
	s_lshl_b64 s[10:11], s[2:3], s20
	s_lshl_b32 s2, s8, 2
	v_lshl_add_u64 v[2:3], v[142:143], 0, s[2:3]
	s_lshl_b32 s2, s8, 3
	v_lshl_add_u64 v[4:5], v[142:143], 0, s[2:3]
	s_mul_i32 s2, s8, 12
	global_load_dwordx4 v[34:37], v[2:3], off nt
	global_load_dwordx4 v[30:33], v[4:5], off nt
	v_lshl_add_u64 v[2:3], v[142:143], 0, s[2:3]
	s_lshl_b32 s2, s8, 4
	v_lshl_add_u64 v[4:5], v[142:143], 0, s[2:3]
	s_mul_i32 s2, s8, 20
	global_load_dwordx4 v[58:61], v[2:3], off nt
	global_load_dwordx4 v[22:25], v[4:5], off nt
	v_lshl_add_u64 v[2:3], v[142:143], 0, s[2:3]
	s_mul_i32 s2, s8, 24
	v_lshl_add_u64 v[4:5], v[142:143], 0, s[2:3]
	s_mul_i32 s2, s8, 28
	global_load_dwordx4 v[54:57], v[2:3], off nt
	global_load_dwordx4 v[6:9], v[4:5], off nt
	v_lshl_add_u64 v[2:3], v[142:143], 0, s[2:3]
	s_lshl_b32 s2, s8, 5
	v_lshl_add_u64 v[4:5], v[142:143], 0, s[2:3]
	s_mul_i32 s2, s8, 36
	global_load_dwordx4 v[38:41], v[2:3], off nt
	global_load_dwordx4 v[10:13], v[4:5], off nt
	v_lshl_add_u64 v[2:3], v[142:143], 0, s[2:3]
	s_mul_i32 s2, s8, 40
	v_lshl_add_u64 v[4:5], v[142:143], 0, s[2:3]
	s_mul_i32 s2, s8, 44
	global_load_dwordx4 v[42:45], v[2:3], off nt
	global_load_dwordx4 v[18:21], v[4:5], off nt
	v_lshl_add_u64 v[2:3], v[142:143], 0, s[2:3]
	s_mul_i32 s2, s8, 48
	v_lshl_add_u64 v[4:5], v[142:143], 0, s[2:3]
	s_mul_i32 s2, s8, 52
	global_load_dwordx4 v[50:53], v[2:3], off nt
	global_load_dwordx4 v[14:17], v[4:5], off nt
	v_lshl_add_u64 v[2:3], v[142:143], 0, s[2:3]
	s_mul_i32 s2, s8, 56
	v_lshl_add_u64 v[4:5], v[142:143], 0, s[2:3]
	s_mul_i32 s2, s8, 60
	v_lshl_add_u64 v[26:27], v[142:143], 0, s[2:3]
	global_load_dwordx4 v[46:49], v[2:3], off nt
	s_nop 0
	global_load_dwordx4 v[2:5], v[4:5], off nt
	s_nop 0
	global_load_dwordx4 v[62:65], v[142:143], off nt
	s_nop 0
	global_load_dwordx4 v[26:29], v[26:27], off nt
	s_add_u32 s2, s21, s10
	s_addc_u32 s9, s22, s11
	s_add_u32 s10, s2, s26
	s_addc_u32 s11, s9, 0

; __device__ __forceinline__ unsigned pk4_fp8(float a, float b, float c, float d) { unsigned w = 0u; w = __builtin_amdgcn_cvt_pk_fp8_f32(a, b, w, false); w = __builtin_amdgcn_cvt_pk_fp8_f32(c, d, w, true); return w; }
; #define LAS __attribute__((address_space(3)))
; #define CVT_LOAD(v, c, s_) do { _Pragma("unroll") for (int i_ = 0; i_ < 16; ++i_) v[i_] = *(const f32x4*)((c).src + (size_t)(64 * (s_) + i_) * (c).N); } while (0)
; __device__ __forceinline__ void cvt_pack8(const f32x4 (&v)[16], const CvtItem& c, LAS unsigned char* blk, int s4, int lane) {
;     const float w = c.wscale; const int cb = lane & 15, j = 4 * s4 + (lane >> 4);
; #pragma unroll
;     for (int jn = 0; jn < 4; ++jn) {
;         v4u o; o.x = pg8::pk4_fp8(v[0][jn] * w, v[1][jn] * w, v[2][jn] * w, v[3][jn] * w); o.y = pg8::pk4_fp8(v[4][jn] * w, v[5][jn] * w, v[6][jn] * w, v[7][jn] * w);
;         o.z = pg8::pk4_fp8(v[8][jn] * w, v[9][jn] * w, v[10][jn] * w, v[11][jn] * w); o.w = pg8::pk4_fp8(v[12][jn] * w, v[13][jn] * w, v[14][jn] * w, v[15][jn] * w);
;         *(LAS v4u*)(blk + (4 * cb + jn) * 256 + ((j ^ cb) * 16)) = o; }
; }
; __device__ __forceinline__ void cvt_moe_pipe2(const CvtSrc& A, const CvtSrc& B, LAS float* scr, int gw, int NGW, int lane) {
;     ...
;     while (it < it1) {
;         const int i1 = it + NGW; const bool more = i1 < it1;
;         CVT_LOAD(vb, c, 1); cvt_pack8(va, c, blk, 0, lane);
;         CVT_LOAD(va, c, 2); cvt_pack8(vb, c, blk, 1, lane);
;         CVT_LOAD(vb, c, 3); cvt_pack8(va, c, blk, 2, lane);
.LBB0_35:
	s_ashr_i32 s9, s8, 31
	s_lshl_b64 s[18:19], s[8:9], 8
	v_lshl_add_u64 v[66:67], v[142:143], 0, s[18:19]
	s_lshl_b64 s[18:19], s[8:9], 2
	v_lshl_add_u64 v[68:69], v[66:67], 0, s[18:19]
	global_load_dwordx4 v[74:77], v[66:67], off nt
	global_load_dwordx4 v[78:81], v[68:69], off nt
	v_lshl_add_u64 v[66:67], v[68:69], 0, s[18:19]
	v_lshl_add_u64 v[68:69], v[66:67], 0, s[18:19]
	global_load_dwordx4 v[118:121], v[66:67], off nt
	global_load_dwordx4 v[122:125], v[68:69], off nt
	v_lshl_add_u64 v[66:67], v[68:69], 0, s[18:19]
	v_lshl_add_u64 v[68:69], v[66:67], 0, s[18:19]
	global_load_dwordx4 v[106:109], v[66:67], off nt
	global_load_dwordx4 v[110:113], v[68:69], off nt
	v_lshl_add_u64 v[66:67], v[68:69], 0, s[18:19]
	v_lshl_add_u64 v[68:69], v[66:67], 0, s[18:19]
	global_load_dwordx4 v[82:85], v[66:67], off nt
	global_load_dwordx4 v[86:89], v[68:69], off nt
	v_lshl_add_u64 v[66:67], v[68:69], 0, s[18:19]
	v_lshl_add_u64 v[68:69], v[66:67], 0, s[18:19]
	global_load_dwordx4 v[94:97], v[66:67], off nt
	global_load_dwordx4 v[98:101], v[68:69], off nt
	v_lshl_add_u64 v[66:67], v[68:69], 0, s[18:19]
	global_load_dwordx4 v[114:117], v[66:67], off nt
	v_lshl_add_u64 v[66:67], v[66:67], 0, s[18:19]
	global_load_dwordx4 v[126:129], v[66:67], off nt
	v_lshl_add_u64 v[66:67], v[66:67], 0, s[18:19]
	global_load_dwordx4 v[90:93], v[66:67], off nt
	v_lshl_add_u64 v[66:67], v[66:67], 0, s[18:19]
	global_load_dwordx4 v[102:105], v[66:67], off nt
	v_lshl_add_u64 v[70:71], v[66:67], 0, s[18:19]
	v_lshl_add_u64 v[210:211], v[70:71], 0, s[18:19]
	global_load_dwordx4 v[66:69], v[70:71], off nt
	s_waitcnt vmcnt(15)
	v_mul_f32_e32 v62, v62, v149
	global_load_dwordx4 v[70:73], v[210:211], off nt
	v_mul_f32_e32 v34, v34, v149
	v_mov_b32_e32 v198, 0
	v_cvt_pk_fp8_f32 v198, v62, v34
	v_mul_f32_e32 v22, v22, v149
	v_mul_f32_e32 v34, v54, v149
	v_mov_b32_e32 v199, 0
	v_cvt_pk_fp8_f32 v199, v22, v34
	v_mul_f32_e32 v6, v6, v149
	v_mul_f32_e32 v22, v38, v149
	v_mov_b32_e32 v200, 0
	v_cvt_pk_fp8_f32 v199, v6, v22 op_sel:[0,0,1]
	v_mul_f32_e32 v6, v10, v149
	v_mul_f32_e32 v10, v42, v149
	v_cvt_pk_fp8_f32 v200, v6, v10
	v_mul_f32_e32 v6, v14, v149
	v_mul_f32_e32 v10, v46, v149
	v_mov_b32_e32 v201, 0
	v_cvt_pk_fp8_f32 v201, v6, v10
	v_mul_f32_e32 v2, v2, v149
	v_mul_f32_e32 v6, v26, v149
	v_mov_b32_e32 v202, 0
	v_cvt_pk_fp8_f32 v201, v2, v6 op_sel:[0,0,1]
	v_mul_f32_e32 v2, v63, v149
	v_mul_f32_e32 v6, v35, v149
	v_cvt_pk_fp8_f32 v202, v2, v6
	v_mul_f32_e32 v2, v23, v149
	v_mul_f32_e32 v6, v55, v149
	v_mov_b32_e32 v203, 0
	v_cvt_pk_fp8_f32 v203, v2, v6
	v_mul_f32_e32 v2, v7, v149
	v_mul_f32_e32 v6, v39, v149
	v_mov_b32_e32 v204, 0
	v_cvt_pk_fp8_f32 v203, v2, v6 op_sel:[0,0,1]
	v_mul_f32_e32 v2, v11, v149
	v_mul_f32_e32 v6, v43, v149
	v_cvt_pk_fp8_f32 v204, v2, v6
	v_mul_f32_e32 v2, v15, v149
	v_mul_f32_e32 v6, v47, v149
	v_mov_b32_e32 v205, 0
	v_cvt_pk_fp8_f32 v205, v2, v6
	v_mul_f32_e32 v2, v3, v149
	v_mul_f32_e32 v3, v27, v149
	v_mov_b32_e32 v206, 0
	v_cvt_pk_fp8_f32 v205, v2, v3 op_sel:[0,0,1]
	v_mul_f32_e32 v2, v64, v149
	v_mul_f32_e32 v3, v36, v149
	v_cvt_pk_fp8_f32 v206, v2, v3
	v_mul_f32_e32 v2, v24, v149
	v_mul_f32_e32 v3, v56, v149
	v_mov_b32_e32 v207, 0
	v_cvt_pk_fp8_f32 v207, v2, v3
	v_mul_f32_e32 v2, v8, v149
	v_mul_f32_e32 v3, v40, v149
	v_mov_b32_e32 v208, 0
	v_cvt_pk_fp8_f32 v207, v2, v3 op_sel:[0,0,1]
	v_mul_f32_e32 v2, v12, v149
	v_mul_f32_e32 v3, v44, v149
	v_cvt_pk_fp8_f32 v208, v2, v3
	v_mul_f32_e32 v2, v16, v149
	v_mul_f32_e32 v3, v48, v149
	v_mov_b32_e32 v209, 0
	v_mul_f32_e32 v10, v31, v149
	v_mul_f32_e32 v14, v59, v149
	v_cvt_pk_fp8_f32 v209, v2, v3
	v_cvt_pk_fp8_f32 v202, v10, v14 op_sel:[0,0,1]
	v_mul_f32_e32 v7, v19, v149
	v_mul_f32_e32 v10, v51, v149
	v_cvt_pk_fp8_f32 v204, v7, v10 op_sel:[0,0,1]
	v_mul_f32_e32 v6, v32, v149
	v_mul_f32_e32 v7, v60, v149
	v_cvt_pk_fp8_f32 v206, v6, v7 op_sel:[0,0,1]
	v_mul_f32_e32 v6, v20, v149
	v_mul_f32_e32 v7, v52, v149
	v_mul_f32_e32 v2, v4, v149
	v_mul_f32_e32 v3, v28, v149
	v_cvt_pk_fp8_f32 v208, v6, v7 op_sel:[0,0,1]
	v_cvt_pk_fp8_f32 v209, v2, v3 op_sel:[0,0,1]
	v_mul_f32_e32 v2, v65, v149
	v_mul_f32_e32 v3, v37, v149
	v_mov_b32_e32 v6, 0
	v_cvt_pk_fp8_f32 v6, v2, v3
	v_mul_f32_e32 v2, v25, v149
	v_mul_f32_e32 v3, v57, v149
	v_mov_b32_e32 v7, 0
	v_cvt_pk_fp8_f32 v7, v2, v3
	v_mul_f32_e32 v4, v33, v149
	v_mul_f32_e32 v8, v61, v149
	v_mul_f32_e32 v2, v9, v149
	v_mul_f32_e32 v3, v41, v149
	v_cvt_pk_fp8_f32 v6, v4, v8 op_sel:[0,0,1]
	v_cvt_pk_fp8_f32 v7, v2, v3 op_sel:[0,0,1]
	v_mul_f32_e32 v2, v13, v149
	v_mul_f32_e32 v3, v45, v149
	v_mov_b32_e32 v8, 0
	v_cvt_pk_fp8_f32 v8, v2, v3
	v_mul_f32_e32 v2, v17, v149
	v_mul_f32_e32 v3, v49, v149
	v_mov_b32_e32 v9, 0
	v_mul_f32_e32 v30, v30, v149
	v_mul_f32_e32 v58, v58, v149
	v_mul_f32_e32 v18, v18, v149
	v_mul_f32_e32 v22, v50, v149
	v_cvt_pk_fp8_f32 v9, v2, v3
	v_cvt_pk_fp8_f32 v198, v30, v58 op_sel:[0,0,1]
	v_cvt_pk_fp8_f32 v200, v18, v22 op_sel:[0,0,1]
	v_mul_f32_e32 v4, v21, v149
	v_mul_f32_e32 v10, v53, v149
	v_mul_f32_e32 v2, v5, v149
	v_mul_f32_e32 v3, v29, v149
	v_cvt_pk_fp8_f32 v8, v4, v10 op_sel:[0,0,1]
	v_cvt_pk_fp8_f32 v9, v2, v3 op_sel:[0,0,1]
	ds_write_b128 v163, v[198:201]
	ds_write_b128 v163, v[202:205] offset:256
	ds_write_b128 v163, v[206:209] offset:512
	ds_write_b128 v163, v[6:9] offset:768
	s_waitcnt vmcnt(15)
	v_mul_f32_e32 v74, v149, v74
	s_waitcnt vmcnt(14)
	v_mul_f32_e32 v78, v149, v78
	v_mov_b32_e32 v198, 0
	v_cvt_pk_fp8_f32 v198, v74, v78
	s_waitcnt vmcnt(11)
	v_mul_f32_e32 v74, v149, v106
	s_waitcnt vmcnt(10)
	v_mul_f32_e32 v78, v149, v110
	v_mov_b32_e32 v199, 0
	v_cvt_pk_fp8_f32 v199, v74, v78
	s_waitcnt vmcnt(9)
; __device__ __forceinline__ unsigned pk4_fp8(float a, float b, float c, float d) { unsigned w = 0u; w = __builtin_amdgcn_cvt_pk_fp8_f32(a, b, w, false); w = __builtin_amdgcn_cvt_pk_fp8_f32(c, d, w, true); return w; }
; #define LAS __attribute__((address_space(3)))
; #define CVT_LOAD(v, c, s_) do { _Pragma("unroll") for (int i_ = 0; i_ < 16; ++i_) v[i_] = *(const f32x4*)((c).src + (size_t)(64 * (s_) + i_) * (c).N); } while (0)
; __device__ __forceinline__ void cvt_pack8(const f32x4 (&v)[16], const CvtItem& c, LAS unsigned char* blk, int s4, int lane) {
;     const float w = c.wscale; const int cb = lane & 15, j = 4 * s4 + (lane >> 4);
; #pragma unroll
;     for (int jn = 0; jn < 4; ++jn) {
;         v4u o; o.x = pg8::pk4_fp8(v[0][jn] * w, v[1][jn] * w, v[2][jn] * w, v[3][jn] * w); o.y = pg8::pk4_fp8(v[4][jn] * w, v[5][jn] * w, v[6][jn] * w, v[7][jn] * w);
;         o.z = pg8::pk4_fp8(v[8][jn] * w, v[9][jn] * w, v[10][jn] * w, v[11][jn] * w); o.w = pg8::pk4_fp8(v[12][jn] * w, v[13][jn] * w, v[14][jn] * w, v[15][jn] * w);
;         *(LAS v4u*)(blk + (4 * cb + jn) * 256 + ((j ^ cb) * 16)) = o; }
; }
; __device__ __forceinline__ void cvt_moe_pipe2(const CvtSrc& A, const CvtSrc& B, LAS float* scr, int gw, int NGW, int lane) {
;     ...
;     while (it < it1) {
;         const int i1 = it + NGW; const bool more = i1 < it1;
;         CVT_LOAD(vb, c, 1); cvt_pack8(va, c, blk, 0, lane);
;         CVT_LOAD(va, c, 2); cvt_pack8(vb, c, blk, 1, lane);
;         CVT_LOAD(vb, c, 3); cvt_pack8(va, c, blk, 2, lane);
;         if (more) { cn = cvt_moe_item2(i1, A, B, lane); CVT_LOAD(va, cn, 0); }
;         cvt_pack8(vb, c, blk, 3, lane);
	v_mul_f32_e32 v74, v149, v82
	s_waitcnt vmcnt(8)
	v_mul_f32_e32 v78, v149, v86
	v_mov_b32_e32 v200, 0
	v_cvt_pk_fp8_f32 v199, v74, v78 op_sel:[0,0,1]
	s_waitcnt vmcnt(7)
	v_mul_f32_e32 v74, v149, v94
	s_waitcnt vmcnt(6)
	v_mul_f32_e32 v78, v149, v98
	v_cvt_pk_fp8_f32 v200, v74, v78
	s_waitcnt vmcnt(3)
	v_mul_f32_e32 v74, v149, v90
	s_waitcnt vmcnt(2)
	v_mul_f32_e32 v78, v149, v102
	v_mov_b32_e32 v201, 0
	v_cvt_pk_fp8_f32 v201, v74, v78
	v_mad_i64_i32 v[2:3], s[20:21], s8, v144, v[210:211]
	global_load_dwordx4 v[62:65], v[2:3], off nt
	v_lshl_add_u64 v[2:3], v[2:3], 0, s[18:19]
	global_load_dwordx4 v[34:37], v[2:3], off nt
	v_lshl_add_u64 v[2:3], v[2:3], 0, s[18:19]
	s_waitcnt vmcnt(3)
	v_mul_f32_e32 v66, v149, v66
	s_waitcnt vmcnt(2)
	v_mul_f32_e32 v70, v149, v70
	global_load_dwordx4 v[30:33], v[2:3], off nt
	v_lshl_add_u64 v[2:3], v[2:3], 0, s[18:19]
	v_cvt_pk_fp8_f32 v201, v66, v70 op_sel:[0,0,1]
	v_mul_f32_e32 v66, v149, v75
	v_mul_f32_e32 v70, v149, v79
	v_mov_b32_e32 v202, 0
	global_load_dwordx4 v[58:61], v[2:3], off nt
	v_lshl_add_u64 v[2:3], v[2:3], 0, s[18:19]
	v_cvt_pk_fp8_f32 v202, v66, v70
	v_mul_f32_e32 v66, v149, v107
	v_mul_f32_e32 v70, v149, v111
	v_mov_b32_e32 v203, 0
	global_load_dwordx4 v[22:25], v[2:3], off nt
	v_lshl_add_u64 v[2:3], v[2:3], 0, s[18:19]
	v_cvt_pk_fp8_f32 v203, v66, v70
	global_load_dwordx4 v[54:57], v[2:3], off nt
	v_lshl_add_u64 v[2:3], v[2:3], 0, s[18:19]
	global_load_dwordx4 v[6:9], v[2:3], off nt
	v_lshl_add_u64 v[2:3], v[2:3], 0, s[18:19]
	global_load_dwordx4 v[38:41], v[2:3], off nt
	v_lshl_add_u64 v[2:3], v[2:3], 0, s[18:19]
	v_mul_f32_e32 v66, v149, v83
	v_mul_f32_e32 v70, v149, v87
	global_load_dwordx4 v[10:13], v[2:3], off nt
	v_lshl_add_u64 v[2:3], v[2:3], 0, s[18:19]
	v_cvt_pk_fp8_f32 v203, v66, v70 op_sel:[0,0,1]
	v_mul_f32_e32 v66, v149, v95
	v_mul_f32_e32 v70, v149, v99
	v_mov_b32_e32 v204, 0
	global_load_dwordx4 v[42:45], v[2:3], off nt
	v_lshl_add_u64 v[2:3], v[2:3], 0, s[18:19]
	v_cvt_pk_fp8_f32 v204, v66, v70
	v_mul_f32_e32 v66, v149, v91
	v_mul_f32_e32 v70, v149, v103
	v_mov_b32_e32 v205, 0
	global_load_dwordx4 v[18:21], v[2:3], off nt
	v_lshl_add_u64 v[2:3], v[2:3], 0, s[18:19]
	v_cvt_pk_fp8_f32 v205, v66, v70
	global_load_dwordx4 v[50:53], v[2:3], off nt
	v_lshl_add_u64 v[2:3], v[2:3], 0, s[18:19]
	global_load_dwordx4 v[14:17], v[2:3], off nt
	v_lshl_add_u64 v[2:3], v[2:3], 0, s[18:19]
	global_load_dwordx4 v[46:49], v[2:3], off nt
	v_mul_f32_e32 v66, v149, v67
	v_mul_f32_e32 v67, v149, v71
	v_cvt_pk_fp8_f32 v205, v66, v67 op_sel:[0,0,1]
	v_mul_f32_e32 v66, v149, v76
	v_mul_f32_e32 v67, v149, v80
	v_mov_b32_e32 v206, 0
	v_lshl_add_u64 v[26:27], v[2:3], 0, s[18:19]
	v_cvt_pk_fp8_f32 v206, v66, v67
	v_mul_f32_e32 v66, v149, v108
	v_mul_f32_e32 v67, v149, v112
	v_mov_b32_e32 v207, 0
	v_lshl_add_u64 v[210:211], v[26:27], 0, s[18:19]
	v_cvt_pk_fp8_f32 v207, v66, v67
	global_load_dwordx4 v[2:5], v[26:27], off nt
	v_mul_f32_e32 v66, v149, v84
	global_load_dwordx4 v[26:29], v[210:211], off nt
	v_mul_f32_e32 v67, v149, v88
	v_cvt_pk_fp8_f32 v207, v66, v67 op_sel:[0,0,1]
	v_mul_f32_e32 v66, v149, v96
	v_mul_f32_e32 v67, v149, v100
	v_mov_b32_e32 v208, 0
	v_cvt_pk_fp8_f32 v208, v66, v67
	v_mul_f32_e32 v66, v149, v92
	v_mul_f32_e32 v67, v149, v104
	v_mov_b32_e32 v209, 0
	v_cvt_pk_fp8_f32 v209, v66, v67
	v_mul_f32_e32 v74, v149, v119
	v_mul_f32_e32 v75, v149, v123
	v_cvt_pk_fp8_f32 v202, v74, v75 op_sel:[0,0,1]
	v_mul_f32_e32 v74, v149, v115
	v_mul_f32_e32 v75, v149, v127
	v_mul_f32_e32 v66, v149, v68
	v_mul_f32_e32 v67, v149, v72
	v_cvt_pk_fp8_f32 v204, v74, v75 op_sel:[0,0,1]
	v_cvt_pk_fp8_f32 v209, v66, v67 op_sel:[0,0,1]
	v_mul_f32_e32 v66, v149, v77
	v_mul_f32_e32 v67, v149, v81
	v_mov_b32_e32 v74, 0
	v_cvt_pk_fp8_f32 v74, v66, v67
	v_mul_f32_e32 v66, v149, v109
	v_mul_f32_e32 v67, v149, v113
	v_mov_b32_e32 v75, 0
	v_cvt_pk_fp8_f32 v75, v66, v67
	v_mul_f32_e32 v66, v149, v85
	v_mul_f32_e32 v67, v149, v89
	v_mov_b32_e32 v76, 0
	v_cvt_pk_fp8_f32 v75, v66, v67 op_sel:[0,0,1]
	v_mul_f32_e32 v66, v149, v97
	v_mul_f32_e32 v67, v149, v101
	v_cvt_pk_fp8_f32 v76, v66, v67
	v_mul_f32_e32 v66, v149, v93
	v_mul_f32_e32 v67, v149, v105
	v_mov_b32_e32 v77, 0
	v_mul_f32_e32 v118, v149, v118
	v_mul_f32_e32 v122, v149, v122
	v_mul_f32_e32 v82, v149, v114
	v_mul_f32_e32 v86, v149, v126
	v_mul_f32_e32 v70, v149, v120
	v_mul_f32_e32 v71, v149, v124
	v_cvt_pk_fp8_f32 v77, v66, v67
	v_cvt_pk_fp8_f32 v198, v118, v122 op_sel:[0,0,1]
	v_cvt_pk_fp8_f32 v200, v82, v86 op_sel:[0,0,1]
	v_cvt_pk_fp8_f32 v206, v70, v71 op_sel:[0,0,1]
	v_mul_f32_e32 v70, v149, v116
	v_mul_f32_e32 v71, v149, v128
	v_cvt_pk_fp8_f32 v208, v70, v71 op_sel:[0,0,1]
	v_mul_f32_e32 v68, v149, v121
	v_mul_f32_e32 v70, v149, v125
	v_cvt_pk_fp8_f32 v74, v68, v70 op_sel:[0,0,1]
	v_mul_f32_e32 v68, v149, v117
	v_mul_f32_e32 v70, v149, v129
	v_mul_f32_e32 v66, v149, v69
	v_mul_f32_e32 v67, v149, v73
	v_cvt_pk_fp8_f32 v76, v68, v70 op_sel:[0,0,1]
	v_cvt_pk_fp8_f32 v77, v66, v67 op_sel:[0,0,1]
	ds_write_b128 v164, v[198:201]
	ds_write_b128 v164, v[202:205] offset:256
	ds_write_b128 v164, v[206:209] offset:512
	ds_write_b128 v164, v[74:77] offset:768
	v_mad_i64_i32 v[66:67], s[20:21], s8, v144, v[210:211]
	global_load_dwordx4 v[102:105], v[66:67], off nt
	v_lshl_add_u64 v[66:67], v[66:67], 0, s[18:19]
	global_load_dwordx4 v[114:117], v[66:67], off nt
	v_lshl_add_u64 v[66:67], v[66:67], 0, s[18:19]
	global_load_dwordx4 v[122:125], v[66:67], off nt
	v_lshl_add_u64 v[66:67], v[66:67], 0, s[18:19]
	global_load_dwordx4 v[126:129], v[66:67], off nt
	v_lshl_add_u64 v[66:67], v[66:67], 0, s[18:19]
	global_load_dwordx4 v[106:109], v[66:67], off nt
	v_lshl_add_u64 v[66:67], v[66:67], 0, s[18:19]
	global_load_dwordx4 v[118:121], v[66:67], off nt
	v_lshl_add_u64 v[66:67], v[66:67], 0, s[18:19]
	global_load_dwordx4 v[74:77], v[66:67], off nt
	v_lshl_add_u64 v[66:67], v[66:67], 0, s[18:19]
	global_load_dwordx4 v[86:89], v[66:67], off nt
	v_lshl_add_u64 v[66:67], v[66:67], 0, s[18:19]
	global_load_dwordx4 v[78:81], v[66:67], off nt
	v_lshl_add_u64 v[66:67], v[66:67], 0, s[18:19]
	global_load_dwordx4 v[90:93], v[66:67], off nt
	v_lshl_add_u64 v[66:67], v[66:67], 0, s[18:19]
	global_load_dwordx4 v[98:101], v[66:67], off nt
	v_lshl_add_u64 v[66:67], v[66:67], 0, s[18:19]
	global_load_dwordx4 v[110:113], v[66:67], off nt
	v_lshl_add_u64 v[66:67], v[66:67], 0, s[18:19]
	global_load_dwordx4 v[82:85], v[66:67], off nt
	v_lshl_add_u64 v[66:67], v[66:67], 0, s[18:19]
	v_lshl_add_u64 v[70:71], v[66:67], 0, s[18:19]
	global_load_dwordx4 v[94:97], v[66:67], off nt
	s_waitcnt vmcnt(29)
; __device__ __forceinline__ unsigned pk4_fp8(float a, float b, float c, float d) { unsigned w = 0u; w = __builtin_amdgcn_cvt_pk_fp8_f32(a, b, w, false); w = __builtin_amdgcn_cvt_pk_fp8_f32(c, d, w, true); return w; }
; #define LAS __attribute__((address_space(3)))
; #define CVT_LOAD(v, c, s_) do { _Pragma("unroll") for (int i_ = 0; i_ < 16; ++i_) v[i_] = *(const f32x4*)((c).src + (size_t)(64 * (s_) + i_) * (c).N); } while (0)
; __device__ __forceinline__ void cvt_pack8(const f32x4 (&v)[16], const CvtItem& c, LAS unsigned char* blk, int s4, int lane) {
;     const float w = c.wscale; const int cb = lane & 15, j = 4 * s4 + (lane >> 4);
; #pragma unroll
;     for (int jn = 0; jn < 4; ++jn) {
;         v4u o; o.x = pg8::pk4_fp8(v[0][jn] * w, v[1][jn] * w, v[2][jn] * w, v[3][jn] * w); o.y = pg8::pk4_fp8(v[4][jn] * w, v[5][jn] * w, v[6][jn] * w, v[7][jn] * w);
;         o.z = pg8::pk4_fp8(v[8][jn] * w, v[9][jn] * w, v[10][jn] * w, v[11][jn] * w); o.w = pg8::pk4_fp8(v[12][jn] * w, v[13][jn] * w, v[14][jn] * w, v[15][jn] * w);
;         *(LAS v4u*)(blk + (4 * cb + jn) * 256 + ((j ^ cb) * 16)) = o; }
; }
; __device__ __forceinline__ void cvt_moe_pipe2(const CvtSrc& A, const CvtSrc& B, LAS float* scr, int gw, int NGW, int lane) {
;     ...
;     while (it < it1) {
;         const int i1 = it + NGW; const bool more = i1 < it1;
;         CVT_LOAD(vb, c, 1); cvt_pack8(va, c, blk, 0, lane);
;         CVT_LOAD(va, c, 2); cvt_pack8(vb, c, blk, 1, lane);
;         CVT_LOAD(vb, c, 3); cvt_pack8(va, c, blk, 2, lane);
;         if (more) { cn = cvt_moe_item2(i1, A, B, lane); CVT_LOAD(va, cn, 0); }
;         cvt_pack8(vb, c, blk, 3, lane);
	v_mul_f32_e32 v138, v149, v62
	global_load_dwordx4 v[66:69], v[70:71], off nt
	v_lshl_add_u64 v[70:71], v[70:71], 0, s[18:19]
	global_load_dwordx4 v[70:73], v[70:71], off nt
	s_waitcnt vmcnt(30)
	v_mul_f32_e32 v141, v149, v34
	v_mov_b32_e32 v198, 0
	v_cvt_pk_fp8_f32 v198, v138, v141
	s_waitcnt vmcnt(27)
	v_mul_f32_e32 v138, v149, v22
	s_waitcnt vmcnt(26)
	v_mul_f32_e32 v141, v149, v54
	v_mov_b32_e32 v199, 0
	v_cvt_pk_fp8_f32 v199, v138, v141
	v_mul_f32_e32 v200, v149, v30
	v_mul_f32_e32 v201, v149, v58
	s_waitcnt vmcnt(25)
	v_mul_f32_e32 v138, v149, v6
	s_waitcnt vmcnt(24)
	v_mul_f32_e32 v141, v149, v38
	v_cvt_pk_fp8_f32 v198, v200, v201 op_sel:[0,0,1]
	v_cvt_pk_fp8_f32 v199, v138, v141 op_sel:[0,0,1]
	s_waitcnt vmcnt(23)
	v_mul_f32_e32 v138, v149, v10
	s_waitcnt vmcnt(22)
	v_mul_f32_e32 v141, v149, v42
	v_mov_b32_e32 v200, 0
	v_cvt_pk_fp8_f32 v200, v138, v141
	s_waitcnt vmcnt(19)
	v_mul_f32_e32 v138, v149, v14
	s_waitcnt vmcnt(18)
	v_mul_f32_e32 v141, v149, v46
	v_mov_b32_e32 v201, 0
	v_cvt_pk_fp8_f32 v201, v138, v141
	v_mul_f32_e32 v202, v149, v18
	v_mul_f32_e32 v203, v149, v50
	s_waitcnt vmcnt(17)
	v_mul_f32_e32 v138, v149, v2
	s_waitcnt vmcnt(16)
	v_mul_f32_e32 v141, v149, v26
	v_cvt_pk_fp8_f32 v200, v202, v203 op_sel:[0,0,1]
	v_cvt_pk_fp8_f32 v201, v138, v141 op_sel:[0,0,1]
	v_mul_f32_e32 v138, v149, v63
	v_mul_f32_e32 v141, v149, v35
	v_mov_b32_e32 v202, 0
	v_cvt_pk_fp8_f32 v202, v138, v141
	v_mul_f32_e32 v138, v149, v23
	v_mul_f32_e32 v141, v149, v55
	v_mov_b32_e32 v203, 0
	v_cvt_pk_fp8_f32 v203, v138, v141
	v_mul_f32_e32 v204, v149, v31
	v_mul_f32_e32 v205, v149, v59
	v_mul_f32_e32 v138, v149, v7
	v_mul_f32_e32 v141, v149, v39
	v_cvt_pk_fp8_f32 v202, v204, v205 op_sel:[0,0,1]
	v_cvt_pk_fp8_f32 v203, v138, v141 op_sel:[0,0,1]
	v_mul_f32_e32 v138, v149, v11
	v_mul_f32_e32 v141, v149, v43
	v_mov_b32_e32 v204, 0
	v_cvt_pk_fp8_f32 v204, v138, v141
	v_mul_f32_e32 v138, v149, v15
	v_mul_f32_e32 v141, v149, v47
	v_mov_b32_e32 v205, 0
	v_cvt_pk_fp8_f32 v205, v138, v141
	v_mul_f32_e32 v206, v149, v19
	v_mul_f32_e32 v207, v149, v51
	v_mul_f32_e32 v138, v149, v3
	v_mul_f32_e32 v141, v149, v27
	v_cvt_pk_fp8_f32 v204, v206, v207 op_sel:[0,0,1]
	v_cvt_pk_fp8_f32 v205, v138, v141 op_sel:[0,0,1]
	v_mul_f32_e32 v138, v149, v64
	v_mul_f32_e32 v141, v149, v36
	v_mov_b32_e32 v206, 0
	v_cvt_pk_fp8_f32 v206, v138, v141
	v_mul_f32_e32 v138, v149, v24
	v_mul_f32_e32 v141, v149, v56
	v_mov_b32_e32 v207, 0
	v_cvt_pk_fp8_f32 v207, v138, v141
	v_mul_f32_e32 v208, v149, v32
	v_mul_f32_e32 v209, v149, v60
	v_mul_f32_e32 v138, v149, v8
	v_mul_f32_e32 v141, v149, v40
	v_cvt_pk_fp8_f32 v206, v208, v209 op_sel:[0,0,1]
	v_cvt_pk_fp8_f32 v207, v138, v141 op_sel:[0,0,1]
	v_mul_f32_e32 v138, v149, v12
	v_mul_f32_e32 v141, v149, v44
	v_mov_b32_e32 v208, 0
	v_cvt_pk_fp8_f32 v208, v138, v141
	v_mul_f32_e32 v138, v149, v16
	v_mul_f32_e32 v141, v149, v48
	v_mov_b32_e32 v209, 0
	v_cvt_pk_fp8_f32 v209, v138, v141
	v_mul_f32_e32 v210, v149, v20
	v_mul_f32_e32 v211, v149, v52
	v_mul_f32_e32 v138, v149, v4
	v_mul_f32_e32 v141, v149, v28
	v_cvt_pk_fp8_f32 v208, v210, v211 op_sel:[0,0,1]
	v_cvt_pk_fp8_f32 v209, v138, v141 op_sel:[0,0,1]
	v_mul_f32_e32 v138, v149, v65
	v_mul_f32_e32 v141, v149, v37
	v_mov_b32_e32 v210, 0
	v_cvt_pk_fp8_f32 v210, v138, v141
	v_mul_f32_e32 v138, v149, v25
	v_mul_f32_e32 v141, v149, v57
	v_mov_b32_e32 v211, 0
	v_cvt_pk_fp8_f32 v211, v138, v141
	v_mul_f32_e32 v212, v149, v33
	v_mul_f32_e32 v213, v149, v61
	v_mul_f32_e32 v138, v149, v9
	v_mul_f32_e32 v141, v149, v41
	v_cvt_pk_fp8_f32 v210, v212, v213 op_sel:[0,0,1]
	v_cvt_pk_fp8_f32 v211, v138, v141 op_sel:[0,0,1]
	v_mul_f32_e32 v138, v149, v13
	v_mul_f32_e32 v141, v149, v45
	v_mov_b32_e32 v212, 0
	v_cvt_pk_fp8_f32 v212, v138, v141
	v_mul_f32_e32 v138, v149, v17
	v_mul_f32_e32 v141, v149, v49
	v_mov_b32_e32 v213, 0
	v_readlane_b32 s2, v254, 52
	v_cvt_pk_fp8_f32 v213, v138, v141
	s_add_i32 s1, s1, s2
	s_cmpk_gt_i32 s1, 0x17ff
	s_cselect_b64 s[18:19], -1, 0
	v_mul_f32_e32 v214, v149, v21
	v_mul_f32_e32 v215, v149, v53
	v_mul_f32_e32 v138, v149, v5
	v_mul_f32_e32 v141, v149, v29
	v_cvt_pk_fp8_f32 v212, v214, v215 op_sel:[0,0,1]
	v_cvt_pk_fp8_f32 v213, v138, v141 op_sel:[0,0,1]
	s_and_b64 vcc, exec, s[18:19]
	ds_write_b128 v165, v[198:201]
	ds_write_b128 v165, v[202:205] offset:256
	ds_write_b128 v165, v[206:209] offset:512
	ds_write_b128 v165, v[210:213] offset:768
	s_cbranch_vccnz .LBB0_34
	s_ashr_i32 s0, s1, 11
	s_and_b32 s2, s1, 0x7f
	s_cmp_gt_i32 s0, 1
	s_mov_b64 s[8:9], -1
	s_cbranch_scc0 .LBB0_38
	v_readlane_b32 s20, v254, 2
	s_lshl_b32 s8, s2, 4
	v_readlane_b32 s21, v254, 3
	s_and_b32 s24, s1, 15
	s_and_b32 s26, s8, 0x700
	s_mov_b64 s[8:9], 0
	v_readlane_b32 s22, v254, 4
	v_readlane_b32 s23, v254, 5
	s_mov_b64 s[10:11], s[20:21]

; __device__ __forceinline__ void rms_row2_to_fp8(const float* xrow, const float* g, unsigned char* orow, int lane) {
;     const f32x4* xr = (const f32x4*)xrow + lane; const f32x4* gr = (const f32x4*)g + lane;
;     f32x4 v[2][4]; float s0 = 0.f, s1 = 0.f;
; #pragma unroll
;     for (int j = 0; j < 4; ++j) { v[0][j] = xr[64 * j]; v[1][j] = xr[256 + 64 * j]; }
; #pragma unroll
;     for (int j = 0; j < 4; ++j) { s0 += (v[0][j].x * v[0][j].x + v[0][j].y * v[0][j].y) + (v[0][j].z * v[0][j].z + v[0][j].w * v[0][j].w); s1 += (v[1][j].x * v[1][j].x + v[1][j].y * v[1][j].y) + (v[1][j].z * v[1][j].z + v[1][j].w * v[1][j].w); }
;     const float r0 = 1.0f / sqrtf(wave_sum(s0) * (1.f / DM) + RMS_EPS), r1 = 1.0f / sqrtf(wave_sum(s1) * (1.f / DM) + RMS_EPS);
.LBB0_49:
	global_load_dwordx4 v[14:17], v[26:27], off offset:-3072 nt
	global_load_dwordx4 v[10:13], v[26:27], off offset:-2048 nt
	global_load_dwordx4 v[6:9], v[26:27], off offset:-1024 nt
	global_load_dwordx4 v[2:5], v[26:27], off nt
	v_add_co_u32_e32 v18, vcc, 0xfffff000, v26
	global_load_dwordx4 v[36:39], v[22:23], off
	s_nop 0
	v_addc_co_u32_e32 v19, vcc, -1, v27, vcc
	global_load_dwordx4 v[40:43], v[18:19], off offset:-3072 nt
	global_load_dwordx4 v[44:47], v[18:19], off offset:-2048 nt
	global_load_dwordx4 v[48:51], v[18:19], off offset:-1024 nt
	s_nop 0
	global_load_dwordx4 v[18:21], v[26:27], off offset:-4096 nt
	v_mov_b32_e32 v35, 0
	v_mov_b32_e32 v52, 0
	s_add_i32 s8, s8, s10
	s_cmp_lt_i32 s8, 0x8000
	v_lshl_add_u64 v[26:27], v[26:27], 0, s[20:21]
	s_waitcnt vmcnt(8)
	v_mul_f32_e32 v53, v15, v15
	v_mul_f32_e32 v54, v17, v17
	s_waitcnt vmcnt(7)
	v_mul_f32_e32 v55, v11, v11
	v_mul_f32_e32 v56, v13, v13
	s_waitcnt vmcnt(6)
	v_mul_f32_e32 v57, v7, v7
	v_mul_f32_e32 v58, v9, v9
	v_fmac_f32_e32 v53, v14, v14
	v_fmac_f32_e32 v54, v16, v16
	v_fmac_f32_e32 v55, v10, v10
	v_fmac_f32_e32 v56, v12, v12
	s_waitcnt vmcnt(5)
	v_mul_f32_e32 v59, v3, v3
	v_mul_f32_e32 v60, v5, v5
	v_fmac_f32_e32 v57, v6, v6
	v_fmac_f32_e32 v58, v8, v8
	s_waitcnt vmcnt(3)
	v_mul_f32_e32 v61, v41, v41
	v_mul_f32_e32 v62, v43, v43
	v_add_f32_e32 v53, v53, v54
	s_waitcnt vmcnt(2)
	v_mul_f32_e32 v54, v45, v45
	v_mul_f32_e32 v63, v47, v47
	v_add_f32_e32 v55, v55, v56
	v_fmac_f32_e32 v59, v2, v2
	v_fmac_f32_e32 v60, v4, v4
	s_waitcnt vmcnt(1)
	v_mul_f32_e32 v56, v49, v49
	v_mul_f32_e32 v64, v51, v51
	v_add_f32_e32 v57, v57, v58
	v_fmac_f32_e32 v61, v40, v40
	v_fmac_f32_e32 v62, v42, v42
	v_fmac_f32_e32 v54, v44, v44
	v_fmac_f32_e32 v63, v46, v46
	v_add_f32_e32 v53, v53, v55
	s_waitcnt vmcnt(0)
	v_mul_f32_e32 v58, v19, v19
	v_mul_f32_e32 v65, v21, v21
	v_add_f32_e32 v59, v59, v60
	v_fmac_f32_e32 v56, v48, v48
	v_fmac_f32_e32 v64, v50, v50
	v_add_f32_e32 v55, v61, v62
	v_add_f32_e32 v54, v54, v63
	v_add_f32_e32 v53, v53, v57
	v_fmac_f32_e32 v58, v18, v18
	v_fmac_f32_e32 v65, v20, v20
	v_add_f32_e32 v56, v56, v64
	v_add_f32_e32 v54, v55, v54
	v_add_f32_e32 v53, v53, v59
	v_add_f32_e32 v57, v58, v65
	v_add_f32_e32 v54, v54, v56
	ds_bpermute_b32 v55, v1, v53
	v_add_f32_e32 v54, v54, v57
	ds_bpermute_b32 v56, v1, v54
	s_waitcnt lgkmcnt(1)
	v_add_f32_e32 v53, v53, v55
	ds_bpermute_b32 v55, v28, v53
	s_waitcnt lgkmcnt(1)
	v_add_f32_e32 v54, v54, v56
	ds_bpermute_b32 v56, v28, v54
	s_waitcnt lgkmcnt(1)
	v_add_f32_e32 v53, v53, v55
	ds_bpermute_b32 v55, v29, v53
	s_waitcnt lgkmcnt(1)
	v_add_f32_e32 v54, v54, v56
	ds_bpermute_b32 v56, v29, v54
	s_waitcnt lgkmcnt(1)
	v_add_f32_e32 v53, v53, v55
	ds_bpermute_b32 v55, v30, v53
	s_waitcnt lgkmcnt(1)
	v_add_f32_e32 v54, v54, v56
	ds_bpermute_b32 v56, v30, v54
	s_waitcnt lgkmcnt(1)
	v_add_f32_e32 v53, v53, v55
	ds_bpermute_b32 v55, v31, v53
	s_waitcnt lgkmcnt(1)
	v_add_f32_e32 v54, v54, v56
	ds_bpermute_b32 v56, v31, v54
	s_waitcnt lgkmcnt(1)
	v_add_f32_e32 v53, v53, v55
	ds_bpermute_b32 v55, v32, v53
	s_waitcnt lgkmcnt(1)
	v_add_f32_e32 v54, v54, v56
	ds_bpermute_b32 v56, v32, v54
	s_waitcnt lgkmcnt(1)
	v_add_f32_e32 v53, v53, v55
	v_fmamk_f32 v53, v53, 0x3a800000, v33
	s_waitcnt lgkmcnt(0)
; __device__ __forceinline__ unsigned pk4_fp8(float a, float b, float c, float d) { unsigned w = 0u; w = __builtin_amdgcn_cvt_pk_fp8_f32(a, b, w, false); w = __builtin_amdgcn_cvt_pk_fp8_f32(c, d, w, true); return w; }
; __device__ __forceinline__ void rms_row2_to_fp8(const float* xrow, const float* g, unsigned char* orow, int lane) {
;     ...
;     const float r0 = 1.0f / sqrtf(wave_sum(s0) * (1.f / DM) + RMS_EPS), r1 = 1.0f / sqrtf(wave_sum(s1) * (1.f / DM) + RMS_EPS);
;     unsigned* o4 = (unsigned*)orow + lane;
; #pragma unroll
;     for (int j = 0; j < 4; ++j) { const f32x4 gg = gr[64 * j];
;         o4[64 * j] = pg8::pk4_fp8(v[0][j].x * r0 * gg.x, v[0][j].y * r0 * gg.y, v[0][j].z * r0 * gg.z, v[0][j].w * r0 * gg.w);
;         o4[256 + 64 * j] = pg8::pk4_fp8(v[1][j].x * r1 * gg.x, v[1][j].y * r1 * gg.y, v[1][j].z * r1 * gg.z, v[1][j].w * r1 * gg.w); }
; }
	v_add_f32_e32 v54, v54, v56
	v_mul_f32_e32 v55, 0x4f800000, v53
	v_cmp_gt_f32_e32 vcc, s0, v53
	v_fmamk_f32 v54, v54, 0x3a800000, v33
	v_cmp_gt_f32_e64 s[2:3], s0, v54
	v_cndmask_b32_e32 v53, v53, v55, vcc
	v_mul_f32_e32 v55, 0x4f800000, v54
	v_sqrt_f32_e32 v56, v53
	v_cndmask_b32_e64 v54, v54, v55, s[2:3]
	v_sqrt_f32_e32 v55, v54
	v_add_u32_e32 v57, -1, v56
	v_add_u32_e32 v58, 1, v56
	v_fma_f32 v59, -v57, v56, v53
	v_fma_f32 v60, -v58, v56, v53
	v_add_u32_e32 v61, -1, v55
	v_cmp_ge_f32_e64 s[4:5], 0, v59
	v_add_u32_e32 v62, 1, v55
	v_fma_f32 v59, -v62, v55, v54
	v_cndmask_b32_e64 v56, v56, v57, s[4:5]
	v_cmp_lt_f32_e64 s[4:5], 0, v60
	v_fma_f32 v57, -v61, v55, v54
	s_nop 0
	v_cndmask_b32_e64 v56, v56, v58, s[4:5]
	v_cmp_ge_f32_e64 s[4:5], 0, v57
	v_mul_f32_e32 v57, 0x37800000, v56
	v_cndmask_b32_e32 v56, v56, v57, vcc
	v_cndmask_b32_e64 v55, v55, v61, s[4:5]
	v_cmp_lt_f32_e64 s[4:5], 0, v59
	v_cmp_class_f32_e32 vcc, v53, v34
	s_nop 0
	v_cndmask_b32_e64 v55, v55, v62, s[4:5]
	v_mul_f32_e32 v57, 0x37800000, v55
	v_cndmask_b32_e32 v53, v56, v53, vcc
	v_cndmask_b32_e64 v55, v55, v57, s[2:3]
	v_cmp_class_f32_e32 vcc, v54, v34
	v_div_scale_f32 v56, s[2:3], v53, v53, 1.0
	s_nop 0
	v_cndmask_b32_e32 v54, v55, v54, vcc
	v_rcp_f32_e32 v55, v56
	v_div_scale_f32 v58, s[4:5], v54, v54, 1.0
	v_rcp_f32_e32 v60, v58
	v_fma_f32 v61, -v56, v55, 1.0
	v_div_scale_f32 v57, s[2:3], 1.0, v53, 1.0
	v_fmac_f32_e32 v55, v61, v55
	v_fma_f32 v61, -v58, v60, 1.0
	v_div_scale_f32 v59, vcc, 1.0, v54, 1.0
	v_mul_f32_e32 v62, v57, v55
	v_fmac_f32_e32 v60, v61, v60
	v_fma_f32 v61, -v56, v62, v57
	v_mul_f32_e32 v63, v59, v60
	v_fmac_f32_e32 v62, v61, v55
	v_fma_f32 v61, -v58, v63, v59
	v_fmac_f32_e32 v63, v61, v60
	v_fma_f32 v56, -v56, v62, v57
	v_fma_f32 v57, -v58, v63, v59
	v_div_fmas_f32 v57, v57, v60, v63
	s_mov_b64 vcc, s[2:3]
	v_div_fixup_f32 v54, v57, v54, 1.0
	v_div_fmas_f32 v55, v56, v55, v62
	v_div_fixup_f32 v53, v55, v53, 1.0
	v_mul_f32_e32 v40, v40, v54
	v_mul_f32_e32 v41, v41, v54
	v_mul_f32_e32 v40, v40, v36
	v_mul_f32_e32 v41, v41, v37
	v_mul_f32_e32 v14, v14, v53
	v_mul_f32_e32 v15, v15, v53
	v_cvt_pk_fp8_f32 v35, v40, v41
	v_mul_f32_e32 v14, v36, v14
	v_mul_f32_e32 v15, v37, v15
	v_cvt_pk_fp8_f32 v52, v14, v15
	v_mul_f32_e32 v42, v42, v54
	v_mul_f32_e32 v43, v43, v54
	v_mul_f32_e32 v42, v42, v38
	v_mul_f32_e32 v43, v43, v39
	v_mul_f32_e32 v16, v16, v53
	v_mul_f32_e32 v17, v17, v53
	v_mul_f32_e32 v16, v38, v16
	v_mul_f32_e32 v17, v39, v17
	v_cvt_pk_fp8_f32 v35, v42, v43 op_sel:[0,0,1]
	v_cvt_pk_fp8_f32 v52, v16, v17 op_sel:[0,0,1]
	global_store_dword v[24:25], v35, off offset:-1792
	global_store_dword v[24:25], v52, off offset:-768
	global_load_dwordx4 v[14:17], v[22:23], off offset:1024
	v_mul_f32_e32 v37, v44, v54
	v_mul_f32_e32 v38, v45, v54
	v_mov_b32_e32 v35, 0
	v_mul_f32_e32 v10, v10, v53
	v_mul_f32_e32 v11, v11, v53
	v_mov_b32_e32 v36, 0
	v_mul_f32_e32 v39, v46, v54
	v_mul_f32_e32 v40, v47, v54
	v_mul_f32_e32 v12, v12, v53
	v_mul_f32_e32 v13, v13, v53
	v_mul_f32_e32 v6, v6, v53
	v_mul_f32_e32 v7, v7, v53
	v_mul_f32_e32 v8, v8, v53
	v_mul_f32_e32 v9, v9, v53
	v_mul_f32_e32 v2, v2, v53
	v_mul_f32_e32 v3, v3, v53
	v_mul_f32_e32 v4, v4, v53
	v_mul_f32_e32 v5, v5, v53
	s_waitcnt vmcnt(0)
	v_mul_f32_e32 v37, v37, v14
	v_mul_f32_e32 v38, v38, v15
	v_mul_f32_e32 v10, v10, v14
	v_mul_f32_e32 v11, v11, v15
	v_cvt_pk_fp8_f32 v35, v37, v38
	v_cvt_pk_fp8_f32 v36, v10, v11
	v_mul_f32_e32 v39, v39, v16
	v_mul_f32_e32 v40, v40, v17
	v_mul_f32_e32 v12, v12, v16
	v_mul_f32_e32 v13, v13, v17
	v_cvt_pk_fp8_f32 v35, v39, v40 op_sel:[0,0,1]
	v_cvt_pk_fp8_f32 v36, v12, v13 op_sel:[0,0,1]
	global_store_dword v[24:25], v35, off offset:-1536
	global_store_dword v[24:25], v36, off offset:-512
	global_load_dwordx4 v[10:13], v[22:23], off offset:2048
	v_mul_f32_e32 v16, v48, v54
	v_mul_f32_e32 v17, v49, v54
	v_mov_b32_e32 v14, 0
	v_mov_b32_e32 v15, 0
	v_mul_f32_e32 v35, v50, v54
	v_mul_f32_e32 v36, v51, v54
	s_waitcnt vmcnt(0)
	v_mul_f32_e32 v16, v16, v10
	v_mul_f32_e32 v17, v17, v11
	v_mul_f32_e32 v6, v6, v10
	v_mul_f32_e32 v7, v7, v11
	v_cvt_pk_fp8_f32 v14, v16, v17
	v_cvt_pk_fp8_f32 v15, v6, v7
	v_mul_f32_e32 v35, v35, v12
	v_mul_f32_e32 v36, v36, v13
	v_mul_f32_e32 v8, v8, v12
	v_mul_f32_e32 v9, v9, v13
	v_cvt_pk_fp8_f32 v14, v35, v36 op_sel:[0,0,1]
	v_cvt_pk_fp8_f32 v15, v8, v9 op_sel:[0,0,1]
	global_store_dword v[24:25], v14, off offset:-1280
	global_store_dword v[24:25], v15, off offset:-256
	global_load_dwordx4 v[6:9], v[22:23], off offset:3072
	v_mul_f32_e32 v12, v18, v54
	v_mul_f32_e32 v13, v19, v54
	v_mov_b32_e32 v10, 0
	v_mov_b32_e32 v11, 0
	v_mul_f32_e32 v14, v20, v54
	v_mul_f32_e32 v15, v21, v54
	s_waitcnt vmcnt(0)
	v_mul_f32_e32 v12, v12, v6
	v_mul_f32_e32 v13, v13, v7
	v_mul_f32_e32 v2, v2, v6
	v_mul_f32_e32 v3, v3, v7
	v_cvt_pk_fp8_f32 v10, v12, v13
	v_cvt_pk_fp8_f32 v11, v2, v3
	v_mul_f32_e32 v14, v14, v8
	v_mul_f32_e32 v15, v15, v9
	v_mul_f32_e32 v4, v4, v8
	v_mul_f32_e32 v2, v5, v9
	v_cvt_pk_fp8_f32 v10, v14, v15 op_sel:[0,0,1]
	v_cvt_pk_fp8_f32 v11, v4, v2 op_sel:[0,0,1]
	global_store_dword v[24:25], v10, off offset:-1024
	global_store_dword v[24:25], v11, off
	v_lshl_add_u64 v[24:25], v[24:25], 0, s[18:19]
	s_cbranch_scc1 .LBB0_49

; #define LAS __attribute__((address_space(3)))
; #define CVT_LOAD(v, c, s_) do { _Pragma("unroll") for (int i_ = 0; i_ < 16; ++i_) v[i_] = *(const f32x4*)((c).src + (size_t)(64 * (s_) + i_) * (c).N); } while (0)
; __device__ __forceinline__ CvtItem cvt_moe_item(int it, const float* wg, const float* wu, const float* wd, unsigned char* WGU, unsigned char* WDN, int lane) {
;     const int which = it >> 11, r = it & 2047, e = r >> 7, q = r & 127; CvtItem c; c.which = which;
;     if (which < 2) { const int nb = q & 31, k0 = (q >> 5) * 256; c.nb = nb;
;         c.N = DFF; c.K = DM; c.wscale = which ? 64.f / LOG2E : 64.f * LOG2E; c.src = (which ? wu : wg) + (size_t)e * DM * DFF + (size_t)(k0 + 16 * (lane >> 4)) * DFF + nb * 64 + 4 * (lane & 15);
;         c.dst = WGU + (size_t)e * 4096 * DM + k0; }
;     else { const int nb = q & 15, k0 = (q >> 4) * 256; c.nb = nb;
;         c.N = DM; c.K = DFF; c.wscale = 64.f; c.src = wd + (size_t)e * DFF * DM + (size_t)(k0 + 16 * (lane >> 4)) * DM + nb * 64 + 4 * (lane & 15);
;         c.dst = WDN + (size_t)e * DM * DFF + k0; }
;     return c;
; }
; __device__ __forceinline__ CvtItem cvt_moe_item2(int j, const CvtSrc& A, const CvtSrc& B, int lane) {
;     return (j < A.n) ? cvt_moe_item(A.it0 + j, A.wg, A.wu, A.wd, A.WGU, A.WDN, lane) : cvt_moe_item(B.it0 + (j - A.n), B.wg, B.wu, B.wd, B.WGU, B.WDN, lane);
; }
; __device__ __forceinline__ void cvt_moe_pipe2(const CvtSrc& A, const CvtSrc& B, LAS float* scr, int gw, int NGW, int lane) {
;     LAS unsigned char* blk = (LAS unsigned char*)scr;
;     f32x4 va[16], vb[16]; CvtItem c, cn;
;     const int it1 = A.n + B.n; int it = gw;
;     if (it < it1) { c = cvt_moe_item2(it, A, B, lane); CVT_LOAD(va, c, 0); }
.LBB0_106:
	s_bfe_u32 s8, s18, 0x40007
	s_mov_b32 s9, 0
	s_lshl_b32 s38, s0, 3
	s_lshl_b64 s[10:11], s[8:9], s10
	s_add_u32 s0, s24, s10
	s_addc_u32 s11, s25, s11
	s_add_u32 s10, s0, s1
	s_addc_u32 s11, s11, 0
	s_lshl_b32 s0, s8, 23
	v_and_b32_e32 v1, 48, v66
	s_add_u32 s18, s22, s0
	v_or_b32_e32 v2, s1, v1
	s_addc_u32 s19, s23, 0
	v_lshlrev_b32_e32 v130, s5, v2
	v_mov_b32_e32 v131, 0
	v_lshlrev_b32_e32 v4, 2, v66
	v_lshl_add_u64 v[2:3], v[130:131], 2, s[18:19]
	s_lshl_b32 s8, s39, 6
	v_and_b32_e32 v68, 60, v4
	v_lshl_add_u64 v[2:3], s[8:9], 2, v[2:3]
	v_lshlrev_b32_e32 v130, 2, v68
	v_lshl_add_u64 v[136:137], v[2:3], 0, v[130:131]
	s_mul_i32 s8, s4, 15
	v_lshl_add_u64 v[2:3], s[8:9], 2, v[136:137]
	s_mul_i32 s8, s4, 14
	v_lshl_add_u64 v[4:5], s[8:9], 2, v[136:137]
	s_mul_i32 s8, s4, 13
	global_load_dwordx4 v[18:21], v[2:3], off nt
	global_load_dwordx4 v[6:9], v[4:5], off nt
	v_lshl_add_u64 v[2:3], s[8:9], 2, v[136:137]
	s_mul_i32 s8, s4, 12
	v_lshl_add_u64 v[4:5], s[8:9], 2, v[136:137]
	s_mul_i32 s8, s4, 11
	v_lshl_add_u64 v[10:11], s[8:9], 2, v[136:137]
	s_mul_i32 s8, s4, 10
	v_lshl_add_u64 v[12:13], s[8:9], 2, v[136:137]
	s_mul_i32 s8, s4, 9
	global_load_dwordx4 v[22:25], v[2:3], off nt
	s_nop 0
	global_load_dwordx4 v[2:5], v[4:5], off nt
	s_nop 0
	global_load_dwordx4 v[30:33], v[10:11], off nt
	global_load_dwordx4 v[14:17], v[12:13], off nt
	v_lshl_add_u64 v[10:11], s[8:9], 2, v[136:137]
	s_lshl_b32 s8, s4, 3
	v_lshl_add_u64 v[12:13], s[8:9], 2, v[136:137]
	s_mul_i32 s8, s4, 7
	v_lshl_add_u64 v[34:35], s[8:9], 2, v[136:137]
	s_mul_i32 s8, s4, 6
	v_lshl_add_u64 v[36:37], s[8:9], 2, v[136:137]
	s_mul_i32 s8, s4, 5
	global_load_dwordx4 v[26:29], v[10:11], off nt
	s_nop 0
	global_load_dwordx4 v[10:13], v[12:13], off nt
	s_nop 0
	global_load_dwordx4 v[54:57], v[34:35], off nt
	global_load_dwordx4 v[38:41], v[36:37], off nt
	v_lshl_add_u64 v[34:35], s[8:9], 2, v[136:137]
	s_lshl_b32 s8, s4, 2
	v_lshl_add_u64 v[36:37], s[8:9], 2, v[136:137]
	s_mul_i32 s8, s4, 3
	v_lshl_add_u64 v[42:43], s[8:9], 2, v[136:137]
	s_lshl_b32 s8, s4, 1
	s_mov_b32 s5, s9
	v_lshl_add_u64 v[44:45], s[8:9], 2, v[136:137]
	v_lshl_add_u64 v[46:47], s[4:5], 2, v[136:137]
	global_load_dwordx4 v[50:53], v[34:35], off nt
	s_nop 0
	global_load_dwordx4 v[34:37], v[36:37], off nt
	s_nop 0
	global_load_dwordx4 v[58:61], v[42:43], off nt
	s_nop 0
	global_load_dwordx4 v[42:45], v[44:45], off nt
	s_nop 0
	global_load_dwordx4 v[46:49], v[46:47], off nt
	s_nop 0
	global_load_dwordx4 v[62:65], v[136:137], off nt
	v_bfe_u32 v140, v66, 4, 2
	v_and_b32_e32 v67, 15, v66
	v_lshrrev_b32_e32 v69, 4, v66
	v_readlane_b32 s0, v254, 60
	v_or_b32_e32 v141, 4, v140
	v_or_b32_e32 v142, 8, v140
	v_or_b32_e32 v143, 12, v140
	v_or_b32_e32 v144, 16, v140
	v_or_b32_e32 v145, 20, v140
	v_or_b32_e32 v146, 24, v140
	v_or_b32_e32 v147, 28, v140
	v_or_b32_e32 v148, 32, v140
	v_or_b32_e32 v149, 36, v140
	v_or_b32_e32 v150, 40, v140
	v_or_b32_e32 v151, 44, v140
	v_or_b32_e32 v152, 48, v140
	v_or_b32_e32 v153, 52, v140
	v_or_b32_e32 v154, 56, v140
	v_or_b32_e32 v155, 60, v140
	v_lshl_add_u32 v66, v67, 10, s0
	v_bitop3_b32 v69, v69, v67, 3 bitop3:0x6c
	v_bitop3_b32 v70, v140, v67, 4 bitop3:0x36
	v_bitop3_b32 v71, v140, v67, 8 bitop3:0x36
	v_bitop3_b32 v72, v140, v67, 12 bitop3:0x36
	v_lshlrev_b32_e32 v132, 4, v67
	v_lshl_add_u32 v67, v140, 8, s0
	v_lshl_add_u32 v73, v141, 8, s0
	v_lshl_add_u32 v75, v142, 8, s0
	v_lshl_add_u32 v77, v143, 8, s0
	v_lshl_add_u32 v79, v144, 8, s0
	v_lshl_add_u32 v81, v145, 8, s0
	v_lshl_add_u32 v83, v146, 8, s0
	v_lshl_add_u32 v85, v147, 8, s0
	v_lshl_add_u32 v87, v148, 8, s0
	v_lshl_add_u32 v89, v149, 8, s0
	v_lshl_add_u32 v91, v150, 8, s0
	v_lshl_add_u32 v93, v151, 8, s0
	v_lshl_add_u32 v95, v152, 8, s0
	v_lshl_add_u32 v97, v153, 8, s0
	v_lshl_add_u32 v99, v154, 8, s0
	v_lshl_add_u32 v101, v155, 8, s0
	v_readlane_b32 s0, v254, 52
	s_add_i32 s0, s36, s0
	s_lshl_b32 s1, s74, 3
	s_sub_i32 s0, s0, s1
	v_readlane_b32 s8, v254, 9
	s_addk_i32 s0, 0xf220
	s_lshl_b32 s1, s8, 7
	s_lshl_b32 s5, s74, 7
	v_lshlrev_b32_e32 v69, 4, v69
	v_lshlrev_b32_e32 v70, 4, v70
	v_lshlrev_b32_e32 v71, 4, v71
	v_lshlrev_b32_e32 v72, 4, v72
	v_xor_b32_e32 v74, 16, v132
	v_xor_b32_e32 v76, 32, v132
	v_xor_b32_e32 v78, 48, v132
	v_xor_b32_e32 v80, 64, v132
	v_xor_b32_e32 v82, 0x50, v132
	v_xor_b32_e32 v84, 0x60, v132
	v_xor_b32_e32 v86, 0x70, v132
	v_xor_b32_e32 v88, 0x80, v132
	v_xor_b32_e32 v90, 0x90, v132
	v_xor_b32_e32 v92, 0xa0, v132
	v_xor_b32_e32 v94, 0xb0, v132
	v_xor_b32_e32 v96, 0xc0, v132
	v_xor_b32_e32 v98, 0xd0, v132
	v_xor_b32_e32 v100, 0xe0, v132
	v_xor_b32_e32 v102, 0xf0, v132
	s_lshl_b32 s41, s0, 4
	s_sub_i32 s42, s1, s5
	s_lshl_b32 s43, s0, 3
	s_lshl_b32 s0, s8, 6
	s_lshl_b32 s1, s74, 6
	v_mov_b32_e32 v133, v131
	s_sub_i32 s44, s0, s1
	v_add_u32_e32 v156, v66, v69
	v_add_u32_e32 v157, v66, v70
	v_add_u32_e32 v158, v66, v71
	v_lshlrev_b32_e32 v134, 2, v68
	v_add_u32_e32 v159, v66, v72
	v_add_u32_e32 v160, v67, v132
	v_add_u32_e32 v161, v73, v74
	v_add_u32_e32 v162, v75, v76
	v_add_u32_e32 v163, v77, v78
	v_add_u32_e32 v164, v79, v80
	v_add_u32_e32 v165, v81, v82
	v_add_u32_e32 v166, v83, v84
	v_add_u32_e32 v167, v85, v86
	v_add_u32_e32 v168, v87, v88
	v_add_u32_e32 v169, v89, v90
	v_add_u32_e32 v170, v91, v92
	v_add_u32_e32 v171, v93, v94
	v_add_u32_e32 v172, v95, v96
	v_add_u32_e32 v173, v97, v98
	v_add_u32_e32 v174, v99, v100
	v_add_u32_e32 v175, v101, v102
	v_mov_b32_e32 v176, 0xc4
	v_mov_b32_e32 v177, 0x42317218
	v_mov_b32_e32 v178, 0x42b8aa3b
	v_mov_b32_e32 v179, 0x43
	v_mov_b32_e32 v180, 0x47
	v_mov_b32_e32 v181, 0x4b
	v_mov_b32_e32 v182, 0x4f
	v_mov_b32_e32 v183, 0x53
	v_mov_b32_e32 v184, 0x57
	v_mov_b32_e32 v185, 0x5b
	v_mov_b32_e32 v186, 0x5f
	v_mov_b32_e32 v187, 0x63
	v_mov_b32_e32 v188, 0x67
	v_mov_b32_e32 v189, 0x6b
	v_mov_b32_e32 v190, 0x6f
	v_mov_b32_e32 v191, 0x73
	v_mov_b32_e32 v192, 0x77
	v_mov_b32_e32 v193, 0x7b
	v_mov_b32_e32 v194, 0x7f
	s_branch .LBB0_111

; #define LAS __attribute__((address_space(3)))
; #define CVT_LOAD(v, c, s_) do { _Pragma("unroll") for (int i_ = 0; i_ < 16; ++i_) v[i_] = *(const f32x4*)((c).src + (size_t)(64 * (s_) + i_) * (c).N); } while (0)
; __device__ __forceinline__ CvtItem cvt_moe_item(int it, const float* wg, const float* wu, const float* wd, unsigned char* WGU, unsigned char* WDN, int lane) {
;     const int which = it >> 11, r = it & 2047, e = r >> 7, q = r & 127; CvtItem c; c.which = which;
;     if (which < 2) { const int nb = q & 31, k0 = (q >> 5) * 256; c.nb = nb;
;         c.N = DFF; c.K = DM; c.wscale = which ? 64.f / LOG2E : 64.f * LOG2E; c.src = (which ? wu : wg) + (size_t)e * DM * DFF + (size_t)(k0 + 16 * (lane >> 4)) * DFF + nb * 64 + 4 * (lane & 15);
;         c.dst = WGU + (size_t)e * 4096 * DM + k0; }
;     else { const int nb = q & 15, k0 = (q >> 4) * 256; c.nb = nb;
;         c.N = DM; c.K = DFF; c.wscale = 64.f; c.src = wd + (size_t)e * DFF * DM + (size_t)(k0 + 16 * (lane >> 4)) * DM + nb * 64 + 4 * (lane & 15);
;         c.dst = WDN + (size_t)e * DM * DFF + k0; }
;     return c;
; }
; __device__ __forceinline__ CvtItem cvt_moe_item2(int j, const CvtSrc& A, const CvtSrc& B, int lane) {
;     return (j < A.n) ? cvt_moe_item(A.it0 + j, A.wg, A.wu, A.wd, A.WGU, A.WDN, lane) : cvt_moe_item(B.it0 + (j - A.n), B.wg, B.wu, B.wd, B.WGU, B.WDN, lane);
; }
; __device__ __forceinline__ void cvt_moe_pipe2(const CvtSrc& A, const CvtSrc& B, LAS float* scr, int gw, int NGW, int lane) {
;     LAS unsigned char* blk = (LAS unsigned char*)scr;
;     f32x4 va[16], vb[16]; CvtItem c, cn;
;     const int it1 = A.n + B.n; int it = gw;
;     if (it < it1) { c = cvt_moe_item2(it, A, B, lane); CVT_LOAD(va, c, 0); }
;     while (it < it1) {
;         const int i1 = it + NGW; const bool more = i1 < it1;
;         CVT_LOAD(vb, c, 1); cvt_pack8(va, c, blk, 0, lane);
;         CVT_LOAD(va, c, 2); cvt_pack8(vb, c, blk, 1, lane);
;         CVT_LOAD(vb, c, 3); cvt_pack8(va, c, blk, 2, lane);
;         if (more) { cn = cvt_moe_item2(i1, A, B, lane); CVT_LOAD(va, cn, 0); }
.LBB0_109:
	s_bfe_u32 s8, s8, 0x40007
	s_lshl_b32 s5, s8, 23
	s_add_u32 s18, s26, s5
	v_or_b32_e32 v2, s0, v1
	s_addc_u32 s19, s27, 0
	v_lshlrev_b32_e32 v130, s1, v2
	v_lshl_add_u64 v[2:3], v[130:131], 2, s[18:19]
	s_lshl_b32 s18, s45, 6
	s_mov_b32 s19, s9
	v_lshl_add_u64 v[2:3], s[18:19], 2, v[2:3]
	v_mov_b32_e32 v135, v131
	v_lshl_add_u64 v[136:137], v[2:3], 0, v[134:135]
	s_lshl_b64 s[18:19], s[8:9], s28
	s_mov_b32 s5, s9
	s_lshl_b32 s8, s4, 1
	v_lshl_add_u64 v[2:3], s[4:5], 2, v[136:137]
	v_lshl_add_u64 v[4:5], s[8:9], 2, v[136:137]
	s_mul_i32 s8, s4, 3
	global_load_dwordx4 v[46:49], v[2:3], off nt
	global_load_dwordx4 v[42:45], v[4:5], off nt
	v_lshl_add_u64 v[2:3], s[8:9], 2, v[136:137]
	s_lshl_b32 s8, s4, 2
	v_lshl_add_u64 v[4:5], s[8:9], 2, v[136:137]
	s_mul_i32 s8, s4, 5
	global_load_dwordx4 v[58:61], v[2:3], off nt
	global_load_dwordx4 v[34:37], v[4:5], off nt
	v_lshl_add_u64 v[2:3], s[8:9], 2, v[136:137]
	s_mul_i32 s8, s4, 6
	v_lshl_add_u64 v[4:5], s[8:9], 2, v[136:137]
	s_mul_i32 s8, s4, 7
	global_load_dwordx4 v[50:53], v[2:3], off nt
	global_load_dwordx4 v[38:41], v[4:5], off nt
	v_lshl_add_u64 v[2:3], s[8:9], 2, v[136:137]
	s_lshl_b32 s8, s4, 3
	v_lshl_add_u64 v[4:5], s[8:9], 2, v[136:137]
	s_mul_i32 s8, s4, 9
	global_load_dwordx4 v[54:57], v[2:3], off nt
	global_load_dwordx4 v[10:13], v[4:5], off nt
	v_lshl_add_u64 v[2:3], s[8:9], 2, v[136:137]
	s_mul_i32 s8, s4, 10
	v_lshl_add_u64 v[4:5], s[8:9], 2, v[136:137]
	s_mul_i32 s8, s4, 11
	global_load_dwordx4 v[26:29], v[2:3], off nt
	global_load_dwordx4 v[14:17], v[4:5], off nt
	v_lshl_add_u64 v[2:3], s[8:9], 2, v[136:137]
	s_mul_i32 s8, s4, 12
	v_lshl_add_u64 v[4:5], s[8:9], 2, v[136:137]
	s_mul_i32 s8, s4, 13
	v_lshl_add_u64 v[6:7], s[8:9], 2, v[136:137]
	s_mul_i32 s8, s4, 14
	v_lshl_add_u64 v[8:9], s[8:9], 2, v[136:137]
	s_mul_i32 s8, s4, 15
	v_lshl_add_u64 v[18:19], s[8:9], 2, v[136:137]
	global_load_dwordx4 v[30:33], v[2:3], off nt
	s_nop 0
	global_load_dwordx4 v[2:5], v[4:5], off nt
	s_nop 0
	global_load_dwordx4 v[22:25], v[6:7], off nt
	s_nop 0
	global_load_dwordx4 v[6:9], v[8:9], off nt
	s_nop 0
	global_load_dwordx4 v[62:65], v[136:137], off nt
	s_nop 0
	global_load_dwordx4 v[18:21], v[18:19], off nt
	s_add_u32 s1, s22, s18
	s_addc_u32 s5, s23, s19
	s_add_u32 s22, s1, s0
	s_addc_u32 s23, s5, 0

; __device__ __forceinline__ unsigned pk4_fp8(float a, float b, float c, float d) { unsigned w = 0u; w = __builtin_amdgcn_cvt_pk_fp8_f32(a, b, w, false); w = __builtin_amdgcn_cvt_pk_fp8_f32(c, d, w, true); return w; }
; #define LAS __attribute__((address_space(3)))
; #define CVT_LOAD(v, c, s_) do { _Pragma("unroll") for (int i_ = 0; i_ < 16; ++i_) v[i_] = *(const f32x4*)((c).src + (size_t)(64 * (s_) + i_) * (c).N); } while (0)
; __device__ __forceinline__ void cvt_pack8(const f32x4 (&v)[16], const CvtItem& c, LAS unsigned char* blk, int s4, int lane) {
;     const float w = c.wscale; const int cb = lane & 15, j = 4 * s4 + (lane >> 4);
; #pragma unroll
;     for (int jn = 0; jn < 4; ++jn) {
;         v4u o; o.x = pg8::pk4_fp8(v[0][jn] * w, v[1][jn] * w, v[2][jn] * w, v[3][jn] * w); o.y = pg8::pk4_fp8(v[4][jn] * w, v[5][jn] * w, v[6][jn] * w, v[7][jn] * w);
;         o.z = pg8::pk4_fp8(v[8][jn] * w, v[9][jn] * w, v[10][jn] * w, v[11][jn] * w); o.w = pg8::pk4_fp8(v[12][jn] * w, v[13][jn] * w, v[14][jn] * w, v[15][jn] * w);
;         *(LAS v4u*)(blk + (4 * cb + jn) * 256 + ((j ^ cb) * 16)) = o; }
; }
; __device__ __forceinline__ void cvt_moe_pipe2(const CvtSrc& A, const CvtSrc& B, LAS float* scr, int gw, int NGW, int lane) {
;     ...
;     while (it < it1) {
;         const int i1 = it + NGW; const bool more = i1 < it1;
;         CVT_LOAD(vb, c, 1); cvt_pack8(va, c, blk, 0, lane);
;         CVT_LOAD(va, c, 2); cvt_pack8(vb, c, blk, 1, lane);
;         CVT_LOAD(vb, c, 3); cvt_pack8(va, c, blk, 2, lane);
;         if (more) { cn = cvt_moe_item2(i1, A, B, lane); CVT_LOAD(va, cn, 0); }
;         cvt_pack8(vb, c, blk, 3, lane);
.LBB0_111:
	s_ashr_i32 s5, s4, 31
	s_lshl_b64 s[0:1], s[4:5], 8
	v_lshl_add_u64 v[66:67], v[136:137], 0, s[0:1]
	s_lshl_b64 s[24:25], s[4:5], 2
	global_load_dwordx4 v[70:73], v[66:67], off nt
	v_lshl_add_u64 v[66:67], v[66:67], 0, s[24:25]
	global_load_dwordx4 v[98:101], v[66:67], off nt
	v_lshl_add_u64 v[66:67], v[66:67], 0, s[24:25]
	global_load_dwordx4 v[110:113], v[66:67], off nt
	v_lshl_add_u64 v[66:67], v[66:67], 0, s[24:25]
	global_load_dwordx4 v[118:121], v[66:67], off nt
	v_lshl_add_u64 v[66:67], v[66:67], 0, s[24:25]
	global_load_dwordx4 v[102:105], v[66:67], off nt
	v_lshl_add_u64 v[66:67], v[66:67], 0, s[24:25]
	global_load_dwordx4 v[114:117], v[66:67], off nt
	v_lshl_add_u64 v[66:67], v[66:67], 0, s[24:25]
	global_load_dwordx4 v[122:125], v[66:67], off nt
	v_lshl_add_u64 v[66:67], v[66:67], 0, s[24:25]
	v_lshl_add_u64 v[74:75], v[66:67], 0, s[24:25]
	global_load_dwordx4 v[126:129], v[66:67], off nt
	s_waitcnt vmcnt(8)
	v_mul_f32_e32 v62, v62, v195
	global_load_dwordx4 v[66:69], v[74:75], off nt
	v_lshl_add_u64 v[74:75], v[74:75], 0, s[24:25]
	global_load_dwordx4 v[90:93], v[74:75], off nt
	v_lshl_add_u64 v[74:75], v[74:75], 0, s[24:25]
	global_load_dwordx4 v[94:97], v[74:75], off nt
	v_lshl_add_u64 v[74:75], v[74:75], 0, s[24:25]
	v_lshl_add_u64 v[78:79], v[74:75], 0, s[24:25]
	v_lshl_add_u64 v[82:83], v[78:79], 0, s[24:25]
	global_load_dwordx4 v[106:109], v[74:75], off nt
	v_lshl_add_u64 v[86:87], v[82:83], 0, s[24:25]
	global_load_dwordx4 v[74:77], v[78:79], off nt
	v_lshl_add_u64 v[138:139], v[86:87], 0, s[24:25]
	global_load_dwordx4 v[78:81], v[82:83], off nt
	v_mul_f32_e32 v46, v46, v195
	global_load_dwordx4 v[82:85], v[86:87], off nt
	v_mov_b32_e32 v198, 0
	global_load_dwordx4 v[86:89], v[138:139], off nt
	v_cvt_pk_fp8_f32 v198, v62, v46
	v_mul_f32_e32 v42, v42, v195
	v_mul_f32_e32 v58, v58, v195
	v_mul_f32_e32 v10, v10, v195
	v_mul_f32_e32 v26, v26, v195
	v_mov_b32_e32 v200, 0
	v_cvt_pk_fp8_f32 v198, v42, v58 op_sel:[0,0,1]
	v_mul_f32_e32 v34, v34, v195
	v_mul_f32_e32 v42, v50, v195
	v_mov_b32_e32 v199, 0
	v_cvt_pk_fp8_f32 v200, v10, v26
	v_mul_f32_e32 v2, v2, v195
	v_mul_f32_e32 v10, v22, v195
	v_mov_b32_e32 v201, 0
	v_cvt_pk_fp8_f32 v199, v34, v42
	v_cvt_pk_fp8_f32 v201, v2, v10
	v_mul_f32_e32 v14, v14, v195
	v_mul_f32_e32 v30, v30, v195
	v_mul_f32_e32 v38, v38, v195
	v_mul_f32_e32 v46, v54, v195
	v_cvt_pk_fp8_f32 v200, v14, v30 op_sel:[0,0,1]
	v_mul_f32_e32 v6, v6, v195
	v_mul_f32_e32 v14, v18, v195
	v_cvt_pk_fp8_f32 v199, v38, v46 op_sel:[0,0,1]
	v_cvt_pk_fp8_f32 v201, v6, v14 op_sel:[0,0,1]
	v_mul_f32_e32 v2, v63, v195
	v_mul_f32_e32 v6, v47, v195
	v_mul_f32_e32 v10, v43, v195
	ds_write_b128 v156, v[198:201]
	v_mov_b32_e32 v198, 0
	v_cvt_pk_fp8_f32 v198, v2, v6
	v_mul_f32_e32 v2, v35, v195
	v_mul_f32_e32 v6, v51, v195
	v_mov_b32_e32 v199, 0
	v_cvt_pk_fp8_f32 v199, v2, v6
	v_mul_f32_e32 v2, v11, v195
	v_mul_f32_e32 v6, v27, v195
	v_mov_b32_e32 v200, 0
	v_cvt_pk_fp8_f32 v200, v2, v6
	v_mul_f32_e32 v2, v3, v195
	v_mul_f32_e32 v3, v23, v195
	v_mov_b32_e32 v201, 0
	v_cvt_pk_fp8_f32 v201, v2, v3
	v_mul_f32_e32 v14, v59, v195
	v_cvt_pk_fp8_f32 v198, v10, v14 op_sel:[0,0,1]
	v_mul_f32_e32 v10, v39, v195
	v_mul_f32_e32 v14, v55, v195
	v_cvt_pk_fp8_f32 v199, v10, v14 op_sel:[0,0,1]
	v_mul_f32_e32 v10, v15, v195
	v_mul_f32_e32 v11, v31, v195
	v_mul_f32_e32 v6, v7, v195
	v_mul_f32_e32 v7, v19, v195
	v_cvt_pk_fp8_f32 v200, v10, v11 op_sel:[0,0,1]
	v_cvt_pk_fp8_f32 v201, v6, v7 op_sel:[0,0,1]
	v_mul_f32_e32 v2, v64, v195
	v_mul_f32_e32 v3, v48, v195
	v_mul_f32_e32 v6, v44, v195
	ds_write_b128 v156, v[198:201] offset:256
	v_mov_b32_e32 v198, 0
	v_cvt_pk_fp8_f32 v198, v2, v3
	v_mul_f32_e32 v2, v36, v195
	v_mul_f32_e32 v3, v52, v195
	v_mov_b32_e32 v199, 0
	v_cvt_pk_fp8_f32 v199, v2, v3
	v_mul_f32_e32 v2, v12, v195
	v_mul_f32_e32 v3, v28, v195
	v_mov_b32_e32 v200, 0
	v_cvt_pk_fp8_f32 v200, v2, v3
	v_mul_f32_e32 v2, v4, v195
	v_mul_f32_e32 v3, v24, v195
	v_mov_b32_e32 v201, 0
	v_mul_f32_e32 v7, v60, v195
	v_cvt_pk_fp8_f32 v201, v2, v3
	v_cvt_pk_fp8_f32 v198, v6, v7 op_sel:[0,0,1]
	v_mul_f32_e32 v6, v40, v195
	v_mul_f32_e32 v7, v56, v195
	v_cvt_pk_fp8_f32 v199, v6, v7 op_sel:[0,0,1]
	v_mul_f32_e32 v6, v16, v195
	v_mul_f32_e32 v7, v32, v195
	v_cvt_pk_fp8_f32 v200, v6, v7 op_sel:[0,0,1]
	v_mul_f32_e32 v4, v8, v195
	v_mul_f32_e32 v6, v20, v195
	v_cvt_pk_fp8_f32 v201, v4, v6 op_sel:[0,0,1]
	v_mul_f32_e32 v3, v65, v195
	v_mul_f32_e32 v4, v49, v195
	v_mov_b32_e32 v2, 0
	v_cvt_pk_fp8_f32 v2, v3, v4
	v_mul_f32_e32 v6, v45, v195
	v_mul_f32_e32 v7, v61, v195
	v_mul_f32_e32 v4, v37, v195
	v_cvt_pk_fp8_f32 v2, v6, v7 op_sel:[0,0,1]
	v_mul_f32_e32 v6, v53, v195
	v_mov_b32_e32 v3, 0
	v_cvt_pk_fp8_f32 v3, v4, v6
	v_mul_f32_e32 v7, v41, v195
	v_mul_f32_e32 v8, v57, v195
	v_mul_f32_e32 v6, v13, v195
	v_cvt_pk_fp8_f32 v3, v7, v8 op_sel:[0,0,1]
	v_mul_f32_e32 v7, v29, v195
	v_mov_b32_e32 v4, 0
	ds_write_b128 v156, v[198:201] offset:512
	v_cvt_pk_fp8_f32 v4, v6, v7
	v_mul_f32_e32 v6, v5, v195
	v_mul_f32_e32 v7, v25, v195
	v_mov_b32_e32 v5, 0
	s_waitcnt vmcnt(15)
	v_mul_f32_e32 v70, v195, v70
	s_waitcnt vmcnt(14)
	v_mul_f32_e32 v98, v195, v98
	v_mov_b32_e32 v198, 0
	v_cvt_pk_fp8_f32 v5, v6, v7
	v_cvt_pk_fp8_f32 v198, v70, v98
	s_waitcnt vmcnt(11)
	v_mul_f32_e32 v70, v195, v102
	s_waitcnt vmcnt(10)
	v_mul_f32_e32 v98, v195, v114
	v_mov_b32_e32 v199, 0
	v_cvt_pk_fp8_f32 v199, v70, v98
	s_waitcnt vmcnt(7)
	v_mul_f32_e32 v66, v195, v66
	s_waitcnt vmcnt(6)
	v_mul_f32_e32 v70, v195, v90
	v_mov_b32_e32 v200, 0
	v_mul_f32_e32 v8, v17, v195
	v_mul_f32_e32 v10, v33, v195
	v_cvt_pk_fp8_f32 v200, v66, v70
	s_waitcnt vmcnt(3)
	v_mul_f32_e32 v66, v195, v74
	s_waitcnt vmcnt(2)
; __device__ __forceinline__ unsigned pk4_fp8(float a, float b, float c, float d) { unsigned w = 0u; w = __builtin_amdgcn_cvt_pk_fp8_f32(a, b, w, false); w = __builtin_amdgcn_cvt_pk_fp8_f32(c, d, w, true); return w; }
; #define LAS __attribute__((address_space(3)))
; #define CVT_LOAD(v, c, s_) do { _Pragma("unroll") for (int i_ = 0; i_ < 16; ++i_) v[i_] = *(const f32x4*)((c).src + (size_t)(64 * (s_) + i_) * (c).N); } while (0)
; __device__ __forceinline__ void cvt_pack8(const f32x4 (&v)[16], const CvtItem& c, LAS unsigned char* blk, int s4, int lane) {
;     const float w = c.wscale; const int cb = lane & 15, j = 4 * s4 + (lane >> 4);
; #pragma unroll
;     for (int jn = 0; jn < 4; ++jn) {
;         v4u o; o.x = pg8::pk4_fp8(v[0][jn] * w, v[1][jn] * w, v[2][jn] * w, v[3][jn] * w); o.y = pg8::pk4_fp8(v[4][jn] * w, v[5][jn] * w, v[6][jn] * w, v[7][jn] * w);
;         o.z = pg8::pk4_fp8(v[8][jn] * w, v[9][jn] * w, v[10][jn] * w, v[11][jn] * w); o.w = pg8::pk4_fp8(v[12][jn] * w, v[13][jn] * w, v[14][jn] * w, v[15][jn] * w);
;         *(LAS v4u*)(blk + (4 * cb + jn) * 256 + ((j ^ cb) * 16)) = o; }
; }
; __device__ __forceinline__ void cvt_moe_pipe2(const CvtSrc& A, const CvtSrc& B, LAS float* scr, int gw, int NGW, int lane) {
;     ...
;     while (it < it1) {
;         const int i1 = it + NGW; const bool more = i1 < it1;
;         CVT_LOAD(vb, c, 1); cvt_pack8(va, c, blk, 0, lane);
;         CVT_LOAD(va, c, 2); cvt_pack8(vb, c, blk, 1, lane);
;         CVT_LOAD(vb, c, 3); cvt_pack8(va, c, blk, 2, lane);
;         if (more) { cn = cvt_moe_item2(i1, A, B, lane); CVT_LOAD(va, cn, 0); }
;         cvt_pack8(vb, c, blk, 3, lane);
	v_mul_f32_e32 v70, v195, v78
	v_mov_b32_e32 v201, 0
	v_cvt_pk_fp8_f32 v4, v8, v10 op_sel:[0,0,1]
	v_mul_f32_e32 v8, v9, v195
	v_mul_f32_e32 v9, v21, v195
	v_cvt_pk_fp8_f32 v201, v66, v70
	v_cvt_pk_fp8_f32 v5, v8, v9 op_sel:[0,0,1]
	v_mul_f32_e32 v110, v195, v110
	v_mul_f32_e32 v118, v195, v118
	v_cvt_pk_fp8_f32 v198, v110, v118 op_sel:[0,0,1]
	v_mul_f32_e32 v102, v195, v122
	v_mul_f32_e32 v110, v195, v126
	v_mul_f32_e32 v90, v195, v94
	v_mul_f32_e32 v94, v195, v106
	s_waitcnt vmcnt(1)
	v_mul_f32_e32 v74, v195, v82
	s_waitcnt vmcnt(0)
	v_mul_f32_e32 v78, v195, v86
	v_cvt_pk_fp8_f32 v199, v102, v110 op_sel:[0,0,1]
	v_cvt_pk_fp8_f32 v200, v90, v94 op_sel:[0,0,1]
	v_cvt_pk_fp8_f32 v201, v74, v78 op_sel:[0,0,1]
	ds_write_b128 v156, v[2:5] offset:768
	v_mad_i64_i32 v[2:3], s[0:1], s4, v176, v[138:139]
	global_load_dwordx4 v[62:65], v[2:3], off nt
	v_lshl_add_u64 v[2:3], v[2:3], 0, s[24:25]
	global_load_dwordx4 v[46:49], v[2:3], off nt
	v_lshl_add_u64 v[2:3], v[2:3], 0, s[24:25]
	global_load_dwordx4 v[42:45], v[2:3], off nt
	v_lshl_add_u64 v[2:3], v[2:3], 0, s[24:25]
	ds_write_b128 v157, v[198:201]
	v_mul_f32_e32 v66, v195, v71
	v_mul_f32_e32 v70, v195, v99
	v_mov_b32_e32 v198, 0
	global_load_dwordx4 v[58:61], v[2:3], off nt
	v_lshl_add_u64 v[2:3], v[2:3], 0, s[24:25]
	v_cvt_pk_fp8_f32 v198, v66, v70
	v_mul_f32_e32 v66, v195, v103
	v_mul_f32_e32 v70, v195, v115
	v_mov_b32_e32 v199, 0
	global_load_dwordx4 v[34:37], v[2:3], off nt
	v_lshl_add_u64 v[2:3], v[2:3], 0, s[24:25]
	v_cvt_pk_fp8_f32 v199, v66, v70
	v_mul_f32_e32 v66, v195, v67
	v_mul_f32_e32 v67, v195, v91
	v_mov_b32_e32 v200, 0
	global_load_dwordx4 v[50:53], v[2:3], off nt
	v_lshl_add_u64 v[2:3], v[2:3], 0, s[24:25]
	v_cvt_pk_fp8_f32 v200, v66, v67
	v_mul_f32_e32 v66, v195, v75
	v_mul_f32_e32 v67, v195, v79
	v_mov_b32_e32 v201, 0
	global_load_dwordx4 v[38:41], v[2:3], off nt
	v_lshl_add_u64 v[2:3], v[2:3], 0, s[24:25]
	v_mul_f32_e32 v71, v195, v111
	v_mul_f32_e32 v74, v195, v119
	v_cvt_pk_fp8_f32 v201, v66, v67
	global_load_dwordx4 v[54:57], v[2:3], off nt
	v_lshl_add_u64 v[2:3], v[2:3], 0, s[24:25]
	v_cvt_pk_fp8_f32 v198, v71, v74 op_sel:[0,0,1]
	v_mul_f32_e32 v71, v195, v123
	v_mul_f32_e32 v74, v195, v127
	global_load_dwordx4 v[10:13], v[2:3], off nt
	v_lshl_add_u64 v[2:3], v[2:3], 0, s[24:25]
	v_cvt_pk_fp8_f32 v199, v71, v74 op_sel:[0,0,1]
	v_mul_f32_e32 v70, v195, v95
	v_mul_f32_e32 v71, v195, v107
	global_load_dwordx4 v[26:29], v[2:3], off nt
	v_lshl_add_u64 v[2:3], v[2:3], 0, s[24:25]
	v_cvt_pk_fp8_f32 v200, v70, v71 op_sel:[0,0,1]
	v_mul_f32_e32 v70, v195, v83
	v_mul_f32_e32 v71, v195, v87
	global_load_dwordx4 v[14:17], v[2:3], off nt
	v_lshl_add_u64 v[2:3], v[2:3], 0, s[24:25]
	v_cvt_pk_fp8_f32 v201, v70, v71 op_sel:[0,0,1]
	v_lshl_add_u64 v[6:7], v[2:3], 0, s[24:25]
	global_load_dwordx4 v[30:33], v[2:3], off nt
	v_mul_f32_e32 v66, v195, v72
	global_load_dwordx4 v[2:5], v[6:7], off nt
	v_lshl_add_u64 v[6:7], v[6:7], 0, s[24:25]
	global_load_dwordx4 v[22:25], v[6:7], off nt
	ds_write_b128 v157, v[198:201] offset:256
	v_mul_f32_e32 v67, v195, v100
	v_mov_b32_e32 v198, 0
	v_lshl_add_u64 v[18:19], v[6:7], 0, s[24:25]
	v_cvt_pk_fp8_f32 v198, v66, v67
	v_mul_f32_e32 v66, v195, v104
	v_mul_f32_e32 v67, v195, v116
	v_mov_b32_e32 v199, 0
	v_lshl_add_u64 v[138:139], v[18:19], 0, s[24:25]
	v_cvt_pk_fp8_f32 v199, v66, v67
	v_mul_f32_e32 v66, v195, v68
	v_mul_f32_e32 v67, v195, v92
	v_mov_b32_e32 v200, 0
	global_load_dwordx4 v[6:9], v[18:19], off nt
	v_cvt_pk_fp8_f32 v200, v66, v67
	global_load_dwordx4 v[18:21], v[138:139], off nt
	v_mul_f32_e32 v66, v195, v76
	v_mul_f32_e32 v67, v195, v80
	v_mov_b32_e32 v201, 0
	v_mul_f32_e32 v70, v195, v112
	v_mul_f32_e32 v71, v195, v120
	v_cvt_pk_fp8_f32 v201, v66, v67
	v_cvt_pk_fp8_f32 v198, v70, v71 op_sel:[0,0,1]
	v_mul_f32_e32 v70, v195, v124
	v_mul_f32_e32 v71, v195, v128
	v_cvt_pk_fp8_f32 v199, v70, v71 op_sel:[0,0,1]
	v_mul_f32_e32 v68, v195, v96
	v_mul_f32_e32 v70, v195, v108
	v_cvt_pk_fp8_f32 v200, v68, v70 op_sel:[0,0,1]
	v_mul_f32_e32 v68, v195, v84
	v_mul_f32_e32 v70, v195, v88
	v_cvt_pk_fp8_f32 v201, v68, v70 op_sel:[0,0,1]
	v_mul_f32_e32 v67, v195, v73
	v_mul_f32_e32 v68, v195, v101
	v_mov_b32_e32 v66, 0
	v_cvt_pk_fp8_f32 v66, v67, v68
	v_mul_f32_e32 v70, v195, v113
	v_mul_f32_e32 v71, v195, v121
	v_mul_f32_e32 v68, v195, v105
	v_cvt_pk_fp8_f32 v66, v70, v71 op_sel:[0,0,1]
	v_mul_f32_e32 v70, v195, v117
	v_mov_b32_e32 v67, 0
	v_cvt_pk_fp8_f32 v67, v68, v70
	v_mul_f32_e32 v69, v195, v69
	v_mul_f32_e32 v70, v195, v93
	v_mov_b32_e32 v68, 0
	v_cvt_pk_fp8_f32 v68, v69, v70
	v_mul_f32_e32 v71, v195, v125
	v_mul_f32_e32 v72, v195, v129
	v_cvt_pk_fp8_f32 v67, v71, v72 op_sel:[0,0,1]
	v_mul_f32_e32 v71, v195, v97
	v_mul_f32_e32 v72, v195, v109
	v_cvt_pk_fp8_f32 v68, v71, v72 op_sel:[0,0,1]
	v_mul_f32_e32 v70, v195, v77
	v_mul_f32_e32 v71, v195, v81
	v_mov_b32_e32 v69, 0
	v_cvt_pk_fp8_f32 v69, v70, v71
	v_mul_f32_e32 v72, v195, v85
	v_mul_f32_e32 v73, v195, v89
	ds_write_b128 v157, v[198:201] offset:512
	v_cvt_pk_fp8_f32 v69, v72, v73 op_sel:[0,0,1]
	s_waitcnt vmcnt(15)
	v_mul_f32_e32 v130, v195, v62
	s_waitcnt vmcnt(14)
; __device__ __forceinline__ unsigned pk4_fp8(float a, float b, float c, float d) { unsigned w = 0u; w = __builtin_amdgcn_cvt_pk_fp8_f32(a, b, w, false); w = __builtin_amdgcn_cvt_pk_fp8_f32(c, d, w, true); return w; }
; #define LAS __attribute__((address_space(3)))
; #define CVT_LOAD(v, c, s_) do { _Pragma("unroll") for (int i_ = 0; i_ < 16; ++i_) v[i_] = *(const f32x4*)((c).src + (size_t)(64 * (s_) + i_) * (c).N); } while (0)
; __device__ __forceinline__ void cvt_pack8(const f32x4 (&v)[16], const CvtItem& c, LAS unsigned char* blk, int s4, int lane) {
;     const float w = c.wscale; const int cb = lane & 15, j = 4 * s4 + (lane >> 4);
; #pragma unroll
;     for (int jn = 0; jn < 4; ++jn) {
;         v4u o; o.x = pg8::pk4_fp8(v[0][jn] * w, v[1][jn] * w, v[2][jn] * w, v[3][jn] * w); o.y = pg8::pk4_fp8(v[4][jn] * w, v[5][jn] * w, v[6][jn] * w, v[7][jn] * w);
;         o.z = pg8::pk4_fp8(v[8][jn] * w, v[9][jn] * w, v[10][jn] * w, v[11][jn] * w); o.w = pg8::pk4_fp8(v[12][jn] * w, v[13][jn] * w, v[14][jn] * w, v[15][jn] * w);
;         *(LAS v4u*)(blk + (4 * cb + jn) * 256 + ((j ^ cb) * 16)) = o; }
; }
; __device__ __forceinline__ void cvt_moe_pipe2(const CvtSrc& A, const CvtSrc& B, LAS float* scr, int gw, int NGW, int lane) {
;     ...
;     while (it < it1) {
;         const int i1 = it + NGW; const bool more = i1 < it1;
;         CVT_LOAD(vb, c, 1); cvt_pack8(va, c, blk, 0, lane);
;         CVT_LOAD(va, c, 2); cvt_pack8(vb, c, blk, 1, lane);
;         CVT_LOAD(vb, c, 3); cvt_pack8(va, c, blk, 2, lane);
;         if (more) { cn = cvt_moe_item2(i1, A, B, lane); CVT_LOAD(va, cn, 0); }
	v_mul_f32_e32 v135, v195, v46
	v_mov_b32_e32 v198, 0
	ds_write_b128 v157, v[66:69] offset:768
	v_mad_i64_i32 v[66:67], s[0:1], s4, v176, v[138:139]
	global_load_dwordx4 v[110:113], v[66:67], off nt
	v_lshl_add_u64 v[66:67], v[66:67], 0, s[24:25]
	global_load_dwordx4 v[118:121], v[66:67], off nt
	v_lshl_add_u64 v[66:67], v[66:67], 0, s[24:25]
	global_load_dwordx4 v[122:125], v[66:67], off nt
	v_lshl_add_u64 v[66:67], v[66:67], 0, s[24:25]
	global_load_dwordx4 v[126:129], v[66:67], off nt
	v_lshl_add_u64 v[66:67], v[66:67], 0, s[24:25]
	global_load_dwordx4 v[98:101], v[66:67], off nt
	v_lshl_add_u64 v[66:67], v[66:67], 0, s[24:25]
	global_load_dwordx4 v[102:105], v[66:67], off nt
	v_lshl_add_u64 v[66:67], v[66:67], 0, s[24:25]
	global_load_dwordx4 v[106:109], v[66:67], off nt
	v_lshl_add_u64 v[66:67], v[66:67], 0, s[24:25]
	global_load_dwordx4 v[114:117], v[66:67], off nt
	v_lshl_add_u64 v[66:67], v[66:67], 0, s[24:25]
	global_load_dwordx4 v[78:81], v[66:67], off nt
	v_lshl_add_u64 v[66:67], v[66:67], 0, s[24:25]
	global_load_dwordx4 v[86:89], v[66:67], off nt
	v_lshl_add_u64 v[66:67], v[66:67], 0, s[24:25]
	global_load_dwordx4 v[90:93], v[66:67], off nt
	v_lshl_add_u64 v[66:67], v[66:67], 0, s[24:25]
	v_lshl_add_u64 v[70:71], v[66:67], 0, s[24:25]
	v_lshl_add_u64 v[74:75], v[70:71], 0, s[24:25]
	v_lshl_add_u64 v[82:83], v[74:75], 0, s[24:25]
	global_load_dwordx4 v[94:97], v[66:67], off nt
	v_cvt_pk_fp8_f32 v198, v130, v135
	global_load_dwordx4 v[66:69], v[70:71], off nt
	s_waitcnt vmcnt(24)
	v_mul_f32_e32 v130, v195, v34
	global_load_dwordx4 v[70:73], v[74:75], off nt
	s_waitcnt vmcnt(24)
	v_mul_f32_e32 v135, v195, v50
	global_load_dwordx4 v[74:77], v[82:83], off nt
	v_lshl_add_u64 v[82:83], v[82:83], 0, s[24:25]
	global_load_dwordx4 v[82:85], v[82:83], off nt
	v_mov_b32_e32 v199, 0
	v_cvt_pk_fp8_f32 v199, v130, v135
	s_waitcnt vmcnt(23)
	v_mul_f32_e32 v130, v195, v10
	s_waitcnt vmcnt(22)
	v_mul_f32_e32 v135, v195, v26
	v_mov_b32_e32 v200, 0
	v_cvt_pk_fp8_f32 v200, v130, v135
	s_waitcnt vmcnt(19)
	v_mul_f32_e32 v130, v195, v2
	s_waitcnt vmcnt(18)
	v_mul_f32_e32 v135, v195, v22
	v_mov_b32_e32 v201, 0
	v_mul_f32_e32 v138, v195, v42
	v_mul_f32_e32 v139, v195, v58
	v_cvt_pk_fp8_f32 v201, v130, v135
	v_cvt_pk_fp8_f32 v198, v138, v139 op_sel:[0,0,1]
	v_mul_f32_e32 v138, v195, v38
	v_mul_f32_e32 v139, v195, v54
	v_cvt_pk_fp8_f32 v199, v138, v139 op_sel:[0,0,1]
	v_mul_f32_e32 v138, v195, v14
	v_mul_f32_e32 v139, v195, v30
	v_cvt_pk_fp8_f32 v200, v138, v139 op_sel:[0,0,1]
	s_waitcnt vmcnt(17)
	v_mul_f32_e32 v138, v195, v6
	s_waitcnt vmcnt(16)
	v_mul_f32_e32 v139, v195, v18
	v_cvt_pk_fp8_f32 v201, v138, v139 op_sel:[0,0,1]
	v_mul_f32_e32 v130, v195, v63
	v_mul_f32_e32 v135, v195, v47
	v_mul_f32_e32 v138, v195, v43
	ds_write_b128 v158, v[198:201]
	v_mov_b32_e32 v198, 0
	v_cvt_pk_fp8_f32 v198, v130, v135
	v_mul_f32_e32 v130, v195, v35
	v_mul_f32_e32 v135, v195, v51
	v_mov_b32_e32 v199, 0
	v_cvt_pk_fp8_f32 v199, v130, v135
	v_mul_f32_e32 v130, v195, v11
	v_mul_f32_e32 v135, v195, v27
	v_mov_b32_e32 v200, 0
	v_cvt_pk_fp8_f32 v200, v130, v135
	v_mul_f32_e32 v130, v195, v3
	v_mul_f32_e32 v135, v195, v23
	v_mov_b32_e32 v201, 0
	v_mul_f32_e32 v139, v195, v59
	v_cvt_pk_fp8_f32 v201, v130, v135
	v_cvt_pk_fp8_f32 v198, v138, v139 op_sel:[0,0,1]
	v_mul_f32_e32 v138, v195, v39
	v_mul_f32_e32 v139, v195, v55
	v_cvt_pk_fp8_f32 v199, v138, v139 op_sel:[0,0,1]
	v_mul_f32_e32 v138, v195, v15
	v_mul_f32_e32 v139, v195, v31
	v_cvt_pk_fp8_f32 v200, v138, v139 op_sel:[0,0,1]
	v_mul_f32_e32 v138, v195, v7
	v_mul_f32_e32 v139, v195, v19
	v_cvt_pk_fp8_f32 v201, v138, v139 op_sel:[0,0,1]
	v_mul_f32_e32 v130, v195, v64
	v_mul_f32_e32 v135, v195, v48
	v_mul_f32_e32 v138, v195, v44
	ds_write_b128 v158, v[198:201] offset:256
	v_mov_b32_e32 v198, 0
	v_cvt_pk_fp8_f32 v198, v130, v135
	v_mul_f32_e32 v130, v195, v36
	v_mul_f32_e32 v135, v195, v52
	v_mov_b32_e32 v199, 0
	v_cvt_pk_fp8_f32 v199, v130, v135
	v_mul_f32_e32 v130, v195, v12
	v_mul_f32_e32 v135, v195, v28
	v_mov_b32_e32 v200, 0
	v_cvt_pk_fp8_f32 v200, v130, v135
	v_mul_f32_e32 v130, v195, v4
	v_mul_f32_e32 v135, v195, v24
	v_mov_b32_e32 v201, 0
	v_mul_f32_e32 v139, v195, v60
	v_cvt_pk_fp8_f32 v201, v130, v135
	v_cvt_pk_fp8_f32 v198, v138, v139 op_sel:[0,0,1]
	v_mul_f32_e32 v138, v195, v40
	v_mul_f32_e32 v139, v195, v56
	v_cvt_pk_fp8_f32 v199, v138, v139 op_sel:[0,0,1]
	v_mul_f32_e32 v138, v195, v16
	v_mul_f32_e32 v139, v195, v32
	v_cvt_pk_fp8_f32 v200, v138, v139 op_sel:[0,0,1]
	v_mul_f32_e32 v138, v195, v8
	v_mul_f32_e32 v139, v195, v20
	v_cvt_pk_fp8_f32 v201, v138, v139 op_sel:[0,0,1]
	v_mul_f32_e32 v130, v195, v65
	v_mul_f32_e32 v135, v195, v49
	v_mul_f32_e32 v138, v195, v45
	ds_write_b128 v158, v[198:201] offset:512
	v_mov_b32_e32 v198, 0
	v_cvt_pk_fp8_f32 v198, v130, v135
	v_mul_f32_e32 v130, v195, v37
	v_mul_f32_e32 v135, v195, v53
	v_mov_b32_e32 v199, 0
	v_cvt_pk_fp8_f32 v199, v130, v135
	v_mul_f32_e32 v130, v195, v13
	v_mul_f32_e32 v135, v195, v29
	v_mov_b32_e32 v200, 0
	v_cvt_pk_fp8_f32 v200, v130, v135
	v_mul_f32_e32 v130, v195, v5
	v_mul_f32_e32 v135, v195, v25
	v_mov_b32_e32 v201, 0
	v_mul_f32_e32 v139, v195, v61
	v_cvt_pk_fp8_f32 v201, v130, v135
	v_cvt_pk_fp8_f32 v198, v138, v139 op_sel:[0,0,1]
	v_mul_f32_e32 v138, v195, v41
	v_mul_f32_e32 v139, v195, v57
	v_cvt_pk_fp8_f32 v199, v138, v139 op_sel:[0,0,1]
	v_mul_f32_e32 v138, v195, v17
	v_mul_f32_e32 v139, v195, v33
	v_cvt_pk_fp8_f32 v200, v138, v139 op_sel:[0,0,1]
	v_mul_f32_e32 v138, v195, v9
	v_mul_f32_e32 v139, v195, v21
	s_add_i32 s36, s36, s38
	v_cvt_pk_fp8_f32 v201, v138, v139 op_sel:[0,0,1]
	s_cmpk_gt_i32 s36, 0x25df
	s_cselect_b64 s[24:25], -1, 0
	s_and_b64 vcc, exec, s[24:25]
	ds_write_b128 v158, v[198:201] offset:768
	s_cbranch_vccnz .LBB0_110
	s_cmpk_gt_i32 s36, 0x17ff
	s_mov_b64 s[30:31], -1
	s_cbranch_scc0 .LBB0_116
	s_add_i32 s8, s36, 0xfffff220
	s_cmpk_gt_u32 s8, 0xfff
	s_cbranch_scc0 .LBB0_121
	v_readlane_b32 s28, v254, 2
	v_readlane_b32 s29, v254, 3
	s_and_b32 s45, s36, 15
	s_and_b32 s0, s41, 0x700
	v_readlane_b32 s30, v254, 4
	v_readlane_b32 s31, v254, 5
	s_mov_b64 s[26:27], s[28:29]
	s_cbranch_execz .LBB0_122
	v_readlane_b32 s22, v255, 3
	s_mov_b32 s1, 10
	s_mov_b64 s[28:29], 21
	s_movk_i32 s4, 0x400
	s_movk_i32 s47, 0x800
	s_mov_b32 s46, 2
	s_mov_b32 s5, 0x42800000
	v_readlane_b32 s23, v255, 4
	s_mov_b64 s[30:31], 0

; __device__ __forceinline__ unsigned cvt_pk_bf16(float lo, float hi) { unsigned r; asm volatile("v_cvt_pk_bf16_f32 %0, %1, %2" : "=v"(r) : "v"(lo), "v"(hi)); return r; }
;     __device__ __forceinline__ void operator()(const f32x4 (&acc)[2][2][4][2], const Unit& u, int wr, int wc, int fr, int fq) const {
;     ...
;             for (int m = 0; m < 4; ++m) { const size_t off = (size_t)(row0 + ai * HALF + m * 16) * ldc + col0;
;                 f32x4 r[4];
;                 if constexpr (RESID_F32) {
; #pragma unroll
;                     for (int p = 0; p < 4; ++p) r[p] = *(const f32x4*)((const float*)resid + off + 4 * p); }
;                 else { const u32x4 w0 = *(const u32x4*)((const bf16_t*)resid + off), w1 = *(const u32x4*)((const bf16_t*)resid + off + 8);
;                     r[0] = (f32x4){__uint_as_float(w0.x << 16), __uint_as_float(w0.x & 0xffff0000u), __uint_as_float(w0.y << 16), __uint_as_float(w0.y & 0xffff0000u)};
;                     r[1] = (f32x4){__uint_as_float(w0.z << 16), __uint_as_float(w0.z & 0xffff0000u), __uint_as_float(w0.w << 16), __uint_as_float(w0.w & 0xffff0000u)};
;                     r[2] = (f32x4){__uint_as_float(w1.x << 16), __uint_as_float(w1.x & 0xffff0000u), __uint_as_float(w1.y << 16), __uint_as_float(w1.y & 0xffff0000u)};
;                     r[3] = (f32x4){__uint_as_float(w1.z << 16), __uint_as_float(w1.z & 0xffff0000u), __uint_as_float(w1.w << 16), __uint_as_float(w1.w & 0xffff0000u)}; }
;                 unsigned o[8];
; #pragma unroll
;                 for (int bj = 0; bj < 2; ++bj)
; #pragma unroll
;                     for (int n = 0; n < 2; ++n) { const f32x4 v = r[2 * bj + n] + acc[ai][bj][m][n]; o[4 * bj + 2 * n] = cvt_pk_bf16(v[0], v[1]); o[4 * bj + 2 * n + 1] = cvt_pk_bf16(v[2], v[3]); }
;                 *(u32x4*)(out + off) = (u32x4){o[0], o[1], o[2], o[3]}; *(u32x4*)(out + off + 8) = (u32x4){o[4], o[5], o[6], o[7]}; }
.LBB0_477:
	v_lshl_add_u32 v6, s20, 8, v1
	v_lshl_or_b32 v4, s0, 8, v187
	v_readlane_b32 s44, v254, 14
	v_readlane_b32 s45, v254, 15
	v_readlane_b32 s0, v255, 11
	v_readlane_b32 s1, v255, 12
	s_andn2_b64 vcc, exec, s[2:3]
	v_readlane_b32 s46, v254, 16
	v_readlane_b32 s47, v254, 17
	v_readlane_b32 s48, v254, 18
	v_readlane_b32 s49, v254, 19
	v_readlane_b32 s50, v254, 20
	v_readlane_b32 s51, v254, 21
	v_readlane_b32 s52, v254, 22
	v_readlane_b32 s53, v254, 23
	v_readlane_b32 s54, v254, 24
	v_readlane_b32 s55, v254, 25
	v_readlane_b32 s56, v254, 26
	v_readlane_b32 s57, v254, 27
	v_readlane_b32 s58, v254, 28
	v_readlane_b32 s59, v254, 29
	v_lshl_add_u32 v178, v6, 10, v4
	v_lshlrev_b32_e32 v179, 2, v178
	v_lshlrev_b32_e32 v180, 1, v178
	s_nop 4
	global_load_dwordx4 v[2:5], v179, s[44:45] nt
	global_load_dwordx4 v[6:9], v179, s[44:45] offset:16 nt
	global_load_dwordx4 v[10:13], v179, s[44:45] offset:32 nt
	global_load_dwordx4 v[14:17], v179, s[44:45] offset:48 nt
	v_add_u32_e32 v181, 0x10000, v179
	global_load_dwordx4 v[18:21], v181, s[44:45] nt
	global_load_dwordx4 v[22:25], v181, s[44:45] offset:16 nt
	global_load_dwordx4 v[26:29], v181, s[44:45] offset:32 nt
	global_load_dwordx4 v[30:33], v181, s[44:45] offset:48 nt
	v_add_u32_e32 v182, 0x20000, v179
	global_load_dwordx4 v[194:197], v182, s[44:45] nt
	global_load_dwordx4 v[198:201], v182, s[44:45] offset:16 nt
	global_load_dwordx4 v[202:205], v182, s[44:45] offset:32 nt
	global_load_dwordx4 v[206:209], v182, s[44:45] offset:48 nt
	v_add_u32_e32 v183, 0x30000, v179
	global_load_dwordx4 v[210:213], v183, s[44:45] nt
	global_load_dwordx4 v[214:217], v183, s[44:45] offset:16 nt
	global_load_dwordx4 v[218:221], v183, s[44:45] offset:32 nt
	global_load_dwordx4 v[222:225], v183, s[44:45] offset:48 nt
	v_add_u32_e32 v184, 0x80000, v179
	global_load_dwordx4 v[228:231], v184, s[44:45] nt
	global_load_dwordx4 v[232:235], v184, s[44:45] offset:16 nt
	global_load_dwordx4 v[236:239], v184, s[44:45] offset:32 nt
	global_load_dwordx4 v[240:243], v184, s[44:45] offset:48 nt
	s_waitcnt vmcnt(16)
	v_pk_add_f32 v[2:3], v[158:159], v[2:3]
	v_pk_add_f32 v[4:5], v[160:161], v[4:5]
	v_pk_add_f32 v[6:7], v[154:155], v[6:7]
	v_pk_add_f32 v[8:9], v[156:157], v[8:9]
	v_pk_add_f32 v[10:11], v[150:151], v[10:11]
	v_pk_add_f32 v[12:13], v[152:153], v[12:13]
	v_pk_add_f32 v[14:15], v[146:147], v[14:15]
	v_pk_add_f32 v[16:17], v[148:149], v[16:17]
	v_cvt_pk_bf16_f32 v2, v2, v3
	v_cvt_pk_bf16_f32 v3, v4, v5
	v_cvt_pk_bf16_f32 v4, v6, v7
	v_cvt_pk_bf16_f32 v5, v8, v9
	v_cvt_pk_bf16_f32 v6, v10, v11
	v_cvt_pk_bf16_f32 v7, v12, v13
	v_cvt_pk_bf16_f32 v8, v14, v15
	v_cvt_pk_bf16_f32 v9, v16, v17
	global_store_dwordx4 v180, v[2:5], s[0:1]
	global_store_dwordx4 v180, v[6:9], s[0:1] offset:16
	v_add_u32_e32 v181, 0x90000, v179
	global_load_dwordx4 v[146:149], v181, s[44:45] nt
	global_load_dwordx4 v[150:153], v181, s[44:45] offset:16 nt
	global_load_dwordx4 v[154:157], v181, s[44:45] offset:32 nt
	global_load_dwordx4 v[158:161], v181, s[44:45] offset:48 nt
	s_waitcnt vmcnt(18)
	v_pk_add_f32 v[18:19], v[142:143], v[18:19]
	v_pk_add_f32 v[20:21], v[144:145], v[20:21]
	v_pk_add_f32 v[22:23], v[138:139], v[22:23]
	v_pk_add_f32 v[24:25], v[140:141], v[24:25]
	v_pk_add_f32 v[26:27], v[134:135], v[26:27]
	v_pk_add_f32 v[28:29], v[136:137], v[28:29]
	v_pk_add_f32 v[30:31], v[130:131], v[30:31]
	v_pk_add_f32 v[32:33], v[132:133], v[32:33]
	v_cvt_pk_bf16_f32 v18, v18, v19
	v_cvt_pk_bf16_f32 v19, v20, v21
	v_cvt_pk_bf16_f32 v20, v22, v23
	v_cvt_pk_bf16_f32 v21, v24, v25
	v_cvt_pk_bf16_f32 v22, v26, v27
	v_cvt_pk_bf16_f32 v23, v28, v29
	v_cvt_pk_bf16_f32 v24, v30, v31
	v_cvt_pk_bf16_f32 v25, v32, v33
	v_add_u32_e32 v185, 0x8000, v180
	global_store_dwordx4 v185, v[18:21], s[0:1]
	global_store_dwordx4 v185, v[22:25], s[0:1] offset:16
	v_add_u32_e32 v182, 0xa0000, v179
	global_load_dwordx4 v[130:133], v182, s[44:45] nt
	global_load_dwordx4 v[134:137], v182, s[44:45] offset:16 nt
	global_load_dwordx4 v[138:141], v182, s[44:45] offset:32 nt
	global_load_dwordx4 v[142:145], v182, s[44:45] offset:48 nt
	s_waitcnt vmcnt(20)
	v_pk_add_f32 v[194:195], v[126:127], v[194:195]
	v_pk_add_f32 v[196:197], v[128:129], v[196:197]
	v_pk_add_f32 v[198:199], v[122:123], v[198:199]
	v_pk_add_f32 v[200:201], v[124:125], v[200:201]
	v_pk_add_f32 v[202:203], v[118:119], v[202:203]
	v_pk_add_f32 v[204:205], v[120:121], v[204:205]
	v_pk_add_f32 v[206:207], v[114:115], v[206:207]
	v_pk_add_f32 v[208:209], v[116:117], v[208:209]
	v_cvt_pk_bf16_f32 v194, v194, v195
	v_cvt_pk_bf16_f32 v195, v196, v197
	v_cvt_pk_bf16_f32 v196, v198, v199
	v_cvt_pk_bf16_f32 v197, v200, v201
	v_cvt_pk_bf16_f32 v198, v202, v203
	v_cvt_pk_bf16_f32 v199, v204, v205
	v_cvt_pk_bf16_f32 v200, v206, v207
	v_cvt_pk_bf16_f32 v201, v208, v209
	v_add_u32_e32 v185, 0x10000, v180
	global_store_dwordx4 v185, v[194:197], s[0:1]
	global_store_dwordx4 v185, v[198:201], s[0:1] offset:16
	v_add_u32_e32 v183, 0xb0000, v179
	global_load_dwordx4 v[114:117], v183, s[44:45] nt
	global_load_dwordx4 v[118:121], v183, s[44:45] offset:16 nt
	global_load_dwordx4 v[122:125], v183, s[44:45] offset:32 nt
	global_load_dwordx4 v[126:129], v183, s[44:45] offset:48 nt
	s_waitcnt vmcnt(22)
; __device__ __forceinline__ unsigned cvt_pk_bf16(float lo, float hi) { unsigned r; asm volatile("v_cvt_pk_bf16_f32 %0, %1, %2" : "=v"(r) : "v"(lo), "v"(hi)); return r; }
;     __device__ __forceinline__ void operator()(const f32x4 (&acc)[2][2][4][2], const Unit& u, int wr, int wc, int fr, int fq) const {
;     ...
; #pragma unroll
;                 for (int bj = 0; bj < 2; ++bj)
; #pragma unroll
;                     for (int n = 0; n < 2; ++n) { const f32x4 v = r[2 * bj + n] + acc[ai][bj][m][n]; o[4 * bj + 2 * n] = cvt_pk_bf16(v[0], v[1]); o[4 * bj + 2 * n + 1] = cvt_pk_bf16(v[2], v[3]); }
;                 *(u32x4*)(out + off) = (u32x4){o[0], o[1], o[2], o[3]}; *(u32x4*)(out + off + 8) = (u32x4){o[4], o[5], o[6], o[7]}; }
	v_pk_add_f32 v[210:211], v[110:111], v[210:211]
	v_pk_add_f32 v[212:213], v[112:113], v[212:213]
	v_pk_add_f32 v[214:215], v[106:107], v[214:215]
	v_pk_add_f32 v[216:217], v[108:109], v[216:217]
	v_pk_add_f32 v[218:219], v[102:103], v[218:219]
	v_pk_add_f32 v[220:221], v[104:105], v[220:221]
	v_pk_add_f32 v[222:223], v[98:99], v[222:223]
	v_pk_add_f32 v[224:225], v[100:101], v[224:225]
	v_cvt_pk_bf16_f32 v210, v210, v211
	v_cvt_pk_bf16_f32 v211, v212, v213
	v_cvt_pk_bf16_f32 v212, v214, v215
	v_cvt_pk_bf16_f32 v213, v216, v217
	v_cvt_pk_bf16_f32 v214, v218, v219
	v_cvt_pk_bf16_f32 v215, v220, v221
	v_cvt_pk_bf16_f32 v216, v222, v223
	v_cvt_pk_bf16_f32 v217, v224, v225
	v_add_u32_e32 v185, 0x18000, v180
	global_store_dwordx4 v185, v[210:213], s[0:1]
	global_store_dwordx4 v185, v[214:217], s[0:1] offset:16
	s_waitcnt vmcnt(20)
	v_pk_add_f32 v[228:229], v[94:95], v[228:229]
	v_pk_add_f32 v[230:231], v[96:97], v[230:231]
	v_pk_add_f32 v[232:233], v[90:91], v[232:233]
	v_pk_add_f32 v[234:235], v[92:93], v[234:235]
	v_pk_add_f32 v[236:237], v[86:87], v[236:237]
	v_pk_add_f32 v[238:239], v[88:89], v[238:239]
	v_pk_add_f32 v[240:241], v[82:83], v[240:241]
	v_pk_add_f32 v[242:243], v[84:85], v[242:243]
	v_cvt_pk_bf16_f32 v228, v228, v229
	v_cvt_pk_bf16_f32 v229, v230, v231
	v_cvt_pk_bf16_f32 v230, v232, v233
	v_cvt_pk_bf16_f32 v231, v234, v235
	v_cvt_pk_bf16_f32 v232, v236, v237
	v_cvt_pk_bf16_f32 v233, v238, v239
	v_cvt_pk_bf16_f32 v234, v240, v241
	v_cvt_pk_bf16_f32 v235, v242, v243
	v_add_u32_e32 v185, 0x40000, v180
	global_store_dwordx4 v185, v[228:231], s[0:1]
	global_store_dwordx4 v185, v[232:235], s[0:1] offset:16
	s_waitcnt vmcnt(16)
	v_pk_add_f32 v[146:147], v[78:79], v[146:147]
	v_pk_add_f32 v[148:149], v[80:81], v[148:149]
	v_pk_add_f32 v[150:151], v[74:75], v[150:151]
	v_pk_add_f32 v[152:153], v[76:77], v[152:153]
	v_pk_add_f32 v[154:155], v[70:71], v[154:155]
	v_pk_add_f32 v[156:157], v[72:73], v[156:157]
	v_pk_add_f32 v[158:159], v[66:67], v[158:159]
	v_pk_add_f32 v[160:161], v[68:69], v[160:161]
	v_cvt_pk_bf16_f32 v146, v146, v147
	v_cvt_pk_bf16_f32 v147, v148, v149
	v_cvt_pk_bf16_f32 v148, v150, v151
	v_cvt_pk_bf16_f32 v149, v152, v153
	v_cvt_pk_bf16_f32 v150, v154, v155
	v_cvt_pk_bf16_f32 v151, v156, v157
	v_cvt_pk_bf16_f32 v152, v158, v159
	v_cvt_pk_bf16_f32 v153, v160, v161
	v_add_u32_e32 v185, 0x48000, v180
	global_store_dwordx4 v185, v[146:149], s[0:1]
	global_store_dwordx4 v185, v[150:153], s[0:1] offset:16
	s_waitcnt vmcnt(12)
	v_pk_add_f32 v[130:131], v[62:63], v[130:131]
	v_pk_add_f32 v[132:133], v[64:65], v[132:133]
	v_pk_add_f32 v[134:135], v[58:59], v[134:135]
	v_pk_add_f32 v[136:137], v[60:61], v[136:137]
	v_pk_add_f32 v[138:139], v[54:55], v[138:139]
	v_pk_add_f32 v[140:141], v[56:57], v[140:141]
	v_pk_add_f32 v[142:143], v[50:51], v[142:143]
	v_pk_add_f32 v[144:145], v[52:53], v[144:145]
	v_cvt_pk_bf16_f32 v130, v130, v131
	v_cvt_pk_bf16_f32 v131, v132, v133
	v_cvt_pk_bf16_f32 v132, v134, v135
	v_cvt_pk_bf16_f32 v133, v136, v137
	v_cvt_pk_bf16_f32 v134, v138, v139
	v_cvt_pk_bf16_f32 v135, v140, v141
	v_cvt_pk_bf16_f32 v136, v142, v143
	v_cvt_pk_bf16_f32 v137, v144, v145
	v_add_u32_e32 v185, 0x50000, v180
	global_store_dwordx4 v185, v[130:133], s[0:1]
	global_store_dwordx4 v185, v[134:137], s[0:1] offset:16
	s_waitcnt vmcnt(8)
	v_pk_add_f32 v[114:115], v[46:47], v[114:115]
	v_pk_add_f32 v[116:117], v[48:49], v[116:117]
	v_pk_add_f32 v[118:119], v[42:43], v[118:119]
	v_pk_add_f32 v[120:121], v[44:45], v[120:121]
	v_pk_add_f32 v[122:123], v[38:39], v[122:123]
	v_pk_add_f32 v[124:125], v[40:41], v[124:125]
	v_pk_add_f32 v[126:127], v[34:35], v[126:127]
	v_pk_add_f32 v[128:129], v[36:37], v[128:129]
	v_cvt_pk_bf16_f32 v114, v114, v115
	v_cvt_pk_bf16_f32 v115, v116, v117
	v_cvt_pk_bf16_f32 v116, v118, v119
	v_cvt_pk_bf16_f32 v117, v120, v121
	v_cvt_pk_bf16_f32 v118, v122, v123
	v_cvt_pk_bf16_f32 v119, v124, v125
	v_cvt_pk_bf16_f32 v120, v126, v127
	v_cvt_pk_bf16_f32 v121, v128, v129
	v_add_u32_e32 v185, 0x58000, v180
	global_store_dwordx4 v185, v[114:117], s[0:1]
	global_store_dwordx4 v185, v[118:121], s[0:1] offset:16
	s_mov_b64 s[20:21], 0x20000
	s_mov_b64 s[20:21], 0x24000
	s_mov_b64 s[20:21], 0x28000
	s_mov_b64 s[20:21], 0x2c000
	s_mov_b64 s[20:21], -1
	s_cbranch_vccnz .LBB0_466
	s_andn2_b64 vcc, exec, s[6:7]
	s_cbranch_vccnz .LBB0_465
	s_barrier
	s_branch .LBB0_465

; #define LAS __attribute__((address_space(3)))
; #define PHASE_IDS() do { int t_ = tid_k; asm volatile("" : "+v"(t_)); tid = t_; lane = t_ & 63; } while (0)
; #define xcd_barrier_wait_if_single(p) xcd_barrier_wait(*(p))
; __global__ void __launch_bounds__(NWAVES * 64, 2) enc_fwd(Args args) {
;     ...
;     if (IN(6)) { PHASE_IDS(); topk_phase(AFF, IDX, GATE, SEL, (LAS unsigned*)lds, G, blk, tid, lane, wave);
;         if (G > 64 && blk >= 64) { cvt_moe(args.in[22], args.in[23], args.in[24], WGU1, WDN1, scr, (blk - 64) * NWAVES + wave, (G - 64) * NWAVES, lane, 0, CVT1_P6); if (MK_SINGLE && IN(5)) xcd_barrier_wait_if_single(bar_ptr); }
;         else if (G <= 64) { __syncthreads(); cvt_moe(args.in[22], args.in[23], args.in[24], WGU1, WDN1, scr, gw, NGW, lane, 0, CVT1_P6); } }
.LBB0_713:
	v_readlane_b32 s2, v254, 9
	s_cmpk_lt_i32 s2, 0x41
	v_readlane_b32 s4, v254, 10
	s_cselect_b64 s[2:3], -1, 0
	s_cmp_lt_i32 s4, 64
	s_cselect_b64 s[4:5], -1, 0
	s_or_b64 s[4:5], s[4:5], s[2:3]
	s_mov_b64 s[2:3], -1
	s_and_b64 vcc, exec, s[4:5]
	s_cbranch_vccz .LBB0_721
	v_readlane_b32 s2, v254, 9
	s_cmp_gt_i32 s2, 64
	s_cbranch_scc1 .LBB0_720
	v_readlane_b32 s2, v254, 51
	s_cmpk_gt_i32 s2, 0x50f
	s_waitcnt vmcnt(0) lgkmcnt(0)
	s_barrier
	s_cbranch_scc1 .LBB0_720
; #define LAS __attribute__((address_space(3)))
; #define CVT_LOAD(v, c, s_) do { _Pragma("unroll") for (int i_ = 0; i_ < 16; ++i_) v[i_] = *(const f32x4*)((c).src + (size_t)(64 * (s_) + i_) * (c).N); } while (0)
; __device__ __forceinline__ CvtItem cvt_moe_item(int it, const float* wg, const float* wu, const float* wd, unsigned char* WGU, unsigned char* WDN, int lane) {
;     const int which = it >> 11, r = it & 2047, e = r >> 7, q = r & 127; CvtItem c; c.which = which;
;     if (which < 2) { const int nb = q & 31, k0 = (q >> 5) * 256; c.nb = nb;
;         c.N = DFF; c.K = DM; c.wscale = which ? 64.f / LOG2E : 64.f * LOG2E; c.src = (which ? wu : wg) + (size_t)e * DM * DFF + (size_t)(k0 + 16 * (lane >> 4)) * DFF + nb * 64 + 4 * (lane & 15);
;         c.dst = WGU + (size_t)e * 4096 * DM + k0; }
;     else { const int nb = q & 15, k0 = (q >> 4) * 256; c.nb = nb;
;         c.N = DM; c.K = DFF; c.wscale = 64.f; c.src = wd + (size_t)e * DFF * DM + (size_t)(k0 + 16 * (lane >> 4)) * DM + nb * 64 + 4 * (lane & 15);
;         c.dst = WDN + (size_t)e * DM * DFF + k0; }
;     return c;
; }
; __device__ __forceinline__ void cvt_moe_pipe2(const CvtSrc& A, const CvtSrc& B, LAS float* scr, int gw, int NGW, int lane) {
;     LAS unsigned char* blk = (LAS unsigned char*)scr;
;     f32x4 va[16], vb[16]; CvtItem c, cn;
;     const int it1 = A.n + B.n; int it = gw;
;     if (it < it1) { c = cvt_moe_item2(it, A, B, lane); CVT_LOAD(va, c, 0); }
	v_readlane_b32 s29, v254, 51
	s_lshl_b32 s2, s29, 3
	s_ashr_i32 s30, s29, 11
	s_and_b32 s31, s29, 31
	s_and_b32 s4, s2, 0x300
	s_cmpk_lt_u32 s29, 0x800
	s_cselect_b64 vcc, -1, 0
	v_readlane_b32 s8, v254, 30
	s_and_b64 s[2:3], vcc, exec
	v_readlane_b32 s20, v254, 42
	v_readlane_b32 s21, v254, 43
	v_readlane_b32 s22, v254, 44
	v_readlane_b32 s23, v254, 45
	v_readlane_b32 s10, v254, 32
	v_readlane_b32 s11, v254, 33
	s_cselect_b32 s3, s21, s23
	s_cselect_b32 s2, s20, s22
	s_bfe_u32 s8, s29, 0x40007
	s_lshl_b32 s6, s8, 22
	v_readlane_b32 s10, v255, 1
	v_readlane_b32 s11, v255, 2
	s_add_u32 s6, s10, s6
	s_addc_u32 s7, s11, 0
	s_add_u32 s6, s6, s4
	s_addc_u32 s7, s7, 0
	s_lshl_b32 s8, s8, 23
	v_and_b32_e32 v141, 48, v1
	s_add_u32 s2, s2, s8
	v_or_b32_e32 v2, s4, v141
	s_addc_u32 s3, s3, 0
	v_lshlrev_b32_e32 v130, 13, v2
	v_mov_b32_e32 v131, 0
	v_lshlrev_b32_e32 v4, 2, v138
	s_mov_b32 s5, 0
	v_lshl_add_u64 v[2:3], s[2:3], 0, v[130:131]
	s_lshl_b32 s4, s31, 8
	v_and_b32_e32 v66, 60, v4
	v_lshl_add_u64 v[2:3], v[2:3], 0, s[4:5]
	v_lshlrev_b32_e32 v130, 2, v66
	v_mov_b32_e32 v139, 0x42317218
	v_mov_b32_e32 v140, 0x42b8aa3b
	v_lshl_add_u64 v[132:133], v[2:3], 0, v[130:131]
	s_mov_b32 s10, 0x1e000
	v_cndmask_b32_e32 v179, v139, v140, vcc
	v_add_co_u32_e32 v2, vcc, s10, v132
	s_mov_b32 s11, 0x1c000
	s_nop 0
	v_addc_co_u32_e32 v3, vcc, 0, v133, vcc
	v_readlane_b32 s12, v254, 34
	v_add_co_u32_e32 v4, vcc, s11, v132
	s_mov_b32 s12, 0x1a000
	s_nop 0
	v_addc_co_u32_e32 v5, vcc, 0, v133, vcc
	v_readlane_b32 s13, v254, 35
	global_load_dwordx4 v[58:61], v[2:3], off nt
	global_load_dwordx4 v[50:53], v[4:5], off nt
	v_add_co_u32_e32 v2, vcc, s12, v132
	s_mov_b32 s13, 0x18000
	s_nop 0
	v_addc_co_u32_e32 v3, vcc, 0, v133, vcc
	v_readlane_b32 s14, v254, 36
	v_add_co_u32_e32 v4, vcc, s13, v132
	s_mov_b32 s14, 0x16000
	s_nop 0
	v_addc_co_u32_e32 v5, vcc, 0, v133, vcc
	v_readlane_b32 s15, v254, 37
	global_load_dwordx4 v[54:57], v[2:3], off nt
	global_load_dwordx4 v[38:41], v[4:5], off nt
	v_add_co_u32_e32 v2, vcc, s14, v132
	s_mov_b32 s15, 0x14000
	s_nop 0
	v_addc_co_u32_e32 v3, vcc, 0, v133, vcc
	v_readlane_b32 s16, v254, 38
	v_add_co_u32_e32 v4, vcc, s15, v132
	s_mov_b32 s16, 0x12000
	s_nop 0
	v_addc_co_u32_e32 v5, vcc, 0, v133, vcc
	v_readlane_b32 s17, v254, 39
	global_load_dwordx4 v[46:49], v[2:3], off nt
	global_load_dwordx4 v[30:33], v[4:5], off nt
	v_add_co_u32_e32 v2, vcc, s16, v132
	s_mov_b32 s17, 0x10000
	s_nop 0
	v_addc_co_u32_e32 v3, vcc, 0, v133, vcc
	v_readlane_b32 s18, v254, 40
	v_add_co_u32_e32 v4, vcc, s17, v132
	s_mov_b32 s18, 0xe000
	s_nop 0
	v_addc_co_u32_e32 v5, vcc, 0, v133, vcc
	v_readlane_b32 s19, v254, 41
	global_load_dwordx4 v[34:37], v[2:3], off nt
	global_load_dwordx4 v[14:17], v[4:5], off nt
	v_add_co_u32_e32 v2, vcc, s18, v132
	s_mov_b32 s19, 0xc000
	s_nop 0
	v_addc_co_u32_e32 v3, vcc, 0, v133, vcc
	v_add_co_u32_e32 v4, vcc, s19, v132
	s_mov_b32 s20, 0xa000
	s_nop 0
	v_addc_co_u32_e32 v5, vcc, 0, v133, vcc
	global_load_dwordx4 v[42:45], v[2:3], off nt
	global_load_dwordx4 v[22:25], v[4:5], off nt
	v_add_co_u32_e32 v2, vcc, s20, v132
	s_mov_b32 s21, 0x8000
	s_nop 0
	v_addc_co_u32_e32 v3, vcc, 0, v133, vcc
	v_add_co_u32_e32 v4, vcc, s21, v132
	s_movk_i32 s22, 0x6000
	s_nop 0
	v_addc_co_u32_e32 v5, vcc, 0, v133, vcc
	global_load_dwordx4 v[26:29], v[2:3], off nt
	global_load_dwordx4 v[10:13], v[4:5], off nt
	v_add_co_u32_e32 v2, vcc, s22, v132
	s_movk_i32 s23, 0x4000
	s_nop 0
	v_addc_co_u32_e32 v3, vcc, 0, v133, vcc
	v_add_co_u32_e32 v4, vcc, s23, v132
	s_movk_i32 s24, 0x2000
	s_nop 0
	v_addc_co_u32_e32 v5, vcc, 0, v133, vcc
	v_add_co_u32_e32 v6, vcc, s24, v132
	global_load_dwordx4 v[18:21], v[2:3], off nt
	s_nop 0
	global_load_dwordx4 v[2:5], v[4:5], off nt
	v_addc_co_u32_e32 v7, vcc, 0, v133, vcc
	global_load_dwordx4 v[6:9], v[6:7], off nt
	s_nop 0
	global_load_dwordx4 v[62:65], v[132:133], off nt
	v_lshrrev_b32_e32 v142, 4, v138
	v_and_b32_e32 v67, 15, v1
	v_readlane_b32 s2, v254, 60
	v_or_b32_e32 v143, 4, v142
	v_or_b32_e32 v144, 8, v142
	v_or_b32_e32 v145, 12, v142
	v_or_b32_e32 v146, 16, v142
	v_or_b32_e32 v147, 20, v142
	v_or_b32_e32 v148, 24, v142
	v_or_b32_e32 v149, 28, v142
	v_or_b32_e32 v150, 32, v142
	v_or_b32_e32 v151, 36, v142
	v_or_b32_e32 v152, 40, v142
	v_or_b32_e32 v153, 44, v142
	v_or_b32_e32 v154, 48, v142
	v_or_b32_e32 v155, 52, v142
	v_or_b32_e32 v156, 56, v142
	v_or_b32_e32 v157, 60, v142
	v_lshl_add_u32 v68, v67, 10, s2
	v_bitop3_b32 v70, v142, v67, 4 bitop3:0x36
	v_bitop3_b32 v71, v142, v67, 8 bitop3:0x36
	v_bitop3_b32 v72, v142, v67, 12 bitop3:0x36
	v_lshlrev_b32_e32 v134, 4, v67
	v_lshl_add_u32 v67, v142, 8, s2
	v_lshl_add_u32 v73, v143, 8, s2
	v_lshl_add_u32 v75, v144, 8, s2
	v_lshl_add_u32 v77, v145, 8, s2
	v_lshl_add_u32 v79, v146, 8, s2
	v_lshl_add_u32 v81, v147, 8, s2
	v_lshl_add_u32 v83, v148, 8, s2
	v_lshl_add_u32 v85, v149, 8, s2
	v_lshl_add_u32 v87, v150, 8, s2
	v_lshl_add_u32 v89, v151, 8, s2
	v_lshl_add_u32 v91, v152, 8, s2
	v_lshl_add_u32 v93, v153, 8, s2
	v_lshl_add_u32 v95, v154, 8, s2
	v_lshl_add_u32 v97, v155, 8, s2
	v_lshl_add_u32 v99, v156, 8, s2
	v_lshl_add_u32 v101, v157, 8, s2
	v_readlane_b32 s2, v254, 52
	v_bitop3_b32 v69, v142, v1, 15 bitop3:0x78
	s_add_i32 s2, s29, s2
	v_lshlrev_b32_e32 v69, 4, v69
	v_lshlrev_b32_e32 v70, 4, v70
	v_lshlrev_b32_e32 v71, 4, v71
	v_lshlrev_b32_e32 v72, 4, v72
	v_xor_b32_e32 v74, 16, v134
	v_xor_b32_e32 v76, 32, v134
	v_xor_b32_e32 v78, 48, v134
	v_xor_b32_e32 v80, 64, v134
	v_xor_b32_e32 v82, 0x50, v134
	v_xor_b32_e32 v84, 0x60, v134
	v_xor_b32_e32 v86, 0x70, v134
	v_xor_b32_e32 v88, 0x80, v134
	v_xor_b32_e32 v90, 0x90, v134
	v_xor_b32_e32 v92, 0xa0, v134
	v_xor_b32_e32 v94, 0xb0, v134
	v_xor_b32_e32 v96, 0xc0, v134
	v_xor_b32_e32 v98, 0xd0, v134
	v_xor_b32_e32 v100, 0xe0, v134
	v_xor_b32_e32 v102, 0xf0, v134
	s_lshl_b32 s25, s2, 3
	v_readlane_b32 s2, v254, 9
	v_readlane_b32 s9, v254, 31
	v_mov_b32_e32 v135, v131
	s_lshl_b32 s26, s2, 6
	v_add_u32_e32 v158, v68, v69
	v_add_u32_e32 v159, v68, v70
	v_add_u32_e32 v160, v68, v71
	v_lshlrev_b32_e32 v136, 2, v66
	v_add_u32_e32 v161, v68, v72
	v_add_u32_e32 v162, v67, v134
	v_add_u32_e32 v163, v73, v74
	v_add_u32_e32 v164, v75, v76
	v_add_u32_e32 v165, v77, v78
	v_add_u32_e32 v166, v79, v80
	v_add_u32_e32 v167, v81, v82
	v_add_u32_e32 v168, v83, v84
	v_add_u32_e32 v169, v85, v86
	v_add_u32_e32 v170, v87, v88
	v_add_u32_e32 v171, v89, v90
	v_add_u32_e32 v172, v91, v92
	v_add_u32_e32 v173, v93, v94
	v_add_u32_e32 v174, v95, v96
	v_add_u32_e32 v175, v97, v98
	v_add_u32_e32 v176, v99, v100
	v_add_u32_e32 v177, v101, v102
	s_branch .LBB0_718

; __device__ __forceinline__ unsigned pk4_fp8(float a, float b, float c, float d) { unsigned w = 0u; w = __builtin_amdgcn_cvt_pk_fp8_f32(a, b, w, false); w = __builtin_amdgcn_cvt_pk_fp8_f32(c, d, w, true); return w; }
; #define LAS __attribute__((address_space(3)))
; #define CVT_LOAD(v, c, s_) do { _Pragma("unroll") for (int i_ = 0; i_ < 16; ++i_) v[i_] = *(const f32x4*)((c).src + (size_t)(64 * (s_) + i_) * (c).N); } while (0)
; __device__ __forceinline__ void cvt_pack8(const f32x4 (&v)[16], const CvtItem& c, LAS unsigned char* blk, int s4, int lane) {
;     const float w = c.wscale; const int cb = lane & 15, j = 4 * s4 + (lane >> 4);
; #pragma unroll
;     for (int jn = 0; jn < 4; ++jn) {
;         v4u o; o.x = pg8::pk4_fp8(v[0][jn] * w, v[1][jn] * w, v[2][jn] * w, v[3][jn] * w); o.y = pg8::pk4_fp8(v[4][jn] * w, v[5][jn] * w, v[6][jn] * w, v[7][jn] * w);
;         o.z = pg8::pk4_fp8(v[8][jn] * w, v[9][jn] * w, v[10][jn] * w, v[11][jn] * w); o.w = pg8::pk4_fp8(v[12][jn] * w, v[13][jn] * w, v[14][jn] * w, v[15][jn] * w);
;         *(LAS v4u*)(blk + (4 * cb + jn) * 256 + ((j ^ cb) * 16)) = o; }
; }
; __device__ __forceinline__ void cvt_moe_pipe2(const CvtSrc& A, const CvtSrc& B, LAS float* scr, int gw, int NGW, int lane) {
;     ...
;     while (it < it1) {
;         const int i1 = it + NGW; const bool more = i1 < it1;
;         CVT_LOAD(vb, c, 1); cvt_pack8(va, c, blk, 0, lane);
;         CVT_LOAD(va, c, 2); cvt_pack8(vb, c, blk, 1, lane);
;         CVT_LOAD(vb, c, 3); cvt_pack8(va, c, blk, 2, lane);
.LBB0_718:
	v_readlane_b32 s2, v254, 52
	s_add_i32 s29, s29, s2
	s_mov_b32 s2, 0x80000
	v_add_co_u32_e32 v66, vcc, s2, v132
	s_mov_b32 s2, 0x82000
	s_nop 0
	v_addc_co_u32_e32 v67, vcc, 0, v133, vcc
	v_add_co_u32_e32 v70, vcc, s2, v132
	s_mov_b32 s2, 0x84000
	s_nop 0
	v_addc_co_u32_e32 v71, vcc, 0, v133, vcc
	v_add_co_u32_e32 v74, vcc, s2, v132
	s_mov_b32 s2, 0x86000
	s_nop 0
	v_addc_co_u32_e32 v75, vcc, 0, v133, vcc
	v_add_co_u32_e32 v78, vcc, s2, v132
	s_mov_b32 s2, 0x88000
	s_nop 0
	v_addc_co_u32_e32 v79, vcc, 0, v133, vcc
	global_load_dwordx4 v[82:85], v[78:79], off nt
	v_add_co_u32_e32 v78, vcc, s2, v132
	s_mov_b32 s2, 0x8a000
	s_nop 0
	v_addc_co_u32_e32 v79, vcc, 0, v133, vcc
	v_add_co_u32_e32 v86, vcc, s2, v132
	s_mov_b32 s2, 0x8c000
	s_nop 0
	v_addc_co_u32_e32 v87, vcc, 0, v133, vcc
	global_load_dwordx4 v[90:93], v[86:87], off nt
	v_add_co_u32_e32 v86, vcc, s2, v132
	s_mov_b32 s2, 0x8e000
	s_nop 0
	v_addc_co_u32_e32 v87, vcc, 0, v133, vcc
	global_load_dwordx4 v[94:97], v[86:87], off nt
	v_add_co_u32_e32 v86, vcc, s2, v132
	s_mov_b32 s2, 0x90000
	s_nop 0
	v_addc_co_u32_e32 v87, vcc, 0, v133, vcc
	global_load_dwordx4 v[106:109], v[86:87], off nt
	v_add_co_u32_e32 v86, vcc, s2, v132
	s_mov_b32 s2, 0x92000
	s_nop 0
	v_addc_co_u32_e32 v87, vcc, 0, v133, vcc
	v_add_co_u32_e32 v98, vcc, s2, v132
	s_mov_b32 s2, 0x94000
	s_nop 0
	v_addc_co_u32_e32 v99, vcc, 0, v133, vcc
	v_add_co_u32_e32 v102, vcc, s2, v132
	s_waitcnt vmcnt(4)
	v_mul_f32_e32 v62, v62, v179
	v_mul_f32_e32 v6, v6, v179
	v_mov_b32_e32 v180, 0
	v_addc_co_u32_e32 v103, vcc, 0, v133, vcc
	s_mov_b32 s2, 0x96000
	v_cvt_pk_fp8_f32 v180, v62, v6
	v_add_co_u32_e32 v110, vcc, s2, v132
	s_mov_b32 s2, 0x98000
	s_nop 0
	v_addc_co_u32_e32 v111, vcc, 0, v133, vcc
	global_load_dwordx4 v[102:105], v[102:103], off nt
	v_mul_f32_e32 v2, v2, v179
	global_load_dwordx4 v[114:117], v[110:111], off nt
	v_add_co_u32_e32 v110, vcc, s2, v132
	v_mul_f32_e32 v18, v18, v179
	global_load_dwordx4 v[66:69], v[66:67], off nt
	v_addc_co_u32_e32 v111, vcc, 0, v133, vcc
	global_load_dwordx4 v[70:73], v[70:71], off nt
	s_mov_b32 s2, 0x9a000
	v_cvt_pk_fp8_f32 v180, v2, v18 op_sel:[0,0,1]
	v_mul_f32_e32 v2, v10, v179
	v_mul_f32_e32 v6, v26, v179
	v_mov_b32_e32 v181, 0
	global_load_dwordx4 v[78:81], v[78:79], off nt
	v_add_co_u32_e32 v118, vcc, s2, v132
	v_cvt_pk_fp8_f32 v181, v2, v6
	v_mul_f32_e32 v2, v14, v179
	v_mul_f32_e32 v6, v34, v179
	v_mov_b32_e32 v182, 0
	global_load_dwordx4 v[86:89], v[86:87], off nt
	v_addc_co_u32_e32 v119, vcc, 0, v133, vcc
	global_load_dwordx4 v[98:101], v[98:99], off nt
	s_mov_b32 s2, 0x9c000
	v_cvt_pk_fp8_f32 v182, v2, v6
	v_mul_f32_e32 v2, v38, v179
	v_mul_f32_e32 v6, v54, v179
	v_mov_b32_e32 v183, 0
	global_load_dwordx4 v[110:113], v[110:111], off nt
	v_add_co_u32_e32 v122, vcc, s2, v132
	global_load_dwordx4 v[118:121], v[118:119], off nt
	v_cvt_pk_fp8_f32 v183, v2, v6
	global_load_dwordx4 v[74:77], v[74:75], off nt
	v_addc_co_u32_e32 v123, vcc, 0, v133, vcc
	s_mov_b32 s2, 0x9e000
	v_mul_f32_e32 v10, v22, v179
	v_mul_f32_e32 v18, v42, v179
	v_add_co_u32_e32 v126, vcc, s2, v132
	v_cvt_pk_fp8_f32 v181, v10, v18 op_sel:[0,0,1]
	v_mul_f32_e32 v10, v30, v179
	v_mul_f32_e32 v14, v46, v179
	v_addc_co_u32_e32 v127, vcc, 0, v133, vcc
	v_cvt_pk_fp8_f32 v182, v10, v14 op_sel:[0,0,1]
	v_mul_f32_e32 v10, v50, v179
	v_mul_f32_e32 v14, v58, v179
	global_load_dwordx4 v[122:125], v[122:123], off nt
	v_cvt_pk_fp8_f32 v183, v10, v14 op_sel:[0,0,1]
	global_load_dwordx4 v[126:129], v[126:127], off nt
	v_mul_f32_e32 v2, v63, v179
	v_mul_f32_e32 v6, v7, v179
	ds_write_b128 v158, v[180:183]
	v_mov_b32_e32 v180, 0
	v_cvt_pk_fp8_f32 v180, v2, v6
	v_mul_f32_e32 v3, v3, v179
	v_mul_f32_e32 v7, v19, v179
	v_mul_f32_e32 v2, v11, v179
	v_cvt_pk_fp8_f32 v180, v3, v7 op_sel:[0,0,1]
	v_mul_f32_e32 v3, v27, v179
	v_mov_b32_e32 v181, 0
	v_cvt_pk_fp8_f32 v181, v2, v3
	v_mul_f32_e32 v2, v15, v179
	v_mul_f32_e32 v3, v35, v179
	v_mov_b32_e32 v182, 0
	v_cvt_pk_fp8_f32 v182, v2, v3
	v_mul_f32_e32 v2, v39, v179
	v_mul_f32_e32 v3, v55, v179
	v_mov_b32_e32 v183, 0
	v_cvt_pk_fp8_f32 v183, v2, v3
	v_mul_f32_e32 v6, v23, v179
	v_mul_f32_e32 v7, v43, v179
	v_cvt_pk_fp8_f32 v181, v6, v7 op_sel:[0,0,1]
	v_mul_f32_e32 v6, v31, v179
	v_mul_f32_e32 v7, v47, v179
	v_cvt_pk_fp8_f32 v182, v6, v7 op_sel:[0,0,1]
	v_mul_f32_e32 v6, v51, v179
	v_mul_f32_e32 v7, v59, v179
	v_cvt_pk_fp8_f32 v183, v6, v7 op_sel:[0,0,1]
	v_mul_f32_e32 v2, v64, v179
	v_mul_f32_e32 v3, v8, v179
	v_mul_f32_e32 v4, v4, v179
	ds_write_b128 v158, v[180:183] offset:256
	v_mov_b32_e32 v180, 0
	v_cvt_pk_fp8_f32 v180, v2, v3
	v_mul_f32_e32 v2, v12, v179
	v_mul_f32_e32 v3, v28, v179
	v_mov_b32_e32 v181, 0
	v_cvt_pk_fp8_f32 v181, v2, v3
	v_mul_f32_e32 v2, v16, v179
	v_mul_f32_e32 v3, v36, v179
	v_mov_b32_e32 v182, 0
	v_cvt_pk_fp8_f32 v182, v2, v3
	v_mul_f32_e32 v2, v40, v179
	v_mul_f32_e32 v3, v56, v179
	v_mov_b32_e32 v183, 0
	v_mul_f32_e32 v6, v20, v179
	v_cvt_pk_fp8_f32 v183, v2, v3
	v_cvt_pk_fp8_f32 v180, v4, v6 op_sel:[0,0,1]
	v_mul_f32_e32 v4, v24, v179
	v_mul_f32_e32 v6, v44, v179
	v_cvt_pk_fp8_f32 v181, v4, v6 op_sel:[0,0,1]
	v_mul_f32_e32 v4, v32, v179
	v_mul_f32_e32 v6, v48, v179
	v_cvt_pk_fp8_f32 v182, v4, v6 op_sel:[0,0,1]
	v_mul_f32_e32 v4, v52, v179
	v_mul_f32_e32 v6, v60, v179
	v_cvt_pk_fp8_f32 v183, v4, v6 op_sel:[0,0,1]
	v_mul_f32_e32 v3, v65, v179
	v_mul_f32_e32 v4, v9, v179
	v_mov_b32_e32 v2, 0
	v_cvt_pk_fp8_f32 v2, v3, v4
	v_mul_f32_e32 v5, v5, v179
	v_mul_f32_e32 v6, v21, v179
	v_mul_f32_e32 v4, v13, v179
	v_cvt_pk_fp8_f32 v2, v5, v6 op_sel:[0,0,1]
	v_mul_f32_e32 v5, v29, v179
	v_mov_b32_e32 v3, 0
	v_cvt_pk_fp8_f32 v3, v4, v5
	v_mul_f32_e32 v6, v25, v179
	v_mul_f32_e32 v7, v45, v179
	v_mul_f32_e32 v5, v17, v179
	v_cvt_pk_fp8_f32 v3, v6, v7 op_sel:[0,0,1]
	v_mul_f32_e32 v6, v37, v179
	v_mov_b32_e32 v4, 0
	v_cvt_pk_fp8_f32 v4, v5, v6
	v_mul_f32_e32 v7, v33, v179
	v_mul_f32_e32 v8, v49, v179
	v_mul_f32_e32 v6, v41, v179
	v_cvt_pk_fp8_f32 v4, v7, v8 op_sel:[0,0,1]
	v_mul_f32_e32 v7, v57, v179
	v_mov_b32_e32 v5, 0
	v_cvt_pk_fp8_f32 v5, v6, v7
	v_mul_f32_e32 v8, v53, v179
	v_mul_f32_e32 v9, v61, v179
	s_mov_b32 s2, 0x100000
	v_cvt_pk_fp8_f32 v5, v8, v9 op_sel:[0,0,1]
	ds_write_b128 v158, v[180:183] offset:512
	v_mov_b32_e32 v180, 0
	v_mov_b32_e32 v181, 0
	ds_write_b128 v158, v[2:5] offset:768
	v_add_co_u32_e32 v2, vcc, s2, v132
	s_mov_b32 s2, 0x102000
	s_nop 0
	v_addc_co_u32_e32 v3, vcc, 0, v133, vcc
	global_load_dwordx4 v[62:65], v[2:3], off nt
	v_add_co_u32_e32 v2, vcc, s2, v132
	s_mov_b32 s2, 0x104000
	s_nop 0
	v_addc_co_u32_e32 v3, vcc, 0, v133, vcc
	global_load_dwordx4 v[6:9], v[2:3], off nt
	v_add_co_u32_e32 v2, vcc, s2, v132
	s_mov_b32 s2, 0x106000
	s_nop 0
	v_addc_co_u32_e32 v3, vcc, 0, v133, vcc
	v_add_co_u32_e32 v10, vcc, s2, v132
	s_mov_b32 s2, 0x108000
	s_nop 0
	v_addc_co_u32_e32 v11, vcc, 0, v133, vcc
	global_load_dwordx4 v[2:5], v[2:3], off nt
	s_waitcnt vmcnt(12)
; __device__ __forceinline__ unsigned pk4_fp8(float a, float b, float c, float d) { unsigned w = 0u; w = __builtin_amdgcn_cvt_pk_fp8_f32(a, b, w, false); w = __builtin_amdgcn_cvt_pk_fp8_f32(c, d, w, true); return w; }
; #define LAS __attribute__((address_space(3)))
; #define CVT_LOAD(v, c, s_) do { _Pragma("unroll") for (int i_ = 0; i_ < 16; ++i_) v[i_] = *(const f32x4*)((c).src + (size_t)(64 * (s_) + i_) * (c).N); } while (0)
; __device__ __forceinline__ void cvt_pack8(const f32x4 (&v)[16], const CvtItem& c, LAS unsigned char* blk, int s4, int lane) {
;     const float w = c.wscale; const int cb = lane & 15, j = 4 * s4 + (lane >> 4);
; #pragma unroll
;     for (int jn = 0; jn < 4; ++jn) {
;         v4u o; o.x = pg8::pk4_fp8(v[0][jn] * w, v[1][jn] * w, v[2][jn] * w, v[3][jn] * w); o.y = pg8::pk4_fp8(v[4][jn] * w, v[5][jn] * w, v[6][jn] * w, v[7][jn] * w);
;         o.z = pg8::pk4_fp8(v[8][jn] * w, v[9][jn] * w, v[10][jn] * w, v[11][jn] * w); o.w = pg8::pk4_fp8(v[12][jn] * w, v[13][jn] * w, v[14][jn] * w, v[15][jn] * w);
;         *(LAS v4u*)(blk + (4 * cb + jn) * 256 + ((j ^ cb) * 16)) = o; }
; }
; __device__ __forceinline__ void cvt_moe_pipe2(const CvtSrc& A, const CvtSrc& B, LAS float* scr, int gw, int NGW, int lane) {
;     ...
;     while (it < it1) {
;         const int i1 = it + NGW; const bool more = i1 < it1;
;         CVT_LOAD(vb, c, 1); cvt_pack8(va, c, blk, 0, lane);
;         CVT_LOAD(va, c, 2); cvt_pack8(vb, c, blk, 1, lane);
;         CVT_LOAD(vb, c, 3); cvt_pack8(va, c, blk, 2, lane);
	v_mul_f32_e32 v66, v179, v66
	global_load_dwordx4 v[18:21], v[10:11], off nt
	v_add_co_u32_e32 v10, vcc, s2, v132
	s_mov_b32 s2, 0x10a000
	s_nop 0
	v_addc_co_u32_e32 v11, vcc, 0, v133, vcc
	v_add_co_u32_e32 v14, vcc, s2, v132
	s_mov_b32 s2, 0x10c000
	s_nop 0
	v_addc_co_u32_e32 v15, vcc, 0, v133, vcc
	global_load_dwordx4 v[10:13], v[10:11], off nt
	s_waitcnt vmcnt(13)
	v_mul_f32_e32 v70, v179, v70
	global_load_dwordx4 v[26:29], v[14:15], off nt
	v_add_co_u32_e32 v14, vcc, s2, v132
	s_mov_b32 s2, 0x10e000
	s_nop 0
	v_addc_co_u32_e32 v15, vcc, 0, v133, vcc
	global_load_dwordx4 v[22:25], v[14:15], off nt
	v_add_co_u32_e32 v14, vcc, s2, v132
	s_mov_b32 s2, 0x110000
	s_nop 0
	v_addc_co_u32_e32 v15, vcc, 0, v133, vcc
	global_load_dwordx4 v[42:45], v[14:15], off nt
	v_add_co_u32_e32 v14, vcc, s2, v132
	s_mov_b32 s2, 0x112000
	s_nop 0
	v_addc_co_u32_e32 v15, vcc, 0, v133, vcc
	v_add_co_u32_e32 v30, vcc, s2, v132
	s_mov_b32 s2, 0x114000
	s_nop 0
	v_addc_co_u32_e32 v31, vcc, 0, v133, vcc
	global_load_dwordx4 v[14:17], v[14:15], off nt
	v_cvt_pk_fp8_f32 v180, v66, v70
	global_load_dwordx4 v[34:37], v[30:31], off nt
	v_add_co_u32_e32 v30, vcc, s2, v132
	s_mov_b32 s2, 0x116000
	s_nop 0
	v_addc_co_u32_e32 v31, vcc, 0, v133, vcc
	v_add_co_u32_e32 v38, vcc, s2, v132
	s_waitcnt vmcnt(17)
	v_mul_f32_e32 v66, v179, v78
	v_mul_f32_e32 v70, v179, v90
	v_addc_co_u32_e32 v39, vcc, 0, v133, vcc
	s_mov_b32 s2, 0x118000
	v_cvt_pk_fp8_f32 v181, v66, v70
	s_waitcnt vmcnt(16)
	v_mul_f32_e32 v66, v179, v86
	s_waitcnt vmcnt(15)
	v_mul_f32_e32 v70, v179, v98
	v_mov_b32_e32 v182, 0
	global_load_dwordx4 v[30:33], v[30:31], off nt
	v_cvt_pk_fp8_f32 v182, v66, v70
	global_load_dwordx4 v[46:49], v[38:39], off nt
	v_add_co_u32_e32 v38, vcc, s2, v132
	s_waitcnt vmcnt(16)
	v_mul_f32_e32 v66, v179, v110
	s_waitcnt vmcnt(15)
	v_mul_f32_e32 v70, v179, v118
	v_mov_b32_e32 v183, 0
	v_addc_co_u32_e32 v39, vcc, 0, v133, vcc
	s_mov_b32 s2, 0x11a000
	s_waitcnt vmcnt(14)
	v_mul_f32_e32 v74, v179, v74
	v_mul_f32_e32 v82, v179, v82
	v_cvt_pk_fp8_f32 v183, v66, v70
	v_add_co_u32_e32 v50, vcc, s2, v132
	v_cvt_pk_fp8_f32 v180, v74, v82 op_sel:[0,0,1]
	v_mul_f32_e32 v74, v179, v94
	v_mul_f32_e32 v78, v179, v106
	v_addc_co_u32_e32 v51, vcc, 0, v133, vcc
	s_mov_b32 s2, 0x11c000
	v_cvt_pk_fp8_f32 v181, v74, v78 op_sel:[0,0,1]
	v_mul_f32_e32 v74, v179, v102
	v_mul_f32_e32 v78, v179, v114
	global_load_dwordx4 v[38:41], v[38:39], off nt
	v_cvt_pk_fp8_f32 v182, v74, v78 op_sel:[0,0,1]
	global_load_dwordx4 v[54:57], v[50:51], off nt
	v_add_co_u32_e32 v50, vcc, s2, v132
	s_waitcnt vmcnt(15)
	v_mul_f32_e32 v74, v179, v122
	s_waitcnt vmcnt(14)
	v_mul_f32_e32 v78, v179, v126
	v_addc_co_u32_e32 v51, vcc, 0, v133, vcc
	s_mov_b32 s2, 0x11e000
	v_cvt_pk_fp8_f32 v183, v74, v78 op_sel:[0,0,1]
	v_add_co_u32_e32 v58, vcc, s2, v132
	global_load_dwordx4 v[50:53], v[50:51], off nt
	s_nop 0
	v_addc_co_u32_e32 v59, vcc, 0, v133, vcc
	global_load_dwordx4 v[58:61], v[58:59], off nt
	ds_write_b128 v159, v[180:183]
	v_mul_f32_e32 v66, v179, v67
	v_mul_f32_e32 v67, v179, v71
	v_mov_b32_e32 v180, 0
	v_cvt_pk_fp8_f32 v180, v66, v67
	v_mul_f32_e32 v66, v179, v79
	v_mul_f32_e32 v67, v179, v91
	v_mov_b32_e32 v181, 0
	v_cvt_pk_fp8_f32 v181, v66, v67
	v_mul_f32_e32 v66, v179, v87
	v_mul_f32_e32 v67, v179, v99
	v_mov_b32_e32 v182, 0
	v_cvt_pk_fp8_f32 v182, v66, v67
	v_mul_f32_e32 v66, v179, v111
	v_mul_f32_e32 v67, v179, v119
	v_mov_b32_e32 v183, 0
	v_mul_f32_e32 v70, v179, v75
	v_mul_f32_e32 v71, v179, v83
	v_cvt_pk_fp8_f32 v183, v66, v67
	v_cvt_pk_fp8_f32 v180, v70, v71 op_sel:[0,0,1]
	v_mul_f32_e32 v70, v179, v95
	v_mul_f32_e32 v71, v179, v107
	v_cvt_pk_fp8_f32 v181, v70, v71 op_sel:[0,0,1]
	v_mul_f32_e32 v70, v179, v103
	v_mul_f32_e32 v71, v179, v115
	v_cvt_pk_fp8_f32 v182, v70, v71 op_sel:[0,0,1]
	v_mul_f32_e32 v70, v179, v123
	v_mul_f32_e32 v71, v179, v127
	v_cvt_pk_fp8_f32 v183, v70, v71 op_sel:[0,0,1]
	v_mul_f32_e32 v66, v179, v68
	v_mul_f32_e32 v67, v179, v72
	v_mul_f32_e32 v68, v179, v76
	ds_write_b128 v159, v[180:183] offset:256
	v_mov_b32_e32 v180, 0
	v_cvt_pk_fp8_f32 v180, v66, v67
	v_mul_f32_e32 v66, v179, v80
	v_mul_f32_e32 v67, v179, v92
	v_mov_b32_e32 v181, 0
	v_cvt_pk_fp8_f32 v181, v66, v67
	v_mul_f32_e32 v66, v179, v88
	v_mul_f32_e32 v67, v179, v100
	v_mov_b32_e32 v182, 0
	v_cvt_pk_fp8_f32 v182, v66, v67
	v_mul_f32_e32 v66, v179, v112
	v_mul_f32_e32 v67, v179, v120
	v_mov_b32_e32 v183, 0
	v_mul_f32_e32 v70, v179, v84
	v_cvt_pk_fp8_f32 v183, v66, v67
	v_cvt_pk_fp8_f32 v180, v68, v70 op_sel:[0,0,1]
	v_mul_f32_e32 v68, v179, v96
	v_mul_f32_e32 v70, v179, v108
	v_cvt_pk_fp8_f32 v181, v68, v70 op_sel:[0,0,1]
	v_mul_f32_e32 v68, v179, v104
	v_mul_f32_e32 v70, v179, v116
	v_cvt_pk_fp8_f32 v182, v68, v70 op_sel:[0,0,1]
	v_mul_f32_e32 v68, v179, v124
	v_mul_f32_e32 v70, v179, v128
	v_cvt_pk_fp8_f32 v183, v68, v70 op_sel:[0,0,1]
	v_mul_f32_e32 v67, v179, v69
	v_mul_f32_e32 v68, v179, v73
	v_mov_b32_e32 v66, 0
	v_cvt_pk_fp8_f32 v66, v67, v68
	v_mul_f32_e32 v69, v179, v77
	v_mul_f32_e32 v70, v179, v85
	v_mul_f32_e32 v68, v179, v81
	v_cvt_pk_fp8_f32 v66, v69, v70 op_sel:[0,0,1]
	v_mul_f32_e32 v69, v179, v93
	v_mov_b32_e32 v67, 0
	v_cvt_pk_fp8_f32 v67, v68, v69
	v_mul_f32_e32 v70, v179, v97
	v_mul_f32_e32 v71, v179, v109
	v_mul_f32_e32 v69, v179, v89
	v_cvt_pk_fp8_f32 v67, v70, v71 op_sel:[0,0,1]
	v_mul_f32_e32 v70, v179, v101
	v_mov_b32_e32 v68, 0
	v_cvt_pk_fp8_f32 v68, v69, v70
	v_mul_f32_e32 v71, v179, v105
	v_mul_f32_e32 v72, v179, v117
	v_mul_f32_e32 v70, v179, v113
	v_cvt_pk_fp8_f32 v68, v71, v72 op_sel:[0,0,1]
	v_mul_f32_e32 v71, v179, v121
	v_mov_b32_e32 v69, 0
	v_cvt_pk_fp8_f32 v69, v70, v71
	v_mul_f32_e32 v72, v179, v125
	v_mul_f32_e32 v73, v179, v129
	s_mov_b32 s2, 0x180000
	v_cvt_pk_fp8_f32 v69, v72, v73 op_sel:[0,0,1]
	ds_write_b128 v159, v[180:183] offset:512
	s_waitcnt vmcnt(15)
; __device__ __forceinline__ unsigned pk4_fp8(float a, float b, float c, float d) { unsigned w = 0u; w = __builtin_amdgcn_cvt_pk_fp8_f32(a, b, w, false); w = __builtin_amdgcn_cvt_pk_fp8_f32(c, d, w, true); return w; }
; #define LAS __attribute__((address_space(3)))
; #define CVT_LOAD(v, c, s_) do { _Pragma("unroll") for (int i_ = 0; i_ < 16; ++i_) v[i_] = *(const f32x4*)((c).src + (size_t)(64 * (s_) + i_) * (c).N); } while (0)
; __device__ __forceinline__ void cvt_pack8(const f32x4 (&v)[16], const CvtItem& c, LAS unsigned char* blk, int s4, int lane) {
;     const float w = c.wscale; const int cb = lane & 15, j = 4 * s4 + (lane >> 4);
; #pragma unroll
;     for (int jn = 0; jn < 4; ++jn) {
;         v4u o; o.x = pg8::pk4_fp8(v[0][jn] * w, v[1][jn] * w, v[2][jn] * w, v[3][jn] * w); o.y = pg8::pk4_fp8(v[4][jn] * w, v[5][jn] * w, v[6][jn] * w, v[7][jn] * w);
;         o.z = pg8::pk4_fp8(v[8][jn] * w, v[9][jn] * w, v[10][jn] * w, v[11][jn] * w); o.w = pg8::pk4_fp8(v[12][jn] * w, v[13][jn] * w, v[14][jn] * w, v[15][jn] * w);
;         *(LAS v4u*)(blk + (4 * cb + jn) * 256 + ((j ^ cb) * 16)) = o; }
; }
; __device__ __forceinline__ void cvt_moe_pipe2(const CvtSrc& A, const CvtSrc& B, LAS float* scr, int gw, int NGW, int lane) {
;     ...
;     while (it < it1) {
;         const int i1 = it + NGW; const bool more = i1 < it1;
;         CVT_LOAD(vb, c, 1); cvt_pack8(va, c, blk, 0, lane);
;         CVT_LOAD(va, c, 2); cvt_pack8(vb, c, blk, 1, lane);
;         CVT_LOAD(vb, c, 3); cvt_pack8(va, c, blk, 2, lane);
;         if (more) { cn = cvt_moe_item2(i1, A, B, lane); CVT_LOAD(va, cn, 0); }
;         cvt_pack8(vb, c, blk, 3, lane);
	v_mul_f32_e32 v130, v179, v62
	s_waitcnt vmcnt(14)
	v_mul_f32_e32 v137, v179, v6
	ds_write_b128 v159, v[66:69] offset:768
	v_add_co_u32_e32 v66, vcc, s2, v132
	s_mov_b32 s2, 0x182000
	s_nop 0
	v_addc_co_u32_e32 v67, vcc, 0, v133, vcc
	v_add_co_u32_e32 v70, vcc, s2, v132
	s_mov_b32 s2, 0x184000
	s_nop 0
	v_addc_co_u32_e32 v71, vcc, 0, v133, vcc
	v_add_co_u32_e32 v74, vcc, s2, v132
	s_mov_b32 s2, 0x186000
	s_nop 0
	v_addc_co_u32_e32 v75, vcc, 0, v133, vcc
	v_add_co_u32_e32 v78, vcc, s2, v132
	s_mov_b32 s2, 0x188000
	s_nop 0
	v_addc_co_u32_e32 v79, vcc, 0, v133, vcc
	global_load_dwordx4 v[74:77], v[74:75], off nt
	v_mov_b32_e32 v180, 0
	global_load_dwordx4 v[82:85], v[78:79], off nt
	v_add_co_u32_e32 v78, vcc, s2, v132
	s_mov_b32 s2, 0x18a000
	s_nop 0
	v_addc_co_u32_e32 v79, vcc, 0, v133, vcc
	v_add_co_u32_e32 v86, vcc, s2, v132
	s_mov_b32 s2, 0x18c000
	s_nop 0
	v_addc_co_u32_e32 v87, vcc, 0, v133, vcc
	global_load_dwordx4 v[78:81], v[78:79], off nt
	v_cvt_pk_fp8_f32 v180, v130, v137
	global_load_dwordx4 v[90:93], v[86:87], off nt
	v_add_co_u32_e32 v86, vcc, s2, v132
	s_mov_b32 s2, 0x18e000
	s_nop 0
	v_addc_co_u32_e32 v87, vcc, 0, v133, vcc
	global_load_dwordx4 v[94:97], v[86:87], off nt
	v_add_co_u32_e32 v86, vcc, s2, v132
	s_mov_b32 s2, 0x190000
	s_nop 0
	v_addc_co_u32_e32 v87, vcc, 0, v133, vcc
	global_load_dwordx4 v[106:109], v[86:87], off nt
	v_add_co_u32_e32 v86, vcc, s2, v132
	s_mov_b32 s2, 0x192000
	s_nop 0
	v_addc_co_u32_e32 v87, vcc, 0, v133, vcc
	v_add_co_u32_e32 v98, vcc, s2, v132
	s_mov_b32 s2, 0x194000
	s_nop 0
	v_addc_co_u32_e32 v99, vcc, 0, v133, vcc
	v_add_co_u32_e32 v102, vcc, s2, v132
	s_waitcnt vmcnt(19)
	v_mul_f32_e32 v181, v179, v2
	s_waitcnt vmcnt(18)
	v_mul_f32_e32 v182, v179, v18
	v_addc_co_u32_e32 v103, vcc, 0, v133, vcc
	s_mov_b32 s2, 0x196000
	v_cvt_pk_fp8_f32 v180, v181, v182 op_sel:[0,0,1]
	s_waitcnt vmcnt(17)
	v_mul_f32_e32 v130, v179, v10
	s_waitcnt vmcnt(16)
	v_mul_f32_e32 v137, v179, v26
	v_mov_b32_e32 v181, 0
	v_add_co_u32_e32 v110, vcc, s2, v132
	v_cvt_pk_fp8_f32 v181, v130, v137
	s_nop 0
	v_addc_co_u32_e32 v111, vcc, 0, v133, vcc
	s_mov_b32 s2, 0x198000
	global_load_dwordx4 v[102:105], v[102:103], off nt
	s_waitcnt vmcnt(16)
	v_mul_f32_e32 v182, v179, v22
	global_load_dwordx4 v[114:117], v[110:111], off nt
	v_add_co_u32_e32 v110, vcc, s2, v132
	s_mov_b32 s2, 0x19a000
	s_nop 0
	v_addc_co_u32_e32 v111, vcc, 0, v133, vcc
	s_waitcnt vmcnt(16)
	v_mul_f32_e32 v183, v179, v42
	v_add_co_u32_e32 v118, vcc, s2, v132
	v_cvt_pk_fp8_f32 v181, v182, v183 op_sel:[0,0,1]
	s_waitcnt vmcnt(15)
	v_mul_f32_e32 v130, v179, v14
	s_waitcnt vmcnt(14)
	v_mul_f32_e32 v137, v179, v34
	v_mov_b32_e32 v182, 0
	v_addc_co_u32_e32 v119, vcc, 0, v133, vcc
	s_mov_b32 s2, 0x19c000
	v_cvt_pk_fp8_f32 v182, v130, v137
	v_add_co_u32_e32 v122, vcc, s2, v132
	s_mov_b32 s2, 0x19e000
	s_nop 0
	v_addc_co_u32_e32 v123, vcc, 0, v133, vcc
	v_add_co_u32_e32 v126, vcc, s2, v132
	s_waitcnt vmcnt(13)
	v_mul_f32_e32 v183, v179, v30
	s_waitcnt vmcnt(12)
	v_mul_f32_e32 v184, v179, v46
	v_addc_co_u32_e32 v127, vcc, 0, v133, vcc
	v_cvt_pk_fp8_f32 v182, v183, v184 op_sel:[0,0,1]
	s_waitcnt vmcnt(11)
	v_mul_f32_e32 v130, v179, v38
	s_waitcnt vmcnt(10)
	v_mul_f32_e32 v137, v179, v54
	v_mov_b32_e32 v183, 0
	global_load_dwordx4 v[66:69], v[66:67], off nt
	v_cvt_pk_fp8_f32 v183, v130, v137
	global_load_dwordx4 v[70:73], v[70:71], off nt
	s_waitcnt vmcnt(11)
	v_mul_f32_e32 v184, v179, v50
	global_load_dwordx4 v[86:89], v[86:87], off nt
	s_waitcnt vmcnt(11)
	v_mul_f32_e32 v185, v179, v58
	global_load_dwordx4 v[98:101], v[98:99], off nt
	v_cvt_pk_fp8_f32 v183, v184, v185 op_sel:[0,0,1]
	global_load_dwordx4 v[110:113], v[110:111], off nt
	v_mul_f32_e32 v130, v179, v63
	global_load_dwordx4 v[118:121], v[118:119], off nt
	ds_write_b128 v160, v[180:183]
	global_load_dwordx4 v[122:125], v[122:123], off nt
	v_mul_f32_e32 v137, v179, v7
	global_load_dwordx4 v[126:129], v[126:127], off nt
	v_mov_b32_e32 v180, 0
	v_cvt_pk_fp8_f32 v180, v130, v137
	v_mul_f32_e32 v181, v179, v3
	v_mul_f32_e32 v182, v179, v19
	v_mul_f32_e32 v130, v179, v11
	v_cvt_pk_fp8_f32 v180, v181, v182 op_sel:[0,0,1]
	v_mul_f32_e32 v137, v179, v27
	v_mov_b32_e32 v181, 0
	v_cvt_pk_fp8_f32 v181, v130, v137
	v_mul_f32_e32 v182, v179, v23
	v_mul_f32_e32 v183, v179, v43
	v_mul_f32_e32 v130, v179, v15
	v_cvt_pk_fp8_f32 v181, v182, v183 op_sel:[0,0,1]
	v_mul_f32_e32 v137, v179, v35
	v_mov_b32_e32 v182, 0
	v_cvt_pk_fp8_f32 v182, v130, v137
	v_mul_f32_e32 v183, v179, v31
	v_mul_f32_e32 v184, v179, v47
	v_mul_f32_e32 v130, v179, v39
	v_cvt_pk_fp8_f32 v182, v183, v184 op_sel:[0,0,1]
	v_mul_f32_e32 v137, v179, v55
	v_mov_b32_e32 v183, 0
	v_cvt_pk_fp8_f32 v183, v130, v137
	v_mul_f32_e32 v184, v179, v51
	v_mul_f32_e32 v185, v179, v59
	v_mul_f32_e32 v130, v179, v64
	v_cvt_pk_fp8_f32 v183, v184, v185 op_sel:[0,0,1]
	v_mul_f32_e32 v137, v179, v8
	v_mul_f32_e32 v184, v179, v48
	v_mul_f32_e32 v185, v179, v60
	ds_write_b128 v160, v[180:183] offset:256
	v_mov_b32_e32 v180, 0
	v_cvt_pk_fp8_f32 v180, v130, v137
	v_mul_f32_e32 v181, v179, v4
	v_mul_f32_e32 v182, v179, v20
	v_mul_f32_e32 v130, v179, v12
	v_cvt_pk_fp8_f32 v180, v181, v182 op_sel:[0,0,1]
	v_mul_f32_e32 v137, v179, v28
	v_mov_b32_e32 v181, 0
	v_cvt_pk_fp8_f32 v181, v130, v137
	v_mul_f32_e32 v182, v179, v24
	v_mul_f32_e32 v183, v179, v44
	v_mul_f32_e32 v130, v179, v16
	v_cvt_pk_fp8_f32 v181, v182, v183 op_sel:[0,0,1]
	v_mul_f32_e32 v137, v179, v36
	v_mov_b32_e32 v182, 0
	v_cvt_pk_fp8_f32 v182, v130, v137
	v_mul_f32_e32 v183, v179, v32
	v_mul_f32_e32 v130, v179, v40
	v_mul_f32_e32 v137, v179, v56
	v_cvt_pk_fp8_f32 v182, v183, v184 op_sel:[0,0,1]
	v_mov_b32_e32 v183, 0
	v_cvt_pk_fp8_f32 v183, v130, v137
	v_mul_f32_e32 v184, v179, v52
	v_mul_f32_e32 v130, v179, v65
	v_mul_f32_e32 v137, v179, v9
	v_cvt_pk_fp8_f32 v183, v184, v185 op_sel:[0,0,1]
	v_mul_f32_e32 v184, v179, v49
	v_mul_f32_e32 v185, v179, v61
	s_cmpk_gt_i32 s29, 0x50f
	ds_write_b128 v160, v[180:183] offset:512
	v_mov_b32_e32 v180, 0
	v_cvt_pk_fp8_f32 v180, v130, v137
	v_mul_f32_e32 v181, v179, v5
	v_mul_f32_e32 v182, v179, v21
	v_mul_f32_e32 v130, v179, v13
	v_cvt_pk_fp8_f32 v180, v181, v182 op_sel:[0,0,1]
	v_mul_f32_e32 v137, v179, v29
	v_mov_b32_e32 v181, 0
	v_cvt_pk_fp8_f32 v181, v130, v137
	v_mul_f32_e32 v182, v179, v25
	v_mul_f32_e32 v183, v179, v45
	v_mul_f32_e32 v130, v179, v17
	v_cvt_pk_fp8_f32 v181, v182, v183 op_sel:[0,0,1]
	v_mul_f32_e32 v137, v179, v37
	v_mov_b32_e32 v182, 0
	v_cvt_pk_fp8_f32 v182, v130, v137
	v_mul_f32_e32 v183, v179, v33
	v_mul_f32_e32 v130, v179, v41
	v_mul_f32_e32 v137, v179, v57
	v_cvt_pk_fp8_f32 v182, v183, v184 op_sel:[0,0,1]
	v_mov_b32_e32 v183, 0
	v_cvt_pk_fp8_f32 v183, v130, v137
	v_mul_f32_e32 v184, v179, v53
	s_cselect_b64 s[2:3], -1, 0
	s_and_b64 vcc, exec, s[2:3]
	v_cvt_pk_fp8_f32 v183, v184, v185 op_sel:[0,0,1]
	ds_write_b128 v160, v[180:183] offset:768
	s_cbranch_vccnz .LBB0_717
; #define CVT_LOAD(v, c, s_) do { _Pragma("unroll") for (int i_ = 0; i_ < 16; ++i_) v[i_] = *(const f32x4*)((c).src + (size_t)(64 * (s_) + i_) * (c).N); } while (0)
; __device__ __forceinline__ CvtItem cvt_moe_item(int it, const float* wg, const float* wu, const float* wd, unsigned char* WGU, unsigned char* WDN, int lane) {
;     const int which = it >> 11, r = it & 2047, e = r >> 7, q = r & 127; CvtItem c; c.which = which;
;     if (which < 2) { const int nb = q & 31, k0 = (q >> 5) * 256; c.nb = nb;
;         c.N = DFF; c.K = DM; c.wscale = which ? 64.f / LOG2E : 64.f * LOG2E; c.src = (which ? wu : wg) + (size_t)e * DM * DFF + (size_t)(k0 + 16 * (lane >> 4)) * DFF + nb * 64 + 4 * (lane & 15);
;         c.dst = WGU + (size_t)e * 4096 * DM + k0; }
;     else { const int nb = q & 15, k0 = (q >> 4) * 256; c.nb = nb;
;         c.N = DM; c.K = DFF; c.wscale = 64.f; c.src = wd + (size_t)e * DFF * DM + (size_t)(k0 + 16 * (lane >> 4)) * DM + nb * 64 + 4 * (lane & 15);
;         c.dst = WDN + (size_t)e * DM * DFF + k0; }
;     return c;
; }
; __device__ __forceinline__ void cvt_moe_pipe2(const CvtSrc& A, const CvtSrc& B, LAS float* scr, int gw, int NGW, int lane) {
;     ...
;         if (more) { cn = cvt_moe_item2(i1, A, B, lane); CVT_LOAD(va, cn, 0); }
	s_ashr_i32 s27, s29, 11
	s_and_b32 s28, s29, 31
	s_and_b32 s33, s25, 0x300
	s_cmpk_lt_u32 s29, 0x800
	s_cselect_b64 vcc, -1, 0
	v_readlane_b32 s36, v254, 30
	s_and_b64 s[8:9], vcc, exec
	v_readlane_b32 s48, v254, 42
	v_readlane_b32 s49, v254, 43
	v_readlane_b32 s50, v254, 44
	v_readlane_b32 s51, v254, 45
	s_cselect_b32 s4, s49, s51
	s_cselect_b32 s8, s48, s50
	s_bfe_u32 s34, s29, 0x40007
	s_lshl_b32 s9, s34, 23
	s_add_u32 s8, s8, s9
	v_or_b32_e32 v2, s33, v141
	s_addc_u32 s9, s4, 0
	v_lshlrev_b32_e32 v130, 13, v2
	v_lshl_add_u64 v[2:3], s[8:9], 0, v[130:131]
	s_lshl_b32 s4, s28, 8
	v_lshl_add_u64 v[2:3], v[2:3], 0, s[4:5]
	v_mov_b32_e32 v137, v131
	v_lshl_add_u64 v[132:133], v[2:3], 0, v[136:137]
	v_cndmask_b32_e32 v178, v139, v140, vcc
	v_add_co_u32_e32 v2, vcc, s24, v132
	s_lshl_b32 s4, s34, 22
	s_nop 0
	v_addc_co_u32_e32 v3, vcc, 0, v133, vcc
	v_add_co_u32_e32 v4, vcc, s23, v132
	v_readlane_b32 s8, v255, 1
	s_nop 0
	v_addc_co_u32_e32 v5, vcc, 0, v133, vcc
	v_add_co_u32_e32 v10, vcc, s22, v132
	global_load_dwordx4 v[6:9], v[2:3], off nt
	s_nop 0
	global_load_dwordx4 v[2:5], v[4:5], off nt
	v_addc_co_u32_e32 v11, vcc, 0, v133, vcc
	v_add_co_u32_e32 v12, vcc, s21, v132
	v_readlane_b32 s9, v255, 2
	s_nop 0
	v_addc_co_u32_e32 v13, vcc, 0, v133, vcc
	v_add_co_u32_e32 v14, vcc, s20, v132
	global_load_dwordx4 v[18:21], v[10:11], off nt
	s_nop 0
	global_load_dwordx4 v[10:13], v[12:13], off nt
	v_addc_co_u32_e32 v15, vcc, 0, v133, vcc
	v_add_co_u32_e32 v16, vcc, s19, v132
	s_add_u32 s4, s8, s4
	s_nop 0
	v_addc_co_u32_e32 v17, vcc, 0, v133, vcc
	global_load_dwordx4 v[26:29], v[14:15], off nt
	global_load_dwordx4 v[22:25], v[16:17], off nt
	v_add_co_u32_e32 v14, vcc, s18, v132
	s_addc_u32 s9, s9, 0
	s_nop 0
	v_addc_co_u32_e32 v15, vcc, 0, v133, vcc
	v_add_co_u32_e32 v16, vcc, s17, v132
	s_add_u32 s8, s4, s33
	s_nop 0
	v_addc_co_u32_e32 v17, vcc, 0, v133, vcc
	v_add_co_u32_e32 v30, vcc, s16, v132
	global_load_dwordx4 v[42:45], v[14:15], off nt
	s_nop 0
	global_load_dwordx4 v[14:17], v[16:17], off nt
	v_addc_co_u32_e32 v31, vcc, 0, v133, vcc
	v_add_co_u32_e32 v32, vcc, s15, v132
	s_addc_u32 s9, s9, 0
	s_nop 0
	v_addc_co_u32_e32 v33, vcc, 0, v133, vcc
	v_add_co_u32_e32 v38, vcc, s14, v132
	global_load_dwordx4 v[34:37], v[30:31], off nt
	s_nop 0
	global_load_dwordx4 v[30:33], v[32:33], off nt
	v_addc_co_u32_e32 v39, vcc, 0, v133, vcc
	v_add_co_u32_e32 v40, vcc, s13, v132
	v_readlane_b32 s37, v254, 31
	s_nop 0
	v_addc_co_u32_e32 v41, vcc, 0, v133, vcc
	v_add_co_u32_e32 v50, vcc, s12, v132
	global_load_dwordx4 v[46:49], v[38:39], off nt
	s_nop 0
	global_load_dwordx4 v[38:41], v[40:41], off nt
	v_addc_co_u32_e32 v51, vcc, 0, v133, vcc
	v_add_co_u32_e32 v52, vcc, s11, v132
	v_readlane_b32 s38, v254, 32
	s_nop 0
	v_addc_co_u32_e32 v53, vcc, 0, v133, vcc
	v_add_co_u32_e32 v58, vcc, s10, v132
	global_load_dwordx4 v[54:57], v[50:51], off nt
	s_nop 0
	global_load_dwordx4 v[50:53], v[52:53], off nt
	v_addc_co_u32_e32 v59, vcc, 0, v133, vcc
	global_load_dwordx4 v[62:65], v[132:133], off nt
	s_nop 0
	global_load_dwordx4 v[58:61], v[58:59], off nt
	v_readlane_b32 s39, v254, 33
	v_readlane_b32 s40, v254, 34
	v_readlane_b32 s41, v254, 35
	v_readlane_b32 s42, v254, 36
	v_readlane_b32 s43, v254, 37
	v_readlane_b32 s44, v254, 38
	v_readlane_b32 s45, v254, 39
	v_readlane_b32 s46, v254, 40
	v_readlane_b32 s47, v254, 41
	s_branch .LBB0_717

; #define LAS __attribute__((address_space(3)))
; #define CVT_LOAD(v, c, s_) do { _Pragma("unroll") for (int i_ = 0; i_ < 16; ++i_) v[i_] = *(const f32x4*)((c).src + (size_t)(64 * (s_) + i_) * (c).N); } while (0)
; __device__ __forceinline__ CvtItem cvt_moe_item(int it, const float* wg, const float* wu, const float* wd, unsigned char* WGU, unsigned char* WDN, int lane) {
;     const int which = it >> 11, r = it & 2047, e = r >> 7, q = r & 127; CvtItem c; c.which = which;
;     if (which < 2) { const int nb = q & 31, k0 = (q >> 5) * 256; c.nb = nb;
;         c.N = DFF; c.K = DM; c.wscale = which ? 64.f / LOG2E : 64.f * LOG2E; c.src = (which ? wu : wg) + (size_t)e * DM * DFF + (size_t)(k0 + 16 * (lane >> 4)) * DFF + nb * 64 + 4 * (lane & 15);
;         c.dst = WGU + (size_t)e * 4096 * DM + k0; }
;     else { const int nb = q & 15, k0 = (q >> 4) * 256; c.nb = nb;
;         c.N = DM; c.K = DFF; c.wscale = 64.f; c.src = wd + (size_t)e * DFF * DM + (size_t)(k0 + 16 * (lane >> 4)) * DM + nb * 64 + 4 * (lane & 15);
;         c.dst = WDN + (size_t)e * DM * DFF + k0; }
;     return c;
; }
; __device__ __forceinline__ void cvt_moe_pipe2(const CvtSrc& A, const CvtSrc& B, LAS float* scr, int gw, int NGW, int lane) {
;     LAS unsigned char* blk = (LAS unsigned char*)scr;
;     f32x4 va[16], vb[16]; CvtItem c, cn;
;     const int it1 = A.n + B.n; int it = gw;
;     if (it < it1) { c = cvt_moe_item2(it, A, B, lane); CVT_LOAD(va, c, 0); }
.LBB0_721:
	s_andn2_b64 vcc, exec, s[2:3]
	s_cbranch_vccnz .LBB0_744
	v_readlane_b32 s2, v254, 10
	s_lshl_b32 s8, s2, 3
	v_readlane_b32 s2, v254, 59
	s_add_i32 s8, s8, s2
	s_add_i32 s2, s8, 0xfffffe00
	s_cmpk_gt_i32 s2, 0x50f
	s_cbranch_scc1 .LBB0_727
	v_readlane_b32 s28, v254, 52
	s_lshl_b32 s4, s2, 3
	s_add_i32 s3, s28, 0xfffffe00
	s_ashr_i32 s29, s2, 11
	s_and_b32 s30, s2, 31
	s_and_b32 s9, s4, 0x300
	s_cmpk_lt_u32 s2, 0x800
	s_cselect_b64 vcc, -1, 0
	v_readlane_b32 s12, v254, 30
	s_and_b64 s[4:5], vcc, exec
	v_readlane_b32 s24, v254, 42
	v_readlane_b32 s25, v254, 43
	v_readlane_b32 s26, v254, 44
	v_readlane_b32 s27, v254, 45
	v_readlane_b32 s13, v254, 31
	s_cselect_b32 s4, s25, s27
	s_cselect_b32 s10, s24, s26
	s_bfe_u32 s11, s2, 0x40007
	s_lshl_b32 s6, s11, 22
	v_readlane_b32 s12, v255, 1
	v_readlane_b32 s13, v255, 2
	s_add_u32 s6, s12, s6
	s_addc_u32 s7, s13, 0
	s_add_u32 s6, s6, s9
	s_addc_u32 s7, s7, 0
	s_lshl_b32 s11, s11, 23
	v_and_b32_e32 v141, 48, v1
	s_add_u32 s10, s10, s11
	v_or_b32_e32 v2, s9, v141
	s_addc_u32 s11, s4, 0
	v_lshlrev_b32_e32 v130, 13, v2
	v_mov_b32_e32 v131, 0
	v_lshlrev_b32_e32 v4, 2, v138
	s_mov_b32 s5, 0
	v_lshl_add_u64 v[2:3], s[10:11], 0, v[130:131]
	s_lshl_b32 s4, s30, 8
	s_waitcnt vmcnt(0)
	v_and_b32_e32 v66, 60, v4
	v_lshl_add_u64 v[2:3], v[2:3], 0, s[4:5]
	v_lshlrev_b32_e32 v130, 2, v66
	v_mov_b32_e32 v139, 0x42317218
	v_mov_b32_e32 v140, 0x42b8aa3b
	v_lshl_add_u64 v[132:133], v[2:3], 0, v[130:131]
	s_mov_b32 s10, 0x1e000
	v_cndmask_b32_e32 v177, v139, v140, vcc
	v_add_co_u32_e32 v2, vcc, s10, v132
	s_mov_b32 s11, 0x1c000
	s_nop 0
	v_addc_co_u32_e32 v3, vcc, 0, v133, vcc
	v_add_co_u32_e32 v4, vcc, s11, v132
	s_mov_b32 s12, 0x1a000
	s_nop 0
	v_addc_co_u32_e32 v5, vcc, 0, v133, vcc
	global_load_dwordx4 v[58:61], v[2:3], off nt
	global_load_dwordx4 v[50:53], v[4:5], off nt
	v_add_co_u32_e32 v2, vcc, s12, v132
	s_mov_b32 s13, 0x18000
	s_nop 0
	v_addc_co_u32_e32 v3, vcc, 0, v133, vcc
	v_readlane_b32 s14, v254, 32
	v_add_co_u32_e32 v4, vcc, s13, v132
	s_mov_b32 s14, 0x16000
	s_nop 0
	v_addc_co_u32_e32 v5, vcc, 0, v133, vcc
	v_readlane_b32 s15, v254, 33
	global_load_dwordx4 v[54:57], v[2:3], off nt
	global_load_dwordx4 v[38:41], v[4:5], off nt
	v_add_co_u32_e32 v2, vcc, s14, v132
	s_mov_b32 s15, 0x14000
	s_nop 0
	v_addc_co_u32_e32 v3, vcc, 0, v133, vcc
	v_readlane_b32 s16, v254, 34
	v_add_co_u32_e32 v4, vcc, s15, v132
	s_mov_b32 s16, 0x12000
	s_nop 0
	v_addc_co_u32_e32 v5, vcc, 0, v133, vcc
	v_readlane_b32 s17, v254, 35
	global_load_dwordx4 v[46:49], v[2:3], off nt
	global_load_dwordx4 v[30:33], v[4:5], off nt
	v_add_co_u32_e32 v2, vcc, s16, v132
	s_mov_b32 s17, 0x10000
	s_nop 0
	v_addc_co_u32_e32 v3, vcc, 0, v133, vcc
	v_readlane_b32 s18, v254, 36
	v_add_co_u32_e32 v4, vcc, s17, v132
	s_mov_b32 s18, 0xe000
	s_nop 0
	v_addc_co_u32_e32 v5, vcc, 0, v133, vcc
	v_readlane_b32 s19, v254, 37
	global_load_dwordx4 v[34:37], v[2:3], off nt
	global_load_dwordx4 v[14:17], v[4:5], off nt
	v_add_co_u32_e32 v2, vcc, s18, v132
	s_mov_b32 s19, 0xc000
	s_nop 0
	v_addc_co_u32_e32 v3, vcc, 0, v133, vcc
	v_readlane_b32 s20, v254, 38
	v_add_co_u32_e32 v4, vcc, s19, v132
	s_mov_b32 s20, 0xa000
	s_nop 0
	v_addc_co_u32_e32 v5, vcc, 0, v133, vcc
	v_readlane_b32 s21, v254, 39
	global_load_dwordx4 v[42:45], v[2:3], off nt
	global_load_dwordx4 v[22:25], v[4:5], off nt
	v_add_co_u32_e32 v2, vcc, s20, v132
	s_mov_b32 s21, 0x8000
	s_nop 0
	v_addc_co_u32_e32 v3, vcc, 0, v133, vcc
	v_readlane_b32 s22, v254, 40
	v_add_co_u32_e32 v4, vcc, s21, v132
	s_movk_i32 s22, 0x6000
	s_nop 0
	v_addc_co_u32_e32 v5, vcc, 0, v133, vcc
	v_readlane_b32 s23, v254, 41
	global_load_dwordx4 v[26:29], v[2:3], off nt
	global_load_dwordx4 v[10:13], v[4:5], off nt
	v_add_co_u32_e32 v2, vcc, s22, v132
	s_movk_i32 s23, 0x4000
	s_nop 0
	v_addc_co_u32_e32 v3, vcc, 0, v133, vcc
	v_add_co_u32_e32 v4, vcc, s23, v132
	s_movk_i32 s24, 0x2000
	s_nop 0
	v_addc_co_u32_e32 v5, vcc, 0, v133, vcc
	v_add_co_u32_e32 v6, vcc, s24, v132
	global_load_dwordx4 v[18:21], v[2:3], off nt
	s_nop 0
	global_load_dwordx4 v[2:5], v[4:5], off nt
	v_addc_co_u32_e32 v7, vcc, 0, v133, vcc
	global_load_dwordx4 v[6:9], v[6:7], off nt
	s_nop 0
	global_load_dwordx4 v[62:65], v[132:133], off nt
	v_lshrrev_b32_e32 v138, 4, v138
	v_and_b32_e32 v67, 15, v1
	v_bitop3_b32 v1, v138, v1, 15 bitop3:0x78
	v_readlane_b32 s4, v254, 60
	v_lshlrev_b32_e32 v69, 4, v1
	v_or_b32_e32 v1, 4, v138
	v_or_b32_e32 v142, 8, v138
	v_or_b32_e32 v143, 12, v138
	v_or_b32_e32 v144, 16, v138
	v_or_b32_e32 v145, 20, v138
	v_or_b32_e32 v146, 24, v138
	v_or_b32_e32 v147, 28, v138
	v_or_b32_e32 v148, 32, v138
	v_or_b32_e32 v149, 36, v138
	v_or_b32_e32 v150, 40, v138
	v_or_b32_e32 v151, 44, v138
	v_or_b32_e32 v152, 48, v138
	v_or_b32_e32 v153, 52, v138
	v_or_b32_e32 v154, 56, v138
	v_or_b32_e32 v155, 60, v138
	s_add_i32 s8, s8, s28
	v_lshl_add_u32 v68, v67, 10, s4
	v_bitop3_b32 v70, v138, v67, 4 bitop3:0x36
	v_bitop3_b32 v71, v138, v67, 8 bitop3:0x36
	v_bitop3_b32 v72, v138, v67, 12 bitop3:0x36
	v_lshlrev_b32_e32 v134, 4, v67
	v_lshl_add_u32 v67, v138, 8, s4
	v_lshl_add_u32 v73, v1, 8, s4
	v_lshl_add_u32 v75, v142, 8, s4
	v_lshl_add_u32 v77, v143, 8, s4
	v_lshl_add_u32 v79, v144, 8, s4
	v_lshl_add_u32 v81, v145, 8, s4
	v_lshl_add_u32 v83, v146, 8, s4
	v_lshl_add_u32 v85, v147, 8, s4
	v_lshl_add_u32 v87, v148, 8, s4
	v_lshl_add_u32 v89, v149, 8, s4
	v_lshl_add_u32 v91, v150, 8, s4
	v_lshl_add_u32 v93, v151, 8, s4
	v_lshl_add_u32 v95, v152, 8, s4
	v_lshl_add_u32 v97, v153, 8, s4
	v_lshl_add_u32 v99, v154, 8, s4
	v_lshl_add_u32 v101, v155, 8, s4
	s_lshl_b32 s4, s8, 3
	s_add_i32 s25, s4, 0xffffe000
	v_readlane_b32 s4, v254, 9
	v_lshlrev_b32_e32 v70, 4, v70
	v_lshlrev_b32_e32 v71, 4, v71
	v_lshlrev_b32_e32 v72, 4, v72
	v_xor_b32_e32 v74, 16, v134
	v_xor_b32_e32 v76, 32, v134
	v_xor_b32_e32 v78, 48, v134
	v_xor_b32_e32 v80, 64, v134
	v_xor_b32_e32 v82, 0x50, v134
	v_xor_b32_e32 v84, 0x60, v134
	v_xor_b32_e32 v86, 0x70, v134
	v_xor_b32_e32 v88, 0x80, v134
	v_xor_b32_e32 v90, 0x90, v134
	v_xor_b32_e32 v92, 0xa0, v134
	v_xor_b32_e32 v94, 0xb0, v134
	v_xor_b32_e32 v96, 0xc0, v134
	v_xor_b32_e32 v98, 0xd0, v134
	v_xor_b32_e32 v100, 0xe0, v134
	v_xor_b32_e32 v102, 0xf0, v134
	s_lshl_b32 s26, s4, 6
	v_mov_b32_e32 v135, v131
	s_addk_i32 s26, 0xf000
	v_add_u32_e32 v156, v68, v69
	v_add_u32_e32 v157, v68, v70
	v_add_u32_e32 v158, v68, v71
	v_lshlrev_b32_e32 v136, 2, v66
	v_add_u32_e32 v159, v68, v72
	v_add_u32_e32 v160, v67, v134
	v_add_u32_e32 v161, v73, v74
	v_add_u32_e32 v162, v75, v76
	v_add_u32_e32 v163, v77, v78
	v_add_u32_e32 v164, v79, v80
	v_add_u32_e32 v165, v81, v82
	v_add_u32_e32 v166, v83, v84
	v_add_u32_e32 v167, v85, v86
	v_add_u32_e32 v168, v87, v88
	v_add_u32_e32 v169, v89, v90
	v_add_u32_e32 v170, v91, v92
	v_add_u32_e32 v171, v93, v94
	v_add_u32_e32 v172, v95, v96
	v_add_u32_e32 v173, v97, v98
	v_add_u32_e32 v174, v99, v100
	v_add_u32_e32 v175, v101, v102
	s_branch .LBB0_725

; __device__ __forceinline__ unsigned pk4_fp8(float a, float b, float c, float d) { unsigned w = 0u; w = __builtin_amdgcn_cvt_pk_fp8_f32(a, b, w, false); w = __builtin_amdgcn_cvt_pk_fp8_f32(c, d, w, true); return w; }
; #define LAS __attribute__((address_space(3)))
; #define CVT_LOAD(v, c, s_) do { _Pragma("unroll") for (int i_ = 0; i_ < 16; ++i_) v[i_] = *(const f32x4*)((c).src + (size_t)(64 * (s_) + i_) * (c).N); } while (0)
; __device__ __forceinline__ void cvt_pack8(const f32x4 (&v)[16], const CvtItem& c, LAS unsigned char* blk, int s4, int lane) {
;     const float w = c.wscale; const int cb = lane & 15, j = 4 * s4 + (lane >> 4);
; #pragma unroll
;     for (int jn = 0; jn < 4; ++jn) {
;         v4u o; o.x = pg8::pk4_fp8(v[0][jn] * w, v[1][jn] * w, v[2][jn] * w, v[3][jn] * w); o.y = pg8::pk4_fp8(v[4][jn] * w, v[5][jn] * w, v[6][jn] * w, v[7][jn] * w);
;         o.z = pg8::pk4_fp8(v[8][jn] * w, v[9][jn] * w, v[10][jn] * w, v[11][jn] * w); o.w = pg8::pk4_fp8(v[12][jn] * w, v[13][jn] * w, v[14][jn] * w, v[15][jn] * w);
;         *(LAS v4u*)(blk + (4 * cb + jn) * 256 + ((j ^ cb) * 16)) = o; }
; }
; __device__ __forceinline__ void cvt_moe_pipe2(const CvtSrc& A, const CvtSrc& B, LAS float* scr, int gw, int NGW, int lane) {
;     ...
;     while (it < it1) {
;         const int i1 = it + NGW; const bool more = i1 < it1;
;         CVT_LOAD(vb, c, 1); cvt_pack8(va, c, blk, 0, lane);
;         CVT_LOAD(va, c, 2); cvt_pack8(vb, c, blk, 1, lane);
;         CVT_LOAD(vb, c, 3); cvt_pack8(va, c, blk, 2, lane);
.LBB0_725:
	s_mov_b32 s31, 0x80000
	v_add_co_u32_e32 v66, vcc, s31, v132
	s_mov_b32 s31, 0x82000
	s_nop 0
	v_addc_co_u32_e32 v67, vcc, 0, v133, vcc
	v_add_co_u32_e32 v70, vcc, s31, v132
	s_mov_b32 s31, 0x84000
	s_nop 0
	v_addc_co_u32_e32 v71, vcc, 0, v133, vcc
	v_add_co_u32_e32 v74, vcc, s31, v132
	s_mov_b32 s31, 0x86000
	s_nop 0
	v_addc_co_u32_e32 v75, vcc, 0, v133, vcc
	v_add_co_u32_e32 v78, vcc, s31, v132
	s_mov_b32 s31, 0x88000
	s_nop 0
	v_addc_co_u32_e32 v79, vcc, 0, v133, vcc
	global_load_dwordx4 v[82:85], v[78:79], off nt
	v_add_co_u32_e32 v78, vcc, s31, v132
	s_mov_b32 s31, 0x8a000
	s_nop 0
	v_addc_co_u32_e32 v79, vcc, 0, v133, vcc
	v_add_co_u32_e32 v86, vcc, s31, v132
	s_mov_b32 s31, 0x8c000
	s_nop 0
	v_addc_co_u32_e32 v87, vcc, 0, v133, vcc
	global_load_dwordx4 v[90:93], v[86:87], off nt
	v_add_co_u32_e32 v86, vcc, s31, v132
	s_mov_b32 s31, 0x8e000
	s_nop 0
	v_addc_co_u32_e32 v87, vcc, 0, v133, vcc
	global_load_dwordx4 v[94:97], v[86:87], off nt
	v_add_co_u32_e32 v86, vcc, s31, v132
	s_mov_b32 s31, 0x90000
	s_nop 0
	v_addc_co_u32_e32 v87, vcc, 0, v133, vcc
	global_load_dwordx4 v[106:109], v[86:87], off nt
	v_add_co_u32_e32 v86, vcc, s31, v132
	s_mov_b32 s31, 0x92000
	s_nop 0
	v_addc_co_u32_e32 v87, vcc, 0, v133, vcc
	v_add_co_u32_e32 v98, vcc, s31, v132
	s_mov_b32 s31, 0x94000
	s_nop 0
	v_addc_co_u32_e32 v99, vcc, 0, v133, vcc
	v_add_co_u32_e32 v102, vcc, s31, v132
	s_waitcnt vmcnt(4)
	v_mul_f32_e32 v62, v62, v177
	v_mul_f32_e32 v6, v6, v177
	v_mov_b32_e32 v178, 0
	v_addc_co_u32_e32 v103, vcc, 0, v133, vcc
	s_mov_b32 s31, 0x96000
	v_cvt_pk_fp8_f32 v178, v62, v6
	v_add_co_u32_e32 v110, vcc, s31, v132
	s_mov_b32 s31, 0x98000
	s_nop 0
	v_addc_co_u32_e32 v111, vcc, 0, v133, vcc
	global_load_dwordx4 v[102:105], v[102:103], off nt
	v_mul_f32_e32 v2, v2, v177
	global_load_dwordx4 v[114:117], v[110:111], off nt
	v_add_co_u32_e32 v110, vcc, s31, v132
	v_mul_f32_e32 v18, v18, v177
	global_load_dwordx4 v[66:69], v[66:67], off nt
	v_addc_co_u32_e32 v111, vcc, 0, v133, vcc
	global_load_dwordx4 v[70:73], v[70:71], off nt
	s_mov_b32 s31, 0x9a000
	v_cvt_pk_fp8_f32 v178, v2, v18 op_sel:[0,0,1]
	v_mul_f32_e32 v2, v10, v177
	v_mul_f32_e32 v6, v26, v177
	v_mov_b32_e32 v179, 0
	global_load_dwordx4 v[78:81], v[78:79], off nt
	v_add_co_u32_e32 v118, vcc, s31, v132
	v_cvt_pk_fp8_f32 v179, v2, v6
	v_mul_f32_e32 v2, v14, v177
	v_mul_f32_e32 v6, v34, v177
	v_mov_b32_e32 v180, 0
	global_load_dwordx4 v[86:89], v[86:87], off nt
	v_addc_co_u32_e32 v119, vcc, 0, v133, vcc
	global_load_dwordx4 v[98:101], v[98:99], off nt
	s_mov_b32 s31, 0x9c000
	v_cvt_pk_fp8_f32 v180, v2, v6
	v_mul_f32_e32 v2, v38, v177
	v_mul_f32_e32 v6, v54, v177
	v_mov_b32_e32 v181, 0
	global_load_dwordx4 v[110:113], v[110:111], off nt
	v_add_co_u32_e32 v122, vcc, s31, v132
	global_load_dwordx4 v[118:121], v[118:119], off nt
	v_cvt_pk_fp8_f32 v181, v2, v6
	global_load_dwordx4 v[74:77], v[74:75], off nt
	v_addc_co_u32_e32 v123, vcc, 0, v133, vcc
	s_mov_b32 s31, 0x9e000
	v_mul_f32_e32 v10, v22, v177
	v_mul_f32_e32 v18, v42, v177
	v_add_co_u32_e32 v126, vcc, s31, v132
	v_cvt_pk_fp8_f32 v179, v10, v18 op_sel:[0,0,1]
	v_mul_f32_e32 v10, v30, v177
	v_mul_f32_e32 v14, v46, v177
	v_addc_co_u32_e32 v127, vcc, 0, v133, vcc
	v_cvt_pk_fp8_f32 v180, v10, v14 op_sel:[0,0,1]
	v_mul_f32_e32 v10, v50, v177
	v_mul_f32_e32 v14, v58, v177
	global_load_dwordx4 v[122:125], v[122:123], off nt
	v_cvt_pk_fp8_f32 v181, v10, v14 op_sel:[0,0,1]
	global_load_dwordx4 v[126:129], v[126:127], off nt
	v_mul_f32_e32 v2, v63, v177
	v_mul_f32_e32 v6, v7, v177
	ds_write_b128 v156, v[178:181]
	v_mov_b32_e32 v178, 0
	v_cvt_pk_fp8_f32 v178, v2, v6
	v_mul_f32_e32 v3, v3, v177
	v_mul_f32_e32 v7, v19, v177
	v_mul_f32_e32 v2, v11, v177
	v_cvt_pk_fp8_f32 v178, v3, v7 op_sel:[0,0,1]
	v_mul_f32_e32 v3, v27, v177
	v_mov_b32_e32 v179, 0
	v_cvt_pk_fp8_f32 v179, v2, v3
	v_mul_f32_e32 v2, v15, v177
	v_mul_f32_e32 v3, v35, v177
	v_mov_b32_e32 v180, 0
	v_cvt_pk_fp8_f32 v180, v2, v3
	v_mul_f32_e32 v2, v39, v177
	v_mul_f32_e32 v3, v55, v177
	v_mov_b32_e32 v181, 0
	v_cvt_pk_fp8_f32 v181, v2, v3
	v_mul_f32_e32 v6, v23, v177
	v_mul_f32_e32 v7, v43, v177
	v_cvt_pk_fp8_f32 v179, v6, v7 op_sel:[0,0,1]
	v_mul_f32_e32 v6, v31, v177
	v_mul_f32_e32 v7, v47, v177
	v_cvt_pk_fp8_f32 v180, v6, v7 op_sel:[0,0,1]
	v_mul_f32_e32 v6, v51, v177
	v_mul_f32_e32 v7, v59, v177
	v_cvt_pk_fp8_f32 v181, v6, v7 op_sel:[0,0,1]
	v_mul_f32_e32 v2, v64, v177
	v_mul_f32_e32 v3, v8, v177
	v_mul_f32_e32 v4, v4, v177
	ds_write_b128 v156, v[178:181] offset:256
	v_mov_b32_e32 v178, 0
	v_cvt_pk_fp8_f32 v178, v2, v3
	v_mul_f32_e32 v2, v12, v177
	v_mul_f32_e32 v3, v28, v177
	v_mov_b32_e32 v179, 0
	v_cvt_pk_fp8_f32 v179, v2, v3
	v_mul_f32_e32 v2, v16, v177
	v_mul_f32_e32 v3, v36, v177
	v_mov_b32_e32 v180, 0
	v_cvt_pk_fp8_f32 v180, v2, v3
	v_mul_f32_e32 v2, v40, v177
	v_mul_f32_e32 v3, v56, v177
	v_mov_b32_e32 v181, 0
	v_mul_f32_e32 v6, v20, v177
	v_cvt_pk_fp8_f32 v181, v2, v3
	v_cvt_pk_fp8_f32 v178, v4, v6 op_sel:[0,0,1]
	v_mul_f32_e32 v4, v24, v177
	v_mul_f32_e32 v6, v44, v177
	v_cvt_pk_fp8_f32 v179, v4, v6 op_sel:[0,0,1]
	v_mul_f32_e32 v4, v32, v177
	v_mul_f32_e32 v6, v48, v177
	v_cvt_pk_fp8_f32 v180, v4, v6 op_sel:[0,0,1]
	v_mul_f32_e32 v4, v52, v177
	v_mul_f32_e32 v6, v60, v177
	v_cvt_pk_fp8_f32 v181, v4, v6 op_sel:[0,0,1]
	v_mul_f32_e32 v3, v65, v177
	v_mul_f32_e32 v4, v9, v177
	v_mov_b32_e32 v2, 0
	v_cvt_pk_fp8_f32 v2, v3, v4
	v_mul_f32_e32 v5, v5, v177
	v_mul_f32_e32 v6, v21, v177
	v_mul_f32_e32 v4, v13, v177
	v_cvt_pk_fp8_f32 v2, v5, v6 op_sel:[0,0,1]
	v_mul_f32_e32 v5, v29, v177
	v_mov_b32_e32 v3, 0
	v_cvt_pk_fp8_f32 v3, v4, v5
	v_mul_f32_e32 v6, v25, v177
	v_mul_f32_e32 v7, v45, v177
	v_mul_f32_e32 v5, v17, v177
	v_cvt_pk_fp8_f32 v3, v6, v7 op_sel:[0,0,1]
	v_mul_f32_e32 v6, v37, v177
	v_mov_b32_e32 v4, 0
	v_cvt_pk_fp8_f32 v4, v5, v6
	v_mul_f32_e32 v7, v33, v177
	v_mul_f32_e32 v8, v49, v177
	v_mul_f32_e32 v6, v41, v177
	v_cvt_pk_fp8_f32 v4, v7, v8 op_sel:[0,0,1]
	v_mul_f32_e32 v7, v57, v177
	v_mov_b32_e32 v5, 0
	v_cvt_pk_fp8_f32 v5, v6, v7
	v_mul_f32_e32 v8, v53, v177
	v_mul_f32_e32 v9, v61, v177
	s_mov_b32 s31, 0x100000
	v_cvt_pk_fp8_f32 v5, v8, v9 op_sel:[0,0,1]
	ds_write_b128 v156, v[178:181] offset:512
	v_mov_b32_e32 v178, 0
	v_mov_b32_e32 v179, 0
	ds_write_b128 v156, v[2:5] offset:768
	v_add_co_u32_e32 v2, vcc, s31, v132
	s_mov_b32 s31, 0x102000
	s_nop 0
	v_addc_co_u32_e32 v3, vcc, 0, v133, vcc
	global_load_dwordx4 v[62:65], v[2:3], off nt
	v_add_co_u32_e32 v2, vcc, s31, v132
	s_mov_b32 s31, 0x104000
	s_nop 0
	v_addc_co_u32_e32 v3, vcc, 0, v133, vcc
	global_load_dwordx4 v[6:9], v[2:3], off nt
	v_add_co_u32_e32 v2, vcc, s31, v132
	s_mov_b32 s31, 0x106000
	s_nop 0
	v_addc_co_u32_e32 v3, vcc, 0, v133, vcc
	v_add_co_u32_e32 v10, vcc, s31, v132
	s_mov_b32 s31, 0x108000
	s_nop 0
	v_addc_co_u32_e32 v11, vcc, 0, v133, vcc
	global_load_dwordx4 v[2:5], v[2:3], off nt
	s_waitcnt vmcnt(12)
; __device__ __forceinline__ unsigned pk4_fp8(float a, float b, float c, float d) { unsigned w = 0u; w = __builtin_amdgcn_cvt_pk_fp8_f32(a, b, w, false); w = __builtin_amdgcn_cvt_pk_fp8_f32(c, d, w, true); return w; }
; #define LAS __attribute__((address_space(3)))
; #define CVT_LOAD(v, c, s_) do { _Pragma("unroll") for (int i_ = 0; i_ < 16; ++i_) v[i_] = *(const f32x4*)((c).src + (size_t)(64 * (s_) + i_) * (c).N); } while (0)
; __device__ __forceinline__ void cvt_pack8(const f32x4 (&v)[16], const CvtItem& c, LAS unsigned char* blk, int s4, int lane) {
;     const float w = c.wscale; const int cb = lane & 15, j = 4 * s4 + (lane >> 4);
; #pragma unroll
;     for (int jn = 0; jn < 4; ++jn) {
;         v4u o; o.x = pg8::pk4_fp8(v[0][jn] * w, v[1][jn] * w, v[2][jn] * w, v[3][jn] * w); o.y = pg8::pk4_fp8(v[4][jn] * w, v[5][jn] * w, v[6][jn] * w, v[7][jn] * w);
;         o.z = pg8::pk4_fp8(v[8][jn] * w, v[9][jn] * w, v[10][jn] * w, v[11][jn] * w); o.w = pg8::pk4_fp8(v[12][jn] * w, v[13][jn] * w, v[14][jn] * w, v[15][jn] * w);
;         *(LAS v4u*)(blk + (4 * cb + jn) * 256 + ((j ^ cb) * 16)) = o; }
; }
; __device__ __forceinline__ void cvt_moe_pipe2(const CvtSrc& A, const CvtSrc& B, LAS float* scr, int gw, int NGW, int lane) {
;     ...
;     while (it < it1) {
;         const int i1 = it + NGW; const bool more = i1 < it1;
;         CVT_LOAD(vb, c, 1); cvt_pack8(va, c, blk, 0, lane);
;         CVT_LOAD(va, c, 2); cvt_pack8(vb, c, blk, 1, lane);
;         CVT_LOAD(vb, c, 3); cvt_pack8(va, c, blk, 2, lane);
	v_mul_f32_e32 v66, v177, v66
	global_load_dwordx4 v[18:21], v[10:11], off nt
	v_add_co_u32_e32 v10, vcc, s31, v132
	s_mov_b32 s31, 0x10a000
	s_nop 0
	v_addc_co_u32_e32 v11, vcc, 0, v133, vcc
	v_add_co_u32_e32 v14, vcc, s31, v132
	s_mov_b32 s31, 0x10c000
	s_nop 0
	v_addc_co_u32_e32 v15, vcc, 0, v133, vcc
	global_load_dwordx4 v[10:13], v[10:11], off nt
	s_waitcnt vmcnt(13)
	v_mul_f32_e32 v70, v177, v70
	global_load_dwordx4 v[26:29], v[14:15], off nt
	v_add_co_u32_e32 v14, vcc, s31, v132
	s_mov_b32 s31, 0x10e000
	s_nop 0
	v_addc_co_u32_e32 v15, vcc, 0, v133, vcc
	global_load_dwordx4 v[22:25], v[14:15], off nt
	v_add_co_u32_e32 v14, vcc, s31, v132
	s_mov_b32 s31, 0x110000
	s_nop 0
	v_addc_co_u32_e32 v15, vcc, 0, v133, vcc
	global_load_dwordx4 v[42:45], v[14:15], off nt
	v_add_co_u32_e32 v14, vcc, s31, v132
	s_mov_b32 s31, 0x112000
	s_nop 0
	v_addc_co_u32_e32 v15, vcc, 0, v133, vcc
	v_add_co_u32_e32 v30, vcc, s31, v132
	s_mov_b32 s31, 0x114000
	s_nop 0
	v_addc_co_u32_e32 v31, vcc, 0, v133, vcc
	global_load_dwordx4 v[14:17], v[14:15], off nt
	v_cvt_pk_fp8_f32 v178, v66, v70
	global_load_dwordx4 v[34:37], v[30:31], off nt
	v_add_co_u32_e32 v30, vcc, s31, v132
	s_mov_b32 s31, 0x116000
	s_nop 0
	v_addc_co_u32_e32 v31, vcc, 0, v133, vcc
	v_add_co_u32_e32 v38, vcc, s31, v132
	s_waitcnt vmcnt(17)
	v_mul_f32_e32 v66, v177, v78
	v_mul_f32_e32 v70, v177, v90
	v_addc_co_u32_e32 v39, vcc, 0, v133, vcc
	s_mov_b32 s31, 0x118000
	v_cvt_pk_fp8_f32 v179, v66, v70
	s_waitcnt vmcnt(16)
	v_mul_f32_e32 v66, v177, v86
	s_waitcnt vmcnt(15)
	v_mul_f32_e32 v70, v177, v98
	v_mov_b32_e32 v180, 0
	global_load_dwordx4 v[30:33], v[30:31], off nt
	v_cvt_pk_fp8_f32 v180, v66, v70
	global_load_dwordx4 v[46:49], v[38:39], off nt
	v_add_co_u32_e32 v38, vcc, s31, v132
	s_waitcnt vmcnt(16)
	v_mul_f32_e32 v66, v177, v110
	s_waitcnt vmcnt(15)
	v_mul_f32_e32 v70, v177, v118
	v_mov_b32_e32 v181, 0
	v_addc_co_u32_e32 v39, vcc, 0, v133, vcc
	s_mov_b32 s31, 0x11a000
	s_waitcnt vmcnt(14)
	v_mul_f32_e32 v74, v177, v74
	v_mul_f32_e32 v82, v177, v82
	v_cvt_pk_fp8_f32 v181, v66, v70
	v_add_co_u32_e32 v50, vcc, s31, v132
	v_cvt_pk_fp8_f32 v178, v74, v82 op_sel:[0,0,1]
	v_mul_f32_e32 v74, v177, v94
	v_mul_f32_e32 v78, v177, v106
	v_addc_co_u32_e32 v51, vcc, 0, v133, vcc
	s_mov_b32 s31, 0x11c000
	v_cvt_pk_fp8_f32 v179, v74, v78 op_sel:[0,0,1]
	v_mul_f32_e32 v74, v177, v102
	v_mul_f32_e32 v78, v177, v114
	global_load_dwordx4 v[38:41], v[38:39], off nt
	v_cvt_pk_fp8_f32 v180, v74, v78 op_sel:[0,0,1]
	global_load_dwordx4 v[54:57], v[50:51], off nt
	v_add_co_u32_e32 v50, vcc, s31, v132
	s_waitcnt vmcnt(15)
	v_mul_f32_e32 v74, v177, v122
	s_waitcnt vmcnt(14)
	v_mul_f32_e32 v78, v177, v126
	v_addc_co_u32_e32 v51, vcc, 0, v133, vcc
	s_mov_b32 s31, 0x11e000
	v_cvt_pk_fp8_f32 v181, v74, v78 op_sel:[0,0,1]
	v_add_co_u32_e32 v58, vcc, s31, v132
	global_load_dwordx4 v[50:53], v[50:51], off nt
	s_nop 0
	v_addc_co_u32_e32 v59, vcc, 0, v133, vcc
	global_load_dwordx4 v[58:61], v[58:59], off nt
	ds_write_b128 v157, v[178:181]
	v_mul_f32_e32 v66, v177, v67
	v_mul_f32_e32 v67, v177, v71
	v_mov_b32_e32 v178, 0
	v_cvt_pk_fp8_f32 v178, v66, v67
	v_mul_f32_e32 v66, v177, v79
	v_mul_f32_e32 v67, v177, v91
	v_mov_b32_e32 v179, 0
	v_cvt_pk_fp8_f32 v179, v66, v67
	v_mul_f32_e32 v66, v177, v87
	v_mul_f32_e32 v67, v177, v99
	v_mov_b32_e32 v180, 0
	v_cvt_pk_fp8_f32 v180, v66, v67
	v_mul_f32_e32 v66, v177, v111
	v_mul_f32_e32 v67, v177, v119
	v_mov_b32_e32 v181, 0
	v_mul_f32_e32 v70, v177, v75
	v_mul_f32_e32 v71, v177, v83
	v_cvt_pk_fp8_f32 v181, v66, v67
	v_cvt_pk_fp8_f32 v178, v70, v71 op_sel:[0,0,1]
	v_mul_f32_e32 v70, v177, v95
	v_mul_f32_e32 v71, v177, v107
	v_cvt_pk_fp8_f32 v179, v70, v71 op_sel:[0,0,1]
	v_mul_f32_e32 v70, v177, v103
	v_mul_f32_e32 v71, v177, v115
	v_cvt_pk_fp8_f32 v180, v70, v71 op_sel:[0,0,1]
	v_mul_f32_e32 v70, v177, v123
	v_mul_f32_e32 v71, v177, v127
	v_cvt_pk_fp8_f32 v181, v70, v71 op_sel:[0,0,1]
	v_mul_f32_e32 v66, v177, v68
	v_mul_f32_e32 v67, v177, v72
	v_mul_f32_e32 v68, v177, v76
	ds_write_b128 v157, v[178:181] offset:256
	v_mov_b32_e32 v178, 0
	v_cvt_pk_fp8_f32 v178, v66, v67
	v_mul_f32_e32 v66, v177, v80
	v_mul_f32_e32 v67, v177, v92
	v_mov_b32_e32 v179, 0
	v_cvt_pk_fp8_f32 v179, v66, v67
	v_mul_f32_e32 v66, v177, v88
	v_mul_f32_e32 v67, v177, v100
	v_mov_b32_e32 v180, 0
	v_cvt_pk_fp8_f32 v180, v66, v67
	v_mul_f32_e32 v66, v177, v112
	v_mul_f32_e32 v67, v177, v120
	v_mov_b32_e32 v181, 0
	v_mul_f32_e32 v70, v177, v84
	v_cvt_pk_fp8_f32 v181, v66, v67
	v_cvt_pk_fp8_f32 v178, v68, v70 op_sel:[0,0,1]
	v_mul_f32_e32 v68, v177, v96
	v_mul_f32_e32 v70, v177, v108
	v_cvt_pk_fp8_f32 v179, v68, v70 op_sel:[0,0,1]
	v_mul_f32_e32 v68, v177, v104
	v_mul_f32_e32 v70, v177, v116
	v_cvt_pk_fp8_f32 v180, v68, v70 op_sel:[0,0,1]
	v_mul_f32_e32 v68, v177, v124
	v_mul_f32_e32 v70, v177, v128
	v_cvt_pk_fp8_f32 v181, v68, v70 op_sel:[0,0,1]
	v_mul_f32_e32 v67, v177, v69
	v_mul_f32_e32 v68, v177, v73
	v_mov_b32_e32 v66, 0
	v_cvt_pk_fp8_f32 v66, v67, v68
	v_mul_f32_e32 v69, v177, v77
	v_mul_f32_e32 v70, v177, v85
	v_mul_f32_e32 v68, v177, v81
	v_cvt_pk_fp8_f32 v66, v69, v70 op_sel:[0,0,1]
	v_mul_f32_e32 v69, v177, v93
	v_mov_b32_e32 v67, 0
	v_cvt_pk_fp8_f32 v67, v68, v69
	v_mul_f32_e32 v70, v177, v97
	v_mul_f32_e32 v71, v177, v109
	v_mul_f32_e32 v69, v177, v89
	v_cvt_pk_fp8_f32 v67, v70, v71 op_sel:[0,0,1]
	v_mul_f32_e32 v70, v177, v101
	v_mov_b32_e32 v68, 0
	v_cvt_pk_fp8_f32 v68, v69, v70
	v_mul_f32_e32 v71, v177, v105
	v_mul_f32_e32 v72, v177, v117
	v_mul_f32_e32 v70, v177, v113
	v_cvt_pk_fp8_f32 v68, v71, v72 op_sel:[0,0,1]
	v_mul_f32_e32 v71, v177, v121
	v_mov_b32_e32 v69, 0
	v_cvt_pk_fp8_f32 v69, v70, v71
	v_mul_f32_e32 v72, v177, v125
	v_mul_f32_e32 v73, v177, v129
	s_mov_b32 s31, 0x180000
	v_cvt_pk_fp8_f32 v69, v72, v73 op_sel:[0,0,1]
	ds_write_b128 v157, v[178:181] offset:512
	s_waitcnt vmcnt(15)
; __device__ __forceinline__ unsigned pk4_fp8(float a, float b, float c, float d) { unsigned w = 0u; w = __builtin_amdgcn_cvt_pk_fp8_f32(a, b, w, false); w = __builtin_amdgcn_cvt_pk_fp8_f32(c, d, w, true); return w; }
; #define LAS __attribute__((address_space(3)))
; #define CVT_LOAD(v, c, s_) do { _Pragma("unroll") for (int i_ = 0; i_ < 16; ++i_) v[i_] = *(const f32x4*)((c).src + (size_t)(64 * (s_) + i_) * (c).N); } while (0)
; __device__ __forceinline__ void cvt_pack8(const f32x4 (&v)[16], const CvtItem& c, LAS unsigned char* blk, int s4, int lane) {
;     const float w = c.wscale; const int cb = lane & 15, j = 4 * s4 + (lane >> 4);
; #pragma unroll
;     for (int jn = 0; jn < 4; ++jn) {
;         v4u o; o.x = pg8::pk4_fp8(v[0][jn] * w, v[1][jn] * w, v[2][jn] * w, v[3][jn] * w); o.y = pg8::pk4_fp8(v[4][jn] * w, v[5][jn] * w, v[6][jn] * w, v[7][jn] * w);
;         o.z = pg8::pk4_fp8(v[8][jn] * w, v[9][jn] * w, v[10][jn] * w, v[11][jn] * w); o.w = pg8::pk4_fp8(v[12][jn] * w, v[13][jn] * w, v[14][jn] * w, v[15][jn] * w);
;         *(LAS v4u*)(blk + (4 * cb + jn) * 256 + ((j ^ cb) * 16)) = o; }
; }
; __device__ __forceinline__ void cvt_moe_pipe2(const CvtSrc& A, const CvtSrc& B, LAS float* scr, int gw, int NGW, int lane) {
;     ...
;     while (it < it1) {
;         const int i1 = it + NGW; const bool more = i1 < it1;
;         CVT_LOAD(vb, c, 1); cvt_pack8(va, c, blk, 0, lane);
;         CVT_LOAD(va, c, 2); cvt_pack8(vb, c, blk, 1, lane);
;         CVT_LOAD(vb, c, 3); cvt_pack8(va, c, blk, 2, lane);
;         if (more) { cn = cvt_moe_item2(i1, A, B, lane); CVT_LOAD(va, cn, 0); }
;         cvt_pack8(vb, c, blk, 3, lane);
	v_mul_f32_e32 v130, v177, v62
	s_waitcnt vmcnt(14)
	v_mul_f32_e32 v137, v177, v6
	ds_write_b128 v157, v[66:69] offset:768
	v_add_co_u32_e32 v66, vcc, s31, v132
	s_mov_b32 s31, 0x182000
	s_nop 0
	v_addc_co_u32_e32 v67, vcc, 0, v133, vcc
	v_add_co_u32_e32 v70, vcc, s31, v132
	s_mov_b32 s31, 0x184000
	s_nop 0
	v_addc_co_u32_e32 v71, vcc, 0, v133, vcc
	v_add_co_u32_e32 v74, vcc, s31, v132
	s_mov_b32 s31, 0x186000
	s_nop 0
	v_addc_co_u32_e32 v75, vcc, 0, v133, vcc
	v_add_co_u32_e32 v78, vcc, s31, v132
	s_mov_b32 s31, 0x188000
	s_nop 0
	v_addc_co_u32_e32 v79, vcc, 0, v133, vcc
	global_load_dwordx4 v[74:77], v[74:75], off nt
	v_mov_b32_e32 v178, 0
	global_load_dwordx4 v[82:85], v[78:79], off nt
	v_add_co_u32_e32 v78, vcc, s31, v132
	s_mov_b32 s31, 0x18a000
	s_nop 0
	v_addc_co_u32_e32 v79, vcc, 0, v133, vcc
	v_add_co_u32_e32 v86, vcc, s31, v132
	s_mov_b32 s31, 0x18c000
	s_nop 0
	v_addc_co_u32_e32 v87, vcc, 0, v133, vcc
	global_load_dwordx4 v[78:81], v[78:79], off nt
	v_cvt_pk_fp8_f32 v178, v130, v137
	global_load_dwordx4 v[90:93], v[86:87], off nt
	v_add_co_u32_e32 v86, vcc, s31, v132
	s_mov_b32 s31, 0x18e000
	s_nop 0
	v_addc_co_u32_e32 v87, vcc, 0, v133, vcc
	global_load_dwordx4 v[94:97], v[86:87], off nt
	v_add_co_u32_e32 v86, vcc, s31, v132
	s_mov_b32 s31, 0x190000
	s_nop 0
	v_addc_co_u32_e32 v87, vcc, 0, v133, vcc
	global_load_dwordx4 v[106:109], v[86:87], off nt
	v_add_co_u32_e32 v86, vcc, s31, v132
	s_mov_b32 s31, 0x192000
	s_nop 0
	v_addc_co_u32_e32 v87, vcc, 0, v133, vcc
	v_add_co_u32_e32 v98, vcc, s31, v132
	s_mov_b32 s31, 0x194000
	s_nop 0
	v_addc_co_u32_e32 v99, vcc, 0, v133, vcc
	v_add_co_u32_e32 v102, vcc, s31, v132
	s_waitcnt vmcnt(19)
	v_mul_f32_e32 v179, v177, v2
	s_waitcnt vmcnt(18)
	v_mul_f32_e32 v180, v177, v18
	v_addc_co_u32_e32 v103, vcc, 0, v133, vcc
	s_mov_b32 s31, 0x196000
	v_cvt_pk_fp8_f32 v178, v179, v180 op_sel:[0,0,1]
	s_waitcnt vmcnt(17)
	v_mul_f32_e32 v130, v177, v10
	s_waitcnt vmcnt(16)
	v_mul_f32_e32 v137, v177, v26
	v_mov_b32_e32 v179, 0
	v_add_co_u32_e32 v110, vcc, s31, v132
	v_cvt_pk_fp8_f32 v179, v130, v137
	s_nop 0
	v_addc_co_u32_e32 v111, vcc, 0, v133, vcc
	s_mov_b32 s31, 0x198000
	global_load_dwordx4 v[102:105], v[102:103], off nt
	s_waitcnt vmcnt(16)
	v_mul_f32_e32 v180, v177, v22
	global_load_dwordx4 v[114:117], v[110:111], off nt
	v_add_co_u32_e32 v110, vcc, s31, v132
	s_mov_b32 s31, 0x19a000
	s_nop 0
	v_addc_co_u32_e32 v111, vcc, 0, v133, vcc
	s_waitcnt vmcnt(16)
	v_mul_f32_e32 v181, v177, v42
	v_add_co_u32_e32 v118, vcc, s31, v132
	v_cvt_pk_fp8_f32 v179, v180, v181 op_sel:[0,0,1]
	s_waitcnt vmcnt(15)
	v_mul_f32_e32 v130, v177, v14
	s_waitcnt vmcnt(14)
	v_mul_f32_e32 v137, v177, v34
	v_mov_b32_e32 v180, 0
	v_addc_co_u32_e32 v119, vcc, 0, v133, vcc
	s_mov_b32 s31, 0x19c000
	v_cvt_pk_fp8_f32 v180, v130, v137
	v_add_co_u32_e32 v122, vcc, s31, v132
	s_mov_b32 s31, 0x19e000
	s_nop 0
	v_addc_co_u32_e32 v123, vcc, 0, v133, vcc
	v_add_co_u32_e32 v126, vcc, s31, v132
	s_waitcnt vmcnt(13)
	v_mul_f32_e32 v181, v177, v30
	s_waitcnt vmcnt(12)
	v_mul_f32_e32 v182, v177, v46
	v_addc_co_u32_e32 v127, vcc, 0, v133, vcc
	v_cvt_pk_fp8_f32 v180, v181, v182 op_sel:[0,0,1]
	s_waitcnt vmcnt(11)
	v_mul_f32_e32 v130, v177, v38
	s_waitcnt vmcnt(10)
	v_mul_f32_e32 v137, v177, v54
	v_mov_b32_e32 v181, 0
	global_load_dwordx4 v[66:69], v[66:67], off nt
	v_cvt_pk_fp8_f32 v181, v130, v137
	global_load_dwordx4 v[70:73], v[70:71], off nt
	s_waitcnt vmcnt(11)
	v_mul_f32_e32 v182, v177, v50
	global_load_dwordx4 v[86:89], v[86:87], off nt
	s_waitcnt vmcnt(11)
	v_mul_f32_e32 v183, v177, v58
	global_load_dwordx4 v[98:101], v[98:99], off nt
	v_cvt_pk_fp8_f32 v181, v182, v183 op_sel:[0,0,1]
	global_load_dwordx4 v[110:113], v[110:111], off nt
	v_mul_f32_e32 v130, v177, v63
	global_load_dwordx4 v[118:121], v[118:119], off nt
	ds_write_b128 v158, v[178:181]
	global_load_dwordx4 v[122:125], v[122:123], off nt
	v_mul_f32_e32 v137, v177, v7
	global_load_dwordx4 v[126:129], v[126:127], off nt
	v_mov_b32_e32 v178, 0
	v_cvt_pk_fp8_f32 v178, v130, v137
	v_mul_f32_e32 v179, v177, v3
	v_mul_f32_e32 v180, v177, v19
	v_mul_f32_e32 v130, v177, v11
	v_cvt_pk_fp8_f32 v178, v179, v180 op_sel:[0,0,1]
	v_mul_f32_e32 v137, v177, v27
	v_mov_b32_e32 v179, 0
	v_cvt_pk_fp8_f32 v179, v130, v137
	v_mul_f32_e32 v180, v177, v23
	v_mul_f32_e32 v181, v177, v43
	v_mul_f32_e32 v130, v177, v15
	v_cvt_pk_fp8_f32 v179, v180, v181 op_sel:[0,0,1]
	v_mul_f32_e32 v137, v177, v35
	v_mov_b32_e32 v180, 0
	v_cvt_pk_fp8_f32 v180, v130, v137
	v_mul_f32_e32 v181, v177, v31
	v_mul_f32_e32 v182, v177, v47
	v_mul_f32_e32 v130, v177, v39
	v_cvt_pk_fp8_f32 v180, v181, v182 op_sel:[0,0,1]
	v_mul_f32_e32 v137, v177, v55
	v_mov_b32_e32 v181, 0
	v_cvt_pk_fp8_f32 v181, v130, v137
	v_mul_f32_e32 v182, v177, v51
	v_mul_f32_e32 v183, v177, v59
	v_mul_f32_e32 v130, v177, v64
	v_cvt_pk_fp8_f32 v181, v182, v183 op_sel:[0,0,1]
	v_mul_f32_e32 v137, v177, v8
	v_mul_f32_e32 v182, v177, v48
	v_mul_f32_e32 v183, v177, v60
	ds_write_b128 v158, v[178:181] offset:256
	v_mov_b32_e32 v178, 0
	v_cvt_pk_fp8_f32 v178, v130, v137
	v_mul_f32_e32 v179, v177, v4
	v_mul_f32_e32 v180, v177, v20
	v_mul_f32_e32 v130, v177, v12
	v_cvt_pk_fp8_f32 v178, v179, v180 op_sel:[0,0,1]
	v_mul_f32_e32 v137, v177, v28
	v_mov_b32_e32 v179, 0
	v_cvt_pk_fp8_f32 v179, v130, v137
	v_mul_f32_e32 v180, v177, v24
	v_mul_f32_e32 v181, v177, v44
	v_mul_f32_e32 v130, v177, v16
	v_cvt_pk_fp8_f32 v179, v180, v181 op_sel:[0,0,1]
	v_mul_f32_e32 v137, v177, v36
	v_mov_b32_e32 v180, 0
	v_cvt_pk_fp8_f32 v180, v130, v137
	v_mul_f32_e32 v181, v177, v32
	v_mul_f32_e32 v130, v177, v40
	v_mul_f32_e32 v137, v177, v56
	v_cvt_pk_fp8_f32 v180, v181, v182 op_sel:[0,0,1]
	v_mov_b32_e32 v181, 0
	v_cvt_pk_fp8_f32 v181, v130, v137
	v_mul_f32_e32 v182, v177, v52
	v_mul_f32_e32 v130, v177, v65
	v_mul_f32_e32 v137, v177, v9
	v_cvt_pk_fp8_f32 v181, v182, v183 op_sel:[0,0,1]
	v_mul_f32_e32 v182, v177, v49
	v_mul_f32_e32 v183, v177, v61
	v_readlane_b32 s4, v254, 52
	ds_write_b128 v158, v[178:181] offset:512
	v_mov_b32_e32 v178, 0
	v_cvt_pk_fp8_f32 v178, v130, v137
	v_mul_f32_e32 v179, v177, v5
	v_mul_f32_e32 v180, v177, v21
	v_mul_f32_e32 v130, v177, v13
	v_cvt_pk_fp8_f32 v178, v179, v180 op_sel:[0,0,1]
	v_mul_f32_e32 v137, v177, v29
	v_mov_b32_e32 v179, 0
	v_cvt_pk_fp8_f32 v179, v130, v137
	v_mul_f32_e32 v180, v177, v25
	v_mul_f32_e32 v181, v177, v45
	v_mul_f32_e32 v130, v177, v17
	v_cvt_pk_fp8_f32 v179, v180, v181 op_sel:[0,0,1]
	v_mul_f32_e32 v137, v177, v37
	v_mov_b32_e32 v180, 0
	v_cvt_pk_fp8_f32 v180, v130, v137
	v_mul_f32_e32 v181, v177, v33
	v_mul_f32_e32 v130, v177, v41
	v_mul_f32_e32 v137, v177, v57
	v_cvt_pk_fp8_f32 v180, v181, v182 op_sel:[0,0,1]
	v_mov_b32_e32 v181, 0
	v_cvt_pk_fp8_f32 v181, v130, v137
	v_mul_f32_e32 v182, v177, v53
	s_add_i32 s4, s4, s2
	s_addk_i32 s4, 0xfe00
	v_cvt_pk_fp8_f32 v181, v182, v183 op_sel:[0,0,1]
	s_cmpk_gt_i32 s4, 0x50f
	ds_write_b128 v158, v[178:181] offset:768
	s_cbranch_scc1 .LBB0_724
; #define CVT_LOAD(v, c, s_) do { _Pragma("unroll") for (int i_ = 0; i_ < 16; ++i_) v[i_] = *(const f32x4*)((c).src + (size_t)(64 * (s_) + i_) * (c).N); } while (0)
; __device__ __forceinline__ CvtItem cvt_moe_item(int it, const float* wg, const float* wu, const float* wd, unsigned char* WGU, unsigned char* WDN, int lane) {
;     const int which = it >> 11, r = it & 2047, e = r >> 7, q = r & 127; CvtItem c; c.which = which;
;     if (which < 2) { const int nb = q & 31, k0 = (q >> 5) * 256; c.nb = nb;
;         c.N = DFF; c.K = DM; c.wscale = which ? 64.f / LOG2E : 64.f * LOG2E; c.src = (which ? wu : wg) + (size_t)e * DM * DFF + (size_t)(k0 + 16 * (lane >> 4)) * DFF + nb * 64 + 4 * (lane & 15);
;         c.dst = WGU + (size_t)e * 4096 * DM + k0; }
;     else { const int nb = q & 15, k0 = (q >> 4) * 256; c.nb = nb;
;         c.N = DM; c.K = DFF; c.wscale = 64.f; c.src = wd + (size_t)e * DFF * DM + (size_t)(k0 + 16 * (lane >> 4)) * DM + nb * 64 + 4 * (lane & 15);
;         c.dst = WDN + (size_t)e * DM * DFF + k0; }
;     return c;
; }
; __device__ __forceinline__ void cvt_moe_pipe2(const CvtSrc& A, const CvtSrc& B, LAS float* scr, int gw, int NGW, int lane) {
;     ...
;         if (more) { cn = cvt_moe_item2(i1, A, B, lane); CVT_LOAD(va, cn, 0); }
	s_ashr_i32 s27, s4, 11
	s_and_b32 s28, s4, 31
	s_and_b32 s31, s25, 0x300
	s_cmpk_lt_u32 s4, 0x800
	s_cselect_b64 vcc, -1, 0
	v_readlane_b32 s36, v254, 30
	s_and_b64 s[8:9], vcc, exec
	v_readlane_b32 s48, v254, 42
	v_readlane_b32 s49, v254, 43
	v_readlane_b32 s50, v254, 44
	v_readlane_b32 s51, v254, 45
	s_cselect_b32 s9, s49, s51
	s_cselect_b32 s8, s48, s50
	s_bfe_u32 s33, s4, 0x40007
	s_lshl_b32 s4, s33, 23
	s_add_u32 s8, s8, s4
	v_or_b32_e32 v2, s31, v141
	s_addc_u32 s9, s9, 0
	v_lshlrev_b32_e32 v130, 13, v2
	v_lshl_add_u64 v[2:3], s[8:9], 0, v[130:131]
	s_lshl_b32 s4, s28, 8
	v_lshl_add_u64 v[2:3], v[2:3], 0, s[4:5]
	v_mov_b32_e32 v137, v131
	v_lshl_add_u64 v[132:133], v[2:3], 0, v[136:137]
	v_cndmask_b32_e32 v176, v139, v140, vcc
	v_add_co_u32_e32 v2, vcc, s24, v132
	s_lshl_b32 s4, s33, 22
	s_nop 0
	v_addc_co_u32_e32 v3, vcc, 0, v133, vcc
	v_add_co_u32_e32 v4, vcc, s23, v132
	v_readlane_b32 s8, v255, 1
	s_nop 0
	v_addc_co_u32_e32 v5, vcc, 0, v133, vcc
	v_add_co_u32_e32 v10, vcc, s22, v132
	global_load_dwordx4 v[6:9], v[2:3], off nt
	s_nop 0
	global_load_dwordx4 v[2:5], v[4:5], off nt
	v_addc_co_u32_e32 v11, vcc, 0, v133, vcc
	v_add_co_u32_e32 v12, vcc, s21, v132
	v_readlane_b32 s9, v255, 2
	s_nop 0
	v_addc_co_u32_e32 v13, vcc, 0, v133, vcc
	v_add_co_u32_e32 v14, vcc, s20, v132
	global_load_dwordx4 v[18:21], v[10:11], off nt
	s_nop 0
	global_load_dwordx4 v[10:13], v[12:13], off nt
	v_addc_co_u32_e32 v15, vcc, 0, v133, vcc
	v_add_co_u32_e32 v16, vcc, s19, v132
	s_add_u32 s4, s8, s4
	s_nop 0
	v_addc_co_u32_e32 v17, vcc, 0, v133, vcc
	global_load_dwordx4 v[26:29], v[14:15], off nt
	global_load_dwordx4 v[22:25], v[16:17], off nt
	v_add_co_u32_e32 v14, vcc, s18, v132
	s_addc_u32 s9, s9, 0
	s_nop 0
	v_addc_co_u32_e32 v15, vcc, 0, v133, vcc
	v_add_co_u32_e32 v16, vcc, s17, v132
	s_add_u32 s8, s4, s31
	s_nop 0
	v_addc_co_u32_e32 v17, vcc, 0, v133, vcc
	v_add_co_u32_e32 v30, vcc, s16, v132
	global_load_dwordx4 v[42:45], v[14:15], off nt
	s_nop 0
	global_load_dwordx4 v[14:17], v[16:17], off nt
	v_addc_co_u32_e32 v31, vcc, 0, v133, vcc
	v_add_co_u32_e32 v32, vcc, s15, v132
	s_addc_u32 s9, s9, 0
	s_nop 0
	v_addc_co_u32_e32 v33, vcc, 0, v133, vcc
	v_add_co_u32_e32 v38, vcc, s14, v132
	global_load_dwordx4 v[34:37], v[30:31], off nt
	s_nop 0
	global_load_dwordx4 v[30:33], v[32:33], off nt
	v_addc_co_u32_e32 v39, vcc, 0, v133, vcc
	v_add_co_u32_e32 v40, vcc, s13, v132
	v_readlane_b32 s37, v254, 31
	s_nop 0
	v_addc_co_u32_e32 v41, vcc, 0, v133, vcc
	v_add_co_u32_e32 v50, vcc, s12, v132
	global_load_dwordx4 v[46:49], v[38:39], off nt
	s_nop 0
	global_load_dwordx4 v[38:41], v[40:41], off nt
	v_addc_co_u32_e32 v51, vcc, 0, v133, vcc
	v_add_co_u32_e32 v52, vcc, s11, v132
	v_readlane_b32 s38, v254, 32
	s_nop 0
	v_addc_co_u32_e32 v53, vcc, 0, v133, vcc
	v_add_co_u32_e32 v58, vcc, s10, v132
	global_load_dwordx4 v[54:57], v[50:51], off nt
	s_nop 0
	global_load_dwordx4 v[50:53], v[52:53], off nt
	v_addc_co_u32_e32 v59, vcc, 0, v133, vcc
	global_load_dwordx4 v[62:65], v[132:133], off nt
	s_nop 0
	global_load_dwordx4 v[58:61], v[58:59], off nt
	v_readlane_b32 s39, v254, 33
	v_readlane_b32 s40, v254, 34
	v_readlane_b32 s41, v254, 35
	v_readlane_b32 s42, v254, 36
	v_readlane_b32 s43, v254, 37
	v_readlane_b32 s44, v254, 38
	v_readlane_b32 s45, v254, 39
	v_readlane_b32 s46, v254, 40
	v_readlane_b32 s47, v254, 41
	s_branch .LBB0_724

; #define LAS __attribute__((address_space(3)))
; #define PHASE_IDS() do { int t_ = tid_k; asm volatile("" : "+v"(t_)); tid = t_; lane = t_ & 63; } while (0)
; #define xcd_barrier_wait_if_single(p) xcd_barrier_wait(*(p))
; __device__ __forceinline__ CvtItem cvt_moe_item(int it, const float* wg, const float* wu, const float* wd, unsigned char* WGU, unsigned char* WDN, int lane) {
;     const int which = it >> 11, r = it & 2047, e = r >> 7, q = r & 127; CvtItem c; c.which = which;
;     if (which < 2) { const int nb = q & 31, k0 = (q >> 5) * 256; c.nb = nb;
;         c.N = DFF; c.K = DM; c.wscale = which ? 64.f / LOG2E : 64.f * LOG2E; c.src = (which ? wu : wg) + (size_t)e * DM * DFF + (size_t)(k0 + 16 * (lane >> 4)) * DFF + nb * 64 + 4 * (lane & 15);
;         c.dst = WGU + (size_t)e * 4096 * DM + k0; }
;     else { const int nb = q & 15, k0 = (q >> 4) * 256; c.nb = nb;
;         c.N = DM; c.K = DFF; c.wscale = 64.f; c.src = wd + (size_t)e * DFF * DM + (size_t)(k0 + 16 * (lane >> 4)) * DM + nb * 64 + 4 * (lane & 15);
;         c.dst = WDN + (size_t)e * DM * DFF + k0; }
;     return c;
; }
; __global__ void __launch_bounds__(NWAVES * 64, 2) enc_fwd(Args args) {
;     ...
;     if (IN(16)) { PHASE_IDS(); topk_phase(AFF, IDX, GATE, SEL, (LAS unsigned*)lds, G, blk, tid, lane, wave);
;         if (G > 64 && blk >= 64) { cvt_moe(args.in[22], args.in[23], args.in[24], WGU1, WDN1, scr, (blk - 64) * NWAVES + wave, (G - 64) * NWAVES, lane, CVT1_P6, CVT1_LATE); if (MK_SINGLE && IN(15)) xcd_barrier_wait_if_single(bar_ptr); }
;         else if (G <= 64) { __syncthreads(); cvt_moe(args.in[22], args.in[23], args.in[24], WGU1, WDN1, scr, gw, NGW, lane, CVT1_P6, CVT1_LATE); } }
.LBB0_1444:
	v_readlane_b32 s2, v254, 9
	s_cmpk_lt_i32 s2, 0x41
	v_readlane_b32 s4, v254, 10
	s_cselect_b64 s[2:3], -1, 0
	s_cmp_lt_i32 s4, 64
	s_cselect_b64 s[4:5], -1, 0
	s_or_b64 s[4:5], s[4:5], s[2:3]
	s_mov_b64 s[2:3], -1
	s_and_b64 vcc, exec, s[4:5]
	s_cbranch_vccz .LBB0_1452
	v_readlane_b32 s2, v254, 9
	s_cmp_gt_i32 s2, 64
	s_cbranch_scc1 .LBB0_1451
	v_readlane_b32 s2, v254, 51
	s_cmpk_gt_i32 s2, 0x50f
	s_waitcnt vmcnt(0) lgkmcnt(0)
	s_barrier
	s_cbranch_scc1 .LBB0_1451
	v_readlane_b32 s55, v254, 51
	s_add_i32 s4, s55, 0x510
	s_lshl_b32 s2, s4, 3
	s_ashr_i32 s56, s4, 11
	s_and_b32 s57, s4, 31
	s_and_b32 s8, s2, 0x300
	v_readlane_b32 s12, v254, 30
	s_cmpk_lt_u32 s4, 0x800
	v_readlane_b32 s13, v254, 31
	v_readlane_b32 s14, v254, 32
	v_readlane_b32 s15, v254, 33
	v_readlane_b32 s24, v254, 42
	v_readlane_b32 s25, v254, 43
	s_cselect_b64 vcc, -1, 0
	v_readlane_b32 s26, v254, 44
	v_readlane_b32 s27, v254, 45
	s_mov_b64 s[12:13], s[24:25]
	s_and_b64 s[2:3], vcc, exec
	s_mov_b64 s[14:15], s[26:27]
	s_cselect_b32 s3, s13, s15
	s_cselect_b32 s2, s12, s14
	s_bfe_u32 s4, s4, 0x40007
	s_lshl_b32 s6, s4, 22
	v_readlane_b32 s10, v255, 1
	v_readlane_b32 s11, v255, 2
	s_add_u32 s6, s10, s6
	s_addc_u32 s7, s11, 0
	s_add_u32 s6, s6, s8
	s_addc_u32 s7, s7, 0
	s_lshl_b32 s4, s4, 23
	v_and_b32_e32 v141, 48, v1
	s_add_u32 s2, s2, s4
	v_or_b32_e32 v2, s8, v141
	s_addc_u32 s3, s3, 0
	v_lshlrev_b32_e32 v130, 13, v2
	v_mov_b32_e32 v131, 0
	v_lshlrev_b32_e32 v4, 2, v138
	s_mov_b32 s5, 0
	v_lshl_add_u64 v[2:3], s[2:3], 0, v[130:131]
	s_lshl_b32 s4, s57, 8
	v_and_b32_e32 v66, 60, v4
	v_lshl_add_u64 v[2:3], v[2:3], 0, s[4:5]
	v_lshlrev_b32_e32 v130, 2, v66
	v_mov_b32_e32 v139, 0x42317218
	v_mov_b32_e32 v140, 0x42b8aa3b
	v_lshl_add_u64 v[132:133], v[2:3], 0, v[130:131]
	s_mov_b32 s10, 0x1e000
	v_cndmask_b32_e32 v179, v139, v140, vcc
	v_add_co_u32_e32 v2, vcc, s10, v132
	s_mov_b32 s11, 0x1c000
	s_nop 0
	v_addc_co_u32_e32 v3, vcc, 0, v133, vcc
	v_add_co_u32_e32 v4, vcc, s11, v132
	s_mov_b32 s12, 0x1a000
	s_nop 0
	v_addc_co_u32_e32 v5, vcc, 0, v133, vcc
	global_load_dwordx4 v[58:61], v[2:3], off nt
	global_load_dwordx4 v[50:53], v[4:5], off nt
	v_add_co_u32_e32 v2, vcc, s12, v132
	s_mov_b32 s13, 0x18000
	s_nop 0
	v_addc_co_u32_e32 v3, vcc, 0, v133, vcc
	v_add_co_u32_e32 v4, vcc, s13, v132
	s_mov_b32 s14, 0x16000
	s_nop 0
	v_addc_co_u32_e32 v5, vcc, 0, v133, vcc
	global_load_dwordx4 v[54:57], v[2:3], off nt
	global_load_dwordx4 v[38:41], v[4:5], off nt
	v_add_co_u32_e32 v2, vcc, s14, v132
	s_mov_b32 s15, 0x14000
	s_nop 0
	v_addc_co_u32_e32 v3, vcc, 0, v133, vcc
	v_readlane_b32 s16, v254, 34
	v_add_co_u32_e32 v4, vcc, s15, v132
	s_mov_b32 s16, 0x12000
	s_nop 0
	v_addc_co_u32_e32 v5, vcc, 0, v133, vcc
	v_readlane_b32 s17, v254, 35
	global_load_dwordx4 v[46:49], v[2:3], off nt
	global_load_dwordx4 v[30:33], v[4:5], off nt
	v_add_co_u32_e32 v2, vcc, s16, v132
	s_mov_b32 s17, 0x10000
	s_nop 0
	v_addc_co_u32_e32 v3, vcc, 0, v133, vcc
	v_readlane_b32 s18, v254, 36
	v_add_co_u32_e32 v4, vcc, s17, v132
	s_mov_b32 s18, 0xe000
	s_nop 0
	v_addc_co_u32_e32 v5, vcc, 0, v133, vcc
	v_readlane_b32 s19, v254, 37
	global_load_dwordx4 v[34:37], v[2:3], off nt
	global_load_dwordx4 v[14:17], v[4:5], off nt
	v_add_co_u32_e32 v2, vcc, s18, v132
	s_mov_b32 s19, 0xc000
	s_nop 0
	v_addc_co_u32_e32 v3, vcc, 0, v133, vcc
	v_readlane_b32 s20, v254, 38
	v_add_co_u32_e32 v4, vcc, s19, v132
	s_mov_b32 s20, 0xa000
	s_nop 0
	v_addc_co_u32_e32 v5, vcc, 0, v133, vcc
	v_readlane_b32 s21, v254, 39
	global_load_dwordx4 v[42:45], v[2:3], off nt
	global_load_dwordx4 v[22:25], v[4:5], off nt
	v_add_co_u32_e32 v2, vcc, s20, v132
	s_mov_b32 s21, 0x8000
	s_nop 0
	v_addc_co_u32_e32 v3, vcc, 0, v133, vcc
	v_readlane_b32 s22, v254, 40
	v_add_co_u32_e32 v4, vcc, s21, v132
	s_movk_i32 s22, 0x6000
	s_nop 0
	v_addc_co_u32_e32 v5, vcc, 0, v133, vcc
	v_readlane_b32 s23, v254, 41
; __device__ __forceinline__ unsigned pk4_fp8(float a, float b, float c, float d) { unsigned w = 0u; w = __builtin_amdgcn_cvt_pk_fp8_f32(a, b, w, false); w = __builtin_amdgcn_cvt_pk_fp8_f32(c, d, w, true); return w; }
; #define LAS __attribute__((address_space(3)))
; #define LDS_WAIT() asm volatile("s_waitcnt lgkmcnt(0)" ::: "memory")
; __device__ __forceinline__ void cvt_pack8(const f32x4 (&v)[16], const CvtItem& c, LAS unsigned char* blk, int s4, int lane) {
;     const float w = c.wscale; const int cb = lane & 15, j = 4 * s4 + (lane >> 4);
; #pragma unroll
;     for (int jn = 0; jn < 4; ++jn) {
;         v4u o; o.x = pg8::pk4_fp8(v[0][jn] * w, v[1][jn] * w, v[2][jn] * w, v[3][jn] * w); o.y = pg8::pk4_fp8(v[4][jn] * w, v[5][jn] * w, v[6][jn] * w, v[7][jn] * w);
;         o.z = pg8::pk4_fp8(v[8][jn] * w, v[9][jn] * w, v[10][jn] * w, v[11][jn] * w); o.w = pg8::pk4_fp8(v[12][jn] * w, v[13][jn] * w, v[14][jn] * w, v[15][jn] * w);
;         *(LAS v4u*)(blk + (4 * cb + jn) * 256 + ((j ^ cb) * 16)) = o; }
; }
; __device__ __forceinline__ void cvt_flush8(const CvtItem& c, const LAS unsigned char* blk, int lane) {
;     LDS_WAIT();
; #pragma unroll
;     for (int t = 0; t < 16; ++t) { const int idx = 64 * t + lane, n = idx >> 4, pc = idx & 15, nn = c.nb * 64 + n;
;         const size_t row = (c.which < 2) ? (size_t)((nn >> 7) * 256 + (nn & 127) + c.which * 128) : (size_t)nn;
;         *(v4u*)(c.dst + row * c.K + 16 * pc) = *(const LAS v4u*)(blk + n * 256 + ((pc ^ ((n >> 2) & 15)) * 16)); }
	global_load_dwordx4 v[26:29], v[2:3], off nt
	global_load_dwordx4 v[10:13], v[4:5], off nt
	v_add_co_u32_e32 v2, vcc, s22, v132
	s_movk_i32 s23, 0x4000
	s_nop 0
	v_addc_co_u32_e32 v3, vcc, 0, v133, vcc
	v_add_co_u32_e32 v4, vcc, s23, v132
	s_movk_i32 s24, 0x2000
	s_nop 0
	v_addc_co_u32_e32 v5, vcc, 0, v133, vcc
	v_add_co_u32_e32 v6, vcc, s24, v132
	global_load_dwordx4 v[18:21], v[2:3], off nt
	s_nop 0
	global_load_dwordx4 v[2:5], v[4:5], off nt
	v_addc_co_u32_e32 v7, vcc, 0, v133, vcc
	global_load_dwordx4 v[6:9], v[6:7], off nt
	s_nop 0
	global_load_dwordx4 v[62:65], v[132:133], off nt
	v_lshrrev_b32_e32 v142, 4, v138
	v_and_b32_e32 v67, 15, v1
	v_readlane_b32 s2, v254, 60
	v_or_b32_e32 v143, 4, v142
	v_or_b32_e32 v144, 8, v142
	v_or_b32_e32 v145, 12, v142
	v_or_b32_e32 v146, 16, v142
	v_or_b32_e32 v147, 20, v142
	v_or_b32_e32 v148, 24, v142
	v_or_b32_e32 v149, 28, v142
	v_or_b32_e32 v150, 32, v142
	v_or_b32_e32 v151, 36, v142
	v_or_b32_e32 v152, 40, v142
	v_or_b32_e32 v153, 44, v142
	v_or_b32_e32 v154, 48, v142
	v_or_b32_e32 v155, 52, v142
	v_or_b32_e32 v156, 56, v142
	v_or_b32_e32 v157, 60, v142
	v_lshl_add_u32 v68, v67, 10, s2
	v_bitop3_b32 v70, v142, v67, 4 bitop3:0x36
	v_bitop3_b32 v71, v142, v67, 8 bitop3:0x36
	v_bitop3_b32 v72, v142, v67, 12 bitop3:0x36
	v_lshlrev_b32_e32 v134, 4, v67
	v_lshl_add_u32 v67, v142, 8, s2
	v_lshl_add_u32 v73, v143, 8, s2
	v_lshl_add_u32 v75, v144, 8, s2
	v_lshl_add_u32 v77, v145, 8, s2
	v_lshl_add_u32 v79, v146, 8, s2
	v_lshl_add_u32 v81, v147, 8, s2
	v_lshl_add_u32 v83, v148, 8, s2
	v_lshl_add_u32 v85, v149, 8, s2
	v_lshl_add_u32 v87, v150, 8, s2
	v_lshl_add_u32 v89, v151, 8, s2
	v_lshl_add_u32 v91, v152, 8, s2
	v_lshl_add_u32 v93, v153, 8, s2
	v_lshl_add_u32 v95, v154, 8, s2
	v_lshl_add_u32 v97, v155, 8, s2
	v_lshl_add_u32 v99, v156, 8, s2
	v_lshl_add_u32 v101, v157, 8, s2
	v_readlane_b32 s2, v254, 52
	s_add_i32 s2, s55, s2
	v_bitop3_b32 v69, v142, v1, 15 bitop3:0x78
	s_lshl_b32 s2, s2, 3
	v_lshlrev_b32_e32 v69, 4, v69
	v_lshlrev_b32_e32 v70, 4, v70
	v_lshlrev_b32_e32 v71, 4, v71
	v_lshlrev_b32_e32 v72, 4, v72
	v_xor_b32_e32 v74, 16, v134
	v_xor_b32_e32 v76, 32, v134
	v_xor_b32_e32 v78, 48, v134
	v_xor_b32_e32 v80, 64, v134
	v_xor_b32_e32 v82, 0x50, v134
	v_xor_b32_e32 v84, 0x60, v134
	v_xor_b32_e32 v86, 0x70, v134
	v_xor_b32_e32 v88, 0x80, v134
	v_xor_b32_e32 v90, 0x90, v134
	v_xor_b32_e32 v92, 0xa0, v134
	v_xor_b32_e32 v94, 0xb0, v134
	v_xor_b32_e32 v96, 0xc0, v134
	v_xor_b32_e32 v98, 0xd0, v134
	v_xor_b32_e32 v100, 0xe0, v134
	v_xor_b32_e32 v102, 0xf0, v134
	s_add_i32 s25, s2, 0x2880
	v_readlane_b32 s2, v254, 9
	v_mov_b32_e32 v135, v131
	s_lshl_b32 s26, s2, 6
	v_add_u32_e32 v158, v68, v69
	s_mov_b32 s27, 0x110000
	s_mov_b32 s28, 0x112000
	s_mov_b32 s29, 0x114000
	s_mov_b32 s30, 0x116000
	s_mov_b32 s31, 0x118000
	s_mov_b32 s34, 0x11a000
	s_mov_b32 s35, 0x11c000
	s_mov_b32 s36, 0x11e000
	v_add_u32_e32 v159, v68, v70
	s_mov_b32 s37, 0x180000
	s_mov_b32 s38, 0x182000
	s_mov_b32 s39, 0x184000
	s_mov_b32 s40, 0x186000
	s_mov_b32 s41, 0x188000
	s_mov_b32 s42, 0x18a000
	s_mov_b32 s43, 0x18c000
	s_mov_b32 s44, 0x18e000
	s_mov_b32 s45, 0x190000
	s_mov_b32 s46, 0x192000
	s_mov_b32 s47, 0x194000
	s_mov_b32 s48, 0x196000
	s_mov_b32 s49, 0x198000
	s_mov_b32 s50, 0x19a000
	s_mov_b32 s51, 0x19c000
	s_mov_b32 s52, 0x19e000
	v_add_u32_e32 v160, v68, v71
	v_lshlrev_b32_e32 v136, 2, v66
	v_add_u32_e32 v161, v68, v72
	v_add_u32_e32 v162, v67, v134
	v_add_u32_e32 v163, v73, v74
	v_add_u32_e32 v164, v75, v76
	v_add_u32_e32 v165, v77, v78
	v_add_u32_e32 v166, v79, v80
	v_add_u32_e32 v167, v81, v82
	v_add_u32_e32 v168, v83, v84
	v_add_u32_e32 v169, v85, v86
	v_add_u32_e32 v170, v87, v88
	v_add_u32_e32 v171, v89, v90
	v_add_u32_e32 v172, v91, v92
	v_add_u32_e32 v173, v93, v94
	v_add_u32_e32 v174, v95, v96
	v_add_u32_e32 v175, v97, v98
	v_add_u32_e32 v176, v99, v100
	v_add_u32_e32 v177, v101, v102
	s_branch .LBB0_1449

; __device__ __forceinline__ unsigned pk4_fp8(float a, float b, float c, float d) { unsigned w = 0u; w = __builtin_amdgcn_cvt_pk_fp8_f32(a, b, w, false); w = __builtin_amdgcn_cvt_pk_fp8_f32(c, d, w, true); return w; }
; #define LAS __attribute__((address_space(3)))
; #define CVT_LOAD(v, c, s_) do { _Pragma("unroll") for (int i_ = 0; i_ < 16; ++i_) v[i_] = *(const f32x4*)((c).src + (size_t)(64 * (s_) + i_) * (c).N); } while (0)
; __device__ __forceinline__ void cvt_pack8(const f32x4 (&v)[16], const CvtItem& c, LAS unsigned char* blk, int s4, int lane) {
;     const float w = c.wscale; const int cb = lane & 15, j = 4 * s4 + (lane >> 4);
; #pragma unroll
;     for (int jn = 0; jn < 4; ++jn) {
;         v4u o; o.x = pg8::pk4_fp8(v[0][jn] * w, v[1][jn] * w, v[2][jn] * w, v[3][jn] * w); o.y = pg8::pk4_fp8(v[4][jn] * w, v[5][jn] * w, v[6][jn] * w, v[7][jn] * w);
;         o.z = pg8::pk4_fp8(v[8][jn] * w, v[9][jn] * w, v[10][jn] * w, v[11][jn] * w); o.w = pg8::pk4_fp8(v[12][jn] * w, v[13][jn] * w, v[14][jn] * w, v[15][jn] * w);
;         *(LAS v4u*)(blk + (4 * cb + jn) * 256 + ((j ^ cb) * 16)) = o; }
; }
; __device__ __forceinline__ void cvt_moe_pipe2(const CvtSrc& A, const CvtSrc& B, LAS float* scr, int gw, int NGW, int lane) {
;     ...
;     while (it < it1) {
;         const int i1 = it + NGW; const bool more = i1 < it1;
;         CVT_LOAD(vb, c, 1); cvt_pack8(va, c, blk, 0, lane);
;         CVT_LOAD(va, c, 2); cvt_pack8(vb, c, blk, 1, lane);
;         CVT_LOAD(vb, c, 3); cvt_pack8(va, c, blk, 2, lane);
.LBB0_1449:
	v_readlane_b32 s2, v254, 52
	s_add_i32 s55, s55, s2
	s_mov_b32 s2, 0x80000
	v_add_co_u32_e32 v66, vcc, s2, v132
	s_mov_b32 s2, 0x82000
	s_nop 0
	v_addc_co_u32_e32 v67, vcc, 0, v133, vcc
	v_add_co_u32_e32 v70, vcc, s2, v132
	s_mov_b32 s2, 0x84000
	s_nop 0
	v_addc_co_u32_e32 v71, vcc, 0, v133, vcc
	v_add_co_u32_e32 v74, vcc, s2, v132
	s_mov_b32 s2, 0x86000
	s_nop 0
	v_addc_co_u32_e32 v75, vcc, 0, v133, vcc
	v_add_co_u32_e32 v78, vcc, s2, v132
	s_mov_b32 s2, 0x88000
	s_nop 0
	v_addc_co_u32_e32 v79, vcc, 0, v133, vcc
	global_load_dwordx4 v[82:85], v[78:79], off nt
	v_add_co_u32_e32 v78, vcc, s2, v132
	s_mov_b32 s2, 0x8a000
	s_nop 0
	v_addc_co_u32_e32 v79, vcc, 0, v133, vcc
	v_add_co_u32_e32 v86, vcc, s2, v132
	s_mov_b32 s2, 0x8c000
	s_nop 0
	v_addc_co_u32_e32 v87, vcc, 0, v133, vcc
	global_load_dwordx4 v[90:93], v[86:87], off nt
	v_add_co_u32_e32 v86, vcc, s2, v132
	s_mov_b32 s2, 0x8e000
	s_nop 0
	v_addc_co_u32_e32 v87, vcc, 0, v133, vcc
	global_load_dwordx4 v[94:97], v[86:87], off nt
	v_add_co_u32_e32 v86, vcc, s2, v132
	s_mov_b32 s2, 0x90000
	s_nop 0
	v_addc_co_u32_e32 v87, vcc, 0, v133, vcc
	global_load_dwordx4 v[106:109], v[86:87], off nt
	v_add_co_u32_e32 v86, vcc, s2, v132
	s_mov_b32 s2, 0x92000
	s_nop 0
	v_addc_co_u32_e32 v87, vcc, 0, v133, vcc
	v_add_co_u32_e32 v98, vcc, s2, v132
	s_mov_b32 s2, 0x94000
	s_nop 0
	v_addc_co_u32_e32 v99, vcc, 0, v133, vcc
	v_add_co_u32_e32 v102, vcc, s2, v132
	s_waitcnt vmcnt(4)
	v_mul_f32_e32 v62, v62, v179
	v_mul_f32_e32 v6, v6, v179
	v_mov_b32_e32 v180, 0
	v_addc_co_u32_e32 v103, vcc, 0, v133, vcc
	s_mov_b32 s2, 0x96000
	v_cvt_pk_fp8_f32 v180, v62, v6
	v_add_co_u32_e32 v110, vcc, s2, v132
	s_mov_b32 s2, 0x98000
	s_nop 0
	v_addc_co_u32_e32 v111, vcc, 0, v133, vcc
	global_load_dwordx4 v[102:105], v[102:103], off nt
	v_mul_f32_e32 v2, v2, v179
	global_load_dwordx4 v[114:117], v[110:111], off nt
	v_add_co_u32_e32 v110, vcc, s2, v132
	v_mul_f32_e32 v18, v18, v179
	global_load_dwordx4 v[66:69], v[66:67], off nt
	v_addc_co_u32_e32 v111, vcc, 0, v133, vcc
	global_load_dwordx4 v[70:73], v[70:71], off nt
	s_mov_b32 s2, 0x9a000
	v_cvt_pk_fp8_f32 v180, v2, v18 op_sel:[0,0,1]
	v_mul_f32_e32 v2, v10, v179
	v_mul_f32_e32 v6, v26, v179
	v_mov_b32_e32 v181, 0
	global_load_dwordx4 v[78:81], v[78:79], off nt
	v_add_co_u32_e32 v118, vcc, s2, v132
	v_cvt_pk_fp8_f32 v181, v2, v6
	v_mul_f32_e32 v2, v14, v179
	v_mul_f32_e32 v6, v34, v179
	v_mov_b32_e32 v182, 0
	global_load_dwordx4 v[86:89], v[86:87], off nt
	v_addc_co_u32_e32 v119, vcc, 0, v133, vcc
	global_load_dwordx4 v[98:101], v[98:99], off nt
	s_mov_b32 s2, 0x9c000
	v_cvt_pk_fp8_f32 v182, v2, v6
	v_mul_f32_e32 v2, v38, v179
	v_mul_f32_e32 v6, v54, v179
	v_mov_b32_e32 v183, 0
	global_load_dwordx4 v[110:113], v[110:111], off nt
	v_add_co_u32_e32 v122, vcc, s2, v132
	global_load_dwordx4 v[118:121], v[118:119], off nt
	v_cvt_pk_fp8_f32 v183, v2, v6
	global_load_dwordx4 v[74:77], v[74:75], off nt
	v_addc_co_u32_e32 v123, vcc, 0, v133, vcc
	s_mov_b32 s2, 0x9e000
	v_mul_f32_e32 v10, v22, v179
	v_mul_f32_e32 v18, v42, v179
	v_add_co_u32_e32 v126, vcc, s2, v132
	v_cvt_pk_fp8_f32 v181, v10, v18 op_sel:[0,0,1]
	v_mul_f32_e32 v10, v30, v179
	v_mul_f32_e32 v14, v46, v179
	v_addc_co_u32_e32 v127, vcc, 0, v133, vcc
	v_cvt_pk_fp8_f32 v182, v10, v14 op_sel:[0,0,1]
	v_mul_f32_e32 v10, v50, v179
	v_mul_f32_e32 v14, v58, v179
	global_load_dwordx4 v[122:125], v[122:123], off nt
	v_cvt_pk_fp8_f32 v183, v10, v14 op_sel:[0,0,1]
	global_load_dwordx4 v[126:129], v[126:127], off nt
	v_mul_f32_e32 v2, v63, v179
	v_mul_f32_e32 v6, v7, v179
	ds_write_b128 v158, v[180:183]
	v_mov_b32_e32 v180, 0
	v_cvt_pk_fp8_f32 v180, v2, v6
	v_mul_f32_e32 v3, v3, v179
	v_mul_f32_e32 v7, v19, v179
	v_mul_f32_e32 v2, v11, v179
	v_cvt_pk_fp8_f32 v180, v3, v7 op_sel:[0,0,1]
	v_mul_f32_e32 v3, v27, v179
	v_mov_b32_e32 v181, 0
	v_cvt_pk_fp8_f32 v181, v2, v3
	v_mul_f32_e32 v2, v15, v179
	v_mul_f32_e32 v3, v35, v179
	v_mov_b32_e32 v182, 0
	v_cvt_pk_fp8_f32 v182, v2, v3
	v_mul_f32_e32 v2, v39, v179
	v_mul_f32_e32 v3, v55, v179
	v_mov_b32_e32 v183, 0
	v_cvt_pk_fp8_f32 v183, v2, v3
	v_mul_f32_e32 v6, v23, v179
	v_mul_f32_e32 v7, v43, v179
	v_cvt_pk_fp8_f32 v181, v6, v7 op_sel:[0,0,1]
	v_mul_f32_e32 v6, v31, v179
	v_mul_f32_e32 v7, v47, v179
	v_cvt_pk_fp8_f32 v182, v6, v7 op_sel:[0,0,1]
	v_mul_f32_e32 v6, v51, v179
	v_mul_f32_e32 v7, v59, v179
	v_cvt_pk_fp8_f32 v183, v6, v7 op_sel:[0,0,1]
	v_mul_f32_e32 v2, v64, v179
	v_mul_f32_e32 v3, v8, v179
	v_mul_f32_e32 v4, v4, v179
	ds_write_b128 v158, v[180:183] offset:256
	v_mov_b32_e32 v180, 0
	v_cvt_pk_fp8_f32 v180, v2, v3
	v_mul_f32_e32 v2, v12, v179
	v_mul_f32_e32 v3, v28, v179
	v_mov_b32_e32 v181, 0
	v_cvt_pk_fp8_f32 v181, v2, v3
	v_mul_f32_e32 v2, v16, v179
	v_mul_f32_e32 v3, v36, v179
	v_mov_b32_e32 v182, 0
	v_cvt_pk_fp8_f32 v182, v2, v3
	v_mul_f32_e32 v2, v40, v179
	v_mul_f32_e32 v3, v56, v179
	v_mov_b32_e32 v183, 0
	v_mul_f32_e32 v6, v20, v179
	v_cvt_pk_fp8_f32 v183, v2, v3
	v_cvt_pk_fp8_f32 v180, v4, v6 op_sel:[0,0,1]
	v_mul_f32_e32 v4, v24, v179
	v_mul_f32_e32 v6, v44, v179
	v_cvt_pk_fp8_f32 v181, v4, v6 op_sel:[0,0,1]
	v_mul_f32_e32 v4, v32, v179
	v_mul_f32_e32 v6, v48, v179
	v_cvt_pk_fp8_f32 v182, v4, v6 op_sel:[0,0,1]
	v_mul_f32_e32 v4, v52, v179
	v_mul_f32_e32 v6, v60, v179
	v_cvt_pk_fp8_f32 v183, v4, v6 op_sel:[0,0,1]
	v_mul_f32_e32 v3, v65, v179
	v_mul_f32_e32 v4, v9, v179
	v_mov_b32_e32 v2, 0
	v_cvt_pk_fp8_f32 v2, v3, v4
	v_mul_f32_e32 v5, v5, v179
	v_mul_f32_e32 v6, v21, v179
	v_mul_f32_e32 v4, v13, v179
	v_cvt_pk_fp8_f32 v2, v5, v6 op_sel:[0,0,1]
	v_mul_f32_e32 v5, v29, v179
	v_mov_b32_e32 v3, 0
	v_cvt_pk_fp8_f32 v3, v4, v5
	v_mul_f32_e32 v6, v25, v179
	v_mul_f32_e32 v7, v45, v179
	v_mul_f32_e32 v5, v17, v179
	v_cvt_pk_fp8_f32 v3, v6, v7 op_sel:[0,0,1]
	v_mul_f32_e32 v6, v37, v179
	v_mov_b32_e32 v4, 0
	v_cvt_pk_fp8_f32 v4, v5, v6
	v_mul_f32_e32 v7, v33, v179
	v_mul_f32_e32 v8, v49, v179
	v_mul_f32_e32 v6, v41, v179
	v_cvt_pk_fp8_f32 v4, v7, v8 op_sel:[0,0,1]
	v_mul_f32_e32 v7, v57, v179
	v_mov_b32_e32 v5, 0
	v_cvt_pk_fp8_f32 v5, v6, v7
	v_mul_f32_e32 v8, v53, v179
	v_mul_f32_e32 v9, v61, v179
	s_mov_b32 s2, 0x100000
	v_cvt_pk_fp8_f32 v5, v8, v9 op_sel:[0,0,1]
	ds_write_b128 v158, v[180:183] offset:512
	v_mov_b32_e32 v180, 0
	v_mov_b32_e32 v181, 0
	ds_write_b128 v158, v[2:5] offset:768
	v_add_co_u32_e32 v2, vcc, s2, v132
	s_mov_b32 s2, 0x102000
	s_nop 0
	v_addc_co_u32_e32 v3, vcc, 0, v133, vcc
	global_load_dwordx4 v[62:65], v[2:3], off nt
	v_add_co_u32_e32 v2, vcc, s2, v132
	s_mov_b32 s2, 0x104000
	s_nop 0
	v_addc_co_u32_e32 v3, vcc, 0, v133, vcc
	global_load_dwordx4 v[6:9], v[2:3], off nt
	v_add_co_u32_e32 v2, vcc, s2, v132
	s_mov_b32 s2, 0x106000
	s_nop 0
	v_addc_co_u32_e32 v3, vcc, 0, v133, vcc
	v_add_co_u32_e32 v10, vcc, s2, v132
	s_mov_b32 s2, 0x108000
	s_nop 0
	v_addc_co_u32_e32 v11, vcc, 0, v133, vcc
	global_load_dwordx4 v[2:5], v[2:3], off nt
	s_waitcnt vmcnt(12)
; __device__ __forceinline__ unsigned pk4_fp8(float a, float b, float c, float d) { unsigned w = 0u; w = __builtin_amdgcn_cvt_pk_fp8_f32(a, b, w, false); w = __builtin_amdgcn_cvt_pk_fp8_f32(c, d, w, true); return w; }
; #define LAS __attribute__((address_space(3)))
; #define CVT_LOAD(v, c, s_) do { _Pragma("unroll") for (int i_ = 0; i_ < 16; ++i_) v[i_] = *(const f32x4*)((c).src + (size_t)(64 * (s_) + i_) * (c).N); } while (0)
; __device__ __forceinline__ void cvt_pack8(const f32x4 (&v)[16], const CvtItem& c, LAS unsigned char* blk, int s4, int lane) {
;     const float w = c.wscale; const int cb = lane & 15, j = 4 * s4 + (lane >> 4);
; #pragma unroll
;     for (int jn = 0; jn < 4; ++jn) {
;         v4u o; o.x = pg8::pk4_fp8(v[0][jn] * w, v[1][jn] * w, v[2][jn] * w, v[3][jn] * w); o.y = pg8::pk4_fp8(v[4][jn] * w, v[5][jn] * w, v[6][jn] * w, v[7][jn] * w);
;         o.z = pg8::pk4_fp8(v[8][jn] * w, v[9][jn] * w, v[10][jn] * w, v[11][jn] * w); o.w = pg8::pk4_fp8(v[12][jn] * w, v[13][jn] * w, v[14][jn] * w, v[15][jn] * w);
;         *(LAS v4u*)(blk + (4 * cb + jn) * 256 + ((j ^ cb) * 16)) = o; }
; }
; __device__ __forceinline__ void cvt_moe_pipe2(const CvtSrc& A, const CvtSrc& B, LAS float* scr, int gw, int NGW, int lane) {
;     ...
;     while (it < it1) {
;         const int i1 = it + NGW; const bool more = i1 < it1;
;         CVT_LOAD(vb, c, 1); cvt_pack8(va, c, blk, 0, lane);
;         CVT_LOAD(va, c, 2); cvt_pack8(vb, c, blk, 1, lane);
;         CVT_LOAD(vb, c, 3); cvt_pack8(va, c, blk, 2, lane);
	v_mul_f32_e32 v66, v179, v66
	global_load_dwordx4 v[18:21], v[10:11], off nt
	v_add_co_u32_e32 v10, vcc, s2, v132
	s_mov_b32 s2, 0x10a000
	s_nop 0
	v_addc_co_u32_e32 v11, vcc, 0, v133, vcc
	v_add_co_u32_e32 v14, vcc, s2, v132
	s_mov_b32 s2, 0x10c000
	s_nop 0
	v_addc_co_u32_e32 v15, vcc, 0, v133, vcc
	global_load_dwordx4 v[10:13], v[10:11], off nt
	s_waitcnt vmcnt(13)
	v_mul_f32_e32 v70, v179, v70
	global_load_dwordx4 v[26:29], v[14:15], off nt
	v_add_co_u32_e32 v14, vcc, s2, v132
	s_mov_b32 s2, 0x10e000
	s_nop 0
	v_addc_co_u32_e32 v15, vcc, 0, v133, vcc
	global_load_dwordx4 v[22:25], v[14:15], off nt
	v_add_co_u32_e32 v14, vcc, s2, v132
	v_cvt_pk_fp8_f32 v180, v66, v70
	s_nop 0
	v_addc_co_u32_e32 v15, vcc, 0, v133, vcc
	global_load_dwordx4 v[42:45], v[14:15], off nt
	v_add_co_u32_e32 v14, vcc, s27, v132
	s_waitcnt vmcnt(15)
	v_mul_f32_e32 v66, v179, v78
	v_addc_co_u32_e32 v15, vcc, 0, v133, vcc
	v_add_co_u32_e32 v30, vcc, s28, v132
	global_load_dwordx4 v[14:17], v[14:15], off nt
	s_nop 0
	v_addc_co_u32_e32 v31, vcc, 0, v133, vcc
	global_load_dwordx4 v[34:37], v[30:31], off nt
	v_add_co_u32_e32 v30, vcc, s29, v132
	v_mul_f32_e32 v70, v179, v90
	s_nop 0
	v_addc_co_u32_e32 v31, vcc, 0, v133, vcc
	v_add_co_u32_e32 v38, vcc, s30, v132
	v_cvt_pk_fp8_f32 v181, v66, v70
	s_nop 0
	v_addc_co_u32_e32 v39, vcc, 0, v133, vcc
	s_waitcnt vmcnt(16)
	v_mul_f32_e32 v66, v179, v86
	s_waitcnt vmcnt(15)
	v_mul_f32_e32 v70, v179, v98
	v_mov_b32_e32 v182, 0
	global_load_dwordx4 v[30:33], v[30:31], off nt
	v_cvt_pk_fp8_f32 v182, v66, v70
	global_load_dwordx4 v[46:49], v[38:39], off nt
	v_add_co_u32_e32 v38, vcc, s31, v132
	s_waitcnt vmcnt(16)
	v_mul_f32_e32 v66, v179, v110
	s_waitcnt vmcnt(15)
	v_mul_f32_e32 v70, v179, v118
	v_mov_b32_e32 v183, 0
	v_addc_co_u32_e32 v39, vcc, 0, v133, vcc
	s_waitcnt vmcnt(14)
	v_mul_f32_e32 v74, v179, v74
	v_mul_f32_e32 v82, v179, v82
	v_cvt_pk_fp8_f32 v183, v66, v70
	v_add_co_u32_e32 v50, vcc, s34, v132
	v_cvt_pk_fp8_f32 v180, v74, v82 op_sel:[0,0,1]
	v_mul_f32_e32 v74, v179, v94
	v_mul_f32_e32 v78, v179, v106
	v_addc_co_u32_e32 v51, vcc, 0, v133, vcc
	v_cvt_pk_fp8_f32 v181, v74, v78 op_sel:[0,0,1]
	v_mul_f32_e32 v74, v179, v102
	v_mul_f32_e32 v78, v179, v114
	global_load_dwordx4 v[38:41], v[38:39], off nt
	v_cvt_pk_fp8_f32 v182, v74, v78 op_sel:[0,0,1]
	global_load_dwordx4 v[54:57], v[50:51], off nt
	v_add_co_u32_e32 v50, vcc, s35, v132
	s_waitcnt vmcnt(15)
	v_mul_f32_e32 v74, v179, v122
	s_waitcnt vmcnt(14)
	v_mul_f32_e32 v78, v179, v126
	v_addc_co_u32_e32 v51, vcc, 0, v133, vcc
	v_cvt_pk_fp8_f32 v183, v74, v78 op_sel:[0,0,1]
	v_add_co_u32_e32 v58, vcc, s36, v132
	global_load_dwordx4 v[50:53], v[50:51], off nt
	s_nop 0
	v_addc_co_u32_e32 v59, vcc, 0, v133, vcc
	global_load_dwordx4 v[58:61], v[58:59], off nt
	ds_write_b128 v159, v[180:183]
	v_mul_f32_e32 v66, v179, v67
	v_mul_f32_e32 v67, v179, v71
	v_mov_b32_e32 v180, 0
	v_cvt_pk_fp8_f32 v180, v66, v67
	v_mul_f32_e32 v66, v179, v79
	v_mul_f32_e32 v67, v179, v91
	v_mov_b32_e32 v181, 0
	v_cvt_pk_fp8_f32 v181, v66, v67
	v_mul_f32_e32 v66, v179, v87
	v_mul_f32_e32 v67, v179, v99
	v_mov_b32_e32 v182, 0
	v_cvt_pk_fp8_f32 v182, v66, v67
	v_mul_f32_e32 v66, v179, v111
	v_mul_f32_e32 v67, v179, v119
	v_mov_b32_e32 v183, 0
	v_mul_f32_e32 v70, v179, v75
	v_mul_f32_e32 v71, v179, v83
	v_cvt_pk_fp8_f32 v183, v66, v67
	v_cvt_pk_fp8_f32 v180, v70, v71 op_sel:[0,0,1]
	v_mul_f32_e32 v70, v179, v95
	v_mul_f32_e32 v71, v179, v107
	v_cvt_pk_fp8_f32 v181, v70, v71 op_sel:[0,0,1]
	v_mul_f32_e32 v70, v179, v103
	v_mul_f32_e32 v71, v179, v115
	v_cvt_pk_fp8_f32 v182, v70, v71 op_sel:[0,0,1]
	v_mul_f32_e32 v70, v179, v123
	v_mul_f32_e32 v71, v179, v127
	v_cvt_pk_fp8_f32 v183, v70, v71 op_sel:[0,0,1]
	v_mul_f32_e32 v66, v179, v68
	v_mul_f32_e32 v67, v179, v72
	v_mul_f32_e32 v68, v179, v76
	ds_write_b128 v159, v[180:183] offset:256
	v_mov_b32_e32 v180, 0
	v_cvt_pk_fp8_f32 v180, v66, v67
	v_mul_f32_e32 v66, v179, v80
	v_mul_f32_e32 v67, v179, v92
	v_mov_b32_e32 v181, 0
	v_cvt_pk_fp8_f32 v181, v66, v67
	v_mul_f32_e32 v66, v179, v88
	v_mul_f32_e32 v67, v179, v100
	v_mov_b32_e32 v182, 0
	v_cvt_pk_fp8_f32 v182, v66, v67
	v_mul_f32_e32 v66, v179, v112
	v_mul_f32_e32 v67, v179, v120
	v_mov_b32_e32 v183, 0
	v_mul_f32_e32 v70, v179, v84
	v_cvt_pk_fp8_f32 v183, v66, v67
	v_cvt_pk_fp8_f32 v180, v68, v70 op_sel:[0,0,1]
	v_mul_f32_e32 v68, v179, v96
	v_mul_f32_e32 v70, v179, v108
	v_cvt_pk_fp8_f32 v181, v68, v70 op_sel:[0,0,1]
	v_mul_f32_e32 v68, v179, v104
	v_mul_f32_e32 v70, v179, v116
	v_cvt_pk_fp8_f32 v182, v68, v70 op_sel:[0,0,1]
	v_mul_f32_e32 v68, v179, v124
	v_mul_f32_e32 v70, v179, v128
	v_cvt_pk_fp8_f32 v183, v68, v70 op_sel:[0,0,1]
	v_mul_f32_e32 v67, v179, v69
	v_mul_f32_e32 v68, v179, v73
	v_mov_b32_e32 v66, 0
	v_cvt_pk_fp8_f32 v66, v67, v68
	v_mul_f32_e32 v69, v179, v77
	v_mul_f32_e32 v70, v179, v85
	v_mul_f32_e32 v68, v179, v81
	v_cvt_pk_fp8_f32 v66, v69, v70 op_sel:[0,0,1]
	v_mul_f32_e32 v69, v179, v93
	v_mov_b32_e32 v67, 0
	v_cvt_pk_fp8_f32 v67, v68, v69
	v_mul_f32_e32 v70, v179, v97
	v_mul_f32_e32 v71, v179, v109
	v_mul_f32_e32 v69, v179, v89
	v_cvt_pk_fp8_f32 v67, v70, v71 op_sel:[0,0,1]
	v_mul_f32_e32 v70, v179, v101
	v_mov_b32_e32 v68, 0
	v_cvt_pk_fp8_f32 v68, v69, v70
	v_mul_f32_e32 v71, v179, v105
	v_mul_f32_e32 v72, v179, v117
	v_mul_f32_e32 v70, v179, v113
	v_cvt_pk_fp8_f32 v68, v71, v72 op_sel:[0,0,1]
	v_mul_f32_e32 v71, v179, v121
	v_mov_b32_e32 v69, 0
	v_cvt_pk_fp8_f32 v69, v70, v71
	v_mul_f32_e32 v72, v179, v125
	v_mul_f32_e32 v73, v179, v129
	ds_write_b128 v159, v[180:183] offset:512
	v_cvt_pk_fp8_f32 v69, v72, v73 op_sel:[0,0,1]
	s_waitcnt vmcnt(15)
	v_mul_f32_e32 v130, v179, v62
	s_waitcnt vmcnt(14)
; __device__ __forceinline__ unsigned pk4_fp8(float a, float b, float c, float d) { unsigned w = 0u; w = __builtin_amdgcn_cvt_pk_fp8_f32(a, b, w, false); w = __builtin_amdgcn_cvt_pk_fp8_f32(c, d, w, true); return w; }
; #define LAS __attribute__((address_space(3)))
; #define CVT_LOAD(v, c, s_) do { _Pragma("unroll") for (int i_ = 0; i_ < 16; ++i_) v[i_] = *(const f32x4*)((c).src + (size_t)(64 * (s_) + i_) * (c).N); } while (0)
; __device__ __forceinline__ void cvt_pack8(const f32x4 (&v)[16], const CvtItem& c, LAS unsigned char* blk, int s4, int lane) {
;     const float w = c.wscale; const int cb = lane & 15, j = 4 * s4 + (lane >> 4);
; #pragma unroll
;     for (int jn = 0; jn < 4; ++jn) {
;         v4u o; o.x = pg8::pk4_fp8(v[0][jn] * w, v[1][jn] * w, v[2][jn] * w, v[3][jn] * w); o.y = pg8::pk4_fp8(v[4][jn] * w, v[5][jn] * w, v[6][jn] * w, v[7][jn] * w);
;         o.z = pg8::pk4_fp8(v[8][jn] * w, v[9][jn] * w, v[10][jn] * w, v[11][jn] * w); o.w = pg8::pk4_fp8(v[12][jn] * w, v[13][jn] * w, v[14][jn] * w, v[15][jn] * w);
;         *(LAS v4u*)(blk + (4 * cb + jn) * 256 + ((j ^ cb) * 16)) = o; }
; }
; __device__ __forceinline__ void cvt_moe_pipe2(const CvtSrc& A, const CvtSrc& B, LAS float* scr, int gw, int NGW, int lane) {
;     ...
;     while (it < it1) {
;         const int i1 = it + NGW; const bool more = i1 < it1;
;         CVT_LOAD(vb, c, 1); cvt_pack8(va, c, blk, 0, lane);
;         CVT_LOAD(va, c, 2); cvt_pack8(vb, c, blk, 1, lane);
;         CVT_LOAD(vb, c, 3); cvt_pack8(va, c, blk, 2, lane);
;         if (more) { cn = cvt_moe_item2(i1, A, B, lane); CVT_LOAD(va, cn, 0); }
;         cvt_pack8(vb, c, blk, 3, lane);
	v_mul_f32_e32 v137, v179, v6
	v_mov_b32_e32 v180, 0
	ds_write_b128 v159, v[66:69] offset:768
	v_add_co_u32_e32 v66, vcc, s37, v132
	v_cvt_pk_fp8_f32 v180, v130, v137
	s_nop 0
	v_addc_co_u32_e32 v67, vcc, 0, v133, vcc
	v_add_co_u32_e32 v70, vcc, s38, v132
	s_waitcnt vmcnt(13)
	v_mul_f32_e32 v181, v179, v2
	v_addc_co_u32_e32 v71, vcc, 0, v133, vcc
	v_add_co_u32_e32 v74, vcc, s39, v132
	s_waitcnt vmcnt(12)
	v_mul_f32_e32 v182, v179, v18
	v_addc_co_u32_e32 v75, vcc, 0, v133, vcc
	v_add_co_u32_e32 v78, vcc, s40, v132
	global_load_dwordx4 v[74:77], v[74:75], off nt
	s_nop 0
	v_addc_co_u32_e32 v79, vcc, 0, v133, vcc
	global_load_dwordx4 v[86:89], v[78:79], off nt
	v_add_co_u32_e32 v78, vcc, s41, v132
	v_cvt_pk_fp8_f32 v180, v181, v182 op_sel:[0,0,1]
	s_nop 0
	v_addc_co_u32_e32 v79, vcc, 0, v133, vcc
	v_add_co_u32_e32 v82, vcc, s42, v132
	global_load_dwordx4 v[78:81], v[78:79], off nt
	s_nop 0
	v_addc_co_u32_e32 v83, vcc, 0, v133, vcc
	global_load_dwordx4 v[90:93], v[82:83], off nt
	v_add_co_u32_e32 v82, vcc, s43, v132
	s_waitcnt vmcnt(15)
	v_mul_f32_e32 v130, v179, v10
	v_addc_co_u32_e32 v83, vcc, 0, v133, vcc
	global_load_dwordx4 v[94:97], v[82:83], off nt
	v_add_co_u32_e32 v82, vcc, s44, v132
	s_waitcnt vmcnt(15)
	v_mul_f32_e32 v137, v179, v26
	v_addc_co_u32_e32 v83, vcc, 0, v133, vcc
	global_load_dwordx4 v[110:113], v[82:83], off nt
	v_add_co_u32_e32 v82, vcc, s45, v132
	v_mov_b32_e32 v181, 0
	s_nop 0
	v_addc_co_u32_e32 v83, vcc, 0, v133, vcc
	v_add_co_u32_e32 v98, vcc, s46, v132
	v_cvt_pk_fp8_f32 v181, v130, v137
	s_nop 0
	v_addc_co_u32_e32 v99, vcc, 0, v133, vcc
	v_add_co_u32_e32 v102, vcc, s47, v132
	s_waitcnt vmcnt(15)
	v_mul_f32_e32 v182, v179, v22
	v_addc_co_u32_e32 v103, vcc, 0, v133, vcc
	v_add_co_u32_e32 v106, vcc, s48, v132
	global_load_dwordx4 v[102:105], v[102:103], off nt
	s_nop 0
	v_addc_co_u32_e32 v107, vcc, 0, v133, vcc
	global_load_dwordx4 v[114:117], v[106:107], off nt
	v_add_co_u32_e32 v106, vcc, s49, v132
	s_waitcnt vmcnt(16)
	v_mul_f32_e32 v183, v179, v42
	v_addc_co_u32_e32 v107, vcc, 0, v133, vcc
	v_add_co_u32_e32 v118, vcc, s50, v132
	v_cvt_pk_fp8_f32 v181, v182, v183 op_sel:[0,0,1]
	s_waitcnt vmcnt(15)
	v_mul_f32_e32 v130, v179, v14
	s_waitcnt vmcnt(14)
	v_mul_f32_e32 v137, v179, v34
	v_mov_b32_e32 v182, 0
	v_addc_co_u32_e32 v119, vcc, 0, v133, vcc
	v_cvt_pk_fp8_f32 v182, v130, v137
	v_add_co_u32_e32 v122, vcc, s51, v132
	s_waitcnt vmcnt(13)
	v_mul_f32_e32 v183, v179, v30
	v_addc_co_u32_e32 v123, vcc, 0, v133, vcc
	v_add_co_u32_e32 v126, vcc, s52, v132
	s_waitcnt vmcnt(12)
	v_mul_f32_e32 v184, v179, v46
	v_addc_co_u32_e32 v127, vcc, 0, v133, vcc
	v_cvt_pk_fp8_f32 v182, v183, v184 op_sel:[0,0,1]
	s_waitcnt vmcnt(11)
	v_mul_f32_e32 v130, v179, v38
	s_waitcnt vmcnt(10)
	v_mul_f32_e32 v137, v179, v54
	v_mov_b32_e32 v183, 0
	global_load_dwordx4 v[66:69], v[66:67], off nt
	v_cvt_pk_fp8_f32 v183, v130, v137
	global_load_dwordx4 v[70:73], v[70:71], off nt
	s_waitcnt vmcnt(11)
	v_mul_f32_e32 v184, v179, v50
	global_load_dwordx4 v[82:85], v[82:83], off nt
	s_waitcnt vmcnt(11)
	v_mul_f32_e32 v185, v179, v58
	global_load_dwordx4 v[98:101], v[98:99], off nt
	v_cvt_pk_fp8_f32 v183, v184, v185 op_sel:[0,0,1]
	global_load_dwordx4 v[106:109], v[106:107], off nt
	v_mul_f32_e32 v130, v179, v63
	global_load_dwordx4 v[118:121], v[118:119], off nt
	ds_write_b128 v160, v[180:183]
	global_load_dwordx4 v[122:125], v[122:123], off nt
	v_mul_f32_e32 v137, v179, v7
	global_load_dwordx4 v[126:129], v[126:127], off nt
	v_mov_b32_e32 v180, 0
	v_cvt_pk_fp8_f32 v180, v130, v137
	v_mul_f32_e32 v181, v179, v3
	v_mul_f32_e32 v182, v179, v19
	v_mul_f32_e32 v130, v179, v11
	v_cvt_pk_fp8_f32 v180, v181, v182 op_sel:[0,0,1]
	v_mul_f32_e32 v137, v179, v27
	v_mov_b32_e32 v181, 0
	v_cvt_pk_fp8_f32 v181, v130, v137
	v_mul_f32_e32 v182, v179, v23
	v_mul_f32_e32 v183, v179, v43
	v_mul_f32_e32 v130, v179, v15
	v_cvt_pk_fp8_f32 v181, v182, v183 op_sel:[0,0,1]
	v_mul_f32_e32 v137, v179, v35
	v_mov_b32_e32 v182, 0
	v_cvt_pk_fp8_f32 v182, v130, v137
	v_mul_f32_e32 v183, v179, v31
	v_mul_f32_e32 v184, v179, v47
	v_mul_f32_e32 v130, v179, v39
	v_cvt_pk_fp8_f32 v182, v183, v184 op_sel:[0,0,1]
	v_mul_f32_e32 v137, v179, v55
	v_mov_b32_e32 v183, 0
	v_cvt_pk_fp8_f32 v183, v130, v137
	v_mul_f32_e32 v184, v179, v51
	v_mul_f32_e32 v185, v179, v59
	v_mul_f32_e32 v130, v179, v64
	v_cvt_pk_fp8_f32 v183, v184, v185 op_sel:[0,0,1]
	v_mul_f32_e32 v137, v179, v8
	v_mul_f32_e32 v184, v179, v48
	v_mul_f32_e32 v185, v179, v60
	ds_write_b128 v160, v[180:183] offset:256
	v_mov_b32_e32 v180, 0
	v_cvt_pk_fp8_f32 v180, v130, v137
	v_mul_f32_e32 v181, v179, v4
	v_mul_f32_e32 v182, v179, v20
	v_mul_f32_e32 v130, v179, v12
	v_cvt_pk_fp8_f32 v180, v181, v182 op_sel:[0,0,1]
	v_mul_f32_e32 v137, v179, v28
	v_mov_b32_e32 v181, 0
	v_cvt_pk_fp8_f32 v181, v130, v137
	v_mul_f32_e32 v182, v179, v24
	v_mul_f32_e32 v183, v179, v44
	v_mul_f32_e32 v130, v179, v16
	v_cvt_pk_fp8_f32 v181, v182, v183 op_sel:[0,0,1]
	v_mul_f32_e32 v137, v179, v36
	v_mov_b32_e32 v182, 0
	v_cvt_pk_fp8_f32 v182, v130, v137
	v_mul_f32_e32 v183, v179, v32
	v_mul_f32_e32 v130, v179, v40
	v_mul_f32_e32 v137, v179, v56
	v_cvt_pk_fp8_f32 v182, v183, v184 op_sel:[0,0,1]
	v_mov_b32_e32 v183, 0
	v_cvt_pk_fp8_f32 v183, v130, v137
	v_mul_f32_e32 v184, v179, v52
	v_mul_f32_e32 v130, v179, v65
	v_mul_f32_e32 v137, v179, v9
	v_cvt_pk_fp8_f32 v183, v184, v185 op_sel:[0,0,1]
	v_mul_f32_e32 v184, v179, v49
	v_mul_f32_e32 v185, v179, v61
	s_cmpk_gt_i32 s55, 0x50f
	ds_write_b128 v160, v[180:183] offset:512
	v_mov_b32_e32 v180, 0
	v_cvt_pk_fp8_f32 v180, v130, v137
	v_mul_f32_e32 v181, v179, v5
	v_mul_f32_e32 v182, v179, v21
	v_mul_f32_e32 v130, v179, v13
	v_cvt_pk_fp8_f32 v180, v181, v182 op_sel:[0,0,1]
	v_mul_f32_e32 v137, v179, v29
	v_mov_b32_e32 v181, 0
	v_cvt_pk_fp8_f32 v181, v130, v137
	v_mul_f32_e32 v182, v179, v25
	v_mul_f32_e32 v183, v179, v45
	v_mul_f32_e32 v130, v179, v17
	v_cvt_pk_fp8_f32 v181, v182, v183 op_sel:[0,0,1]
	v_mul_f32_e32 v137, v179, v37
	v_mov_b32_e32 v182, 0
	v_cvt_pk_fp8_f32 v182, v130, v137
	v_mul_f32_e32 v183, v179, v33
	v_mul_f32_e32 v130, v179, v41
	v_mul_f32_e32 v137, v179, v57
	v_cvt_pk_fp8_f32 v182, v183, v184 op_sel:[0,0,1]
	v_mov_b32_e32 v183, 0
	v_cvt_pk_fp8_f32 v183, v130, v137
	v_mul_f32_e32 v184, v179, v53
	s_cselect_b64 s[2:3], -1, 0
	s_and_b64 vcc, exec, s[2:3]
	v_cvt_pk_fp8_f32 v183, v184, v185 op_sel:[0,0,1]
	ds_write_b128 v160, v[180:183] offset:768
	s_cbranch_vccnz .LBB0_1448
; #define CVT_LOAD(v, c, s_) do { _Pragma("unroll") for (int i_ = 0; i_ < 16; ++i_) v[i_] = *(const f32x4*)((c).src + (size_t)(64 * (s_) + i_) * (c).N); } while (0)
; __device__ __forceinline__ CvtItem cvt_moe_item(int it, const float* wg, const float* wu, const float* wd, unsigned char* WGU, unsigned char* WDN, int lane) {
;     const int which = it >> 11, r = it & 2047, e = r >> 7, q = r & 127; CvtItem c; c.which = which;
;     if (which < 2) { const int nb = q & 31, k0 = (q >> 5) * 256; c.nb = nb;
;         c.N = DFF; c.K = DM; c.wscale = which ? 64.f / LOG2E : 64.f * LOG2E; c.src = (which ? wu : wg) + (size_t)e * DM * DFF + (size_t)(k0 + 16 * (lane >> 4)) * DFF + nb * 64 + 4 * (lane & 15);
;         c.dst = WGU + (size_t)e * 4096 * DM + k0; }
;     else { const int nb = q & 15, k0 = (q >> 4) * 256; c.nb = nb;
;         c.N = DM; c.K = DFF; c.wscale = 64.f; c.src = wd + (size_t)e * DFF * DM + (size_t)(k0 + 16 * (lane >> 4)) * DM + nb * 64 + 4 * (lane & 15);
;         c.dst = WDN + (size_t)e * DM * DFF + k0; }
;     return c;
; }
; __device__ __forceinline__ void cvt_moe_pipe2(const CvtSrc& A, const CvtSrc& B, LAS float* scr, int gw, int NGW, int lane) {
;     ...
;         if (more) { cn = cvt_moe_item2(i1, A, B, lane); CVT_LOAD(va, cn, 0); }
	s_add_i32 s4, s55, 0x510
	s_ashr_i32 s53, s4, 11
	s_and_b32 s54, s4, 31
	s_and_b32 s33, s25, 0x300
	v_readlane_b32 s60, v254, 30
	s_cmpk_lt_u32 s4, 0x800
	v_readlane_b32 s61, v254, 31
	v_readlane_b32 s62, v254, 32
	v_readlane_b32 s63, v254, 33
	v_readlane_b32 s72, v254, 42
	v_readlane_b32 s73, v254, 43
	s_cselect_b64 vcc, -1, 0
	v_readlane_b32 s74, v254, 44
	v_readlane_b32 s75, v254, 45
	s_mov_b64 s[60:61], s[72:73]
	s_and_b64 s[8:9], vcc, exec
	s_mov_b64 s[62:63], s[74:75]
	s_cselect_b32 s9, s61, s63
	s_cselect_b32 s8, s60, s62
	s_bfe_u32 s58, s4, 0x40007
	s_lshl_b32 s4, s58, 23
	s_add_u32 s8, s8, s4
	v_or_b32_e32 v2, s33, v141
	s_addc_u32 s9, s9, 0
	v_lshlrev_b32_e32 v130, 13, v2
	v_lshl_add_u64 v[2:3], s[8:9], 0, v[130:131]
	s_lshl_b32 s4, s54, 8
	v_lshl_add_u64 v[2:3], v[2:3], 0, s[4:5]
	v_mov_b32_e32 v137, v131
	v_lshl_add_u64 v[132:133], v[2:3], 0, v[136:137]
	v_cndmask_b32_e32 v178, v139, v140, vcc
	v_add_co_u32_e32 v2, vcc, s24, v132
	s_lshl_b32 s4, s58, 22
	s_nop 0
	v_addc_co_u32_e32 v3, vcc, 0, v133, vcc
	v_add_co_u32_e32 v4, vcc, s23, v132
	v_readlane_b32 s8, v255, 1
	s_nop 0
	v_addc_co_u32_e32 v5, vcc, 0, v133, vcc
	v_add_co_u32_e32 v10, vcc, s22, v132
	global_load_dwordx4 v[6:9], v[2:3], off nt
	s_nop 0
	global_load_dwordx4 v[2:5], v[4:5], off nt
	v_addc_co_u32_e32 v11, vcc, 0, v133, vcc
	v_add_co_u32_e32 v12, vcc, s21, v132
	v_readlane_b32 s9, v255, 2
	s_nop 0
	v_addc_co_u32_e32 v13, vcc, 0, v133, vcc
	v_add_co_u32_e32 v14, vcc, s20, v132
	global_load_dwordx4 v[18:21], v[10:11], off nt
	s_nop 0
	global_load_dwordx4 v[10:13], v[12:13], off nt
	v_addc_co_u32_e32 v15, vcc, 0, v133, vcc
	v_add_co_u32_e32 v16, vcc, s19, v132
	s_add_u32 s4, s8, s4
	s_nop 0
	v_addc_co_u32_e32 v17, vcc, 0, v133, vcc
	global_load_dwordx4 v[26:29], v[14:15], off nt
	global_load_dwordx4 v[22:25], v[16:17], off nt
	v_add_co_u32_e32 v14, vcc, s18, v132
	s_addc_u32 s9, s9, 0
	s_nop 0
	v_addc_co_u32_e32 v15, vcc, 0, v133, vcc
	v_add_co_u32_e32 v16, vcc, s17, v132
	s_add_u32 s8, s4, s33
	s_nop 0
	v_addc_co_u32_e32 v17, vcc, 0, v133, vcc
	v_add_co_u32_e32 v30, vcc, s16, v132
	global_load_dwordx4 v[42:45], v[14:15], off nt
	s_nop 0
	global_load_dwordx4 v[14:17], v[16:17], off nt
	v_addc_co_u32_e32 v31, vcc, 0, v133, vcc
	v_add_co_u32_e32 v32, vcc, s15, v132
	s_addc_u32 s9, s9, 0
	s_nop 0
	v_addc_co_u32_e32 v33, vcc, 0, v133, vcc
	v_add_co_u32_e32 v38, vcc, s14, v132
	global_load_dwordx4 v[34:37], v[30:31], off nt
	s_nop 0
	global_load_dwordx4 v[30:33], v[32:33], off nt
	v_addc_co_u32_e32 v39, vcc, 0, v133, vcc
	v_add_co_u32_e32 v40, vcc, s13, v132
	v_readlane_b32 s64, v254, 34
	s_nop 0
	v_addc_co_u32_e32 v41, vcc, 0, v133, vcc
	v_add_co_u32_e32 v50, vcc, s12, v132
	global_load_dwordx4 v[46:49], v[38:39], off nt
	s_nop 0
	global_load_dwordx4 v[38:41], v[40:41], off nt
	v_addc_co_u32_e32 v51, vcc, 0, v133, vcc
	v_add_co_u32_e32 v52, vcc, s11, v132
	v_readlane_b32 s65, v254, 35
	s_nop 0
	v_addc_co_u32_e32 v53, vcc, 0, v133, vcc
	v_add_co_u32_e32 v58, vcc, s10, v132
	global_load_dwordx4 v[54:57], v[50:51], off nt
	s_nop 0
	global_load_dwordx4 v[50:53], v[52:53], off nt
	v_addc_co_u32_e32 v59, vcc, 0, v133, vcc
	global_load_dwordx4 v[62:65], v[132:133], off nt
	s_nop 0
	global_load_dwordx4 v[58:61], v[58:59], off nt
	v_readlane_b32 s66, v254, 36
	v_readlane_b32 s67, v254, 37
	v_readlane_b32 s68, v254, 38
	v_readlane_b32 s69, v254, 39
	v_readlane_b32 s70, v254, 40
	v_readlane_b32 s71, v254, 41
	s_branch .LBB0_1448

; #define xcd_barrier_wait_if_single(p) xcd_barrier_wait(*(p))
; __device__ __forceinline__ CvtItem cvt_moe_item(int it, const float* wg, const float* wu, const float* wd, unsigned char* WGU, unsigned char* WDN, int lane) {
;     const int which = it >> 11, r = it & 2047, e = r >> 7, q = r & 127; CvtItem c; c.which = which;
;     if (which < 2) { const int nb = q & 31, k0 = (q >> 5) * 256; c.nb = nb;
;         c.N = DFF; c.K = DM; c.wscale = which ? 64.f / LOG2E : 64.f * LOG2E; c.src = (which ? wu : wg) + (size_t)e * DM * DFF + (size_t)(k0 + 16 * (lane >> 4)) * DFF + nb * 64 + 4 * (lane & 15);
;         c.dst = WGU + (size_t)e * 4096 * DM + k0; }
;     else { const int nb = q & 15, k0 = (q >> 4) * 256; c.nb = nb;
; __global__ void __launch_bounds__(NWAVES * 64, 2) enc_fwd(Args args) {
;     ...
;         if (G > 64 && blk >= 64) { cvt_moe(args.in[22], args.in[23], args.in[24], WGU1, WDN1, scr, (blk - 64) * NWAVES + wave, (G - 64) * NWAVES, lane, CVT1_P6, CVT1_LATE); if (MK_SINGLE && IN(15)) xcd_barrier_wait_if_single(bar_ptr); }
.LBB0_1452:
	s_andn2_b64 vcc, exec, s[2:3]
	s_cbranch_vccnz .LBB0_1475
	v_readlane_b32 s2, v254, 10
	s_lshl_b32 s2, s2, 3
	v_readlane_b32 s3, v254, 59
	s_add_i32 s2, s2, s3
	s_add_i32 s4, s2, 0xfffffe00
	s_cmpk_gt_i32 s4, 0x50f
	s_cbranch_scc1 .LBB0_1458
	s_add_i32 s6, s4, 0x510
	v_readlane_b32 s28, v254, 52
	s_lshl_b32 s4, s6, 3
	s_add_i32 s3, s28, 0xfffffe00
	s_ashr_i32 s56, s6, 11
	s_and_b32 s57, s6, 31
	s_and_b32 s10, s4, 0x300
	v_readlane_b32 s12, v254, 30
	s_cmpk_lt_u32 s6, 0x800
	v_readlane_b32 s13, v254, 31
	v_readlane_b32 s14, v254, 32
	v_readlane_b32 s15, v254, 33
	v_readlane_b32 s24, v254, 42
	v_readlane_b32 s25, v254, 43
	s_cselect_b64 vcc, -1, 0
	v_readlane_b32 s26, v254, 44
	v_readlane_b32 s27, v254, 45
	s_mov_b64 s[12:13], s[24:25]
	s_and_b64 s[4:5], vcc, exec
	s_mov_b64 s[14:15], s[26:27]
	s_cselect_b32 s4, s13, s15
	s_cselect_b32 s8, s12, s14
	s_bfe_u32 s9, s6, 0x40007
	s_lshl_b32 s6, s9, 22
	v_readlane_b32 s12, v255, 1
	v_readlane_b32 s13, v255, 2
	s_add_u32 s6, s12, s6
	s_addc_u32 s7, s13, 0
	s_add_u32 s6, s6, s10
	s_addc_u32 s7, s7, 0
	s_lshl_b32 s9, s9, 23
	v_and_b32_e32 v141, 48, v1
	s_add_u32 s8, s8, s9
	v_or_b32_e32 v2, s10, v141
	s_addc_u32 s9, s4, 0
	v_lshlrev_b32_e32 v130, 13, v2
	v_mov_b32_e32 v131, 0
	v_lshlrev_b32_e32 v4, 2, v138
	s_mov_b32 s5, 0
	v_lshl_add_u64 v[2:3], s[8:9], 0, v[130:131]
	s_lshl_b32 s4, s57, 8
	s_waitcnt vmcnt(0)
; __device__ __forceinline__ unsigned pk4_fp8(float a, float b, float c, float d) { unsigned w = 0u; w = __builtin_amdgcn_cvt_pk_fp8_f32(a, b, w, false); w = __builtin_amdgcn_cvt_pk_fp8_f32(c, d, w, true); return w; }
; #define LAS __attribute__((address_space(3)))
; __device__ __forceinline__ CvtItem cvt_moe_item(int it, const float* wg, const float* wu, const float* wd, unsigned char* WGU, unsigned char* WDN, int lane) {
;     const int which = it >> 11, r = it & 2047, e = r >> 7, q = r & 127; CvtItem c; c.which = which;
;     if (which < 2) { const int nb = q & 31, k0 = (q >> 5) * 256; c.nb = nb;
;         c.N = DFF; c.K = DM; c.wscale = which ? 64.f / LOG2E : 64.f * LOG2E; c.src = (which ? wu : wg) + (size_t)e * DM * DFF + (size_t)(k0 + 16 * (lane >> 4)) * DFF + nb * 64 + 4 * (lane & 15);
;         c.dst = WGU + (size_t)e * 4096 * DM + k0; }
;     else { const int nb = q & 15, k0 = (q >> 4) * 256; c.nb = nb;
;         c.N = DM; c.K = DFF; c.wscale = 64.f; c.src = wd + (size_t)e * DFF * DM + (size_t)(k0 + 16 * (lane >> 4)) * DM + nb * 64 + 4 * (lane & 15);
;         c.dst = WDN + (size_t)e * DM * DFF + k0; }
;     return c;
; }
; __device__ __forceinline__ void cvt_pack8(const f32x4 (&v)[16], const CvtItem& c, LAS unsigned char* blk, int s4, int lane) {
;     const float w = c.wscale; const int cb = lane & 15, j = 4 * s4 + (lane >> 4);
; #pragma unroll
;     for (int jn = 0; jn < 4; ++jn) {
;         v4u o; o.x = pg8::pk4_fp8(v[0][jn] * w, v[1][jn] * w, v[2][jn] * w, v[3][jn] * w); o.y = pg8::pk4_fp8(v[4][jn] * w, v[5][jn] * w, v[6][jn] * w, v[7][jn] * w);
;         o.z = pg8::pk4_fp8(v[8][jn] * w, v[9][jn] * w, v[10][jn] * w, v[11][jn] * w); o.w = pg8::pk4_fp8(v[12][jn] * w, v[13][jn] * w, v[14][jn] * w, v[15][jn] * w);
;         *(LAS v4u*)(blk + (4 * cb + jn) * 256 + ((j ^ cb) * 16)) = o; }
; }
	v_and_b32_e32 v66, 60, v4
	v_lshl_add_u64 v[2:3], v[2:3], 0, s[4:5]
	v_lshlrev_b32_e32 v130, 2, v66
	v_mov_b32_e32 v139, 0x42317218
	v_mov_b32_e32 v140, 0x42b8aa3b
	v_lshl_add_u64 v[132:133], v[2:3], 0, v[130:131]
	s_mov_b32 s10, 0x1e000
	v_cndmask_b32_e32 v177, v139, v140, vcc
	v_add_co_u32_e32 v2, vcc, s10, v132
	s_mov_b32 s11, 0x1c000
	s_nop 0
	v_addc_co_u32_e32 v3, vcc, 0, v133, vcc
	v_add_co_u32_e32 v4, vcc, s11, v132
	s_mov_b32 s12, 0x1a000
	s_nop 0
	v_addc_co_u32_e32 v5, vcc, 0, v133, vcc
	global_load_dwordx4 v[58:61], v[2:3], off nt
	global_load_dwordx4 v[50:53], v[4:5], off nt
	v_add_co_u32_e32 v2, vcc, s12, v132
	s_mov_b32 s13, 0x18000
	s_nop 0
	v_addc_co_u32_e32 v3, vcc, 0, v133, vcc
	v_add_co_u32_e32 v4, vcc, s13, v132
	s_mov_b32 s14, 0x16000
	s_nop 0
	v_addc_co_u32_e32 v5, vcc, 0, v133, vcc
	global_load_dwordx4 v[54:57], v[2:3], off nt
	global_load_dwordx4 v[38:41], v[4:5], off nt
	v_add_co_u32_e32 v2, vcc, s14, v132
	s_mov_b32 s15, 0x14000
	s_nop 0
	v_addc_co_u32_e32 v3, vcc, 0, v133, vcc
	v_readlane_b32 s16, v254, 34
	v_add_co_u32_e32 v4, vcc, s15, v132
	s_mov_b32 s16, 0x12000
	s_nop 0
	v_addc_co_u32_e32 v5, vcc, 0, v133, vcc
	v_readlane_b32 s17, v254, 35
	global_load_dwordx4 v[46:49], v[2:3], off nt
	global_load_dwordx4 v[30:33], v[4:5], off nt
	v_add_co_u32_e32 v2, vcc, s16, v132
	s_mov_b32 s17, 0x10000
	s_nop 0
	v_addc_co_u32_e32 v3, vcc, 0, v133, vcc
	v_readlane_b32 s18, v254, 36
	v_add_co_u32_e32 v4, vcc, s17, v132
	s_mov_b32 s18, 0xe000
	s_nop 0
	v_addc_co_u32_e32 v5, vcc, 0, v133, vcc
	v_readlane_b32 s19, v254, 37
	global_load_dwordx4 v[34:37], v[2:3], off nt
	global_load_dwordx4 v[14:17], v[4:5], off nt
	v_add_co_u32_e32 v2, vcc, s18, v132
	s_mov_b32 s19, 0xc000
	s_nop 0
	v_addc_co_u32_e32 v3, vcc, 0, v133, vcc
	v_readlane_b32 s20, v254, 38
	v_add_co_u32_e32 v4, vcc, s19, v132
	s_mov_b32 s20, 0xa000
	s_nop 0
	v_addc_co_u32_e32 v5, vcc, 0, v133, vcc
	v_readlane_b32 s21, v254, 39
	global_load_dwordx4 v[42:45], v[2:3], off nt
	global_load_dwordx4 v[22:25], v[4:5], off nt
	v_add_co_u32_e32 v2, vcc, s20, v132
	s_mov_b32 s21, 0x8000
	s_nop 0
	v_addc_co_u32_e32 v3, vcc, 0, v133, vcc
	v_readlane_b32 s22, v254, 40
	v_add_co_u32_e32 v4, vcc, s21, v132
	s_movk_i32 s22, 0x6000
	s_nop 0
	v_addc_co_u32_e32 v5, vcc, 0, v133, vcc
	v_readlane_b32 s23, v254, 41
	global_load_dwordx4 v[26:29], v[2:3], off nt
	global_load_dwordx4 v[10:13], v[4:5], off nt
	v_add_co_u32_e32 v2, vcc, s22, v132
	s_movk_i32 s23, 0x4000
	s_nop 0
	v_addc_co_u32_e32 v3, vcc, 0, v133, vcc
	v_add_co_u32_e32 v4, vcc, s23, v132
	s_movk_i32 s24, 0x2000
	s_nop 0
	v_addc_co_u32_e32 v5, vcc, 0, v133, vcc
	v_add_co_u32_e32 v6, vcc, s24, v132
	global_load_dwordx4 v[18:21], v[2:3], off nt
	s_nop 0
	global_load_dwordx4 v[2:5], v[4:5], off nt
	v_addc_co_u32_e32 v7, vcc, 0, v133, vcc
	global_load_dwordx4 v[6:9], v[6:7], off nt
	s_nop 0
	global_load_dwordx4 v[62:65], v[132:133], off nt
	v_lshrrev_b32_e32 v138, 4, v138
	v_and_b32_e32 v67, 15, v1
	v_bitop3_b32 v1, v138, v1, 15 bitop3:0x78
	v_readlane_b32 s4, v254, 60
	v_lshlrev_b32_e32 v69, 4, v1
	v_or_b32_e32 v1, 4, v138
	v_or_b32_e32 v142, 8, v138
	v_or_b32_e32 v143, 12, v138
	v_or_b32_e32 v144, 16, v138
	v_or_b32_e32 v145, 20, v138
	v_or_b32_e32 v146, 24, v138
	v_or_b32_e32 v147, 28, v138
	v_or_b32_e32 v148, 32, v138
	v_or_b32_e32 v149, 36, v138
	v_or_b32_e32 v150, 40, v138
	v_or_b32_e32 v151, 44, v138
	v_or_b32_e32 v152, 48, v138
	v_or_b32_e32 v153, 52, v138
	v_or_b32_e32 v154, 56, v138
	v_or_b32_e32 v155, 60, v138
	v_lshl_add_u32 v68, v67, 10, s4
	v_bitop3_b32 v70, v138, v67, 4 bitop3:0x36
	v_bitop3_b32 v71, v138, v67, 8 bitop3:0x36
	v_bitop3_b32 v72, v138, v67, 12 bitop3:0x36
	v_lshlrev_b32_e32 v134, 4, v67
	v_lshl_add_u32 v67, v138, 8, s4
	v_lshl_add_u32 v73, v1, 8, s4
	v_lshl_add_u32 v75, v142, 8, s4
	v_lshl_add_u32 v77, v143, 8, s4
	v_lshl_add_u32 v79, v144, 8, s4
	v_lshl_add_u32 v81, v145, 8, s4
	v_lshl_add_u32 v83, v146, 8, s4
	v_lshl_add_u32 v85, v147, 8, s4
	v_lshl_add_u32 v87, v148, 8, s4
	v_lshl_add_u32 v89, v149, 8, s4
	v_lshl_add_u32 v91, v150, 8, s4
	v_lshl_add_u32 v93, v151, 8, s4
	v_lshl_add_u32 v95, v152, 8, s4
	v_lshl_add_u32 v97, v153, 8, s4
	v_lshl_add_u32 v99, v154, 8, s4
	v_lshl_add_u32 v101, v155, 8, s4
	s_add_i32 s4, s2, s28
	s_lshl_b32 s4, s4, 3
	s_add_i32 s25, s4, 0x880
	v_readlane_b32 s4, v254, 9
	v_lshlrev_b32_e32 v70, 4, v70
	v_lshlrev_b32_e32 v71, 4, v71
	v_lshlrev_b32_e32 v72, 4, v72
	v_xor_b32_e32 v74, 16, v134
	v_xor_b32_e32 v76, 32, v134
	v_xor_b32_e32 v78, 48, v134
	v_xor_b32_e32 v80, 64, v134
	v_xor_b32_e32 v82, 0x50, v134
	v_xor_b32_e32 v84, 0x60, v134
	v_xor_b32_e32 v86, 0x70, v134
	v_xor_b32_e32 v88, 0x80, v134
	v_xor_b32_e32 v90, 0x90, v134
	v_xor_b32_e32 v92, 0xa0, v134
	v_xor_b32_e32 v94, 0xb0, v134
	v_xor_b32_e32 v96, 0xc0, v134
	v_xor_b32_e32 v98, 0xd0, v134
	v_xor_b32_e32 v100, 0xe0, v134
	v_xor_b32_e32 v102, 0xf0, v134
	s_lshl_b32 s26, s4, 6
	v_mov_b32_e32 v135, v131
	s_addk_i32 s26, 0xf000
	v_add_u32_e32 v156, v68, v69
	s_mov_b32 s27, 0x10e000
	s_mov_b32 s28, 0x110000
	s_mov_b32 s29, 0x112000
	s_mov_b32 s30, 0x114000
	s_mov_b32 s31, 0x116000
	s_mov_b32 s34, 0x118000
	s_mov_b32 s35, 0x11a000
	s_mov_b32 s36, 0x11c000
	s_mov_b32 s37, 0x11e000
	v_add_u32_e32 v157, v68, v70
	s_mov_b32 s38, 0x180000
	s_mov_b32 s39, 0x182000
	s_mov_b32 s40, 0x184000
	s_mov_b32 s41, 0x186000
	s_mov_b32 s42, 0x188000
	s_mov_b32 s43, 0x18a000
	s_mov_b32 s44, 0x18c000
	s_mov_b32 s45, 0x18e000
	s_mov_b32 s46, 0x190000
	s_mov_b32 s47, 0x192000
	s_mov_b32 s48, 0x194000
	s_mov_b32 s49, 0x196000
	s_mov_b32 s50, 0x198000
	s_mov_b32 s51, 0x19a000
	s_mov_b32 s52, 0x19c000
	s_mov_b32 s53, 0x19e000
	v_add_u32_e32 v158, v68, v71
	v_lshlrev_b32_e32 v136, 2, v66
	v_add_u32_e32 v159, v68, v72
	v_add_u32_e32 v160, v67, v134
	v_add_u32_e32 v161, v73, v74
	v_add_u32_e32 v162, v75, v76
	v_add_u32_e32 v163, v77, v78
	v_add_u32_e32 v164, v79, v80
	v_add_u32_e32 v165, v81, v82
	v_add_u32_e32 v166, v83, v84
	v_add_u32_e32 v167, v85, v86
	v_add_u32_e32 v168, v87, v88
	v_add_u32_e32 v169, v89, v90
	v_add_u32_e32 v170, v91, v92
	v_add_u32_e32 v171, v93, v94
	v_add_u32_e32 v172, v95, v96
	v_add_u32_e32 v173, v97, v98
	v_add_u32_e32 v174, v99, v100
	v_add_u32_e32 v175, v101, v102
	s_branch .LBB0_1456

; __device__ __forceinline__ unsigned pk4_fp8(float a, float b, float c, float d) { unsigned w = 0u; w = __builtin_amdgcn_cvt_pk_fp8_f32(a, b, w, false); w = __builtin_amdgcn_cvt_pk_fp8_f32(c, d, w, true); return w; }
; #define LAS __attribute__((address_space(3)))
; #define CVT_LOAD(v, c, s_) do { _Pragma("unroll") for (int i_ = 0; i_ < 16; ++i_) v[i_] = *(const f32x4*)((c).src + (size_t)(64 * (s_) + i_) * (c).N); } while (0)
; __device__ __forceinline__ void cvt_pack8(const f32x4 (&v)[16], const CvtItem& c, LAS unsigned char* blk, int s4, int lane) {
;     const float w = c.wscale; const int cb = lane & 15, j = 4 * s4 + (lane >> 4);
; #pragma unroll
;     for (int jn = 0; jn < 4; ++jn) {
;         v4u o; o.x = pg8::pk4_fp8(v[0][jn] * w, v[1][jn] * w, v[2][jn] * w, v[3][jn] * w); o.y = pg8::pk4_fp8(v[4][jn] * w, v[5][jn] * w, v[6][jn] * w, v[7][jn] * w);
;         o.z = pg8::pk4_fp8(v[8][jn] * w, v[9][jn] * w, v[10][jn] * w, v[11][jn] * w); o.w = pg8::pk4_fp8(v[12][jn] * w, v[13][jn] * w, v[14][jn] * w, v[15][jn] * w);
;         *(LAS v4u*)(blk + (4 * cb + jn) * 256 + ((j ^ cb) * 16)) = o; }
; }
; __device__ __forceinline__ void cvt_moe_pipe2(const CvtSrc& A, const CvtSrc& B, LAS float* scr, int gw, int NGW, int lane) {
;     ...
;     while (it < it1) {
;         const int i1 = it + NGW; const bool more = i1 < it1;
;         CVT_LOAD(vb, c, 1); cvt_pack8(va, c, blk, 0, lane);
;         CVT_LOAD(va, c, 2); cvt_pack8(vb, c, blk, 1, lane);
;         CVT_LOAD(vb, c, 3); cvt_pack8(va, c, blk, 2, lane);
.LBB0_1456:
	s_mov_b32 s58, 0x80000
	v_add_co_u32_e32 v66, vcc, s58, v132
	s_mov_b32 s58, 0x82000
	s_nop 0
	v_addc_co_u32_e32 v67, vcc, 0, v133, vcc
	v_add_co_u32_e32 v70, vcc, s58, v132
	s_mov_b32 s58, 0x84000
	s_nop 0
	v_addc_co_u32_e32 v71, vcc, 0, v133, vcc
	v_add_co_u32_e32 v74, vcc, s58, v132
	s_mov_b32 s58, 0x86000
	s_nop 0
	v_addc_co_u32_e32 v75, vcc, 0, v133, vcc
	v_add_co_u32_e32 v78, vcc, s58, v132
	s_mov_b32 s58, 0x88000
	s_nop 0
	v_addc_co_u32_e32 v79, vcc, 0, v133, vcc
	global_load_dwordx4 v[82:85], v[78:79], off nt
	v_add_co_u32_e32 v78, vcc, s58, v132
	s_mov_b32 s58, 0x8a000
	s_nop 0
	v_addc_co_u32_e32 v79, vcc, 0, v133, vcc
	v_add_co_u32_e32 v86, vcc, s58, v132
	s_mov_b32 s58, 0x8c000
	s_nop 0
	v_addc_co_u32_e32 v87, vcc, 0, v133, vcc
	global_load_dwordx4 v[90:93], v[86:87], off nt
	v_add_co_u32_e32 v86, vcc, s58, v132
	s_mov_b32 s58, 0x8e000
	s_nop 0
	v_addc_co_u32_e32 v87, vcc, 0, v133, vcc
	global_load_dwordx4 v[94:97], v[86:87], off nt
	v_add_co_u32_e32 v86, vcc, s58, v132
	s_mov_b32 s58, 0x90000
	s_nop 0
	v_addc_co_u32_e32 v87, vcc, 0, v133, vcc
	global_load_dwordx4 v[106:109], v[86:87], off nt
	v_add_co_u32_e32 v86, vcc, s58, v132
	s_mov_b32 s58, 0x92000
	s_nop 0
	v_addc_co_u32_e32 v87, vcc, 0, v133, vcc
	v_add_co_u32_e32 v98, vcc, s58, v132
	s_mov_b32 s58, 0x94000
	s_nop 0
	v_addc_co_u32_e32 v99, vcc, 0, v133, vcc
	v_add_co_u32_e32 v102, vcc, s58, v132
	s_waitcnt vmcnt(4)
	v_mul_f32_e32 v62, v62, v177
	v_mul_f32_e32 v6, v6, v177
	v_mov_b32_e32 v178, 0
	v_addc_co_u32_e32 v103, vcc, 0, v133, vcc
	s_mov_b32 s58, 0x96000
	v_cvt_pk_fp8_f32 v178, v62, v6
	v_add_co_u32_e32 v110, vcc, s58, v132
	s_mov_b32 s58, 0x98000
	s_nop 0
	v_addc_co_u32_e32 v111, vcc, 0, v133, vcc
	global_load_dwordx4 v[102:105], v[102:103], off nt
	v_mul_f32_e32 v2, v2, v177
	global_load_dwordx4 v[114:117], v[110:111], off nt
	v_add_co_u32_e32 v110, vcc, s58, v132
	v_mul_f32_e32 v18, v18, v177
	global_load_dwordx4 v[66:69], v[66:67], off nt
	v_addc_co_u32_e32 v111, vcc, 0, v133, vcc
	global_load_dwordx4 v[70:73], v[70:71], off nt
	s_mov_b32 s58, 0x9a000
	v_cvt_pk_fp8_f32 v178, v2, v18 op_sel:[0,0,1]
	v_mul_f32_e32 v2, v10, v177
	v_mul_f32_e32 v6, v26, v177
	v_mov_b32_e32 v179, 0
	global_load_dwordx4 v[78:81], v[78:79], off nt
	v_add_co_u32_e32 v118, vcc, s58, v132
	v_cvt_pk_fp8_f32 v179, v2, v6
	v_mul_f32_e32 v2, v14, v177
	v_mul_f32_e32 v6, v34, v177
	v_mov_b32_e32 v180, 0
	global_load_dwordx4 v[86:89], v[86:87], off nt
	v_addc_co_u32_e32 v119, vcc, 0, v133, vcc
	global_load_dwordx4 v[98:101], v[98:99], off nt
	s_mov_b32 s58, 0x9c000
	v_cvt_pk_fp8_f32 v180, v2, v6
	v_mul_f32_e32 v2, v38, v177
	v_mul_f32_e32 v6, v54, v177
	v_mov_b32_e32 v181, 0
	global_load_dwordx4 v[110:113], v[110:111], off nt
	v_add_co_u32_e32 v122, vcc, s58, v132
	global_load_dwordx4 v[118:121], v[118:119], off nt
	v_cvt_pk_fp8_f32 v181, v2, v6
	global_load_dwordx4 v[74:77], v[74:75], off nt
	v_addc_co_u32_e32 v123, vcc, 0, v133, vcc
	s_mov_b32 s58, 0x9e000
	v_mul_f32_e32 v10, v22, v177
	v_mul_f32_e32 v18, v42, v177
	v_add_co_u32_e32 v126, vcc, s58, v132
	v_cvt_pk_fp8_f32 v179, v10, v18 op_sel:[0,0,1]
	v_mul_f32_e32 v10, v30, v177
	v_mul_f32_e32 v14, v46, v177
	v_addc_co_u32_e32 v127, vcc, 0, v133, vcc
	v_cvt_pk_fp8_f32 v180, v10, v14 op_sel:[0,0,1]
	v_mul_f32_e32 v10, v50, v177
	v_mul_f32_e32 v14, v58, v177
	global_load_dwordx4 v[122:125], v[122:123], off nt
	v_cvt_pk_fp8_f32 v181, v10, v14 op_sel:[0,0,1]
	global_load_dwordx4 v[126:129], v[126:127], off nt
	v_mul_f32_e32 v2, v63, v177
	v_mul_f32_e32 v6, v7, v177
	ds_write_b128 v156, v[178:181]
	v_mov_b32_e32 v178, 0
	v_cvt_pk_fp8_f32 v178, v2, v6
	v_mul_f32_e32 v3, v3, v177
	v_mul_f32_e32 v7, v19, v177
	v_mul_f32_e32 v2, v11, v177
	v_cvt_pk_fp8_f32 v178, v3, v7 op_sel:[0,0,1]
	v_mul_f32_e32 v3, v27, v177
	v_mov_b32_e32 v179, 0
	v_cvt_pk_fp8_f32 v179, v2, v3
	v_mul_f32_e32 v2, v15, v177
	v_mul_f32_e32 v3, v35, v177
	v_mov_b32_e32 v180, 0
	v_cvt_pk_fp8_f32 v180, v2, v3
	v_mul_f32_e32 v2, v39, v177
	v_mul_f32_e32 v3, v55, v177
	v_mov_b32_e32 v181, 0
	v_cvt_pk_fp8_f32 v181, v2, v3
	v_mul_f32_e32 v6, v23, v177
	v_mul_f32_e32 v7, v43, v177
	v_cvt_pk_fp8_f32 v179, v6, v7 op_sel:[0,0,1]
	v_mul_f32_e32 v6, v31, v177
	v_mul_f32_e32 v7, v47, v177
	v_cvt_pk_fp8_f32 v180, v6, v7 op_sel:[0,0,1]
	v_mul_f32_e32 v6, v51, v177
	v_mul_f32_e32 v7, v59, v177
	v_cvt_pk_fp8_f32 v181, v6, v7 op_sel:[0,0,1]
	v_mul_f32_e32 v2, v64, v177
	v_mul_f32_e32 v3, v8, v177
	v_mul_f32_e32 v4, v4, v177
	ds_write_b128 v156, v[178:181] offset:256
	v_mov_b32_e32 v178, 0
	v_cvt_pk_fp8_f32 v178, v2, v3
	v_mul_f32_e32 v2, v12, v177
	v_mul_f32_e32 v3, v28, v177
	v_mov_b32_e32 v179, 0
	v_cvt_pk_fp8_f32 v179, v2, v3
	v_mul_f32_e32 v2, v16, v177
	v_mul_f32_e32 v3, v36, v177
	v_mov_b32_e32 v180, 0
	v_cvt_pk_fp8_f32 v180, v2, v3
	v_mul_f32_e32 v2, v40, v177
	v_mul_f32_e32 v3, v56, v177
	v_mov_b32_e32 v181, 0
	v_mul_f32_e32 v6, v20, v177
	v_cvt_pk_fp8_f32 v181, v2, v3
	v_cvt_pk_fp8_f32 v178, v4, v6 op_sel:[0,0,1]
	v_mul_f32_e32 v4, v24, v177
	v_mul_f32_e32 v6, v44, v177
	v_cvt_pk_fp8_f32 v179, v4, v6 op_sel:[0,0,1]
	v_mul_f32_e32 v4, v32, v177
	v_mul_f32_e32 v6, v48, v177
	v_cvt_pk_fp8_f32 v180, v4, v6 op_sel:[0,0,1]
	v_mul_f32_e32 v4, v52, v177
	v_mul_f32_e32 v6, v60, v177
	v_cvt_pk_fp8_f32 v181, v4, v6 op_sel:[0,0,1]
	v_mul_f32_e32 v3, v65, v177
	v_mul_f32_e32 v4, v9, v177
	v_mov_b32_e32 v2, 0
	v_cvt_pk_fp8_f32 v2, v3, v4
	v_mul_f32_e32 v5, v5, v177
	v_mul_f32_e32 v6, v21, v177
	v_mul_f32_e32 v4, v13, v177
	v_cvt_pk_fp8_f32 v2, v5, v6 op_sel:[0,0,1]
	v_mul_f32_e32 v5, v29, v177
	v_mov_b32_e32 v3, 0
	v_cvt_pk_fp8_f32 v3, v4, v5
	v_mul_f32_e32 v6, v25, v177
	v_mul_f32_e32 v7, v45, v177
	v_mul_f32_e32 v5, v17, v177
	v_cvt_pk_fp8_f32 v3, v6, v7 op_sel:[0,0,1]
	v_mul_f32_e32 v6, v37, v177
	v_mov_b32_e32 v4, 0
	v_cvt_pk_fp8_f32 v4, v5, v6
	v_mul_f32_e32 v7, v33, v177
	v_mul_f32_e32 v8, v49, v177
	v_mul_f32_e32 v6, v41, v177
	v_cvt_pk_fp8_f32 v4, v7, v8 op_sel:[0,0,1]
	v_mul_f32_e32 v7, v57, v177
	v_mov_b32_e32 v5, 0
	v_cvt_pk_fp8_f32 v5, v6, v7
	v_mul_f32_e32 v8, v53, v177
	v_mul_f32_e32 v9, v61, v177
	s_mov_b32 s58, 0x100000
	v_cvt_pk_fp8_f32 v5, v8, v9 op_sel:[0,0,1]
	ds_write_b128 v156, v[178:181] offset:512
	v_mov_b32_e32 v178, 0
	v_mov_b32_e32 v179, 0
	ds_write_b128 v156, v[2:5] offset:768
	v_add_co_u32_e32 v2, vcc, s58, v132
	s_mov_b32 s58, 0x102000
	s_nop 0
	v_addc_co_u32_e32 v3, vcc, 0, v133, vcc
	global_load_dwordx4 v[62:65], v[2:3], off nt
	v_add_co_u32_e32 v2, vcc, s58, v132
	s_mov_b32 s58, 0x104000
	s_nop 0
	v_addc_co_u32_e32 v3, vcc, 0, v133, vcc
	global_load_dwordx4 v[6:9], v[2:3], off nt
	v_add_co_u32_e32 v2, vcc, s58, v132
	s_mov_b32 s58, 0x106000
	s_nop 0
	v_addc_co_u32_e32 v3, vcc, 0, v133, vcc
	v_add_co_u32_e32 v10, vcc, s58, v132
	s_mov_b32 s58, 0x108000
	s_nop 0
	v_addc_co_u32_e32 v11, vcc, 0, v133, vcc
	global_load_dwordx4 v[2:5], v[2:3], off nt
	s_waitcnt vmcnt(12)
; __device__ __forceinline__ unsigned pk4_fp8(float a, float b, float c, float d) { unsigned w = 0u; w = __builtin_amdgcn_cvt_pk_fp8_f32(a, b, w, false); w = __builtin_amdgcn_cvt_pk_fp8_f32(c, d, w, true); return w; }
; #define LAS __attribute__((address_space(3)))
; #define CVT_LOAD(v, c, s_) do { _Pragma("unroll") for (int i_ = 0; i_ < 16; ++i_) v[i_] = *(const f32x4*)((c).src + (size_t)(64 * (s_) + i_) * (c).N); } while (0)
; __device__ __forceinline__ void cvt_pack8(const f32x4 (&v)[16], const CvtItem& c, LAS unsigned char* blk, int s4, int lane) {
;     const float w = c.wscale; const int cb = lane & 15, j = 4 * s4 + (lane >> 4);
; #pragma unroll
;     for (int jn = 0; jn < 4; ++jn) {
;         v4u o; o.x = pg8::pk4_fp8(v[0][jn] * w, v[1][jn] * w, v[2][jn] * w, v[3][jn] * w); o.y = pg8::pk4_fp8(v[4][jn] * w, v[5][jn] * w, v[6][jn] * w, v[7][jn] * w);
;         o.z = pg8::pk4_fp8(v[8][jn] * w, v[9][jn] * w, v[10][jn] * w, v[11][jn] * w); o.w = pg8::pk4_fp8(v[12][jn] * w, v[13][jn] * w, v[14][jn] * w, v[15][jn] * w);
;         *(LAS v4u*)(blk + (4 * cb + jn) * 256 + ((j ^ cb) * 16)) = o; }
; }
; __device__ __forceinline__ void cvt_moe_pipe2(const CvtSrc& A, const CvtSrc& B, LAS float* scr, int gw, int NGW, int lane) {
;     ...
;         CVT_LOAD(vb, c, 1); cvt_pack8(va, c, blk, 0, lane);
;         CVT_LOAD(va, c, 2); cvt_pack8(vb, c, blk, 1, lane);
;         CVT_LOAD(vb, c, 3); cvt_pack8(va, c, blk, 2, lane);
	v_mul_f32_e32 v66, v177, v66
	global_load_dwordx4 v[18:21], v[10:11], off nt
	v_add_co_u32_e32 v10, vcc, s58, v132
	s_mov_b32 s58, 0x10a000
	s_nop 0
	v_addc_co_u32_e32 v11, vcc, 0, v133, vcc
	v_add_co_u32_e32 v14, vcc, s58, v132
	s_mov_b32 s58, 0x10c000
	s_nop 0
	v_addc_co_u32_e32 v15, vcc, 0, v133, vcc
	global_load_dwordx4 v[10:13], v[10:11], off nt
	s_waitcnt vmcnt(13)
	v_mul_f32_e32 v70, v177, v70
	global_load_dwordx4 v[26:29], v[14:15], off nt
	v_add_co_u32_e32 v14, vcc, s58, v132
	v_cvt_pk_fp8_f32 v178, v66, v70
	s_nop 0
	v_addc_co_u32_e32 v15, vcc, 0, v133, vcc
	global_load_dwordx4 v[22:25], v[14:15], off nt
	v_add_co_u32_e32 v14, vcc, s27, v132
	v_mul_f32_e32 v70, v177, v90
	s_nop 0
	v_addc_co_u32_e32 v15, vcc, 0, v133, vcc
	global_load_dwordx4 v[42:45], v[14:15], off nt
	v_add_co_u32_e32 v14, vcc, s28, v132
	s_waitcnt vmcnt(15)
	v_mul_f32_e32 v66, v177, v78
	v_addc_co_u32_e32 v15, vcc, 0, v133, vcc
	v_add_co_u32_e32 v30, vcc, s29, v132
	global_load_dwordx4 v[14:17], v[14:15], off nt
	s_nop 0
	v_addc_co_u32_e32 v31, vcc, 0, v133, vcc
	global_load_dwordx4 v[34:37], v[30:31], off nt
	v_add_co_u32_e32 v30, vcc, s30, v132
	v_cvt_pk_fp8_f32 v179, v66, v70
	s_nop 0
	v_addc_co_u32_e32 v31, vcc, 0, v133, vcc
	v_add_co_u32_e32 v38, vcc, s31, v132
	s_waitcnt vmcnt(16)
	v_mul_f32_e32 v66, v177, v86
	v_addc_co_u32_e32 v39, vcc, 0, v133, vcc
	s_waitcnt vmcnt(15)
	v_mul_f32_e32 v70, v177, v98
	v_mov_b32_e32 v180, 0
	global_load_dwordx4 v[30:33], v[30:31], off nt
	v_cvt_pk_fp8_f32 v180, v66, v70
	global_load_dwordx4 v[46:49], v[38:39], off nt
	v_add_co_u32_e32 v38, vcc, s34, v132
	s_waitcnt vmcnt(16)
	v_mul_f32_e32 v66, v177, v110
	s_waitcnt vmcnt(15)
	v_mul_f32_e32 v70, v177, v118
	v_mov_b32_e32 v181, 0
	v_addc_co_u32_e32 v39, vcc, 0, v133, vcc
	s_waitcnt vmcnt(14)
	v_mul_f32_e32 v74, v177, v74
	v_mul_f32_e32 v82, v177, v82
	v_cvt_pk_fp8_f32 v181, v66, v70
	v_add_co_u32_e32 v50, vcc, s35, v132
	v_cvt_pk_fp8_f32 v178, v74, v82 op_sel:[0,0,1]
	v_mul_f32_e32 v74, v177, v94
	v_mul_f32_e32 v78, v177, v106
	v_addc_co_u32_e32 v51, vcc, 0, v133, vcc
	v_cvt_pk_fp8_f32 v179, v74, v78 op_sel:[0,0,1]
	v_mul_f32_e32 v74, v177, v102
	v_mul_f32_e32 v78, v177, v114
	global_load_dwordx4 v[38:41], v[38:39], off nt
	v_cvt_pk_fp8_f32 v180, v74, v78 op_sel:[0,0,1]
	global_load_dwordx4 v[54:57], v[50:51], off nt
	v_add_co_u32_e32 v50, vcc, s36, v132
	s_waitcnt vmcnt(15)
	v_mul_f32_e32 v74, v177, v122
	s_waitcnt vmcnt(14)
	v_mul_f32_e32 v78, v177, v126
	v_addc_co_u32_e32 v51, vcc, 0, v133, vcc
	v_cvt_pk_fp8_f32 v181, v74, v78 op_sel:[0,0,1]
	v_add_co_u32_e32 v58, vcc, s37, v132
	global_load_dwordx4 v[50:53], v[50:51], off nt
	s_nop 0
	v_addc_co_u32_e32 v59, vcc, 0, v133, vcc
	global_load_dwordx4 v[58:61], v[58:59], off nt
	ds_write_b128 v157, v[178:181]
	v_mul_f32_e32 v66, v177, v67
	v_mul_f32_e32 v67, v177, v71
	v_mov_b32_e32 v178, 0
	v_cvt_pk_fp8_f32 v178, v66, v67
	v_mul_f32_e32 v66, v177, v79
	v_mul_f32_e32 v67, v177, v91
	v_mov_b32_e32 v179, 0
	v_cvt_pk_fp8_f32 v179, v66, v67
	v_mul_f32_e32 v66, v177, v87
	v_mul_f32_e32 v67, v177, v99
	v_mov_b32_e32 v180, 0
	v_cvt_pk_fp8_f32 v180, v66, v67
	v_mul_f32_e32 v66, v177, v111
	v_mul_f32_e32 v67, v177, v119
	v_mov_b32_e32 v181, 0
	v_mul_f32_e32 v70, v177, v75
	v_mul_f32_e32 v71, v177, v83
	v_cvt_pk_fp8_f32 v181, v66, v67
	v_cvt_pk_fp8_f32 v178, v70, v71 op_sel:[0,0,1]
	v_mul_f32_e32 v70, v177, v95
	v_mul_f32_e32 v71, v177, v107
	v_cvt_pk_fp8_f32 v179, v70, v71 op_sel:[0,0,1]
	v_mul_f32_e32 v70, v177, v103
	v_mul_f32_e32 v71, v177, v115
	v_cvt_pk_fp8_f32 v180, v70, v71 op_sel:[0,0,1]
	v_mul_f32_e32 v70, v177, v123
	v_mul_f32_e32 v71, v177, v127
	v_cvt_pk_fp8_f32 v181, v70, v71 op_sel:[0,0,1]
	v_mul_f32_e32 v66, v177, v68
	v_mul_f32_e32 v67, v177, v72
	v_mul_f32_e32 v68, v177, v76
	ds_write_b128 v157, v[178:181] offset:256
	v_mov_b32_e32 v178, 0
	v_cvt_pk_fp8_f32 v178, v66, v67
	v_mul_f32_e32 v66, v177, v80
	v_mul_f32_e32 v67, v177, v92
	v_mov_b32_e32 v179, 0
	v_cvt_pk_fp8_f32 v179, v66, v67
	v_mul_f32_e32 v66, v177, v88
	v_mul_f32_e32 v67, v177, v100
	v_mov_b32_e32 v180, 0
	v_cvt_pk_fp8_f32 v180, v66, v67
	v_mul_f32_e32 v66, v177, v112
	v_mul_f32_e32 v67, v177, v120
	v_mov_b32_e32 v181, 0
	v_mul_f32_e32 v70, v177, v84
	v_cvt_pk_fp8_f32 v181, v66, v67
	v_cvt_pk_fp8_f32 v178, v68, v70 op_sel:[0,0,1]
	v_mul_f32_e32 v68, v177, v96
	v_mul_f32_e32 v70, v177, v108
	v_cvt_pk_fp8_f32 v179, v68, v70 op_sel:[0,0,1]
	v_mul_f32_e32 v68, v177, v104
	v_mul_f32_e32 v70, v177, v116
	v_cvt_pk_fp8_f32 v180, v68, v70 op_sel:[0,0,1]
	v_mul_f32_e32 v68, v177, v124
	v_mul_f32_e32 v70, v177, v128
	v_cvt_pk_fp8_f32 v181, v68, v70 op_sel:[0,0,1]
	v_mul_f32_e32 v67, v177, v69
	v_mul_f32_e32 v68, v177, v73
	v_mov_b32_e32 v66, 0
	v_cvt_pk_fp8_f32 v66, v67, v68
	v_mul_f32_e32 v69, v177, v77
	v_mul_f32_e32 v70, v177, v85
	v_mul_f32_e32 v68, v177, v81
	v_cvt_pk_fp8_f32 v66, v69, v70 op_sel:[0,0,1]
	v_mul_f32_e32 v69, v177, v93
	v_mov_b32_e32 v67, 0
	v_cvt_pk_fp8_f32 v67, v68, v69
	v_mul_f32_e32 v70, v177, v97
	v_mul_f32_e32 v71, v177, v109
	v_mul_f32_e32 v69, v177, v89
	v_cvt_pk_fp8_f32 v67, v70, v71 op_sel:[0,0,1]
	v_mul_f32_e32 v70, v177, v101
	v_mov_b32_e32 v68, 0
	v_cvt_pk_fp8_f32 v68, v69, v70
	v_mul_f32_e32 v71, v177, v105
	v_mul_f32_e32 v72, v177, v117
	v_mul_f32_e32 v70, v177, v113
	v_cvt_pk_fp8_f32 v68, v71, v72 op_sel:[0,0,1]
	v_mul_f32_e32 v71, v177, v121
	v_mov_b32_e32 v69, 0
	v_cvt_pk_fp8_f32 v69, v70, v71
	v_mul_f32_e32 v72, v177, v125
	v_mul_f32_e32 v73, v177, v129
	ds_write_b128 v157, v[178:181] offset:512
	v_cvt_pk_fp8_f32 v69, v72, v73 op_sel:[0,0,1]
	s_waitcnt vmcnt(15)
	v_mul_f32_e32 v130, v177, v62
	s_waitcnt vmcnt(14)
; __device__ __forceinline__ unsigned pk4_fp8(float a, float b, float c, float d) { unsigned w = 0u; w = __builtin_amdgcn_cvt_pk_fp8_f32(a, b, w, false); w = __builtin_amdgcn_cvt_pk_fp8_f32(c, d, w, true); return w; }
; #define LAS __attribute__((address_space(3)))
; #define CVT_LOAD(v, c, s_) do { _Pragma("unroll") for (int i_ = 0; i_ < 16; ++i_) v[i_] = *(const f32x4*)((c).src + (size_t)(64 * (s_) + i_) * (c).N); } while (0)
; __device__ __forceinline__ void cvt_pack8(const f32x4 (&v)[16], const CvtItem& c, LAS unsigned char* blk, int s4, int lane) {
;     const float w = c.wscale; const int cb = lane & 15, j = 4 * s4 + (lane >> 4);
; #pragma unroll
;     for (int jn = 0; jn < 4; ++jn) {
;         v4u o; o.x = pg8::pk4_fp8(v[0][jn] * w, v[1][jn] * w, v[2][jn] * w, v[3][jn] * w); o.y = pg8::pk4_fp8(v[4][jn] * w, v[5][jn] * w, v[6][jn] * w, v[7][jn] * w);
;         o.z = pg8::pk4_fp8(v[8][jn] * w, v[9][jn] * w, v[10][jn] * w, v[11][jn] * w); o.w = pg8::pk4_fp8(v[12][jn] * w, v[13][jn] * w, v[14][jn] * w, v[15][jn] * w);
;         *(LAS v4u*)(blk + (4 * cb + jn) * 256 + ((j ^ cb) * 16)) = o; }
; }
; __device__ __forceinline__ void cvt_moe_pipe2(const CvtSrc& A, const CvtSrc& B, LAS float* scr, int gw, int NGW, int lane) {
;     ...
;     while (it < it1) {
;         const int i1 = it + NGW; const bool more = i1 < it1;
;         CVT_LOAD(vb, c, 1); cvt_pack8(va, c, blk, 0, lane);
;         CVT_LOAD(va, c, 2); cvt_pack8(vb, c, blk, 1, lane);
;         CVT_LOAD(vb, c, 3); cvt_pack8(va, c, blk, 2, lane);
;         if (more) { cn = cvt_moe_item2(i1, A, B, lane); CVT_LOAD(va, cn, 0); }
;         cvt_pack8(vb, c, blk, 3, lane);
;         cvt_flush8(c, blk, lane);
;         if (more) c = cn;
;         it = i1;
	v_mul_f32_e32 v137, v177, v6
	v_mov_b32_e32 v178, 0
	ds_write_b128 v157, v[66:69] offset:768
	v_add_co_u32_e32 v66, vcc, s38, v132
	v_cvt_pk_fp8_f32 v178, v130, v137
	s_nop 0
	v_addc_co_u32_e32 v67, vcc, 0, v133, vcc
	v_add_co_u32_e32 v70, vcc, s39, v132
	s_waitcnt vmcnt(13)
	v_mul_f32_e32 v179, v177, v2
	v_addc_co_u32_e32 v71, vcc, 0, v133, vcc
	v_add_co_u32_e32 v74, vcc, s40, v132
	s_waitcnt vmcnt(12)
	v_mul_f32_e32 v180, v177, v18
	v_addc_co_u32_e32 v75, vcc, 0, v133, vcc
	v_add_co_u32_e32 v78, vcc, s41, v132
	global_load_dwordx4 v[74:77], v[74:75], off nt
	s_nop 0
	v_addc_co_u32_e32 v79, vcc, 0, v133, vcc
	global_load_dwordx4 v[86:89], v[78:79], off nt
	v_add_co_u32_e32 v78, vcc, s42, v132
	v_cvt_pk_fp8_f32 v178, v179, v180 op_sel:[0,0,1]
	s_nop 0
	v_addc_co_u32_e32 v79, vcc, 0, v133, vcc
	v_add_co_u32_e32 v82, vcc, s43, v132
	global_load_dwordx4 v[78:81], v[78:79], off nt
	s_nop 0
	v_addc_co_u32_e32 v83, vcc, 0, v133, vcc
	global_load_dwordx4 v[90:93], v[82:83], off nt
	v_add_co_u32_e32 v82, vcc, s44, v132
	s_waitcnt vmcnt(15)
	v_mul_f32_e32 v130, v177, v10
	v_addc_co_u32_e32 v83, vcc, 0, v133, vcc
	global_load_dwordx4 v[94:97], v[82:83], off nt
	v_add_co_u32_e32 v82, vcc, s45, v132
	s_waitcnt vmcnt(15)
	v_mul_f32_e32 v137, v177, v26
	v_addc_co_u32_e32 v83, vcc, 0, v133, vcc
	global_load_dwordx4 v[110:113], v[82:83], off nt
	v_add_co_u32_e32 v82, vcc, s46, v132
	v_mov_b32_e32 v179, 0
	s_nop 0
	v_addc_co_u32_e32 v83, vcc, 0, v133, vcc
	v_add_co_u32_e32 v98, vcc, s47, v132
	v_cvt_pk_fp8_f32 v179, v130, v137
	s_nop 0
	v_addc_co_u32_e32 v99, vcc, 0, v133, vcc
	v_add_co_u32_e32 v102, vcc, s48, v132
	s_waitcnt vmcnt(15)
	v_mul_f32_e32 v180, v177, v22
	v_addc_co_u32_e32 v103, vcc, 0, v133, vcc
	v_add_co_u32_e32 v106, vcc, s49, v132
	global_load_dwordx4 v[102:105], v[102:103], off nt
	s_nop 0
	v_addc_co_u32_e32 v107, vcc, 0, v133, vcc
	global_load_dwordx4 v[114:117], v[106:107], off nt
	v_add_co_u32_e32 v106, vcc, s50, v132
	s_waitcnt vmcnt(16)
	v_mul_f32_e32 v181, v177, v42
	v_addc_co_u32_e32 v107, vcc, 0, v133, vcc
	v_add_co_u32_e32 v118, vcc, s51, v132
	v_cvt_pk_fp8_f32 v179, v180, v181 op_sel:[0,0,1]
	s_waitcnt vmcnt(15)
	v_mul_f32_e32 v130, v177, v14
	s_waitcnt vmcnt(14)
	v_mul_f32_e32 v137, v177, v34
	v_mov_b32_e32 v180, 0
	v_addc_co_u32_e32 v119, vcc, 0, v133, vcc
	v_cvt_pk_fp8_f32 v180, v130, v137
	v_add_co_u32_e32 v122, vcc, s52, v132
	s_waitcnt vmcnt(13)
	v_mul_f32_e32 v181, v177, v30
	v_addc_co_u32_e32 v123, vcc, 0, v133, vcc
	v_add_co_u32_e32 v126, vcc, s53, v132
	s_waitcnt vmcnt(12)
	v_mul_f32_e32 v182, v177, v46
	v_addc_co_u32_e32 v127, vcc, 0, v133, vcc
	v_cvt_pk_fp8_f32 v180, v181, v182 op_sel:[0,0,1]
	s_waitcnt vmcnt(11)
	v_mul_f32_e32 v130, v177, v38
	s_waitcnt vmcnt(10)
	v_mul_f32_e32 v137, v177, v54
	v_mov_b32_e32 v181, 0
	global_load_dwordx4 v[66:69], v[66:67], off nt
	v_cvt_pk_fp8_f32 v181, v130, v137
	global_load_dwordx4 v[70:73], v[70:71], off nt
	s_waitcnt vmcnt(11)
	v_mul_f32_e32 v182, v177, v50
	global_load_dwordx4 v[82:85], v[82:83], off nt
	s_waitcnt vmcnt(11)
	v_mul_f32_e32 v183, v177, v58
	global_load_dwordx4 v[98:101], v[98:99], off nt
	v_cvt_pk_fp8_f32 v181, v182, v183 op_sel:[0,0,1]
	global_load_dwordx4 v[106:109], v[106:107], off nt
	v_mul_f32_e32 v130, v177, v63
	global_load_dwordx4 v[118:121], v[118:119], off nt
	ds_write_b128 v158, v[178:181]
	global_load_dwordx4 v[122:125], v[122:123], off nt
	v_mul_f32_e32 v137, v177, v7
	global_load_dwordx4 v[126:129], v[126:127], off nt
	v_mov_b32_e32 v178, 0
	v_cvt_pk_fp8_f32 v178, v130, v137
	v_mul_f32_e32 v179, v177, v3
	v_mul_f32_e32 v180, v177, v19
	v_mul_f32_e32 v130, v177, v11
	v_cvt_pk_fp8_f32 v178, v179, v180 op_sel:[0,0,1]
	v_mul_f32_e32 v137, v177, v27
	v_mov_b32_e32 v179, 0
	v_cvt_pk_fp8_f32 v179, v130, v137
	v_mul_f32_e32 v180, v177, v23
	v_mul_f32_e32 v181, v177, v43
	v_mul_f32_e32 v130, v177, v15
	v_cvt_pk_fp8_f32 v179, v180, v181 op_sel:[0,0,1]
	v_mul_f32_e32 v137, v177, v35
	v_mov_b32_e32 v180, 0
	v_cvt_pk_fp8_f32 v180, v130, v137
	v_mul_f32_e32 v181, v177, v31
	v_mul_f32_e32 v182, v177, v47
	v_mul_f32_e32 v130, v177, v39
	v_cvt_pk_fp8_f32 v180, v181, v182 op_sel:[0,0,1]
	v_mul_f32_e32 v137, v177, v55
	v_mov_b32_e32 v181, 0
	v_cvt_pk_fp8_f32 v181, v130, v137
	v_mul_f32_e32 v182, v177, v51
	v_mul_f32_e32 v183, v177, v59
	v_mul_f32_e32 v130, v177, v64
	v_cvt_pk_fp8_f32 v181, v182, v183 op_sel:[0,0,1]
	v_mul_f32_e32 v137, v177, v8
	v_mul_f32_e32 v182, v177, v48
	v_mul_f32_e32 v183, v177, v60
	ds_write_b128 v158, v[178:181] offset:256
	v_mov_b32_e32 v178, 0
	v_cvt_pk_fp8_f32 v178, v130, v137
	v_mul_f32_e32 v179, v177, v4
	v_mul_f32_e32 v180, v177, v20
	v_mul_f32_e32 v130, v177, v12
	v_cvt_pk_fp8_f32 v178, v179, v180 op_sel:[0,0,1]
	v_mul_f32_e32 v137, v177, v28
	v_mov_b32_e32 v179, 0
	v_cvt_pk_fp8_f32 v179, v130, v137
	v_mul_f32_e32 v180, v177, v24
	v_mul_f32_e32 v181, v177, v44
	v_mul_f32_e32 v130, v177, v16
	v_cvt_pk_fp8_f32 v179, v180, v181 op_sel:[0,0,1]
	v_mul_f32_e32 v137, v177, v36
	v_mov_b32_e32 v180, 0
	v_cvt_pk_fp8_f32 v180, v130, v137
	v_mul_f32_e32 v181, v177, v32
	v_mul_f32_e32 v130, v177, v40
	v_mul_f32_e32 v137, v177, v56
	v_cvt_pk_fp8_f32 v180, v181, v182 op_sel:[0,0,1]
	v_mov_b32_e32 v181, 0
	v_cvt_pk_fp8_f32 v181, v130, v137
	v_mul_f32_e32 v182, v177, v52
	v_mul_f32_e32 v130, v177, v65
	v_mul_f32_e32 v137, v177, v9
	v_cvt_pk_fp8_f32 v181, v182, v183 op_sel:[0,0,1]
	v_mul_f32_e32 v182, v177, v49
	v_mul_f32_e32 v183, v177, v61
	v_readlane_b32 s4, v254, 52
	ds_write_b128 v158, v[178:181] offset:512
	v_mov_b32_e32 v178, 0
	v_cvt_pk_fp8_f32 v178, v130, v137
	v_mul_f32_e32 v179, v177, v5
	v_mul_f32_e32 v180, v177, v21
	v_mul_f32_e32 v130, v177, v13
	v_cvt_pk_fp8_f32 v178, v179, v180 op_sel:[0,0,1]
	v_mul_f32_e32 v137, v177, v29
	v_mov_b32_e32 v179, 0
	v_cvt_pk_fp8_f32 v179, v130, v137
	v_mul_f32_e32 v180, v177, v25
	v_mul_f32_e32 v181, v177, v45
	v_mul_f32_e32 v130, v177, v17
	v_cvt_pk_fp8_f32 v179, v180, v181 op_sel:[0,0,1]
	v_mul_f32_e32 v137, v177, v37
	v_mov_b32_e32 v180, 0
	v_cvt_pk_fp8_f32 v180, v130, v137
	v_mul_f32_e32 v181, v177, v33
	v_mul_f32_e32 v130, v177, v41
	v_mul_f32_e32 v137, v177, v57
	v_cvt_pk_fp8_f32 v180, v181, v182 op_sel:[0,0,1]
	v_mov_b32_e32 v181, 0
	v_cvt_pk_fp8_f32 v181, v130, v137
	v_mul_f32_e32 v182, v177, v53
	s_add_i32 s4, s4, s2
	s_add_i32 s33, s4, 0xfffffc00
	v_cvt_pk_fp8_f32 v181, v182, v183 op_sel:[0,0,1]
	s_cmpk_gt_i32 s33, 0x50f
	ds_write_b128 v158, v[178:181] offset:768
	s_cbranch_scc1 .LBB0_1455
; #define CVT_LOAD(v, c, s_) do { _Pragma("unroll") for (int i_ = 0; i_ < 16; ++i_) v[i_] = *(const f32x4*)((c).src + (size_t)(64 * (s_) + i_) * (c).N); } while (0)
; __device__ __forceinline__ CvtItem cvt_moe_item(int it, const float* wg, const float* wu, const float* wd, unsigned char* WGU, unsigned char* WDN, int lane) {
;     const int which = it >> 11, r = it & 2047, e = r >> 7, q = r & 127; CvtItem c; c.which = which;
;     if (which < 2) { const int nb = q & 31, k0 = (q >> 5) * 256; c.nb = nb;
;         c.N = DFF; c.K = DM; c.wscale = which ? 64.f / LOG2E : 64.f * LOG2E; c.src = (which ? wu : wg) + (size_t)e * DM * DFF + (size_t)(k0 + 16 * (lane >> 4)) * DFF + nb * 64 + 4 * (lane & 15);
;         c.dst = WGU + (size_t)e * 4096 * DM + k0; }
;     else { const int nb = q & 15, k0 = (q >> 4) * 256; c.nb = nb;
;         c.N = DM; c.K = DFF; c.wscale = 64.f; c.src = wd + (size_t)e * DFF * DM + (size_t)(k0 + 16 * (lane >> 4)) * DM + nb * 64 + 4 * (lane & 15);
;         c.dst = WDN + (size_t)e * DM * DFF + k0; }
;     return c;
; }
; __device__ __forceinline__ void cvt_moe_pipe2(const CvtSrc& A, const CvtSrc& B, LAS float* scr, int gw, int NGW, int lane) {
;     ...
;         if (more) { cn = cvt_moe_item2(i1, A, B, lane); CVT_LOAD(va, cn, 0); }
	s_addk_i32 s4, 0x110
	s_ashr_i32 s54, s4, 11
	s_and_b32 s55, s4, 31
	s_and_b32 s33, s25, 0x300
	v_readlane_b32 s60, v254, 30
	s_cmpk_lt_u32 s4, 0x800
	v_readlane_b32 s61, v254, 31
	v_readlane_b32 s62, v254, 32
	v_readlane_b32 s63, v254, 33
	v_readlane_b32 s72, v254, 42
	v_readlane_b32 s73, v254, 43
	s_cselect_b64 vcc, -1, 0
	v_readlane_b32 s74, v254, 44
	v_readlane_b32 s75, v254, 45
	s_mov_b64 s[60:61], s[72:73]
	s_and_b64 s[8:9], vcc, exec
	s_mov_b64 s[62:63], s[74:75]
	s_cselect_b32 s9, s61, s63
	s_cselect_b32 s8, s60, s62
	s_bfe_u32 s58, s4, 0x40007
	s_lshl_b32 s4, s58, 23
	s_add_u32 s8, s8, s4
	v_or_b32_e32 v2, s33, v141
	s_addc_u32 s9, s9, 0
	v_lshlrev_b32_e32 v130, 13, v2
	v_lshl_add_u64 v[2:3], s[8:9], 0, v[130:131]
	s_lshl_b32 s4, s55, 8
	v_lshl_add_u64 v[2:3], v[2:3], 0, s[4:5]
	v_mov_b32_e32 v137, v131
	v_lshl_add_u64 v[132:133], v[2:3], 0, v[136:137]
	v_cndmask_b32_e32 v176, v139, v140, vcc
	v_add_co_u32_e32 v2, vcc, s24, v132
	s_lshl_b32 s4, s58, 22
	s_nop 0
	v_addc_co_u32_e32 v3, vcc, 0, v133, vcc
	v_add_co_u32_e32 v4, vcc, s23, v132
	v_readlane_b32 s8, v255, 1
	s_nop 0
	v_addc_co_u32_e32 v5, vcc, 0, v133, vcc
	v_add_co_u32_e32 v10, vcc, s22, v132
	global_load_dwordx4 v[6:9], v[2:3], off nt
	s_nop 0
	global_load_dwordx4 v[2:5], v[4:5], off nt
	v_addc_co_u32_e32 v11, vcc, 0, v133, vcc
	v_add_co_u32_e32 v12, vcc, s21, v132
	v_readlane_b32 s9, v255, 2
	s_nop 0
	v_addc_co_u32_e32 v13, vcc, 0, v133, vcc
	v_add_co_u32_e32 v14, vcc, s20, v132
	global_load_dwordx4 v[18:21], v[10:11], off nt
	s_nop 0
	global_load_dwordx4 v[10:13], v[12:13], off nt
	v_addc_co_u32_e32 v15, vcc, 0, v133, vcc
	v_add_co_u32_e32 v16, vcc, s19, v132
	s_add_u32 s4, s8, s4
	s_nop 0
	v_addc_co_u32_e32 v17, vcc, 0, v133, vcc
	global_load_dwordx4 v[26:29], v[14:15], off nt
	global_load_dwordx4 v[22:25], v[16:17], off nt
	v_add_co_u32_e32 v14, vcc, s18, v132
	s_addc_u32 s9, s9, 0
	s_nop 0
	v_addc_co_u32_e32 v15, vcc, 0, v133, vcc
	v_add_co_u32_e32 v16, vcc, s17, v132
	s_add_u32 s8, s4, s33
	s_nop 0
	v_addc_co_u32_e32 v17, vcc, 0, v133, vcc
	v_add_co_u32_e32 v30, vcc, s16, v132
	global_load_dwordx4 v[42:45], v[14:15], off nt
	s_nop 0
	global_load_dwordx4 v[14:17], v[16:17], off nt
	v_addc_co_u32_e32 v31, vcc, 0, v133, vcc
	v_add_co_u32_e32 v32, vcc, s15, v132
	s_addc_u32 s9, s9, 0
	s_nop 0
	v_addc_co_u32_e32 v33, vcc, 0, v133, vcc
	v_add_co_u32_e32 v38, vcc, s14, v132
	global_load_dwordx4 v[34:37], v[30:31], off nt
	s_nop 0
	global_load_dwordx4 v[30:33], v[32:33], off nt
	v_addc_co_u32_e32 v39, vcc, 0, v133, vcc
	v_add_co_u32_e32 v40, vcc, s13, v132
	v_readlane_b32 s64, v254, 34
	s_nop 0
	v_addc_co_u32_e32 v41, vcc, 0, v133, vcc
	v_add_co_u32_e32 v50, vcc, s12, v132
	global_load_dwordx4 v[46:49], v[38:39], off nt
	s_nop 0
	global_load_dwordx4 v[38:41], v[40:41], off nt
	v_addc_co_u32_e32 v51, vcc, 0, v133, vcc
	v_add_co_u32_e32 v52, vcc, s11, v132
	v_readlane_b32 s65, v254, 35
	s_nop 0
	v_addc_co_u32_e32 v53, vcc, 0, v133, vcc
	v_add_co_u32_e32 v58, vcc, s10, v132
	global_load_dwordx4 v[54:57], v[50:51], off nt
	s_nop 0
	global_load_dwordx4 v[50:53], v[52:53], off nt
	v_addc_co_u32_e32 v59, vcc, 0, v133, vcc
	global_load_dwordx4 v[62:65], v[132:133], off nt
	s_nop 0
	global_load_dwordx4 v[58:61], v[58:59], off nt
	v_readlane_b32 s66, v254, 36
	v_readlane_b32 s67, v254, 37
	v_readlane_b32 s68, v254, 38
	v_readlane_b32 s69, v254, 39
	v_readlane_b32 s70, v254, 40
	v_readlane_b32 s71, v254, 41
	s_branch .LBB0_1455
